# dpp4: lane-xor reductions (sum32 / wave_sum / row-stat half-row sums) via DPP and v_permlane16_swap instead of ds_swizzle round trips (127 of 176 sites), on top of att9
# speedup vs baseline: 1.0098x; 1.0010x over previous
; template <int M> __device__ __forceinline__ float swz_xor(float v) { return __int_as_float(__builtin_amdgcn_ds_swizzle(__float_as_int(v), (M << 10) | 0x1f)); }
; __device__ __forceinline__ void st_bf4(bf16_t* p, f32x4 v) { u32x2 w; w.x = cvt_pk_bf16(v[0], v[1]); w.y = cvt_pk_bf16(v[2], v[3]); *(u32x2*)p = w; }
; __device__ __forceinline__ float half_sum(float v) { auto rr = __builtin_amdgcn_permlane32_swap(__float_as_uint(v), __float_as_uint(v), false, false); return __uint_as_float(rr[0]) + __uint_as_float(rr[1]); }
; __device__ __forceinline__ float sum32(float v) { v += swz_xor<1>(v); v += swz_xor<2>(v); v += swz_xor<4>(v); v += swz_xor<8>(v); v += swz_xor<16>(v); return v; }
; __device__ __forceinline__ float wave_sum(float v) { return half_sum(sum32(v)); }
; __device__ __forceinline__ void memn_row(const float* xrow, const float* g, bf16_t* orow, int lane) {
;     const f32x4* xr = (const f32x4*)xrow + lane; const f32x4* gr = (const f32x4*)g + lane; f32x4 v[4]; float s = 0.f;
; #pragma unroll
;     for (int j = 0; j < 4; ++j) { v[j] = xr[64 * j]; s += (v[j][0] * v[j][0] + v[j][1] * v[j][1]) + (v[j][2] * v[j][2] + v[j][3] * v[j][3]); }
;     const float r = 1.0f / sqrtf(wave_sum(s) * (1.0f / DM) + EPS);
; #pragma unroll
;     for (int j = 0; j < 4; ++j) st_bf4(orow + j * 256 + lane * 4, v[j] * r * gr[64 * j]);
; }
.LBB0_429:
	global_load_dwordx4 v[10:13], v[6:7], off offset:-2048
	global_load_dwordx4 v[14:17], v[6:7], off offset:-1024
	global_load_dwordx4 v[18:21], v[6:7], off
	global_load_dwordx4 v[22:25], v[6:7], off offset:1024
	global_load_dwordx4 v[26:29], v[2:3], off
	s_add_i32 s10, s10, s54
	v_lshl_add_u64 v[6:7], v[6:7], 0, s[8:9]
	s_cmpk_gt_i32 s10, 0x7ff
	s_waitcnt vmcnt(4)
	v_mul_f32_e32 v9, v11, v11
	v_mul_f32_e32 v30, v13, v13
	s_waitcnt vmcnt(3)
	v_mul_f32_e32 v31, v15, v15
	v_mul_f32_e32 v32, v17, v17
	s_waitcnt vmcnt(2)
	v_mul_f32_e32 v33, v19, v19
	v_mul_f32_e32 v34, v21, v21
	v_fmac_f32_e32 v9, v10, v10
	v_fmac_f32_e32 v30, v12, v12
	v_fmac_f32_e32 v31, v14, v14
	v_fmac_f32_e32 v32, v16, v16
	s_waitcnt vmcnt(1)
	v_mul_f32_e32 v35, v23, v23
	v_mul_f32_e32 v36, v25, v25
	v_fmac_f32_e32 v33, v18, v18
	v_fmac_f32_e32 v34, v20, v20
	v_add_f32_e32 v9, v9, v30
	v_add_f32_e32 v30, v31, v32
	v_fmac_f32_e32 v35, v22, v22
	v_fmac_f32_e32 v36, v24, v24
	v_add_f32_e32 v31, v33, v34
	v_add_f32_e32 v9, v9, v30
	v_add_f32_e32 v32, v35, v36
	v_add_f32_e32 v9, v9, v31
	v_add_f32_e32 v9, v9, v32
	s_waitcnt lgkmcnt(0)
	s_nop 1
	v_add_f32_dpp v9, v9, v9 quad_perm:[1,0,3,2] row_mask:0xf bank_mask:0xf
	s_waitcnt lgkmcnt(0)
	s_nop 1
	v_add_f32_dpp v9, v9, v9 quad_perm:[2,3,0,1] row_mask:0xf bank_mask:0xf
	s_waitcnt lgkmcnt(0)
	s_nop 1
	v_add_f32_dpp v9, v9, v9 row_half_mirror row_mask:0xf bank_mask:0xf
	s_waitcnt lgkmcnt(0)
	s_nop 1
	v_add_f32_dpp v9, v9, v9 row_mirror row_mask:0xf bank_mask:0xf
	v_mov_b32_e32 v30, v9
	s_waitcnt lgkmcnt(0)
	s_nop 1
	v_permlane16_swap_b32_e32 v30, v9
	v_add_f32_e32 v9, v9, v30
	v_mov_b32_e32 v30, v9
	s_nop 1
	v_permlane32_swap_b32_e32 v9, v30
	v_add_f32_e32 v9, v9, v30
	v_fmamk_f32 v9, v9, 0x3a800000, v1
	v_mul_f32_e32 v30, 0x4f800000, v9
	v_cmp_gt_f32_e32 vcc, s3, v9
	s_nop 1
	v_cndmask_b32_e32 v9, v9, v30, vcc
	v_sqrt_f32_e32 v30, v9
	s_nop 0
	v_add_u32_e32 v31, -1, v30
	v_add_u32_e32 v32, 1, v30
	v_fma_f32 v33, -v31, v30, v9
	v_fma_f32 v34, -v32, v30, v9
	v_cmp_ge_f32_e64 s[4:5], 0, v33
	s_nop 1
	v_cndmask_b32_e64 v30, v30, v31, s[4:5]
	v_cmp_lt_f32_e64 s[4:5], 0, v34
	s_nop 1
	v_cndmask_b32_e64 v30, v30, v32, s[4:5]
	v_mul_f32_e32 v31, 0x37800000, v30
	v_cndmask_b32_e32 v30, v30, v31, vcc
	v_cmp_class_f32_e32 vcc, v9, v8
	s_nop 1
	v_cndmask_b32_e32 v9, v30, v9, vcc
	v_div_scale_f32 v30, s[4:5], v9, v9, 1.0
	v_rcp_f32_e32 v32, v30
	v_div_scale_f32 v31, vcc, 1.0, v9, 1.0
	v_fma_f32 v33, -v30, v32, 1.0
	v_fmac_f32_e32 v32, v33, v32
	v_mul_f32_e32 v33, v31, v32
	v_fma_f32 v34, -v30, v33, v31
	v_fmac_f32_e32 v33, v34, v32
	v_fma_f32 v30, -v30, v33, v31
	v_div_fmas_f32 v30, v30, v32, v33
	v_div_fixup_f32 v30, v30, v9, 1.0
	v_pk_mul_f32 v[10:11], v[10:11], v[30:31] op_sel_hi:[1,0]
	v_pk_mul_f32 v[12:13], v[12:13], v[30:31] op_sel_hi:[1,0]
	s_waitcnt vmcnt(0)
	v_pk_mul_f32 v[10:11], v[26:27], v[10:11]
	v_pk_mul_f32 v[12:13], v[28:29], v[12:13]
	v_cvt_pk_bf16_f32 v10, v10, v11
	v_pk_mul_f32 v[14:15], v[14:15], v[30:31] op_sel_hi:[1,0]
	v_cvt_pk_bf16_f32 v11, v12, v13
	global_store_dwordx2 v[4:5], v[10:11], off offset:-1536
	global_load_dwordx4 v[10:13], v[2:3], off offset:1024
	v_pk_mul_f32 v[16:17], v[16:17], v[30:31] op_sel_hi:[1,0]
	s_waitcnt vmcnt(0)
	v_pk_mul_f32 v[10:11], v[10:11], v[14:15]
	v_pk_mul_f32 v[12:13], v[12:13], v[16:17]
	v_cvt_pk_bf16_f32 v10, v10, v11
	v_pk_mul_f32 v[14:15], v[18:19], v[30:31] op_sel_hi:[1,0]
	v_cvt_pk_bf16_f32 v11, v12, v13
	global_store_dwordx2 v[4:5], v[10:11], off offset:-1024
	global_load_dwordx4 v[10:13], v[2:3], off offset:2048
	v_pk_mul_f32 v[16:17], v[20:21], v[30:31] op_sel_hi:[1,0]
	s_waitcnt vmcnt(0)
	v_pk_mul_f32 v[10:11], v[10:11], v[14:15]
	v_pk_mul_f32 v[12:13], v[12:13], v[16:17]
	v_cvt_pk_bf16_f32 v10, v10, v11
	v_pk_mul_f32 v[14:15], v[22:23], v[30:31] op_sel_hi:[1,0]
	v_cvt_pk_bf16_f32 v11, v12, v13
	global_store_dwordx2 v[4:5], v[10:11], off offset:-512
	global_load_dwordx4 v[10:13], v[2:3], off offset:3072
	v_pk_mul_f32 v[16:17], v[24:25], v[30:31] op_sel_hi:[1,0]
	s_waitcnt vmcnt(0)
	v_pk_mul_f32 v[10:11], v[14:15], v[10:11]
	v_pk_mul_f32 v[12:13], v[16:17], v[12:13]
	v_cvt_pk_bf16_f32 v10, v10, v11
	s_nop 0
	v_cvt_pk_bf16_f32 v11, v12, v13
	global_store_dwordx2 v[4:5], v[10:11], off
	v_lshl_add_u64 v[4:5], v[4:5], 0, s[6:7]
	s_cbranch_scc0 .LBB0_429

; template <int M> __device__ __forceinline__ float swz_xor(float v) { return __int_as_float(__builtin_amdgcn_ds_swizzle(__float_as_int(v), (M << 10) | 0x1f)); }
; __device__ __forceinline__ void st_bf4(bf16_t* p, f32x4 v) { u32x2 w; w.x = cvt_pk_bf16(v[0], v[1]); w.y = cvt_pk_bf16(v[2], v[3]); *(u32x2*)p = w; }
; __device__ __forceinline__ float half_sum(float v) { auto rr = __builtin_amdgcn_permlane32_swap(__float_as_uint(v), __float_as_uint(v), false, false); return __uint_as_float(rr[0]) + __uint_as_float(rr[1]); }
; __device__ __forceinline__ float sum32(float v) { v += swz_xor<1>(v); v += swz_xor<2>(v); v += swz_xor<4>(v); v += swz_xor<8>(v); v += swz_xor<16>(v); return v; }
; __device__ __forceinline__ float wave_sum(float v) { return half_sum(sum32(v)); }
; __device__ __forceinline__ void x0_row(const float* xrow, bf16_t* xbrow, float* prow, int lane) {
;     const f32x4* xr = (const f32x4*)xrow + lane; float s = 0.f;
; #pragma unroll
;     for (int j = 0; j < 4; ++j) { const f32x4 v = xr[64 * j]; s += (v[0] * v[0] + v[1] * v[1]) + (v[2] * v[2] + v[3] * v[3]); st_bf4(xbrow + j * 256 + lane * 4, v); }
;     s = wave_sum(s);
;     if (lane < 16) prow[lane] = lane == 0 ? s : 0.f;
; }
.LBB0_433:
	v_lshl_add_u64 v[10:11], s[52:53], 0, v[4:5]
	v_add_co_u32_e64 v22, s[6:7], s3, v10
	global_load_dwordx4 v[6:9], v[0:1], off offset:-2048
	s_nop 0
	v_addc_co_u32_e64 v23, s[6:7], 0, v11, s[6:7]
	s_waitcnt vmcnt(0)
	v_cvt_pk_bf16_f32 v10, v6, v7
	v_cvt_pk_bf16_f32 v11, v8, v9
	global_store_dwordx2 v[22:23], v[10:11], off
	global_load_dwordx4 v[10:13], v[0:1], off offset:-1024
	s_waitcnt vmcnt(0)
	v_cvt_pk_bf16_f32 v14, v10, v11
	v_cvt_pk_bf16_f32 v15, v12, v13
	global_store_dwordx2 v[22:23], v[14:15], off offset:512
	global_load_dwordx4 v[14:17], v[0:1], off
	s_waitcnt vmcnt(0)
	v_cvt_pk_bf16_f32 v18, v14, v15
	v_cvt_pk_bf16_f32 v19, v16, v17
	global_store_dwordx2 v[22:23], v[18:19], off offset:1024
	global_load_dwordx4 v[18:21], v[0:1], off offset:1024
	v_mul_f32_e32 v7, v7, v7
	v_mul_f32_e32 v9, v9, v9
	v_fmac_f32_e32 v7, v6, v6
	v_fmac_f32_e32 v9, v8, v8
	v_add_f32_e32 v6, v7, v9
	v_mul_f32_e32 v7, v11, v11
	v_mul_f32_e32 v8, v13, v13
	v_fmac_f32_e32 v7, v10, v10
	v_fmac_f32_e32 v8, v12, v12
	v_add_f32_e32 v7, v7, v8
	v_add_f32_e32 v6, v6, v7
	v_mul_f32_e32 v7, v15, v15
	v_mul_f32_e32 v8, v17, v17
	v_fmac_f32_e32 v7, v14, v14
	v_fmac_f32_e32 v8, v16, v16
	v_add_f32_e32 v7, v7, v8
	v_add_f32_e32 v6, v6, v7
	s_waitcnt vmcnt(0)
	v_mul_f32_e32 v7, v19, v19
	v_mul_f32_e32 v8, v21, v21
	v_fmac_f32_e32 v7, v18, v18
	v_fmac_f32_e32 v8, v20, v20
	v_add_f32_e32 v7, v7, v8
	v_add_f32_e32 v6, v6, v7
	s_waitcnt lgkmcnt(0)
	s_nop 1
	v_add_f32_dpp v6, v6, v6 quad_perm:[1,0,3,2] row_mask:0xf bank_mask:0xf
	s_waitcnt lgkmcnt(0)
	s_nop 1
	v_add_f32_dpp v6, v6, v6 quad_perm:[2,3,0,1] row_mask:0xf bank_mask:0xf
	s_waitcnt lgkmcnt(0)
	s_nop 1
	v_add_f32_dpp v6, v6, v6 row_half_mirror row_mask:0xf bank_mask:0xf
	s_waitcnt lgkmcnt(0)
	s_nop 1
	v_add_f32_dpp v8, v6, v6 row_mirror row_mask:0xf bank_mask:0xf
	ds_swizzle_b32 v9, v8 offset:swizzle(SWAP,16)
	v_cvt_pk_bf16_f32 v6, v18, v19
	v_cvt_pk_bf16_f32 v7, v20, v21
	global_store_dwordx2 v[22:23], v[6:7], off offset:1536
	s_waitcnt lgkmcnt(0)
	v_add_f32_e32 v6, v8, v9
	v_mov_b32_e32 v7, v6
	s_nop 1
	v_permlane32_swap_b32_e32 v6, v7
	s_and_saveexec_b64 s[6:7], vcc
	s_cbranch_execz .LBB0_432
	v_add_f32_e32 v6, v6, v7
	v_cndmask_b32_e64 v8, 0, v6, s[4:5]
	v_lshl_add_u64 v[6:7], s[52:53], 0, v[2:3]
	global_store_dword v[6:7], v8, off
	s_branch .LBB0_432

; template <int M> __device__ __forceinline__ float swz_xor(float v) { return __int_as_float(__builtin_amdgcn_ds_swizzle(__float_as_int(v), (M << 10) | 0x1f)); }
; __device__ __forceinline__ float half_sum(float v) { auto rr = __builtin_amdgcn_permlane32_swap(__float_as_uint(v), __float_as_uint(v), false, false); return __uint_as_float(rr[0]) + __uint_as_float(rr[1]); }
; __device__ __forceinline__ void row_rscale8(const float* part, const int (&rows)[2][4], int fq, float (&rs)[2][4]) {
;     f32x4 v[2][4];
; #pragma unroll
;     for (int ai = 0; ai < 2; ++ai)
; #pragma unroll
;         for (int m = 0; m < 4; ++m) v[ai][m] = *(const f32x4*)(part + (size_t)rows[ai][m] * 16 + fq * 4);
; #pragma unroll
;     for (int ai = 0; ai < 2; ++ai)
; #pragma unroll
;         for (int m = 0; m < 4; ++m) { float s = (v[ai][m][0] + v[ai][m][1]) + (v[ai][m][2] + v[ai][m][3]); s += swz_xor<16>(s); s = half_sum(s); rs[ai][m] = __builtin_amdgcn_rcpf(sqrtf(s * (1.0f / DM) + EPS)); }
;     __device__ __forceinline__ bool operator()(f32x4 (&acc)[2][2][4][2], const pg8::Unit& u, int wr, int wc, int fr, int fq) const {
;         const int pn = u.pn, row0 = u.pm * 256 + wr * 64 + fr;
;         float rs_[2][4]; { int rows_[2][4];
; #pragma unroll
;             for (int ai = 0; ai < 2; ++ai)
; #pragma unroll
;                 for (int m = 0; m < 4; ++m) rows_[ai][m] = row0 + ai * 128 + m * 16;
;             row_rscale8(part, rows_, fq, rs_); }
.LBB0_723:
	v_lshl_add_u32 v184, s30, 8, v199
	v_ashrrev_i32_e32 v185, 31, v184
	v_lshlrev_b64 v[128:129], 6, v[184:185]
	v_lshl_add_u64 v[128:129], v[166:167], 0, v[128:129]
	global_load_dwordx4 v[204:207], v[128:129], off
	v_or_b32_e32 v196, 16, v184
	v_ashrrev_i32_e32 v197, 31, v196
	v_lshlrev_b64 v[128:129], 6, v[196:197]
	v_lshl_add_u64 v[128:129], v[166:167], 0, v[128:129]
	global_load_dwordx4 v[152:155], v[128:129], off
	v_or_b32_e32 v188, 32, v184
	v_ashrrev_i32_e32 v189, 31, v188
	v_lshlrev_b64 v[128:129], 6, v[188:189]
	v_lshl_add_u64 v[128:129], v[166:167], 0, v[128:129]
	global_load_dwordx4 v[148:151], v[128:129], off
	v_or_b32_e32 v186, 48, v184
	v_ashrrev_i32_e32 v187, 31, v186
	v_lshlrev_b64 v[128:129], 6, v[186:187]
	v_lshl_add_u64 v[128:129], v[166:167], 0, v[128:129]
	global_load_dwordx4 v[144:147], v[128:129], off
	v_add_u32_e32 v182, 0x80, v184
	v_ashrrev_i32_e32 v183, 31, v182
	v_lshlrev_b64 v[128:129], 6, v[182:183]
	v_lshl_add_u64 v[128:129], v[166:167], 0, v[128:129]
	global_load_dwordx4 v[140:143], v[128:129], off
	v_add_u32_e32 v180, 0x90, v184
	v_ashrrev_i32_e32 v181, 31, v180
	v_lshlrev_b64 v[128:129], 6, v[180:181]
	v_lshl_add_u64 v[128:129], v[166:167], 0, v[128:129]
	global_load_dwordx4 v[136:139], v[128:129], off
	v_add_u32_e32 v178, 0xa0, v184
	v_ashrrev_i32_e32 v179, 31, v178
	v_lshlrev_b64 v[128:129], 6, v[178:179]
	v_lshl_add_u64 v[128:129], v[166:167], 0, v[128:129]
	global_load_dwordx4 v[132:135], v[128:129], off
	s_mov_b32 s2, 0xf800000
	v_add_u32_e32 v176, 0xb0, v184
	v_ashrrev_i32_e32 v177, 31, v176
	v_lshlrev_b64 v[128:129], 6, v[176:177]
	v_lshl_add_u64 v[128:129], v[166:167], 0, v[128:129]
	global_load_dwordx4 v[128:131], v[128:129], off
	s_cmp_gt_i32 s29, 7
	v_mov_b64_e32 v[230:231], v[210:211]
	s_waitcnt vmcnt(0)
	v_add_f32_e32 v160, v204, v205
	v_add_f32_e32 v190, v206, v207
	v_add_f32_e32 v160, v160, v190
	v_mov_b32_e32 v190, v160
	v_add_f32_e32 v152, v152, v153
	v_add_f32_e32 v153, v154, v155
	v_add_f32_e32 v152, v152, v153
	s_waitcnt lgkmcnt(0)
	s_nop 1
	v_permlane16_swap_b32_e32 v190, v160
	v_add_f32_e32 v160, v160, v190
	v_mov_b32_e32 v190, v160
	s_nop 1
	v_permlane32_swap_b32_e32 v160, v190
	v_add_f32_e32 v160, v160, v190
	v_fmamk_f32 v160, v160, 0x3a800000, v212
	v_cmp_gt_f32_e32 vcc, s2, v160
	v_mul_f32_e32 v190, 0x4f800000, v160
	v_mov_b32_e32 v153, v152
	v_cndmask_b32_e32 v160, v160, v190, vcc
	v_sqrt_f32_e32 v190, v160
	v_add_f32_e32 v148, v148, v149
	v_add_f32_e32 v149, v150, v151
	s_waitcnt lgkmcnt(0)
	s_nop 1
	v_permlane16_swap_b32_e32 v153, v152
	v_add_f32_e32 v152, v152, v153
	v_add_u32_e32 v191, -1, v190
	v_fma_f32 v192, -v191, v190, v160
	v_cmp_ge_f32_e64 s[4:5], 0, v192
	v_add_u32_e32 v192, 1, v190
	v_mov_b32_e32 v153, v152
	v_cndmask_b32_e64 v191, v190, v191, s[4:5]
	v_fma_f32 v190, -v192, v190, v160
	v_cmp_lt_f32_e64 s[4:5], 0, v190
	v_permlane32_swap_b32_e32 v152, v153
	s_nop 0
	v_cndmask_b32_e64 v190, v191, v192, s[4:5]
	v_mul_f32_e32 v191, 0x37800000, v190
	v_add_f32_e32 v152, v152, v153
	v_cndmask_b32_e32 v190, v190, v191, vcc
	v_cmp_class_f32_e32 vcc, v160, v248
	v_fmamk_f32 v152, v152, 0x3a800000, v212
	v_mul_f32_e32 v153, 0x4f800000, v152
	v_cndmask_b32_e32 v160, v190, v160, vcc
	v_cmp_gt_f32_e32 vcc, s2, v152
	v_add_f32_e32 v148, v148, v149
	v_mov_b32_e32 v149, v148
	v_cndmask_b32_e32 v152, v152, v153, vcc
	v_sqrt_f32_e32 v153, v152
	v_add_f32_e32 v144, v144, v145
	v_add_f32_e32 v145, v146, v147
	s_waitcnt lgkmcnt(0)
	s_nop 1
	v_permlane16_swap_b32_e32 v149, v148
	v_add_f32_e32 v148, v148, v149
	v_add_u32_e32 v154, -1, v153
	v_fma_f32 v155, -v154, v153, v152
	v_cmp_ge_f32_e64 s[4:5], 0, v155
	v_add_u32_e32 v155, 1, v153
	v_mov_b32_e32 v149, v148
	v_cndmask_b32_e64 v154, v153, v154, s[4:5]
	v_fma_f32 v153, -v155, v153, v152
	v_cmp_lt_f32_e64 s[4:5], 0, v153
	v_permlane32_swap_b32_e32 v148, v149
	s_nop 0
	v_cndmask_b32_e64 v153, v154, v155, s[4:5]
	v_mul_f32_e32 v154, 0x37800000, v153
	v_add_f32_e32 v148, v148, v149
	v_cndmask_b32_e32 v153, v153, v154, vcc
	v_cmp_class_f32_e32 vcc, v152, v248
	v_fmamk_f32 v148, v148, 0x3a800000, v212
	v_mul_f32_e32 v149, 0x4f800000, v148
	v_cndmask_b32_e32 v152, v153, v152, vcc
	v_cmp_gt_f32_e32 vcc, s2, v148
	v_add_f32_e32 v144, v144, v145
	v_mov_b32_e32 v145, v144
	v_cndmask_b32_e32 v148, v148, v149, vcc
	v_sqrt_f32_e32 v149, v148
	v_add_f32_e32 v140, v140, v141
	v_add_f32_e32 v141, v142, v143
	s_waitcnt lgkmcnt(0)
; template <int M> __device__ __forceinline__ float swz_xor(float v) { return __int_as_float(__builtin_amdgcn_ds_swizzle(__float_as_int(v), (M << 10) | 0x1f)); }
; __device__ __forceinline__ float half_sum(float v) { auto rr = __builtin_amdgcn_permlane32_swap(__float_as_uint(v), __float_as_uint(v), false, false); return __uint_as_float(rr[0]) + __uint_as_float(rr[1]); }
; __device__ __forceinline__ void row_rscale8(const float* part, const int (&rows)[2][4], int fq, float (&rs)[2][4]) {
;     f32x4 v[2][4];
; #pragma unroll
;     for (int ai = 0; ai < 2; ++ai)
; #pragma unroll
;         for (int m = 0; m < 4; ++m) v[ai][m] = *(const f32x4*)(part + (size_t)rows[ai][m] * 16 + fq * 4);
; #pragma unroll
;     for (int ai = 0; ai < 2; ++ai)
; #pragma unroll
;         for (int m = 0; m < 4; ++m) { float s = (v[ai][m][0] + v[ai][m][1]) + (v[ai][m][2] + v[ai][m][3]); s += swz_xor<16>(s); s = half_sum(s); rs[ai][m] = __builtin_amdgcn_rcpf(sqrtf(s * (1.0f / DM) + EPS)); }
;     __device__ __forceinline__ bool operator()(f32x4 (&acc)[2][2][4][2], const pg8::Unit& u, int wr, int wc, int fr, int fq) const {
;         const int pn = u.pn, row0 = u.pm * 256 + wr * 64 + fr;
;         float rs_[2][4]; { int rows_[2][4];
; #pragma unroll
;             for (int ai = 0; ai < 2; ++ai)
; #pragma unroll
;                 for (int m = 0; m < 4; ++m) rows_[ai][m] = row0 + ai * 128 + m * 16;
;             row_rscale8(part, rows_, fq, rs_); }
;     ...
;         if (pn < 8) {
	s_nop 1
	v_permlane16_swap_b32_e32 v145, v144
	v_add_f32_e32 v144, v144, v145
	v_add_u32_e32 v150, -1, v149
	v_fma_f32 v151, -v150, v149, v148
	v_cmp_ge_f32_e64 s[4:5], 0, v151
	v_add_u32_e32 v151, 1, v149
	v_mov_b32_e32 v145, v144
	v_cndmask_b32_e64 v150, v149, v150, s[4:5]
	v_fma_f32 v149, -v151, v149, v148
	v_cmp_lt_f32_e64 s[4:5], 0, v149
	v_permlane32_swap_b32_e32 v144, v145
	s_nop 0
	v_cndmask_b32_e64 v149, v150, v151, s[4:5]
	v_mul_f32_e32 v150, 0x37800000, v149
	v_add_f32_e32 v144, v144, v145
	v_cndmask_b32_e32 v149, v149, v150, vcc
	v_cmp_class_f32_e32 vcc, v148, v248
	v_fmamk_f32 v144, v144, 0x3a800000, v212
	v_mul_f32_e32 v145, 0x4f800000, v144
	v_cndmask_b32_e32 v148, v149, v148, vcc
	v_cmp_gt_f32_e32 vcc, s2, v144
	v_add_f32_e32 v140, v140, v141
	v_mov_b32_e32 v141, v140
	v_cndmask_b32_e32 v144, v144, v145, vcc
	v_sqrt_f32_e32 v145, v144
	v_add_f32_e32 v136, v136, v137
	v_add_f32_e32 v137, v138, v139
	s_waitcnt lgkmcnt(0)
	s_nop 1
	v_permlane16_swap_b32_e32 v141, v140
	v_add_f32_e32 v140, v140, v141
	v_add_u32_e32 v146, -1, v145
	v_fma_f32 v147, -v146, v145, v144
	v_cmp_ge_f32_e64 s[4:5], 0, v147
	v_add_u32_e32 v147, 1, v145
	v_mov_b32_e32 v141, v140
	v_cndmask_b32_e64 v146, v145, v146, s[4:5]
	v_fma_f32 v145, -v147, v145, v144
	v_cmp_lt_f32_e64 s[4:5], 0, v145
	v_permlane32_swap_b32_e32 v140, v141
	s_nop 0
	v_cndmask_b32_e64 v145, v146, v147, s[4:5]
	v_mul_f32_e32 v146, 0x37800000, v145
	v_add_f32_e32 v140, v140, v141
	v_cndmask_b32_e32 v145, v145, v146, vcc
	v_cmp_class_f32_e32 vcc, v144, v248
	v_fmamk_f32 v140, v140, 0x3a800000, v212
	v_mul_f32_e32 v141, 0x4f800000, v140
	v_cndmask_b32_e32 v144, v145, v144, vcc
	v_cmp_gt_f32_e32 vcc, s2, v140
	v_add_f32_e32 v136, v136, v137
	v_mov_b32_e32 v137, v136
	v_cndmask_b32_e32 v140, v140, v141, vcc
	v_sqrt_f32_e32 v141, v140
	v_add_f32_e32 v132, v132, v133
	v_add_f32_e32 v133, v134, v135
	s_waitcnt lgkmcnt(0)
	s_nop 1
	v_permlane16_swap_b32_e32 v137, v136
	v_add_f32_e32 v136, v136, v137
	v_add_u32_e32 v142, -1, v141
	v_fma_f32 v143, -v142, v141, v140
	v_cmp_ge_f32_e64 s[4:5], 0, v143
	v_add_u32_e32 v143, 1, v141
	v_mov_b32_e32 v137, v136
	v_cndmask_b32_e64 v142, v141, v142, s[4:5]
	v_fma_f32 v141, -v143, v141, v140
	v_cmp_lt_f32_e64 s[4:5], 0, v141
	v_permlane32_swap_b32_e32 v136, v137
	s_nop 0
	v_cndmask_b32_e64 v141, v142, v143, s[4:5]
	v_mul_f32_e32 v142, 0x37800000, v141
	v_add_f32_e32 v136, v136, v137
	v_cndmask_b32_e32 v141, v141, v142, vcc
	v_cmp_class_f32_e32 vcc, v140, v248
	v_fmamk_f32 v136, v136, 0x3a800000, v212
	v_mul_f32_e32 v137, 0x4f800000, v136
	v_cndmask_b32_e32 v140, v141, v140, vcc
	v_cmp_gt_f32_e32 vcc, s2, v136
	v_add_f32_e32 v132, v132, v133
	v_mov_b32_e32 v133, v132
	v_cndmask_b32_e32 v136, v136, v137, vcc
	v_sqrt_f32_e32 v137, v136
	v_add_f32_e32 v128, v128, v129
	v_add_f32_e32 v129, v130, v131
	s_waitcnt lgkmcnt(0)
	s_nop 1
	v_permlane16_swap_b32_e32 v133, v132
	v_add_f32_e32 v132, v132, v133
	v_add_u32_e32 v138, -1, v137
	v_fma_f32 v139, -v138, v137, v136
	v_cmp_ge_f32_e64 s[4:5], 0, v139
	v_add_u32_e32 v139, 1, v137
	v_mov_b32_e32 v133, v132
	v_cndmask_b32_e64 v138, v137, v138, s[4:5]
	v_fma_f32 v137, -v139, v137, v136
	v_cmp_lt_f32_e64 s[4:5], 0, v137
	v_permlane32_swap_b32_e32 v132, v133
	s_nop 0
	v_cndmask_b32_e64 v137, v138, v139, s[4:5]
	v_mul_f32_e32 v138, 0x37800000, v137
	v_add_f32_e32 v132, v132, v133
	v_cndmask_b32_e32 v137, v137, v138, vcc
	v_cmp_class_f32_e32 vcc, v136, v248
	v_fmamk_f32 v132, v132, 0x3a800000, v212
	v_mul_f32_e32 v133, 0x4f800000, v132
	v_cndmask_b32_e32 v136, v137, v136, vcc
	v_cmp_gt_f32_e32 vcc, s2, v132
	v_add_f32_e32 v128, v128, v129
	v_mov_b32_e32 v129, v128
	v_cndmask_b32_e32 v132, v132, v133, vcc
	v_sqrt_f32_e32 v133, v132
	v_rcp_f32_e32 v198, v160
	v_rcp_f32_e32 v154, v152
	s_waitcnt lgkmcnt(0)
	s_nop 1
	v_permlane16_swap_b32_e32 v129, v128
	v_add_f32_e32 v128, v128, v129
	v_add_u32_e32 v134, -1, v133
	v_fma_f32 v135, -v134, v133, v132
	v_cmp_ge_f32_e64 s[4:5], 0, v135
	v_add_u32_e32 v135, 1, v133
	v_mov_b32_e32 v129, v128
	v_cndmask_b32_e64 v134, v133, v134, s[4:5]
	v_fma_f32 v133, -v135, v133, v132
	v_cmp_lt_f32_e64 s[4:5], 0, v133
	v_permlane32_swap_b32_e32 v128, v129
	s_nop 0
	v_cndmask_b32_e64 v133, v134, v135, s[4:5]
	v_mul_f32_e32 v134, 0x37800000, v133
	v_add_f32_e32 v128, v128, v129
	v_cndmask_b32_e32 v133, v133, v134, vcc
	v_cmp_class_f32_e32 vcc, v132, v248
	v_fmamk_f32 v128, v128, 0x3a800000, v212
	v_mul_f32_e32 v129, 0x4f800000, v128
	v_cndmask_b32_e32 v132, v133, v132, vcc
	v_cmp_gt_f32_e32 vcc, s2, v128
	v_rcp_f32_e32 v202, v148
	v_rcp_f32_e32 v200, v144
	v_cndmask_b32_e32 v128, v128, v129, vcc
	v_sqrt_f32_e32 v129, v128
	v_rcp_f32_e32 v152, v140
	v_rcp_f32_e32 v150, v136
	v_rcp_f32_e32 v148, v132
	v_add_u32_e32 v130, -1, v129
	v_fma_f32 v131, -v130, v129, v128
	v_cmp_ge_f32_e64 s[4:5], 0, v131
	v_add_u32_e32 v131, 1, v129
	s_nop 0
	v_cndmask_b32_e64 v130, v129, v130, s[4:5]
	v_fma_f32 v129, -v131, v129, v128
	v_cmp_lt_f32_e64 s[4:5], 0, v129
	s_nop 1
	v_cndmask_b32_e64 v129, v130, v131, s[4:5]
	v_mul_f32_e32 v130, 0x37800000, v129
	v_cndmask_b32_e32 v129, v129, v130, vcc
	v_cmp_class_f32_e32 vcc, v128, v248
	s_mov_b64 s[4:5], -1
	s_nop 0
	v_cndmask_b32_e32 v128, v129, v128, vcc
	v_rcp_f32_e32 v146, v128
	s_cbranch_scc1 .LBB0_726
	s_andn2_b64 vcc, exec, s[4:5]
	s_cbranch_vccz .LBB0_735

; __device__ __forceinline__ unsigned cvt_pk_bf16(float lo, float hi) { unsigned r; asm volatile("v_cvt_pk_bf16_f32 %0, %1, %2" : "=v"(r) : "v"(lo), "v"(hi)); return r; }
; __device__ __forceinline__ float bf_lo(unsigned w) { return __uint_as_float(w << 16); }
; __device__ __forceinline__ float bf_hi(unsigned w) { return __uint_as_float(w & 0xffff0000u); }
; __device__ __forceinline__ int fresh_lane() { unsigned m = ~0u; asm volatile("" : "+s"(m)); return (int)__builtin_amdgcn_mbcnt_hi(m, __builtin_amdgcn_mbcnt_lo(m, 0u)); }
; __device__ __forceinline__ void diff_pass(const bf16_t* __restrict__ Qb, const bf16_t* __restrict__ Kh, const bf16_t* __restrict__ Vh, int seq, char* lds, f32x16 (&o)[4], const int wave_) {
;     ...
;     if (hi == 0) li_l[r32] = l_reg; asm volatile("s_waitcnt lgkmcnt(0)" ::: "memory");
; #pragma unroll
;     for (int r = 0; r < 16; ++r) { const float rl = __builtin_amdgcn_rcpf(li_l[crow(r, hi)]);
; #pragma unroll
;         for (int d = 0; d < 4; ++d) o[d][r] *= rl; }
;     ...
; }
; __device__ __forceinline__ void diff_unit(int b, int h, int qb, const bf16_t* Q, const bf16_t* K, const bf16_t* V, bf16_t* YA, float lam, float omli, const float* subln, char* lds, const int wave_) {
;     int tid_ = (wave_ << 6) | fresh_lane(); asm volatile("" : "+v"(tid_));
;     const int tid = tid_, wid = tid >> 6, lane = tid & 63, r32 = lane & 31, hi = lane >> 5;
;     const size_t rowbase = (size_t)b * SEQ; const int q0 = qb * 256;
;     const bf16_t* Qb = Q + (rowbase + q0) * DM + h * 128;
;     const bf16_t* Kh = K + rowbase * DM + h * 128;
;     const bf16_t* Vh = V + rowbase * DM + h * 128;
;     f32x16 o[4];
;     diff_pass(Qb, Kh, Vh, SEQ, lds, o, wave_);
;     unsigned* park = (unsigned*)(lds + DA_LDS) + wid * 2048 + lane;
; #pragma unroll
;     for (int d = 0; d < 4; ++d)
; #pragma unroll
;         for (int r = 0; r < 8; ++r) park[(d * 8 + r) * 64] = cvt_pk_bf16(o[d][2 * r], o[d][2 * r + 1]);
;     diff_pass(Qb + 64, Kh + 64, Vh, SEQ, lds, o, wave_);
;     asm volatile("s_waitcnt lgkmcnt(0)" ::: "memory");
;     float ss[16];
; #pragma unroll
;     for (int r = 0; r < 16; ++r) { float s = 0.f;
; #pragma unroll
;         for (int d = 0; d < 4; ++d) { const unsigned pw = park[(d * 8 + (r >> 1)) * 64]; const float a = (r & 1) ? bf_hi(pw) : bf_lo(pw); const float v = a - lam * o[d][r]; o[d][r] = v; s += v * v; }
.LBB0_821:
	s_or_b64 exec, exec, s[10:11]
	s_waitcnt lgkmcnt(0)
	v_add_u32_e32 v65, v217, v160
	ds_read_b128 v[66:69], v65
	ds_read_b128 v[80:83], v65 offset:32
	s_mov_b32 s2, 0xf800000
	v_and_b32_e32 v64, 31, v207
	s_lshl_b32 s64, s38, 1
	s_waitcnt lgkmcnt(1)
	v_rcp_f32_e32 v66, v66
	s_nop 0
	v_mul_f32_e32 v79, v0, v66
	v_rcp_f32_e32 v0, v67
	v_mul_f32_e32 v73, v32, v66
	v_mul_f32_e32 v76, v48, v66
	v_mul_f32_e32 v16, v16, v66
	v_mul_f32_e32 v92, v1, v0
	v_mul_f32_e32 v93, v49, v0
	v_mul_f32_e32 v94, v33, v0
	v_mul_f32_e32 v95, v17, v0
	v_rcp_f32_e32 v0, v68
	s_nop 0
	v_mul_f32_e32 v96, v2, v0
	v_mul_f32_e32 v97, v50, v0
	v_mul_f32_e32 v98, v34, v0
	v_mul_f32_e32 v99, v18, v0
	v_rcp_f32_e32 v0, v69
	s_nop 0
	v_mul_f32_e32 v100, v3, v0
	v_mul_f32_e32 v101, v51, v0
	v_mul_f32_e32 v102, v35, v0
	v_mul_f32_e32 v103, v19, v0
	s_waitcnt lgkmcnt(0)
	v_rcp_f32_e32 v0, v80
	s_nop 0
	v_mul_f32_e32 v35, v4, v0
	v_mul_f32_e32 v34, v52, v0
	v_mul_f32_e32 v33, v36, v0
	v_mul_f32_e32 v32, v20, v0
	v_rcp_f32_e32 v0, v81
	s_nop 0
	v_mul_f32_e32 v36, v5, v0
	v_mul_f32_e32 v70, v53, v0
	v_mul_f32_e32 v68, v37, v0
	v_mul_f32_e32 v66, v21, v0
	v_rcp_f32_e32 v0, v82
	s_nop 0
	v_mul_f32_e32 v80, v6, v0
	v_mul_f32_e32 v78, v54, v0
	v_mul_f32_e32 v74, v38, v0
	v_mul_f32_e32 v72, v22, v0
	v_rcp_f32_e32 v0, v83
	s_nop 0
	v_mul_f32_e32 v91, v7, v0
	v_mul_f32_e32 v90, v55, v0
	v_mul_f32_e32 v77, v39, v0
	v_mul_f32_e32 v75, v23, v0
	ds_read_b128 v[0:3], v65 offset:64
	s_waitcnt lgkmcnt(0)
	v_rcp_f32_e32 v0, v0
	s_nop 0
	v_mul_f32_e32 v53, v8, v0
	v_mul_f32_e32 v51, v56, v0
	v_mul_f32_e32 v54, v40, v0
	v_mul_f32_e32 v55, v24, v0
	v_rcp_f32_e32 v0, v1
	s_nop 0
	v_mul_f32_e32 v52, v9, v0
	v_mul_f32_e32 v49, v57, v0
	v_mul_f32_e32 v50, v41, v0
	v_mul_f32_e32 v48, v25, v0
	v_rcp_f32_e32 v0, v2
	s_nop 0
	v_mul_f32_e32 v56, v10, v0
	v_mul_f32_e32 v41, v58, v0
	v_mul_f32_e32 v40, v42, v0
	v_mul_f32_e32 v7, v26, v0
	v_rcp_f32_e32 v0, v3
	s_nop 0
	v_mul_f32_e32 v5, v11, v0
	ds_read_b128 v[8:11], v65 offset:96
	v_mul_f32_e32 v3, v59, v0
	s_waitcnt lgkmcnt(0)
	ds_read2st64_b32 v[24:25], v216 offset0:8 offset1:9
	v_mul_f32_e32 v1, v43, v0
	s_waitcnt lgkmcnt(1)
	v_rcp_f32_e32 v8, v8
	v_mul_f32_e32 v0, v27, v0
	ds_read2st64_b32 v[26:27], v216 offset0:16 offset1:17
	ds_read2st64_b32 v[42:43], v216 offset0:10 offset1:11
	v_mul_f32_e32 v2, v12, v8
	v_mul_f32_e32 v4, v60, v8
	v_mul_f32_e32 v6, v44, v8
	v_mul_f32_e32 v59, v28, v8
	v_rcp_f32_e32 v8, v9
	s_nop 0
	v_mul_f32_e32 v67, v13, v8
	v_mul_f32_e32 v61, v61, v8
	v_mul_f32_e32 v65, v45, v8
	v_mul_f32_e32 v60, v29, v8
	v_rcp_f32_e32 v8, v10
	ds_read2st64_b32 v[28:29], v216 offset0:24 offset1:25
	ds_read2st64_b32 v[44:45], v216 offset0:18 offset1:19
	v_mul_f32_e32 v85, v14, v8
	v_mul_f32_e32 v71, v62, v8
	v_mul_f32_e32 v84, v46, v8
	v_mul_f32_e32 v69, v30, v8
	v_rcp_f32_e32 v8, v11
	s_nop 0
	v_mul_f32_e32 v89, v15, v8
	v_mul_f32_e32 v88, v63, v8
	v_mul_f32_e32 v87, v47, v8
	v_mul_f32_e32 v86, v31, v8
	ds_read2st64_b32 v[8:9], v216 offset1:1
	ds_read2st64_b32 v[46:47], v216 offset0:26 offset1:27
	ds_read2st64_b32 v[62:63], v216 offset0:12 offset1:13
	s_waitcnt lgkmcnt(2)
	v_lshlrev_b32_e32 v10, 16, v8
	v_and_b32_e32 v8, 0xffff0000, v8
	v_fma_f32 v21, -v197, v79, v10
	v_lshlrev_b32_e32 v10, 16, v24
	v_fma_f32 v20, -v197, v92, v8
	v_and_b32_e32 v8, 0xffff0000, v24
	v_fma_f32 v19, -v197, v76, v10
	v_lshlrev_b32_e32 v10, 16, v26
	v_fma_f32 v17, -v197, v93, v8
	v_and_b32_e32 v8, 0xffff0000, v26
	v_fma_f32 v22, -v197, v73, v10
	v_lshlrev_b32_e32 v10, 16, v28
	v_fma_f32 v18, -v197, v94, v8
	v_and_b32_e32 v8, 0xffff0000, v28
	v_fma_f32 v23, -v197, v16, v10
	v_fma_f32 v16, -v197, v95, v8
	v_lshlrev_b32_e32 v8, 16, v9
	v_fma_f32 v15, -v197, v96, v8
	v_lshlrev_b32_e32 v8, 16, v25
	v_fma_f32 v13, -v197, v97, v8
	v_lshlrev_b32_e32 v8, 16, v27
	v_fma_f32 v14, -v197, v98, v8
	v_lshlrev_b32_e32 v8, 16, v29
	v_fma_f32 v12, -v197, v99, v8
	v_and_b32_e32 v8, 0xffff0000, v9
	v_fma_f32 v11, -v197, v100, v8
	v_and_b32_e32 v8, 0xffff0000, v25
	ds_read2st64_b32 v[24:25], v216 offset0:2 offset1:3
	v_fma_f32 v9, -v197, v101, v8
	v_and_b32_e32 v8, 0xffff0000, v27
	v_fma_f32 v10, -v197, v102, v8
	v_and_b32_e32 v8, 0xffff0000, v29
	s_waitcnt lgkmcnt(0)
	v_lshlrev_b32_e32 v26, 16, v24
	v_fma_f32 v37, -v197, v35, v26
	v_lshlrev_b32_e32 v26, 16, v42
	v_and_b32_e32 v24, 0xffff0000, v24
	v_fma_f32 v35, -v197, v34, v26
	v_lshlrev_b32_e32 v26, 16, v44
	v_fma_f32 v36, -v197, v36, v24
	v_and_b32_e32 v24, 0xffff0000, v42
	v_fma_f32 v38, -v197, v33, v26
	v_fma_f32 v33, -v197, v70, v24
	v_and_b32_e32 v24, 0xffff0000, v44
	v_lshlrev_b32_e32 v26, 16, v46
	v_fma_f32 v34, -v197, v68, v24
	v_and_b32_e32 v24, 0xffff0000, v46
	v_fma_f32 v39, -v197, v32, v26
	v_fma_f32 v32, -v197, v66, v24
	v_lshlrev_b32_e32 v24, 16, v25
	v_fma_f32 v31, -v197, v80, v24
	v_lshlrev_b32_e32 v24, 16, v43
	v_fma_f32 v29, -v197, v78, v24
	v_lshlrev_b32_e32 v24, 16, v45
	v_fma_f32 v30, -v197, v74, v24
	v_lshlrev_b32_e32 v24, 16, v47
	v_fma_f32 v28, -v197, v72, v24
	v_and_b32_e32 v24, 0xffff0000, v25
	v_fma_f32 v27, -v197, v91, v24
	v_and_b32_e32 v24, 0xffff0000, v43
	ds_read2st64_b32 v[42:43], v216 offset0:4 offset1:5
	ds_read2st64_b32 v[92:93], v216 offset0:28 offset1:29
	v_fma_f32 v25, -v197, v90, v24
	ds_read2st64_b32 v[90:91], v216 offset0:20 offset1:21
	v_and_b32_e32 v24, 0xffff0000, v45
	s_waitcnt lgkmcnt(2)
	v_lshlrev_b32_e32 v44, 16, v42
	v_and_b32_e32 v42, 0xffff0000, v42
	v_fma_f32 v52, -v197, v52, v42
	v_and_b32_e32 v42, 0xffff0000, v62
	v_fma_f32 v49, -v197, v49, v42
	s_waitcnt lgkmcnt(0)
; __device__ __forceinline__ float bf_lo(unsigned w) { return __uint_as_float(w << 16); }
; __device__ __forceinline__ float bf_hi(unsigned w) { return __uint_as_float(w & 0xffff0000u); }
; __device__ __forceinline__ float sum32(float v) { v += swz_xor<1>(v); v += swz_xor<2>(v); v += swz_xor<4>(v); v += swz_xor<8>(v); v += swz_xor<16>(v); return v; }
; __device__ __forceinline__ void diff_unit(int b, int h, int qb, const bf16_t* Q, const bf16_t* K, const bf16_t* V, bf16_t* YA, float lam, float omli, const float* subln, char* lds, const int wave_) {
;     ...
;     for (int r = 0; r < 16; ++r) { float s = 0.f;
; #pragma unroll
;         for (int d = 0; d < 4; ++d) { const unsigned pw = park[(d * 8 + (r >> 1)) * 64]; const float a = (r & 1) ? bf_hi(pw) : bf_lo(pw); const float v = a - lam * o[d][r]; o[d][r] = v; s += v * v; }
;         ss[r] = s; }
; #pragma unroll
;     for (int r = 0; r < 16; ++r) {
;         ss[r] = sum32(ss[r]);
;         ss[r] = omli / sqrtf(ss[r] * (1.0f / 128.0f) + EPS); }
	v_and_b32_e32 v42, 0xffff0000, v90
	v_fma_f32 v50, -v197, v50, v42
	v_and_b32_e32 v42, 0xffff0000, v92
	v_fma_f32 v48, -v197, v48, v42
	v_lshlrev_b32_e32 v42, 16, v43
	v_fma_f32 v26, -v197, v77, v24
	v_and_b32_e32 v24, 0xffff0000, v47
	v_fma_f32 v53, -v197, v53, v44
	v_lshlrev_b32_e32 v44, 16, v62
	v_fma_f32 v47, -v197, v56, v42
	v_lshlrev_b32_e32 v42, 16, v63
	v_fma_f32 v51, -v197, v51, v44
	v_lshlrev_b32_e32 v44, 16, v90
	v_fma_f32 v45, -v197, v41, v42
	v_lshlrev_b32_e32 v41, 16, v91
	v_fma_f32 v54, -v197, v54, v44
	v_lshlrev_b32_e32 v44, 16, v92
	v_fma_f32 v46, -v197, v40, v41
	v_lshlrev_b32_e32 v40, 16, v93
	v_fma_f32 v55, -v197, v55, v44
	v_fma_f32 v44, -v197, v7, v40
	v_and_b32_e32 v7, 0xffff0000, v43
	v_fma_f32 v43, -v197, v5, v7
	v_and_b32_e32 v5, 0xffff0000, v63
	v_fma_f32 v41, -v197, v3, v5
	v_and_b32_e32 v3, 0xffff0000, v91
	v_fma_f32 v42, -v197, v1, v3
	v_and_b32_e32 v1, 0xffff0000, v93
	v_fma_f32 v40, -v197, v0, v1
	ds_read2st64_b32 v[0:1], v216 offset0:6 offset1:7
	v_mul_f32_e32 v83, v19, v19
	v_fmac_f32_e32 v83, v21, v21
	v_fmac_f32_e32 v83, v22, v22
	v_fmac_f32_e32 v83, v23, v23
	s_waitcnt lgkmcnt(0)
	v_lshlrev_b32_e32 v3, 16, v0
	v_fma_f32 v56, -v197, v2, v3
	ds_read2st64_b32 v[2:3], v216 offset0:14 offset1:15
	v_and_b32_e32 v0, 0xffff0000, v0
	v_fma_f32 v67, -v197, v67, v0
	v_mul_f32_e32 v82, v17, v17
	v_fmac_f32_e32 v82, v20, v20
	s_waitcnt lgkmcnt(0)
	v_lshlrev_b32_e32 v5, 16, v2
	v_fma_f32 v57, -v197, v4, v5
	ds_read2st64_b32 v[4:5], v216 offset0:22 offset1:23
	v_and_b32_e32 v0, 0xffff0000, v2
	v_fma_f32 v61, -v197, v61, v0
	v_fmac_f32_e32 v82, v18, v18
	v_fmac_f32_e32 v82, v16, v16
	s_waitcnt lgkmcnt(0)
	v_lshlrev_b32_e32 v7, 16, v4
	v_fma_f32 v58, -v197, v6, v7
	ds_read2st64_b32 v[6:7], v216 offset0:30 offset1:31
	v_and_b32_e32 v0, 0xffff0000, v4
	v_fma_f32 v63, -v197, v65, v0
	v_mul_f32_e32 v81, v13, v13
	v_fmac_f32_e32 v81, v15, v15
	s_waitcnt lgkmcnt(0)
	v_and_b32_e32 v0, 0xffff0000, v6
	v_lshlrev_b32_e32 v62, 16, v6
	v_fma_f32 v65, -v197, v60, v0
	v_lshlrev_b32_e32 v0, 16, v1
	v_fma_f32 v66, -v197, v59, v62
	v_fma_f32 v62, -v197, v85, v0
	v_lshlrev_b32_e32 v0, 16, v3
	v_fma_f32 v59, -v197, v71, v0
	v_lshlrev_b32_e32 v0, 16, v5
	v_fma_f32 v60, -v197, v84, v0
	v_lshlrev_b32_e32 v0, 16, v7
	v_fma_f32 v6, -v197, v69, v0
	v_and_b32_e32 v0, 0xffff0000, v1
	v_fma_f32 v4, -v197, v89, v0
	v_and_b32_e32 v0, 0xffff0000, v3
	v_fma_f32 v1, -v197, v88, v0
	v_and_b32_e32 v0, 0xffff0000, v5
	v_fma_f32 v2, -v197, v87, v0
	v_and_b32_e32 v0, 0xffff0000, v7
	s_waitcnt lgkmcnt(0)
	s_nop 1
	v_add_f32_dpp v3, v83, v83 quad_perm:[1,0,3,2] row_mask:0xf bank_mask:0xf
	v_fmac_f32_e32 v81, v14, v14
	v_fmac_f32_e32 v81, v12, v12
	v_mul_f32_e32 v73, v9, v9
	v_fmac_f32_e32 v73, v11, v11
	s_waitcnt lgkmcnt(0)
	s_nop 1
	v_add_f32_dpp v3, v3, v3 quad_perm:[2,3,0,1] row_mask:0xf bank_mask:0xf
	v_fmac_f32_e32 v73, v10, v10
	v_fma_f32 v8, -v197, v103, v8
	v_fmac_f32_e32 v73, v8, v8
	v_mul_f32_e32 v76, v35, v35
	s_waitcnt lgkmcnt(0)
	s_nop 1
	v_add_f32_dpp v3, v3, v3 row_half_mirror row_mask:0xf bank_mask:0xf
	v_fmac_f32_e32 v76, v37, v37
	v_fmac_f32_e32 v76, v38, v38
	v_fmac_f32_e32 v76, v39, v39
	v_mul_f32_e32 v79, v33, v33
	s_waitcnt lgkmcnt(0)
	s_nop 1
	v_add_f32_dpp v3, v3, v3 row_mirror row_mask:0xf bank_mask:0xf
	v_mov_b32_e32 v5, v3
	v_fmac_f32_e32 v79, v36, v36
	v_fmac_f32_e32 v79, v34, v34
	v_fmac_f32_e32 v79, v32, v32
	v_mul_f32_e32 v80, v29, v29
	s_waitcnt lgkmcnt(0)
	s_nop 1
	v_permlane16_swap_b32_e32 v5, v3
	v_add_f32_e32 v3, v3, v5
	v_fmamk_f32 v3, v3, 0x3c000000, v212
	v_cmp_gt_f32_e32 vcc, s2, v3
	v_mul_f32_e32 v5, 0x4f800000, v3
	v_fmac_f32_e32 v80, v31, v31
	v_cndmask_b32_e32 v3, v3, v5, vcc
	v_sqrt_f32_e32 v5, v3
	v_fmac_f32_e32 v80, v30, v30
	v_fmac_f32_e32 v80, v28, v28
	v_mul_f32_e32 v78, v25, v25
	v_add_u32_e32 v7, -1, v5
	v_fma_f32 v83, -v7, v5, v3
	v_cmp_ge_f32_e64 s[0:1], 0, v83
	v_add_u32_e32 v83, 1, v5
	v_fmac_f32_e32 v78, v27, v27
	v_cndmask_b32_e64 v7, v5, v7, s[0:1]
	v_fma_f32 v5, -v83, v5, v3
	v_cmp_lt_f32_e64 s[0:1], 0, v5
	v_fmac_f32_e32 v78, v26, v26
	v_fma_f32 v24, -v197, v75, v24
	v_cndmask_b32_e64 v5, v7, v83, s[0:1]
	v_mul_f32_e32 v7, 0x37800000, v5
	v_cndmask_b32_e32 v5, v5, v7, vcc
	v_cmp_class_f32_e32 vcc, v3, v248
	v_fmac_f32_e32 v78, v24, v24
	v_mul_f32_e32 v77, v51, v51
	v_cndmask_b32_e32 v3, v5, v3, vcc
	v_div_scale_f32 v5, s[0:1], v3, v3, v206
	v_rcp_f32_e32 v7, v5
	v_fmac_f32_e32 v77, v53, v53
	v_fmac_f32_e32 v77, v54, v54
	v_fmac_f32_e32 v77, v55, v55
	v_fma_f32 v83, -v5, v7, 1.0
	v_fmac_f32_e32 v7, v83, v7
	v_div_scale_f32 v83, vcc, v206, v3, v206
	v_mul_f32_e32 v84, v83, v7
	v_fma_f32 v85, -v5, v84, v83
	v_fmac_f32_e32 v84, v85, v7
	v_fma_f32 v5, -v5, v84, v83
	v_div_fmas_f32 v5, v5, v7, v84
	v_div_fixup_f32 v3, v5, v3, v206
	v_mul_f32_e32 v75, v49, v49
	v_fmac_f32_e32 v75, v52, v52
	v_fmac_f32_e32 v75, v50, v50
	v_fmac_f32_e32 v75, v48, v48
	s_waitcnt lgkmcnt(0)
	s_nop 1
	v_add_f32_dpp v5, v82, v82 quad_perm:[1,0,3,2] row_mask:0xf bank_mask:0xf
	v_mul_f32_e32 v72, v45, v45
	v_fmac_f32_e32 v72, v47, v47
	v_fmac_f32_e32 v72, v46, v46
	v_fmac_f32_e32 v72, v44, v44
	s_waitcnt lgkmcnt(0)
	s_nop 1
	v_add_f32_dpp v5, v5, v5 quad_perm:[2,3,0,1] row_mask:0xf bank_mask:0xf
	v_mul_f32_e32 v68, v41, v41
	v_fmac_f32_e32 v68, v43, v43
	v_fmac_f32_e32 v68, v42, v42
	v_fmac_f32_e32 v68, v40, v40
	s_waitcnt lgkmcnt(0)
	s_nop 1
	v_add_f32_dpp v5, v5, v5 row_half_mirror row_mask:0xf bank_mask:0xf
	v_mul_f32_e32 v70, v57, v57
	v_fmac_f32_e32 v70, v56, v56
	v_fmac_f32_e32 v70, v58, v58
	v_fmac_f32_e32 v70, v66, v66
	s_waitcnt lgkmcnt(0)
; __device__ __forceinline__ float bf_lo(unsigned w) { return __uint_as_float(w << 16); }
; __device__ __forceinline__ float bf_hi(unsigned w) { return __uint_as_float(w & 0xffff0000u); }
; __device__ __forceinline__ float sum32(float v) { v += swz_xor<1>(v); v += swz_xor<2>(v); v += swz_xor<4>(v); v += swz_xor<8>(v); v += swz_xor<16>(v); return v; }
; __device__ __forceinline__ void diff_unit(int b, int h, int qb, const bf16_t* Q, const bf16_t* K, const bf16_t* V, bf16_t* YA, float lam, float omli, const float* subln, char* lds, const int wave_) {
;     ...
;     for (int r = 0; r < 16; ++r) { float s = 0.f;
; #pragma unroll
;         for (int d = 0; d < 4; ++d) { const unsigned pw = park[(d * 8 + (r >> 1)) * 64]; const float a = (r & 1) ? bf_hi(pw) : bf_lo(pw); const float v = a - lam * o[d][r]; o[d][r] = v; s += v * v; }
;         ss[r] = s; }
; #pragma unroll
;     for (int r = 0; r < 16; ++r) {
;         ss[r] = sum32(ss[r]);
;         ss[r] = omli / sqrtf(ss[r] * (1.0f / 128.0f) + EPS); }
	s_nop 1
	v_add_f32_dpp v5, v5, v5 row_mirror row_mask:0xf bank_mask:0xf
	v_mov_b32_e32 v7, v5
	v_mul_f32_e32 v74, v61, v61
	v_fmac_f32_e32 v74, v67, v67
	v_fmac_f32_e32 v74, v63, v63
	v_fmac_f32_e32 v74, v65, v65
	s_waitcnt lgkmcnt(0)
	s_nop 1
	v_permlane16_swap_b32_e32 v7, v5
	v_add_f32_e32 v5, v5, v7
	v_fmamk_f32 v5, v5, 0x3c000000, v212
	v_cmp_gt_f32_e32 vcc, s2, v5
	v_mul_f32_e32 v7, 0x4f800000, v5
	v_mul_f32_e32 v71, v59, v59
	v_cndmask_b32_e32 v5, v5, v7, vcc
	v_sqrt_f32_e32 v7, v5
	v_fmac_f32_e32 v71, v62, v62
	v_fmac_f32_e32 v71, v60, v60
	v_fmac_f32_e32 v71, v6, v6
	v_add_u32_e32 v82, -1, v7
	v_fma_f32 v83, -v82, v7, v5
	v_cmp_ge_f32_e64 s[0:1], 0, v83
	v_add_u32_e32 v83, 1, v7
	v_mul_f32_e32 v69, v1, v1
	v_cndmask_b32_e64 v82, v7, v82, s[0:1]
	v_fma_f32 v7, -v83, v7, v5
	v_cmp_lt_f32_e64 s[0:1], 0, v7
	v_fmac_f32_e32 v69, v4, v4
	v_fmac_f32_e32 v69, v2, v2
	v_cndmask_b32_e64 v7, v82, v83, s[0:1]
	v_mul_f32_e32 v82, 0x37800000, v7
	v_cndmask_b32_e32 v7, v7, v82, vcc
	v_cmp_class_f32_e32 vcc, v5, v248
	v_fma_f32 v0, -v197, v86, v0
	v_fmac_f32_e32 v69, v0, v0
	v_cndmask_b32_e32 v5, v7, v5, vcc
	v_div_scale_f32 v7, s[0:1], v5, v5, v206
	v_rcp_f32_e32 v82, v7
	v_mul_f32_e32 v21, v21, v3
	v_mul_f32_e32 v19, v19, v3
	v_fma_f32 v83, -v7, v82, 1.0
	v_fmac_f32_e32 v82, v83, v82
	v_div_scale_f32 v83, vcc, v206, v5, v206
	v_mul_f32_e32 v84, v83, v82
	v_fma_f32 v85, -v7, v84, v83
	v_fmac_f32_e32 v84, v85, v82
	v_fma_f32 v7, -v7, v84, v83
	v_div_fmas_f32 v7, v7, v82, v84
	v_div_fixup_f32 v5, v7, v5, v206
	s_waitcnt lgkmcnt(0)
	s_nop 1
	v_add_f32_dpp v7, v81, v81 quad_perm:[1,0,3,2] row_mask:0xf bank_mask:0xf
	s_waitcnt lgkmcnt(0)
	s_nop 1
	v_add_f32_dpp v7, v7, v7 quad_perm:[2,3,0,1] row_mask:0xf bank_mask:0xf
	s_waitcnt lgkmcnt(0)
	s_nop 1
	v_add_f32_dpp v7, v7, v7 row_half_mirror row_mask:0xf bank_mask:0xf
	s_waitcnt lgkmcnt(0)
	s_nop 1
	v_add_f32_dpp v7, v7, v7 row_mirror row_mask:0xf bank_mask:0xf
	v_mov_b32_e32 v81, v7
	s_waitcnt lgkmcnt(0)
	s_nop 1
	v_permlane16_swap_b32_e32 v81, v7
	v_add_f32_e32 v7, v7, v81
	v_fmamk_f32 v7, v7, 0x3c000000, v212
	v_cmp_gt_f32_e32 vcc, s2, v7
	v_mul_f32_e32 v81, 0x4f800000, v7
	s_nop 0
	v_cndmask_b32_e32 v7, v7, v81, vcc
	v_sqrt_f32_e32 v81, v7
	s_nop 0
	v_add_u32_e32 v82, -1, v81
	v_fma_f32 v83, -v82, v81, v7
	v_cmp_ge_f32_e64 s[0:1], 0, v83
	v_add_u32_e32 v83, 1, v81
	s_nop 0
	v_cndmask_b32_e64 v82, v81, v82, s[0:1]
	v_fma_f32 v81, -v83, v81, v7
	v_cmp_lt_f32_e64 s[0:1], 0, v81
	s_nop 1
	v_cndmask_b32_e64 v81, v82, v83, s[0:1]
	v_mul_f32_e32 v82, 0x37800000, v81
	v_cndmask_b32_e32 v81, v81, v82, vcc
	v_cmp_class_f32_e32 vcc, v7, v248
	s_nop 1
	v_cndmask_b32_e32 v7, v81, v7, vcc
	v_div_scale_f32 v81, s[0:1], v7, v7, v206
	v_rcp_f32_e32 v82, v81
	s_nop 0
	v_fma_f32 v83, -v81, v82, 1.0
	v_fmac_f32_e32 v82, v83, v82
	v_div_scale_f32 v83, vcc, v206, v7, v206
	v_mul_f32_e32 v84, v83, v82
	v_fma_f32 v85, -v81, v84, v83
	v_fmac_f32_e32 v84, v85, v82
	v_fma_f32 v81, -v81, v84, v83
	v_div_fmas_f32 v81, v81, v82, v84
	v_div_fixup_f32 v7, v81, v7, v206
	s_waitcnt lgkmcnt(0)
	s_nop 1
	v_add_f32_dpp v73, v73, v73 quad_perm:[1,0,3,2] row_mask:0xf bank_mask:0xf
	s_waitcnt lgkmcnt(0)
	s_nop 1
	v_add_f32_dpp v73, v73, v73 quad_perm:[2,3,0,1] row_mask:0xf bank_mask:0xf
	s_waitcnt lgkmcnt(0)
	s_nop 1
	v_add_f32_dpp v73, v73, v73 row_half_mirror row_mask:0xf bank_mask:0xf
	s_waitcnt lgkmcnt(0)
	s_nop 1
	v_add_f32_dpp v73, v73, v73 row_mirror row_mask:0xf bank_mask:0xf
	v_mov_b32_e32 v81, v73
	s_waitcnt lgkmcnt(0)
	s_nop 1
	v_permlane16_swap_b32_e32 v81, v73
	v_add_f32_e32 v73, v73, v81
	v_fmamk_f32 v73, v73, 0x3c000000, v212
	v_cmp_gt_f32_e32 vcc, s2, v73
	v_mul_f32_e32 v81, 0x4f800000, v73
	s_nop 0
	v_cndmask_b32_e32 v73, v73, v81, vcc
	v_sqrt_f32_e32 v81, v73
	s_nop 0
	v_add_u32_e32 v82, -1, v81
	v_fma_f32 v83, -v82, v81, v73
	v_cmp_ge_f32_e64 s[0:1], 0, v83
	v_add_u32_e32 v83, 1, v81
	s_nop 0
	v_cndmask_b32_e64 v82, v81, v82, s[0:1]
	v_fma_f32 v81, -v83, v81, v73
	v_cmp_lt_f32_e64 s[0:1], 0, v81
	s_nop 1
	v_cndmask_b32_e64 v81, v82, v83, s[0:1]
	v_mul_f32_e32 v82, 0x37800000, v81
	v_cndmask_b32_e32 v81, v81, v82, vcc
	v_cmp_class_f32_e32 vcc, v73, v248
	s_nop 1
	v_cndmask_b32_e32 v73, v81, v73, vcc
	v_div_scale_f32 v81, s[0:1], v73, v73, v206
	v_rcp_f32_e32 v82, v81
	s_nop 0
	v_fma_f32 v83, -v81, v82, 1.0
	v_fmac_f32_e32 v82, v83, v82
	v_div_scale_f32 v83, vcc, v206, v73, v206
	v_mul_f32_e32 v84, v83, v82
	v_fma_f32 v85, -v81, v84, v83
	v_fmac_f32_e32 v84, v85, v82
	v_fma_f32 v81, -v81, v84, v83
	v_div_fmas_f32 v81, v81, v82, v84
	v_div_fixup_f32 v73, v81, v73, v206
	s_waitcnt lgkmcnt(0)
	s_nop 1
	v_add_f32_dpp v76, v76, v76 quad_perm:[1,0,3,2] row_mask:0xf bank_mask:0xf
	s_waitcnt lgkmcnt(0)
	s_nop 1
	v_add_f32_dpp v76, v76, v76 quad_perm:[2,3,0,1] row_mask:0xf bank_mask:0xf
	s_waitcnt lgkmcnt(0)
	s_nop 1
	v_add_f32_dpp v76, v76, v76 row_half_mirror row_mask:0xf bank_mask:0xf
	s_waitcnt lgkmcnt(0)
	s_nop 1
	v_add_f32_dpp v76, v76, v76 row_mirror row_mask:0xf bank_mask:0xf
	v_mov_b32_e32 v81, v76
	s_waitcnt lgkmcnt(0)
	s_nop 1
	v_permlane16_swap_b32_e32 v81, v76
	v_add_f32_e32 v76, v76, v81
	v_fmamk_f32 v76, v76, 0x3c000000, v212
	v_cmp_gt_f32_e32 vcc, s2, v76
	v_mul_f32_e32 v81, 0x4f800000, v76
	s_nop 0
	v_cndmask_b32_e32 v76, v76, v81, vcc
	v_sqrt_f32_e32 v81, v76
	s_nop 0
	v_add_u32_e32 v82, -1, v81
	v_fma_f32 v83, -v82, v81, v76
	v_cmp_ge_f32_e64 s[0:1], 0, v83
	v_add_u32_e32 v83, 1, v81
	s_nop 0
	v_cndmask_b32_e64 v82, v81, v82, s[0:1]
	v_fma_f32 v81, -v83, v81, v76
	v_cmp_lt_f32_e64 s[0:1], 0, v81
	s_nop 1
	v_cndmask_b32_e64 v81, v82, v83, s[0:1]
	v_mul_f32_e32 v82, 0x37800000, v81
	v_cndmask_b32_e32 v81, v81, v82, vcc
	v_cmp_class_f32_e32 vcc, v76, v248
	s_nop 1
	v_cndmask_b32_e32 v76, v81, v76, vcc
	v_div_scale_f32 v81, s[0:1], v76, v76, v206
	v_rcp_f32_e32 v82, v81
	s_nop 0
	v_fma_f32 v83, -v81, v82, 1.0
	v_fmac_f32_e32 v82, v83, v82
	v_div_scale_f32 v83, vcc, v206, v76, v206
	v_mul_f32_e32 v84, v83, v82
	v_fma_f32 v85, -v81, v84, v83
	v_fmac_f32_e32 v84, v85, v82
	v_fma_f32 v81, -v81, v84, v83
	v_div_fmas_f32 v81, v81, v82, v84
	v_div_fixup_f32 v76, v81, v76, v206
	s_waitcnt lgkmcnt(0)
; __device__ __forceinline__ float bf_lo(unsigned w) { return __uint_as_float(w << 16); }
; __device__ __forceinline__ float bf_hi(unsigned w) { return __uint_as_float(w & 0xffff0000u); }
; __device__ __forceinline__ float sum32(float v) { v += swz_xor<1>(v); v += swz_xor<2>(v); v += swz_xor<4>(v); v += swz_xor<8>(v); v += swz_xor<16>(v); return v; }
; __device__ __forceinline__ void diff_unit(int b, int h, int qb, const bf16_t* Q, const bf16_t* K, const bf16_t* V, bf16_t* YA, float lam, float omli, const float* subln, char* lds, const int wave_) {
;     ...
;     for (int r = 0; r < 16; ++r) { float s = 0.f;
; #pragma unroll
;         for (int d = 0; d < 4; ++d) { const unsigned pw = park[(d * 8 + (r >> 1)) * 64]; const float a = (r & 1) ? bf_hi(pw) : bf_lo(pw); const float v = a - lam * o[d][r]; o[d][r] = v; s += v * v; }
;         ss[r] = s; }
; #pragma unroll
;     for (int r = 0; r < 16; ++r) {
;         ss[r] = sum32(ss[r]);
;         ss[r] = omli / sqrtf(ss[r] * (1.0f / 128.0f) + EPS); }
	s_nop 1
	v_add_f32_dpp v79, v79, v79 quad_perm:[1,0,3,2] row_mask:0xf bank_mask:0xf
	s_waitcnt lgkmcnt(0)
	s_nop 1
	v_add_f32_dpp v79, v79, v79 quad_perm:[2,3,0,1] row_mask:0xf bank_mask:0xf
	s_waitcnt lgkmcnt(0)
	s_nop 1
	v_add_f32_dpp v79, v79, v79 row_half_mirror row_mask:0xf bank_mask:0xf
	s_waitcnt lgkmcnt(0)
	s_nop 1
	v_add_f32_dpp v79, v79, v79 row_mirror row_mask:0xf bank_mask:0xf
	v_mov_b32_e32 v81, v79
	s_waitcnt lgkmcnt(0)
	s_nop 1
	v_permlane16_swap_b32_e32 v81, v79
	v_add_f32_e32 v79, v79, v81
	v_fmamk_f32 v79, v79, 0x3c000000, v212
	v_cmp_gt_f32_e32 vcc, s2, v79
	v_mul_f32_e32 v81, 0x4f800000, v79
	s_nop 0
	v_cndmask_b32_e32 v79, v79, v81, vcc
	v_sqrt_f32_e32 v81, v79
	s_nop 0
	v_add_u32_e32 v82, -1, v81
	v_fma_f32 v83, -v82, v81, v79
	v_cmp_ge_f32_e64 s[0:1], 0, v83
	v_add_u32_e32 v83, 1, v81
	s_nop 0
	v_cndmask_b32_e64 v82, v81, v82, s[0:1]
	v_fma_f32 v81, -v83, v81, v79
	v_cmp_lt_f32_e64 s[0:1], 0, v81
	s_nop 1
	v_cndmask_b32_e64 v81, v82, v83, s[0:1]
	v_mul_f32_e32 v82, 0x37800000, v81
	v_cndmask_b32_e32 v81, v81, v82, vcc
	v_cmp_class_f32_e32 vcc, v79, v248
	s_nop 1
	v_cndmask_b32_e32 v79, v81, v79, vcc
	v_div_scale_f32 v81, s[0:1], v79, v79, v206
	v_rcp_f32_e32 v82, v81
	s_nop 0
	v_fma_f32 v83, -v81, v82, 1.0
	v_fmac_f32_e32 v82, v83, v82
	v_div_scale_f32 v83, vcc, v206, v79, v206
	v_mul_f32_e32 v84, v83, v82
	v_fma_f32 v85, -v81, v84, v83
	v_fmac_f32_e32 v84, v85, v82
	v_fma_f32 v81, -v81, v84, v83
	v_div_fmas_f32 v81, v81, v82, v84
	v_div_fixup_f32 v79, v81, v79, v206
	s_waitcnt lgkmcnt(0)
	s_nop 1
	v_add_f32_dpp v80, v80, v80 quad_perm:[1,0,3,2] row_mask:0xf bank_mask:0xf
	s_waitcnt lgkmcnt(0)
	s_nop 1
	v_add_f32_dpp v80, v80, v80 quad_perm:[2,3,0,1] row_mask:0xf bank_mask:0xf
	s_waitcnt lgkmcnt(0)
	s_nop 1
	v_add_f32_dpp v80, v80, v80 row_half_mirror row_mask:0xf bank_mask:0xf
	s_waitcnt lgkmcnt(0)
	s_nop 1
	v_add_f32_dpp v80, v80, v80 row_mirror row_mask:0xf bank_mask:0xf
	v_mov_b32_e32 v81, v80
	s_waitcnt lgkmcnt(0)
	s_nop 1
	v_permlane16_swap_b32_e32 v81, v80
	v_add_f32_e32 v80, v80, v81
	v_fmamk_f32 v80, v80, 0x3c000000, v212
	v_cmp_gt_f32_e32 vcc, s2, v80
	v_mul_f32_e32 v81, 0x4f800000, v80
	s_nop 0
	v_cndmask_b32_e32 v80, v80, v81, vcc
	v_sqrt_f32_e32 v81, v80
	s_nop 0
	v_add_u32_e32 v82, -1, v81
	v_fma_f32 v83, -v82, v81, v80
	v_cmp_ge_f32_e64 s[0:1], 0, v83
	v_add_u32_e32 v83, 1, v81
	s_nop 0
	v_cndmask_b32_e64 v82, v81, v82, s[0:1]
	v_fma_f32 v81, -v83, v81, v80
	v_cmp_lt_f32_e64 s[0:1], 0, v81
	s_nop 1
	v_cndmask_b32_e64 v81, v82, v83, s[0:1]
	v_mul_f32_e32 v82, 0x37800000, v81
	v_cndmask_b32_e32 v81, v81, v82, vcc
	v_cmp_class_f32_e32 vcc, v80, v248
	s_nop 1
	v_cndmask_b32_e32 v80, v81, v80, vcc
	v_div_scale_f32 v81, s[0:1], v80, v80, v206
	v_rcp_f32_e32 v82, v81
	s_nop 0
	v_fma_f32 v83, -v81, v82, 1.0
	v_fmac_f32_e32 v82, v83, v82
	v_div_scale_f32 v83, vcc, v206, v80, v206
	v_mul_f32_e32 v84, v83, v82
	v_fma_f32 v85, -v81, v84, v83
	v_fmac_f32_e32 v84, v85, v82
	v_fma_f32 v81, -v81, v84, v83
	v_div_fmas_f32 v81, v81, v82, v84
	v_div_fixup_f32 v80, v81, v80, v206
	s_waitcnt lgkmcnt(0)
	s_nop 1
	v_add_f32_dpp v78, v78, v78 quad_perm:[1,0,3,2] row_mask:0xf bank_mask:0xf
	s_waitcnt lgkmcnt(0)
	s_nop 1
	v_add_f32_dpp v78, v78, v78 quad_perm:[2,3,0,1] row_mask:0xf bank_mask:0xf
	s_waitcnt lgkmcnt(0)
	s_nop 1
	v_add_f32_dpp v78, v78, v78 row_half_mirror row_mask:0xf bank_mask:0xf
	s_waitcnt lgkmcnt(0)
	s_nop 1
	v_add_f32_dpp v78, v78, v78 row_mirror row_mask:0xf bank_mask:0xf
	v_mov_b32_e32 v81, v78
	s_waitcnt lgkmcnt(0)
	s_nop 1
	v_permlane16_swap_b32_e32 v81, v78
	v_add_f32_e32 v78, v78, v81
	v_fmamk_f32 v78, v78, 0x3c000000, v212
	v_cmp_gt_f32_e32 vcc, s2, v78
	v_mul_f32_e32 v81, 0x4f800000, v78
	s_nop 0
	v_cndmask_b32_e32 v78, v78, v81, vcc
	v_sqrt_f32_e32 v81, v78
	s_nop 0
	v_add_u32_e32 v82, -1, v81
	v_fma_f32 v83, -v82, v81, v78
	v_cmp_ge_f32_e64 s[0:1], 0, v83
	v_add_u32_e32 v83, 1, v81
	s_nop 0
	v_cndmask_b32_e64 v82, v81, v82, s[0:1]
	v_fma_f32 v81, -v83, v81, v78
	v_cmp_lt_f32_e64 s[0:1], 0, v81
	s_nop 1
	v_cndmask_b32_e64 v81, v82, v83, s[0:1]
	v_mul_f32_e32 v82, 0x37800000, v81
	v_cndmask_b32_e32 v81, v81, v82, vcc
	v_cmp_class_f32_e32 vcc, v78, v248
	s_nop 1
	v_cndmask_b32_e32 v78, v81, v78, vcc
	v_div_scale_f32 v81, s[0:1], v78, v78, v206
	v_rcp_f32_e32 v82, v81
	s_nop 0
	v_fma_f32 v83, -v81, v82, 1.0
	v_fmac_f32_e32 v82, v83, v82
	v_div_scale_f32 v83, vcc, v206, v78, v206
	v_mul_f32_e32 v84, v83, v82
	v_fma_f32 v85, -v81, v84, v83
	v_fmac_f32_e32 v84, v85, v82
	v_fma_f32 v81, -v81, v84, v83
	v_div_fmas_f32 v81, v81, v82, v84
	v_div_fixup_f32 v78, v81, v78, v206
	s_waitcnt lgkmcnt(0)
	s_nop 1
	v_add_f32_dpp v77, v77, v77 quad_perm:[1,0,3,2] row_mask:0xf bank_mask:0xf
	s_waitcnt lgkmcnt(0)
	s_nop 1
	v_add_f32_dpp v77, v77, v77 quad_perm:[2,3,0,1] row_mask:0xf bank_mask:0xf
	s_waitcnt lgkmcnt(0)
	s_nop 1
	v_add_f32_dpp v77, v77, v77 row_half_mirror row_mask:0xf bank_mask:0xf
	s_waitcnt lgkmcnt(0)
	s_nop 1
	v_add_f32_dpp v77, v77, v77 row_mirror row_mask:0xf bank_mask:0xf
	v_mov_b32_e32 v81, v77
	s_waitcnt lgkmcnt(0)
	s_nop 1
	v_permlane16_swap_b32_e32 v81, v77
	v_add_f32_e32 v77, v77, v81
	v_fmamk_f32 v77, v77, 0x3c000000, v212
	v_cmp_gt_f32_e32 vcc, s2, v77
	v_mul_f32_e32 v81, 0x4f800000, v77
	s_nop 0
	v_cndmask_b32_e32 v77, v77, v81, vcc
	v_sqrt_f32_e32 v81, v77
	s_nop 0
	v_add_u32_e32 v82, -1, v81
	v_fma_f32 v83, -v82, v81, v77
	v_cmp_ge_f32_e64 s[0:1], 0, v83
	v_add_u32_e32 v83, 1, v81
	s_nop 0
	v_cndmask_b32_e64 v82, v81, v82, s[0:1]
	v_fma_f32 v81, -v83, v81, v77
	v_cmp_lt_f32_e64 s[0:1], 0, v81
	s_nop 1
	v_cndmask_b32_e64 v81, v82, v83, s[0:1]
	v_mul_f32_e32 v82, 0x37800000, v81
	v_cndmask_b32_e32 v81, v81, v82, vcc
	v_cmp_class_f32_e32 vcc, v77, v248
	s_nop 1
	v_cndmask_b32_e32 v77, v81, v77, vcc
	v_div_scale_f32 v81, s[0:1], v77, v77, v206
	v_rcp_f32_e32 v82, v81
	s_nop 0
	v_fma_f32 v83, -v81, v82, 1.0
	v_fmac_f32_e32 v82, v83, v82
	v_div_scale_f32 v83, vcc, v206, v77, v206
	v_mul_f32_e32 v84, v83, v82
	v_fma_f32 v85, -v81, v84, v83
	v_fmac_f32_e32 v84, v85, v82
	v_fma_f32 v81, -v81, v84, v83
	v_div_fmas_f32 v81, v81, v82, v84
	v_div_fixup_f32 v77, v81, v77, v206
	s_waitcnt lgkmcnt(0)
; __device__ __forceinline__ float bf_lo(unsigned w) { return __uint_as_float(w << 16); }
; __device__ __forceinline__ float bf_hi(unsigned w) { return __uint_as_float(w & 0xffff0000u); }
; __device__ __forceinline__ float sum32(float v) { v += swz_xor<1>(v); v += swz_xor<2>(v); v += swz_xor<4>(v); v += swz_xor<8>(v); v += swz_xor<16>(v); return v; }
; __device__ __forceinline__ void diff_unit(int b, int h, int qb, const bf16_t* Q, const bf16_t* K, const bf16_t* V, bf16_t* YA, float lam, float omli, const float* subln, char* lds, const int wave_) {
;     ...
;     for (int r = 0; r < 16; ++r) { float s = 0.f;
; #pragma unroll
;         for (int d = 0; d < 4; ++d) { const unsigned pw = park[(d * 8 + (r >> 1)) * 64]; const float a = (r & 1) ? bf_hi(pw) : bf_lo(pw); const float v = a - lam * o[d][r]; o[d][r] = v; s += v * v; }
;         ss[r] = s; }
; #pragma unroll
;     for (int r = 0; r < 16; ++r) {
;         ss[r] = sum32(ss[r]);
;         ss[r] = omli / sqrtf(ss[r] * (1.0f / 128.0f) + EPS); }
	s_nop 1
	v_add_f32_dpp v75, v75, v75 quad_perm:[1,0,3,2] row_mask:0xf bank_mask:0xf
	s_waitcnt lgkmcnt(0)
	s_nop 1
	v_add_f32_dpp v75, v75, v75 quad_perm:[2,3,0,1] row_mask:0xf bank_mask:0xf
	s_waitcnt lgkmcnt(0)
	s_nop 1
	v_add_f32_dpp v75, v75, v75 row_half_mirror row_mask:0xf bank_mask:0xf
	s_waitcnt lgkmcnt(0)
	s_nop 1
	v_add_f32_dpp v75, v75, v75 row_mirror row_mask:0xf bank_mask:0xf
	v_mov_b32_e32 v81, v75
	s_waitcnt lgkmcnt(0)
	s_nop 1
	v_permlane16_swap_b32_e32 v81, v75
	v_add_f32_e32 v75, v75, v81
	v_fmamk_f32 v75, v75, 0x3c000000, v212
	v_cmp_gt_f32_e32 vcc, s2, v75
	v_mul_f32_e32 v81, 0x4f800000, v75
	s_nop 0
	v_cndmask_b32_e32 v75, v75, v81, vcc
	v_sqrt_f32_e32 v81, v75
	s_nop 0
	v_add_u32_e32 v82, -1, v81
	v_fma_f32 v83, -v82, v81, v75
	v_cmp_ge_f32_e64 s[0:1], 0, v83
	v_add_u32_e32 v83, 1, v81
	s_nop 0
	v_cndmask_b32_e64 v82, v81, v82, s[0:1]
	v_fma_f32 v81, -v83, v81, v75
	v_cmp_lt_f32_e64 s[0:1], 0, v81
	s_nop 1
	v_cndmask_b32_e64 v81, v82, v83, s[0:1]
	v_mul_f32_e32 v82, 0x37800000, v81
	v_cndmask_b32_e32 v81, v81, v82, vcc
	v_cmp_class_f32_e32 vcc, v75, v248
	s_nop 1
	v_cndmask_b32_e32 v75, v81, v75, vcc
	v_div_scale_f32 v81, s[0:1], v75, v75, v206
	v_rcp_f32_e32 v82, v81
	s_nop 0
	v_fma_f32 v83, -v81, v82, 1.0
	v_fmac_f32_e32 v82, v83, v82
	v_div_scale_f32 v83, vcc, v206, v75, v206
	v_mul_f32_e32 v84, v83, v82
	v_fma_f32 v85, -v81, v84, v83
	v_fmac_f32_e32 v84, v85, v82
	v_fma_f32 v81, -v81, v84, v83
	v_div_fmas_f32 v81, v81, v82, v84
	v_div_fixup_f32 v75, v81, v75, v206
	s_waitcnt lgkmcnt(0)
	s_nop 1
	v_add_f32_dpp v72, v72, v72 quad_perm:[1,0,3,2] row_mask:0xf bank_mask:0xf
	s_waitcnt lgkmcnt(0)
	s_nop 1
	v_add_f32_dpp v72, v72, v72 quad_perm:[2,3,0,1] row_mask:0xf bank_mask:0xf
	s_waitcnt lgkmcnt(0)
	s_nop 1
	v_add_f32_dpp v72, v72, v72 row_half_mirror row_mask:0xf bank_mask:0xf
	s_waitcnt lgkmcnt(0)
	s_nop 1
	v_add_f32_dpp v72, v72, v72 row_mirror row_mask:0xf bank_mask:0xf
	v_mov_b32_e32 v81, v72
	s_waitcnt lgkmcnt(0)
	s_nop 1
	v_permlane16_swap_b32_e32 v81, v72
	v_add_f32_e32 v72, v72, v81
	v_fmamk_f32 v72, v72, 0x3c000000, v212
	v_cmp_gt_f32_e32 vcc, s2, v72
	v_mul_f32_e32 v81, 0x4f800000, v72
	s_nop 0
	v_cndmask_b32_e32 v72, v72, v81, vcc
	v_sqrt_f32_e32 v81, v72
	s_nop 0
	v_add_u32_e32 v82, -1, v81
	v_fma_f32 v83, -v82, v81, v72
	v_cmp_ge_f32_e64 s[0:1], 0, v83
	v_add_u32_e32 v83, 1, v81
	s_nop 0
	v_cndmask_b32_e64 v82, v81, v82, s[0:1]
	v_fma_f32 v81, -v83, v81, v72
	v_cmp_lt_f32_e64 s[0:1], 0, v81
	s_nop 1
	v_cndmask_b32_e64 v81, v82, v83, s[0:1]
	v_mul_f32_e32 v82, 0x37800000, v81
	v_cndmask_b32_e32 v81, v81, v82, vcc
	v_cmp_class_f32_e32 vcc, v72, v248
	s_nop 1
	v_cndmask_b32_e32 v72, v81, v72, vcc
	v_div_scale_f32 v81, s[0:1], v72, v72, v206
	v_rcp_f32_e32 v82, v81
	s_nop 0
	v_fma_f32 v83, -v81, v82, 1.0
	v_fmac_f32_e32 v82, v83, v82
	v_div_scale_f32 v83, vcc, v206, v72, v206
	v_mul_f32_e32 v84, v83, v82
	v_fma_f32 v85, -v81, v84, v83
	v_fmac_f32_e32 v84, v85, v82
	v_fma_f32 v81, -v81, v84, v83
	v_div_fmas_f32 v81, v81, v82, v84
	v_div_fixup_f32 v72, v81, v72, v206
	s_waitcnt lgkmcnt(0)
	s_nop 1
	v_add_f32_dpp v68, v68, v68 quad_perm:[1,0,3,2] row_mask:0xf bank_mask:0xf
	s_waitcnt lgkmcnt(0)
	s_nop 1
	v_add_f32_dpp v68, v68, v68 quad_perm:[2,3,0,1] row_mask:0xf bank_mask:0xf
	s_waitcnt lgkmcnt(0)
	s_nop 1
	v_add_f32_dpp v68, v68, v68 row_half_mirror row_mask:0xf bank_mask:0xf
	s_waitcnt lgkmcnt(0)
	s_nop 1
	v_add_f32_dpp v68, v68, v68 row_mirror row_mask:0xf bank_mask:0xf
	v_mov_b32_e32 v81, v68
	s_waitcnt lgkmcnt(0)
	s_nop 1
	v_permlane16_swap_b32_e32 v81, v68
	v_add_f32_e32 v68, v68, v81
	v_fmamk_f32 v68, v68, 0x3c000000, v212
	v_cmp_gt_f32_e32 vcc, s2, v68
	v_mul_f32_e32 v81, 0x4f800000, v68
	s_nop 0
	v_cndmask_b32_e32 v68, v68, v81, vcc
	v_sqrt_f32_e32 v81, v68
	s_nop 0
	v_add_u32_e32 v82, -1, v81
	v_fma_f32 v83, -v82, v81, v68
	v_cmp_ge_f32_e64 s[0:1], 0, v83
	v_add_u32_e32 v83, 1, v81
	s_nop 0
	v_cndmask_b32_e64 v82, v81, v82, s[0:1]
	v_fma_f32 v81, -v83, v81, v68
	v_cmp_lt_f32_e64 s[0:1], 0, v81
	s_nop 1
	v_cndmask_b32_e64 v81, v82, v83, s[0:1]
	v_mul_f32_e32 v82, 0x37800000, v81
	v_cndmask_b32_e32 v81, v81, v82, vcc
	v_cmp_class_f32_e32 vcc, v68, v248
	s_nop 1
	v_cndmask_b32_e32 v68, v81, v68, vcc
	v_div_scale_f32 v81, s[0:1], v68, v68, v206
	v_rcp_f32_e32 v82, v81
	s_nop 0
	v_fma_f32 v83, -v81, v82, 1.0
	v_fmac_f32_e32 v82, v83, v82
	v_div_scale_f32 v83, vcc, v206, v68, v206
	v_mul_f32_e32 v84, v83, v82
	v_fma_f32 v85, -v81, v84, v83
	v_fmac_f32_e32 v84, v85, v82
	v_fma_f32 v81, -v81, v84, v83
	v_div_fmas_f32 v81, v81, v82, v84
	v_div_fixup_f32 v68, v81, v68, v206
	s_waitcnt lgkmcnt(0)
	s_nop 1
	v_add_f32_dpp v70, v70, v70 quad_perm:[1,0,3,2] row_mask:0xf bank_mask:0xf
	s_waitcnt lgkmcnt(0)
	s_nop 1
	v_add_f32_dpp v70, v70, v70 quad_perm:[2,3,0,1] row_mask:0xf bank_mask:0xf
	s_waitcnt lgkmcnt(0)
	s_nop 1
	v_add_f32_dpp v70, v70, v70 row_half_mirror row_mask:0xf bank_mask:0xf
	s_waitcnt lgkmcnt(0)
	s_nop 1
	v_add_f32_dpp v70, v70, v70 row_mirror row_mask:0xf bank_mask:0xf
	v_mov_b32_e32 v81, v70
	s_waitcnt lgkmcnt(0)
	s_nop 1
	v_permlane16_swap_b32_e32 v81, v70
	v_add_f32_e32 v70, v70, v81
	v_fmamk_f32 v70, v70, 0x3c000000, v212
	v_cmp_gt_f32_e32 vcc, s2, v70
	v_mul_f32_e32 v81, 0x4f800000, v70
	s_nop 0
	v_cndmask_b32_e32 v70, v70, v81, vcc
	v_sqrt_f32_e32 v81, v70
	s_nop 0
	v_add_u32_e32 v82, -1, v81
	v_fma_f32 v83, -v82, v81, v70
	v_cmp_ge_f32_e64 s[0:1], 0, v83
	v_add_u32_e32 v83, 1, v81
	s_nop 0
	v_cndmask_b32_e64 v82, v81, v82, s[0:1]
	v_fma_f32 v81, -v83, v81, v70
	v_cmp_lt_f32_e64 s[0:1], 0, v81
	s_nop 1
	v_cndmask_b32_e64 v81, v82, v83, s[0:1]
	v_mul_f32_e32 v82, 0x37800000, v81
	v_cndmask_b32_e32 v81, v81, v82, vcc
	v_cmp_class_f32_e32 vcc, v70, v248
	s_nop 1
	v_cndmask_b32_e32 v70, v81, v70, vcc
	v_div_scale_f32 v81, s[0:1], v70, v70, v206
	v_rcp_f32_e32 v82, v81
	s_nop 0
	v_fma_f32 v83, -v81, v82, 1.0
	v_fmac_f32_e32 v82, v83, v82
	v_div_scale_f32 v83, vcc, v206, v70, v206
	v_mul_f32_e32 v84, v83, v82
	v_fma_f32 v85, -v81, v84, v83
	v_fmac_f32_e32 v84, v85, v82
	v_fma_f32 v81, -v81, v84, v83
	v_div_fmas_f32 v81, v81, v82, v84
	v_div_fixup_f32 v70, v81, v70, v206
	s_waitcnt lgkmcnt(0)
; __device__ __forceinline__ unsigned cvt_pk_bf16(float lo, float hi) { unsigned r; asm volatile("v_cvt_pk_bf16_f32 %0, %1, %2" : "=v"(r) : "v"(lo), "v"(hi)); return r; }
; __device__ __forceinline__ float bf_lo(unsigned w) { return __uint_as_float(w << 16); }
; __device__ __forceinline__ float bf_hi(unsigned w) { return __uint_as_float(w & 0xffff0000u); }
; __device__ __forceinline__ float sum32(float v) { v += swz_xor<1>(v); v += swz_xor<2>(v); v += swz_xor<4>(v); v += swz_xor<8>(v); v += swz_xor<16>(v); return v; }
; __device__ __forceinline__ int crow(int r, int hi) { return (r & 3) + 8 * (r >> 2) + 4 * hi; }
; __device__ __forceinline__ void diff_unit(int b, int h, int qb, const bf16_t* Q, const bf16_t* K, const bf16_t* V, bf16_t* YA, float lam, float omli, const float* subln, char* lds, const int wave_) {
;     ...
;     for (int r = 0; r < 16; ++r) { float s = 0.f;
; #pragma unroll
;         for (int d = 0; d < 4; ++d) { const unsigned pw = park[(d * 8 + (r >> 1)) * 64]; const float a = (r & 1) ? bf_hi(pw) : bf_lo(pw); const float v = a - lam * o[d][r]; o[d][r] = v; s += v * v; }
;         ss[r] = s; }
; #pragma unroll
;     for (int r = 0; r < 16; ++r) {
;         ss[r] = sum32(ss[r]);
;         ss[r] = omli / sqrtf(ss[r] * (1.0f / 128.0f) + EPS); }
;     float gl[4];
; #pragma unroll
;     for (int d = 0; d < 4; ++d) gl[d] = subln[32 * d + r32];
;     asm volatile("s_waitcnt lgkmcnt(0)" ::: "memory");
;     bf16_t* stg = (bf16_t*)(lds + DA_LDS) + wid * 4096;
; #pragma unroll
;     for (int r = 0; r < 16; ++r) { const int orow = crow(r, hi);
; #pragma unroll
;         for (int d = 0; d < 4; ++d) stg[orow * 128 + 32 * d + r32] = (bf16_t)(cvt_pk_bf16(o[d][r] * ss[r] * gl[d], 0.f) & 0xffffu); }
	s_nop 1
	v_add_f32_dpp v74, v74, v74 quad_perm:[1,0,3,2] row_mask:0xf bank_mask:0xf
	s_waitcnt lgkmcnt(0)
	s_nop 1
	v_add_f32_dpp v74, v74, v74 quad_perm:[2,3,0,1] row_mask:0xf bank_mask:0xf
	s_waitcnt lgkmcnt(0)
	s_nop 1
	v_add_f32_dpp v74, v74, v74 row_half_mirror row_mask:0xf bank_mask:0xf
	s_waitcnt lgkmcnt(0)
	s_nop 1
	v_add_f32_dpp v74, v74, v74 row_mirror row_mask:0xf bank_mask:0xf
	v_mov_b32_e32 v81, v74
	s_waitcnt lgkmcnt(0)
	s_nop 1
	v_permlane16_swap_b32_e32 v81, v74
	v_add_f32_e32 v74, v74, v81
	v_fmamk_f32 v74, v74, 0x3c000000, v212
	v_cmp_gt_f32_e32 vcc, s2, v74
	v_mul_f32_e32 v81, 0x4f800000, v74
	s_nop 0
	v_cndmask_b32_e32 v74, v74, v81, vcc
	v_sqrt_f32_e32 v81, v74
	s_nop 0
	v_add_u32_e32 v82, -1, v81
	v_fma_f32 v83, -v82, v81, v74
	v_cmp_ge_f32_e64 s[0:1], 0, v83
	v_add_u32_e32 v83, 1, v81
	s_nop 0
	v_cndmask_b32_e64 v82, v81, v82, s[0:1]
	v_fma_f32 v81, -v83, v81, v74
	v_cmp_lt_f32_e64 s[0:1], 0, v81
	s_nop 1
	v_cndmask_b32_e64 v81, v82, v83, s[0:1]
	v_mul_f32_e32 v82, 0x37800000, v81
	v_cndmask_b32_e32 v81, v81, v82, vcc
	v_cmp_class_f32_e32 vcc, v74, v248
	s_nop 1
	v_cndmask_b32_e32 v74, v81, v74, vcc
	v_div_scale_f32 v81, s[0:1], v74, v74, v206
	v_rcp_f32_e32 v82, v81
	s_nop 0
	v_fma_f32 v83, -v81, v82, 1.0
	v_fmac_f32_e32 v82, v83, v82
	v_div_scale_f32 v83, vcc, v206, v74, v206
	v_mul_f32_e32 v84, v83, v82
	v_fma_f32 v85, -v81, v84, v83
	v_fmac_f32_e32 v84, v85, v82
	v_fma_f32 v81, -v81, v84, v83
	v_div_fmas_f32 v81, v81, v82, v84
	v_div_fixup_f32 v74, v81, v74, v206
	s_waitcnt lgkmcnt(0)
	s_nop 1
	v_add_f32_dpp v71, v71, v71 quad_perm:[1,0,3,2] row_mask:0xf bank_mask:0xf
	s_waitcnt lgkmcnt(0)
	s_nop 1
	v_add_f32_dpp v71, v71, v71 quad_perm:[2,3,0,1] row_mask:0xf bank_mask:0xf
	s_waitcnt lgkmcnt(0)
	s_nop 1
	v_add_f32_dpp v71, v71, v71 row_half_mirror row_mask:0xf bank_mask:0xf
	s_waitcnt lgkmcnt(0)
	s_nop 1
	v_add_f32_dpp v71, v71, v71 row_mirror row_mask:0xf bank_mask:0xf
	v_mov_b32_e32 v81, v71
	s_waitcnt lgkmcnt(0)
	s_nop 1
	v_permlane16_swap_b32_e32 v81, v71
	v_add_f32_e32 v71, v71, v81
	v_fmamk_f32 v71, v71, 0x3c000000, v212
	v_cmp_gt_f32_e32 vcc, s2, v71
	v_mul_f32_e32 v81, 0x4f800000, v71
	s_nop 0
	v_cndmask_b32_e32 v71, v71, v81, vcc
	v_sqrt_f32_e32 v81, v71
	s_nop 0
	v_add_u32_e32 v82, -1, v81
	v_fma_f32 v83, -v82, v81, v71
	v_cmp_ge_f32_e64 s[0:1], 0, v83
	v_add_u32_e32 v83, 1, v81
	s_nop 0
	v_cndmask_b32_e64 v82, v81, v82, s[0:1]
	v_fma_f32 v81, -v83, v81, v71
	v_cmp_lt_f32_e64 s[0:1], 0, v81
	s_nop 1
	v_cndmask_b32_e64 v81, v82, v83, s[0:1]
	v_mul_f32_e32 v82, 0x37800000, v81
	v_cndmask_b32_e32 v81, v81, v82, vcc
	v_cmp_class_f32_e32 vcc, v71, v248
	s_nop 1
	v_cndmask_b32_e32 v71, v81, v71, vcc
	v_div_scale_f32 v81, s[0:1], v71, v71, v206
	v_rcp_f32_e32 v82, v81
	s_nop 0
	v_fma_f32 v83, -v81, v82, 1.0
	v_fmac_f32_e32 v82, v83, v82
	v_div_scale_f32 v83, vcc, v206, v71, v206
	v_mul_f32_e32 v84, v83, v82
	v_fma_f32 v85, -v81, v84, v83
	v_fmac_f32_e32 v84, v85, v82
	v_fma_f32 v81, -v81, v84, v83
	v_div_fmas_f32 v81, v81, v82, v84
	v_div_fixup_f32 v71, v81, v71, v206
	s_waitcnt lgkmcnt(0)
	s_nop 1
	v_add_f32_dpp v69, v69, v69 quad_perm:[1,0,3,2] row_mask:0xf bank_mask:0xf
	s_waitcnt lgkmcnt(0)
	s_nop 1
	v_add_f32_dpp v69, v69, v69 quad_perm:[2,3,0,1] row_mask:0xf bank_mask:0xf
	s_waitcnt lgkmcnt(0)
	s_nop 1
	v_add_f32_dpp v69, v69, v69 row_half_mirror row_mask:0xf bank_mask:0xf
	s_waitcnt lgkmcnt(0)
	s_nop 1
	v_add_f32_dpp v69, v69, v69 row_mirror row_mask:0xf bank_mask:0xf
	v_mov_b32_e32 v81, v69
	s_waitcnt lgkmcnt(0)
	s_nop 1
	v_permlane16_swap_b32_e32 v81, v69
	v_add_f32_e32 v69, v69, v81
	v_fmamk_f32 v69, v69, 0x3c000000, v212
	v_cmp_gt_f32_e32 vcc, s2, v69
	v_mul_f32_e32 v81, 0x4f800000, v69
	s_nop 0
	v_cndmask_b32_e32 v69, v69, v81, vcc
	v_sqrt_f32_e32 v81, v69
	s_nop 0
	v_add_u32_e32 v82, -1, v81
	v_fma_f32 v83, -v82, v81, v69
	v_cmp_ge_f32_e64 s[0:1], 0, v83
	v_add_u32_e32 v83, 1, v81
	s_nop 0
	v_cndmask_b32_e64 v82, v81, v82, s[0:1]
	v_fma_f32 v81, -v83, v81, v69
	v_cmp_lt_f32_e64 s[0:1], 0, v81
	s_nop 1
	v_cndmask_b32_e64 v81, v82, v83, s[0:1]
	v_mul_f32_e32 v82, 0x37800000, v81
	v_cndmask_b32_e32 v81, v81, v82, vcc
	v_cmp_class_f32_e32 vcc, v69, v248
	s_nop 1
	v_cndmask_b32_e32 v69, v81, v69, vcc
	v_div_scale_f32 v81, s[0:1], v69, v69, v206
	v_rcp_f32_e32 v82, v81
	v_readlane_b32 s0, v253, 62
	v_readlane_b32 s1, v253, 63
	v_fma_f32 v83, -v81, v82, 1.0
	v_fmac_f32_e32 v82, v83, v82
	v_div_scale_f32 v83, vcc, v206, v69, v206
	v_mul_f32_e32 v84, v83, v82
	v_fma_f32 v85, -v81, v84, v83
	v_fmac_f32_e32 v84, v85, v82
	v_fma_f32 v81, -v81, v84, v83
	v_div_fmas_f32 v81, v81, v82, v84
	v_lshlrev_b32_e32 v83, 2, v64
	v_div_fixup_f32 v69, v81, v69, v206
	global_load_dword v81, v83, s[4:5]
	global_load_dword v82, v83, s[4:5] offset:128
	global_load_dword v84, v83, s[4:5] offset:256
	s_nop 0
	global_load_dword v83, v83, s[4:5] offset:384
	v_lshlrev_b32_e32 v85, 5, v207
	v_lshlrev_b32_e32 v64, 1, v64
	v_and_b32_e32 v85, 0x400, v85
	v_add3_u32 v64, v215, v64, v85
	s_waitcnt lgkmcnt(0)
	v_mul_f32_e32 v1, v1, v69
	v_mul_f32_e32 v0, v0, v69
	s_waitcnt vmcnt(3)
	v_mul_f32_e32 v21, v21, v81
	s_waitcnt vmcnt(2)
	v_mul_f32_e32 v19, v19, v82
	v_cvt_pk_bf16_f32 v21, v21, v161
	ds_write_b16 v64, v21
	v_cvt_pk_bf16_f32 v19, v19, v161
	ds_write_b16 v64, v19 offset:64
	v_mul_f32_e32 v19, v22, v3
	v_mul_f32_e32 v3, v23, v3
	s_waitcnt vmcnt(1)
	v_mul_f32_e32 v19, v19, v84
	s_waitcnt vmcnt(0)
; __device__ __forceinline__ unsigned cvt_pk_bf16(float lo, float hi) { unsigned r; asm volatile("v_cvt_pk_bf16_f32 %0, %1, %2" : "=v"(r) : "v"(lo), "v"(hi)); return r; }
; __device__ __forceinline__ int crow(int r, int hi) { return (r & 3) + 8 * (r >> 2) + 4 * hi; }
; __device__ __forceinline__ void diff_unit(int b, int h, int qb, const bf16_t* Q, const bf16_t* K, const bf16_t* V, bf16_t* YA, float lam, float omli, const float* subln, char* lds, const int wave_) {
;     ...
;     for (int r = 0; r < 16; ++r) { const int orow = crow(r, hi);
; #pragma unroll
;         for (int d = 0; d < 4; ++d) stg[orow * 128 + 32 * d + r32] = (bf16_t)(cvt_pk_bf16(o[d][r] * ss[r] * gl[d], 0.f) & 0xffffu); }
	v_mul_f32_e32 v3, v3, v83
	v_cvt_pk_bf16_f32 v19, v19, v161
	ds_write_b16 v64, v19 offset:128
	v_cvt_pk_bf16_f32 v3, v3, v161
	ds_write_b16 v64, v3 offset:192
	v_mul_f32_e32 v3, v20, v5
	v_mul_f32_e32 v3, v3, v81
	v_cvt_pk_bf16_f32 v3, v3, v161
	ds_write_b16 v64, v3 offset:256
	v_mul_f32_e32 v3, v17, v5
	v_mul_f32_e32 v3, v3, v82
	v_cvt_pk_bf16_f32 v3, v3, v161
	ds_write_b16 v64, v3 offset:320
	v_mul_f32_e32 v3, v18, v5
	v_mul_f32_e32 v3, v3, v84
	v_cvt_pk_bf16_f32 v3, v3, v161
	ds_write_b16 v64, v3 offset:384
	v_mul_f32_e32 v3, v16, v5
	v_mul_f32_e32 v3, v3, v83
	v_cvt_pk_bf16_f32 v3, v3, v161
	ds_write_b16 v64, v3 offset:448
	v_mul_f32_e32 v3, v15, v7
	v_mul_f32_e32 v3, v3, v81
	v_cvt_pk_bf16_f32 v3, v3, v161
	ds_write_b16 v64, v3 offset:512
	v_mul_f32_e32 v3, v13, v7
	v_mul_f32_e32 v3, v3, v82
	v_cvt_pk_bf16_f32 v3, v3, v161
	ds_write_b16 v64, v3 offset:576
	v_mul_f32_e32 v3, v14, v7
	v_mul_f32_e32 v3, v3, v84
	v_cvt_pk_bf16_f32 v3, v3, v161
	ds_write_b16 v64, v3 offset:640
	v_mul_f32_e32 v3, v12, v7
	v_mul_f32_e32 v3, v3, v83
	v_cvt_pk_bf16_f32 v3, v3, v161
	ds_write_b16 v64, v3 offset:704
	v_mul_f32_e32 v3, v11, v73
	v_mul_f32_e32 v3, v3, v81
	v_cvt_pk_bf16_f32 v3, v3, v161
	ds_write_b16 v64, v3 offset:768
	v_mul_f32_e32 v3, v9, v73
	v_mul_f32_e32 v3, v3, v82
	v_cvt_pk_bf16_f32 v3, v3, v161
	ds_write_b16 v64, v3 offset:832
	v_mul_f32_e32 v3, v10, v73
	v_mul_f32_e32 v3, v3, v84
	v_cvt_pk_bf16_f32 v3, v3, v161
	ds_write_b16 v64, v3 offset:896
	v_mul_f32_e32 v3, v8, v73
	v_mul_f32_e32 v3, v3, v83
	v_cvt_pk_bf16_f32 v3, v3, v161
	ds_write_b16 v64, v3 offset:960
	v_mul_f32_e32 v3, v37, v76
	v_mul_f32_e32 v3, v3, v81
	v_cvt_pk_bf16_f32 v3, v3, v161
	ds_write_b16 v64, v3 offset:2048
	v_mul_f32_e32 v3, v35, v76
	v_mul_f32_e32 v3, v3, v82
	v_cvt_pk_bf16_f32 v3, v3, v161
	ds_write_b16 v64, v3 offset:2112
	v_mul_f32_e32 v3, v38, v76
	v_mul_f32_e32 v3, v3, v84
	v_cvt_pk_bf16_f32 v3, v3, v161
	ds_write_b16 v64, v3 offset:2176
	v_mul_f32_e32 v3, v39, v76
	v_mul_f32_e32 v3, v3, v83
	v_cvt_pk_bf16_f32 v3, v3, v161
	ds_write_b16 v64, v3 offset:2240
	v_mul_f32_e32 v3, v36, v79
	v_mul_f32_e32 v3, v3, v81
	v_cvt_pk_bf16_f32 v3, v3, v161
	ds_write_b16 v64, v3 offset:2304
	v_mul_f32_e32 v3, v33, v79
	v_mul_f32_e32 v3, v3, v82
	v_cvt_pk_bf16_f32 v3, v3, v161
	ds_write_b16 v64, v3 offset:2368
	v_mul_f32_e32 v3, v34, v79
	v_mul_f32_e32 v3, v3, v84
	v_cvt_pk_bf16_f32 v3, v3, v161
	ds_write_b16 v64, v3 offset:2432
	v_mul_f32_e32 v3, v32, v79
	v_mul_f32_e32 v3, v3, v83
	v_cvt_pk_bf16_f32 v3, v3, v161
	ds_write_b16 v64, v3 offset:2496
	v_mul_f32_e32 v3, v31, v80
	v_mul_f32_e32 v3, v3, v81
	v_cvt_pk_bf16_f32 v3, v3, v161
	ds_write_b16 v64, v3 offset:2560
	v_mul_f32_e32 v3, v29, v80
	v_mul_f32_e32 v3, v3, v82
	v_cvt_pk_bf16_f32 v3, v3, v161
	ds_write_b16 v64, v3 offset:2624
	v_mul_f32_e32 v3, v30, v80
	v_mul_f32_e32 v3, v3, v84
	v_cvt_pk_bf16_f32 v3, v3, v161
	ds_write_b16 v64, v3 offset:2688
	v_mul_f32_e32 v3, v28, v80
	v_mul_f32_e32 v3, v3, v83
	v_cvt_pk_bf16_f32 v3, v3, v161
	ds_write_b16 v64, v3 offset:2752
	v_mul_f32_e32 v3, v27, v78
	v_mul_f32_e32 v3, v3, v81
	v_cvt_pk_bf16_f32 v3, v3, v161
	ds_write_b16 v64, v3 offset:2816
	v_mul_f32_e32 v3, v25, v78
	v_mul_f32_e32 v3, v3, v82
	v_cvt_pk_bf16_f32 v3, v3, v161
	ds_write_b16 v64, v3 offset:2880
	v_mul_f32_e32 v3, v26, v78
	v_mul_f32_e32 v3, v3, v84
	v_cvt_pk_bf16_f32 v3, v3, v161
	ds_write_b16 v64, v3 offset:2944
	v_mul_f32_e32 v3, v24, v78
	v_mul_f32_e32 v3, v3, v83
	v_cvt_pk_bf16_f32 v3, v3, v161
	ds_write_b16 v64, v3 offset:3008
	v_mul_f32_e32 v3, v53, v77
	v_mul_f32_e32 v3, v3, v81
	v_cvt_pk_bf16_f32 v3, v3, v161
	ds_write_b16 v64, v3 offset:4096
	v_mul_f32_e32 v3, v51, v77
	v_mul_f32_e32 v3, v3, v82
	v_cvt_pk_bf16_f32 v3, v3, v161
	ds_write_b16 v64, v3 offset:4160
	v_mul_f32_e32 v3, v54, v77
	v_mul_f32_e32 v3, v3, v84
	v_cvt_pk_bf16_f32 v3, v3, v161
	ds_write_b16 v64, v3 offset:4224
	v_mul_f32_e32 v3, v55, v77
	v_mul_f32_e32 v3, v3, v83
	v_cvt_pk_bf16_f32 v3, v3, v161
	ds_write_b16 v64, v3 offset:4288
	v_mul_f32_e32 v3, v52, v75
	v_mul_f32_e32 v3, v3, v81
	v_cvt_pk_bf16_f32 v3, v3, v161
	ds_write_b16 v64, v3 offset:4352
	v_mul_f32_e32 v3, v49, v75
	v_mul_f32_e32 v3, v3, v82
	v_cvt_pk_bf16_f32 v3, v3, v161
	ds_write_b16 v64, v3 offset:4416
	v_mul_f32_e32 v3, v50, v75
	v_mul_f32_e32 v3, v3, v84
	v_cvt_pk_bf16_f32 v3, v3, v161
	ds_write_b16 v64, v3 offset:4480
	v_mul_f32_e32 v3, v48, v75
	v_mul_f32_e32 v3, v3, v83
	v_cvt_pk_bf16_f32 v3, v3, v161
	ds_write_b16 v64, v3 offset:4544
	v_mul_f32_e32 v3, v47, v72
	v_mul_f32_e32 v3, v3, v81
	v_cvt_pk_bf16_f32 v3, v3, v161
	ds_write_b16 v64, v3 offset:4608
	v_mul_f32_e32 v3, v45, v72
	v_mul_f32_e32 v3, v3, v82
	v_cvt_pk_bf16_f32 v3, v3, v161
	ds_write_b16 v64, v3 offset:4672
	v_mul_f32_e32 v3, v46, v72
	v_mul_f32_e32 v3, v3, v84
	v_cvt_pk_bf16_f32 v3, v3, v161
	ds_write_b16 v64, v3 offset:4736
; __device__ __forceinline__ unsigned cvt_pk_bf16(float lo, float hi) { unsigned r; asm volatile("v_cvt_pk_bf16_f32 %0, %1, %2" : "=v"(r) : "v"(lo), "v"(hi)); return r; }
; __device__ __forceinline__ int crow(int r, int hi) { return (r & 3) + 8 * (r >> 2) + 4 * hi; }
; __device__ __forceinline__ void diff_unit(int b, int h, int qb, const bf16_t* Q, const bf16_t* K, const bf16_t* V, bf16_t* YA, float lam, float omli, const float* subln, char* lds, const int wave_) {
;     ...
;     for (int r = 0; r < 16; ++r) { const int orow = crow(r, hi);
; #pragma unroll
;         for (int d = 0; d < 4; ++d) stg[orow * 128 + 32 * d + r32] = (bf16_t)(cvt_pk_bf16(o[d][r] * ss[r] * gl[d], 0.f) & 0xffffu); }
;     asm volatile("s_waitcnt lgkmcnt(0)" ::: "memory");
;     bf16_t* Ow = YA + (rowbase + q0 + wid * 32) * DM + h * 128;
; #pragma unroll
;     for (int i = 0; i < 8; ++i) { const int row = i * 4 + (lane >> 4), ch = lane & 15; const u32x4 v = *(const u32x4*)(stg + row * 128 + ch * 8); *(u32x4*)(Ow + (size_t)row * DM + ch * 8) = v; }
;     asm volatile("s_waitcnt lgkmcnt(0)" ::: "memory");
	v_mul_f32_e32 v3, v44, v72
	v_mul_f32_e32 v3, v3, v83
	v_cvt_pk_bf16_f32 v3, v3, v161
	ds_write_b16 v64, v3 offset:4800
	v_mul_f32_e32 v3, v43, v68
	v_mul_f32_e32 v3, v3, v81
	v_cvt_pk_bf16_f32 v3, v3, v161
	ds_write_b16 v64, v3 offset:4864
	v_mul_f32_e32 v3, v41, v68
	v_mul_f32_e32 v3, v3, v82
	v_cvt_pk_bf16_f32 v3, v3, v161
	ds_write_b16 v64, v3 offset:4928
	v_mul_f32_e32 v3, v42, v68
	v_mul_f32_e32 v3, v3, v84
	v_cvt_pk_bf16_f32 v3, v3, v161
	ds_write_b16 v64, v3 offset:4992
	v_mul_f32_e32 v3, v40, v68
	v_mul_f32_e32 v3, v3, v83
	v_cvt_pk_bf16_f32 v3, v3, v161
	ds_write_b16 v64, v3 offset:5056
	v_mul_f32_e32 v3, v56, v70
	v_mul_f32_e32 v3, v3, v81
	v_cvt_pk_bf16_f32 v3, v3, v161
	ds_write_b16 v64, v3 offset:6144
	v_mul_f32_e32 v3, v57, v70
	v_mul_f32_e32 v3, v3, v82
	v_cvt_pk_bf16_f32 v3, v3, v161
	ds_write_b16 v64, v3 offset:6208
	v_mul_f32_e32 v3, v58, v70
	v_mul_f32_e32 v3, v3, v84
	v_cvt_pk_bf16_f32 v3, v3, v161
	ds_write_b16 v64, v3 offset:6272
	v_mul_f32_e32 v3, v66, v70
	v_mul_f32_e32 v3, v3, v83
	v_cvt_pk_bf16_f32 v3, v3, v161
	ds_write_b16 v64, v3 offset:6336
	v_mul_f32_e32 v3, v67, v74
	v_mul_f32_e32 v3, v3, v81
	v_cvt_pk_bf16_f32 v3, v3, v161
	ds_write_b16 v64, v3 offset:6400
	v_mul_f32_e32 v3, v61, v74
	v_mul_f32_e32 v3, v3, v82
	v_cvt_pk_bf16_f32 v3, v3, v161
	ds_write_b16 v64, v3 offset:6464
	v_mul_f32_e32 v3, v63, v74
	v_mul_f32_e32 v3, v3, v84
	v_cvt_pk_bf16_f32 v3, v3, v161
	ds_write_b16 v64, v3 offset:6528
	v_mul_f32_e32 v3, v65, v74
	v_mul_f32_e32 v3, v3, v83
	v_cvt_pk_bf16_f32 v3, v3, v161
	ds_write_b16 v64, v3 offset:6592
	v_mul_f32_e32 v3, v62, v71
	v_mul_f32_e32 v3, v81, v3
	v_cvt_pk_bf16_f32 v3, v3, v161
	ds_write_b16 v64, v3 offset:6656
	v_mul_f32_e32 v3, v59, v71
	v_mul_f32_e32 v3, v3, v82
	v_cvt_pk_bf16_f32 v3, v3, v161
	ds_write_b16 v64, v3 offset:6720
	v_mul_f32_e32 v3, v60, v71
	v_mul_f32_e32 v3, v3, v84
	v_cvt_pk_bf16_f32 v3, v3, v161
	ds_write_b16 v64, v3 offset:6784
	v_mul_f32_e32 v3, v6, v71
	v_mul_f32_e32 v3, v3, v83
	v_cvt_pk_bf16_f32 v3, v3, v161
	ds_write_b16 v64, v3 offset:6848
	v_mul_f32_e32 v3, v4, v69
	v_mul_f32_e32 v3, v81, v3
	v_mul_f32_e32 v1, v82, v1
	v_cvt_pk_bf16_f32 v3, v3, v161
	ds_write_b16 v64, v3 offset:6912
	v_cvt_pk_bf16_f32 v1, v1, v161
	ds_write_b16 v64, v1 offset:6976
	v_mul_f32_e32 v1, v2, v69
	v_mul_f32_e32 v1, v84, v1
	v_mul_f32_e32 v0, v83, v0
	v_cvt_pk_bf16_f32 v1, v1, v161
	ds_write_b16 v64, v1 offset:7040
	v_cvt_pk_bf16_f32 v0, v0, v161
	ds_write_b16 v64, v0 offset:7104
	v_lshlrev_b32_e32 v0, 5, v214
	v_ashrrev_i32_e32 v1, 31, v0
	v_lshl_add_u64 v[0:1], s[6:7], 0, v[0:1]
	v_lshlrev_b64 v[0:1], 11, v[0:1]
	v_lshlrev_b32_e32 v2, 4, v207
	v_lshl_add_u64 v[0:1], s[0:1], 0, v[0:1]
	v_and_b32_e32 v160, 0xf0, v2
	v_lshl_add_u64 v[0:1], v[0:1], 0, s[64:65]
	v_lshrrev_b32_e32 v8, 4, v213
	v_add_u32_e32 v9, v215, v160
	s_waitcnt lgkmcnt(0)
	v_lshl_add_u64 v[4:5], v[0:1], 0, v[160:161]
	v_lshl_add_u32 v0, v8, 8, v9
	ds_read_b128 v[0:3], v0
	v_lshlrev_b32_e32 v160, 11, v8
	v_lshl_add_u64 v[6:7], v[4:5], 0, v[160:161]
	v_readlane_b32 s0, v251, 2
	s_add_i32 s37, s37, s0
	s_waitcnt lgkmcnt(0)
	global_store_dwordx4 v[6:7], v[0:3], off
	v_or_b32_e32 v6, 4, v8
	v_lshlrev_b32_e32 v160, 11, v6
	v_lshl_add_u32 v0, v6, 8, v9
	ds_read_b128 v[0:3], v0
	v_lshl_add_u64 v[6:7], v[4:5], 0, v[160:161]
	v_readlane_b32 s0, v252, 24
	s_add_i32 s36, s36, s0
	s_cmpk_gt_i32 s37, 0x1ff
	s_waitcnt lgkmcnt(0)
	global_store_dwordx4 v[6:7], v[0:3], off
	v_or_b32_e32 v6, 8, v8
	v_lshlrev_b32_e32 v160, 11, v6
	v_lshl_add_u32 v0, v6, 8, v9
	ds_read_b128 v[0:3], v0
	v_lshl_add_u64 v[6:7], v[4:5], 0, v[160:161]
	s_waitcnt lgkmcnt(0)
	global_store_dwordx4 v[6:7], v[0:3], off
	v_or_b32_e32 v6, 12, v8
	s_nop 0
	v_lshl_add_u32 v0, v6, 8, v9
	ds_read_b128 v[0:3], v0
	v_lshlrev_b32_e32 v160, 11, v6
	v_lshl_add_u64 v[6:7], v[4:5], 0, v[160:161]
	s_waitcnt lgkmcnt(0)
	global_store_dwordx4 v[6:7], v[0:3], off
	v_or_b32_e32 v6, 16, v8
	s_nop 0
	v_lshl_add_u32 v0, v6, 8, v9
	ds_read_b128 v[0:3], v0
	v_lshlrev_b32_e32 v160, 11, v6
	v_lshl_add_u64 v[6:7], v[4:5], 0, v[160:161]
	s_waitcnt lgkmcnt(0)
	global_store_dwordx4 v[6:7], v[0:3], off
	v_or_b32_e32 v6, 20, v8
	s_nop 0
	v_lshl_add_u32 v0, v6, 8, v9
	ds_read_b128 v[0:3], v0
	v_lshlrev_b32_e32 v160, 11, v6
	v_lshl_add_u64 v[6:7], v[4:5], 0, v[160:161]
	s_waitcnt lgkmcnt(0)
	global_store_dwordx4 v[6:7], v[0:3], off
	v_or_b32_e32 v6, 24, v8
	s_nop 0
	v_lshl_add_u32 v0, v6, 8, v9
	ds_read_b128 v[0:3], v0
	v_lshlrev_b32_e32 v160, 11, v6
	v_lshl_add_u64 v[6:7], v[4:5], 0, v[160:161]
	s_waitcnt lgkmcnt(0)
	global_store_dwordx4 v[6:7], v[0:3], off
	v_or_b32_e32 v6, 28, v8
	s_nop 0
	v_lshl_add_u32 v0, v6, 8, v9
	ds_read_b128 v[0:3], v0
	v_lshlrev_b32_e32 v160, 11, v6
	v_lshl_add_u64 v[4:5], v[4:5], 0, v[160:161]
	s_waitcnt lgkmcnt(0)
	global_store_dwordx4 v[4:5], v[0:3], off
	s_waitcnt lgkmcnt(0)
	s_cbranch_scc1 .LBB0_870

; __device__ __forceinline__ unsigned cvt_pk_bf16(float lo, float hi) { unsigned r; asm volatile("v_cvt_pk_bf16_f32 %0, %1, %2" : "=v"(r) : "v"(lo), "v"(hi)); return r; }
; __device__ __forceinline__ float bf_lo(unsigned w) { return __uint_as_float(w << 16); }
; __device__ __forceinline__ float bf_hi(unsigned w) { return __uint_as_float(w & 0xffff0000u); }
; template <int M> __device__ __forceinline__ float swz_xor(float v) { return __int_as_float(__builtin_amdgcn_ds_swizzle(__float_as_int(v), (M << 10) | 0x1f)); }
; __device__ __forceinline__ float half_sum(float v) { auto rr = __builtin_amdgcn_permlane32_swap(__float_as_uint(v), __float_as_uint(v), false, false); return __uint_as_float(rr[0]) + __uint_as_float(rr[1]); }
; __device__ __forceinline__ void st16_wt(void* p, u32x4 w) { asm volatile("global_store_dwordx4 %0, %1, off sc1\n\ts_nop 1" :: "v"(p), "v"(w) : "memory"); }
;     __device__ __forceinline__ bool operator()(f32x4 (&acc)[2][2][4][2], const pg8::Unit& u, int wr, int wc, int fr, int fq) const {
;         const int row0 = u.pm * 256 + wr * 64 + fr, colb = u.pn * 256 + wc * 32 + 8 * fq;
; #pragma unroll
;         for (int ai = 0; ai < 2; ++ai) {
;             u32x4 xin[4][2];
; #pragma unroll
;             for (int m = 0; m < 4; ++m)
; #pragma unroll
;                 for (int bj = 0; bj < 2; ++bj) xin[m][bj] = *(const u32x4*)(xbase + (size_t)(row0 + ai * 128 + m * 16) * DM + colb + bj * 128);
; #pragma unroll
;             for (int m = 0; m < 4; ++m) { const int row = row0 + ai * 128 + m * 16; float ss = 0.f;
; #pragma unroll
;                 for (int bj = 0; bj < 2; ++bj) { const size_t off = (size_t)row * DM + colb + bj * 128; const u32x4 xw = xin[m][bj];
;                     f32x4 a = {bf_lo(xw.x), bf_hi(xw.x), bf_lo(xw.y), bf_hi(xw.y)}, b = {bf_lo(xw.z), bf_hi(xw.z), bf_lo(xw.w), bf_hi(xw.w)};
;                     a += acc[ai][bj][m][0]; b += acc[ai][bj][m][1];
;                     ss += ((a[0] * a[0] + a[1] * a[1]) + (a[2] * a[2] + a[3] * a[3])) + ((b[0] * b[0] + b[1] * b[1]) + (b[2] * b[2] + b[3] * b[3]));
;                     { u32x4 w; w.x = cvt_pk_bf16(a[0], a[1]); w.y = cvt_pk_bf16(a[2], a[3]); w.z = cvt_pk_bf16(b[0], b[1]); w.w = cvt_pk_bf16(b[2], b[3]); st16_wt(xb + off, w); } }
;                 ss += swz_xor<16>(ss); ss = half_sum(ss);
;                 if (fq == 0) xch[(ai * 128 + wr * 64 + m * 16 + fr) * 4 + wc] = ss; } }
.LBB0_1031:
	s_lshl_b32 s7, s44, 8
	v_lshl_or_b32 v164, s45, 8, v183
	v_add_u32_e32 v168, s7, v180
	v_ashrrev_i32_e32 v165, 31, v164
	v_readlane_b32 s2, v252, 8
	v_lshlrev_b64 v[176:177], 1, v[164:165]
	v_readlane_b32 s3, v252, 9
	v_ashrrev_i32_e32 v169, 31, v168
	v_lshlrev_b64 v[178:179], 11, v[168:169]
	v_lshl_add_u64 v[166:167], s[2:3], 0, v[176:177]
	v_lshl_add_u64 v[128:129], v[166:167], 0, v[178:179]
	global_load_dwordx4 v[196:199], v[128:129], off
	global_load_dwordx4 v[152:155], v[128:129], off offset:256
	v_or_b32_e32 v128, 16, v168
	v_ashrrev_i32_e32 v129, 31, v128
	v_lshlrev_b64 v[174:175], 11, v[128:129]
	v_lshl_add_u64 v[128:129], v[166:167], 0, v[174:175]
	global_load_dwordx4 v[148:151], v[128:129], off
	global_load_dwordx4 v[144:147], v[128:129], off offset:256
	v_or_b32_e32 v128, 32, v168
	v_ashrrev_i32_e32 v129, 31, v128
	v_lshlrev_b64 v[172:173], 11, v[128:129]
	v_lshl_add_u64 v[128:129], v[166:167], 0, v[172:173]
	global_load_dwordx4 v[140:143], v[128:129], off
	global_load_dwordx4 v[136:139], v[128:129], off offset:256
	v_or_b32_e32 v128, 48, v168
	v_ashrrev_i32_e32 v129, 31, v128
	v_lshlrev_b64 v[170:171], 11, v[128:129]
	v_lshl_add_u64 v[128:129], v[166:167], 0, v[170:171]
	global_load_dwordx4 v[132:135], v[128:129], off
	s_nop 0
	global_load_dwordx4 v[128:131], v[128:129], off offset:256
	s_waitcnt vmcnt(0)
	v_lshlrev_b32_e32 v188, 16, v196
	v_and_b32_e32 v189, 0xffff0000, v196
	v_lshlrev_b32_e32 v190, 16, v197
	v_and_b32_e32 v191, 0xffff0000, v197
	v_lshlrev_b32_e32 v192, 16, v198
	v_and_b32_e32 v193, 0xffff0000, v198
	v_lshlrev_b32_e32 v196, 16, v199
	v_and_b32_e32 v197, 0xffff0000, v199
	v_pk_add_f32 v[126:127], v[126:127], v[190:191]
	v_pk_add_f32 v[124:125], v[124:125], v[188:189]
	v_pk_add_f32 v[188:189], v[122:123], v[196:197]
	v_pk_add_f32 v[122:123], v[120:121], v[192:193]
	v_mul_f32_e32 v120, v125, v125
	v_mul_f32_e32 v121, v127, v127
	v_fmac_f32_e32 v120, v124, v124
	v_fmac_f32_e32 v121, v126, v126
	v_add_f32_e32 v120, v120, v121
	v_mul_f32_e32 v121, v123, v123
	v_mul_f32_e32 v187, v189, v189
	v_fmac_f32_e32 v121, v122, v122
	v_fmac_f32_e32 v187, v188, v188
	v_add_f32_e32 v121, v121, v187
	v_add_f32_e32 v187, v120, v121
	v_cvt_pk_bf16_f32 v120, v124, v125
	v_cvt_pk_bf16_f32 v121, v126, v127
	v_cvt_pk_bf16_f32 v122, v122, v123
	v_cvt_pk_bf16_f32 v123, v188, v189
	v_lshl_add_u64 v[124:125], s[2:3], 0, v[178:179]
	v_lshl_add_u64 v[124:125], v[124:125], 0, v[176:177]
	global_store_dwordx4 v[124:125], v[120:123], off sc1
	s_nop 1
	v_lshlrev_b32_e32 v120, 16, v152
	v_and_b32_e32 v121, 0xffff0000, v152
	v_lshlrev_b32_e32 v122, 16, v153
	v_and_b32_e32 v123, 0xffff0000, v153
	v_lshlrev_b32_e32 v126, 16, v154
	v_and_b32_e32 v127, 0xffff0000, v154
	v_lshlrev_b32_e32 v152, 16, v155
	v_and_b32_e32 v153, 0xffff0000, v155
	v_pk_add_f32 v[118:119], v[118:119], v[122:123]
	v_pk_add_f32 v[116:117], v[116:117], v[120:121]
	v_pk_add_f32 v[120:121], v[114:115], v[152:153]
	v_pk_add_f32 v[114:115], v[112:113], v[126:127]
	v_mul_f32_e32 v112, v117, v117
	v_mul_f32_e32 v113, v119, v119
	v_fmac_f32_e32 v112, v116, v116
	v_fmac_f32_e32 v113, v118, v118
	v_add_f32_e32 v112, v112, v113
	v_mul_f32_e32 v113, v115, v115
	v_mul_f32_e32 v122, v121, v121
	v_fmac_f32_e32 v113, v114, v114
	v_fmac_f32_e32 v122, v120, v120
	v_add_f32_e32 v113, v113, v122
	v_add_f32_e32 v112, v112, v113
	v_add_f32_e32 v122, v187, v112
	v_cvt_pk_bf16_f32 v112, v116, v117
	s_mov_b64 s[2:3], 0x100
	v_cvt_pk_bf16_f32 v113, v118, v119
	v_cvt_pk_bf16_f32 v114, v114, v115
	v_cvt_pk_bf16_f32 v115, v120, v121
	v_lshl_add_u64 v[116:117], v[124:125], 0, s[2:3]
	global_store_dwordx4 v[116:117], v[112:115], off sc1
	s_nop 1
	ds_swizzle_b32 v112, v122 offset:swizzle(SWAP,16)
	s_waitcnt lgkmcnt(0)
	v_add_f32_e32 v112, v122, v112
	v_mov_b32_e32 v113, v112
	s_nop 1
	v_permlane32_swap_b32_e32 v112, v113
	s_and_saveexec_b64 s[4:5], s[10:11]
	v_add_f32_e32 v112, v112, v113
	ds_write_b32 v186, v112
	s_or_b64 exec, exec, s[4:5]
	v_lshlrev_b32_e32 v112, 16, v148
	v_and_b32_e32 v113, 0xffff0000, v148
	v_lshlrev_b32_e32 v114, 16, v149
	v_and_b32_e32 v115, 0xffff0000, v149
	v_lshlrev_b32_e32 v116, 16, v150
	v_and_b32_e32 v117, 0xffff0000, v150
	v_lshlrev_b32_e32 v118, 16, v151
	v_and_b32_e32 v119, 0xffff0000, v151
	v_pk_add_f32 v[110:111], v[110:111], v[114:115]
	v_pk_add_f32 v[108:109], v[108:109], v[112:113]
	v_pk_add_f32 v[112:113], v[106:107], v[118:119]
	v_pk_add_f32 v[106:107], v[104:105], v[116:117]
	v_mul_f32_e32 v104, v109, v109
	v_mul_f32_e32 v105, v111, v111
	v_fmac_f32_e32 v104, v108, v108
	v_fmac_f32_e32 v105, v110, v110
	v_add_f32_e32 v104, v104, v105
	v_mul_f32_e32 v105, v107, v107
	v_mul_f32_e32 v114, v113, v113
	v_fmac_f32_e32 v105, v106, v106
	v_fmac_f32_e32 v114, v112, v112
	v_readlane_b32 s2, v252, 8
	v_add_f32_e32 v105, v105, v114
	v_readlane_b32 s3, v252, 9
	v_add_f32_e32 v114, v104, v105
	v_cvt_pk_bf16_f32 v104, v108, v109
	v_cvt_pk_bf16_f32 v105, v110, v111
	v_cvt_pk_bf16_f32 v106, v106, v107
	v_cvt_pk_bf16_f32 v107, v112, v113
	s_nop 0
	v_lshl_add_u64 v[108:109], s[2:3], 0, v[174:175]
	v_lshl_add_u64 v[108:109], v[164:165], 1, v[108:109]
	global_store_dwordx4 v[108:109], v[104:107], off sc1
	s_nop 1
	v_lshlrev_b32_e32 v104, 16, v144
	v_and_b32_e32 v105, 0xffff0000, v144
	v_lshlrev_b32_e32 v106, 16, v145
	v_and_b32_e32 v107, 0xffff0000, v145
	v_lshlrev_b32_e32 v110, 16, v146
	v_and_b32_e32 v111, 0xffff0000, v146
	v_lshlrev_b32_e32 v112, 16, v147
	v_and_b32_e32 v113, 0xffff0000, v147
	v_pk_add_f32 v[102:103], v[102:103], v[106:107]
	v_pk_add_f32 v[100:101], v[100:101], v[104:105]
	v_pk_add_f32 v[104:105], v[98:99], v[112:113]
	v_pk_add_f32 v[98:99], v[96:97], v[110:111]
	v_mul_f32_e32 v96, v101, v101
	v_mul_f32_e32 v97, v103, v103
	v_fmac_f32_e32 v96, v100, v100
	v_fmac_f32_e32 v97, v102, v102
	v_add_f32_e32 v96, v96, v97
	v_mul_f32_e32 v97, v99, v99
	v_mul_f32_e32 v106, v105, v105
	v_fmac_f32_e32 v97, v98, v98
	v_fmac_f32_e32 v106, v104, v104
	v_add_f32_e32 v97, v97, v106
	v_add_f32_e32 v96, v96, v97
	v_add_f32_e32 v106, v114, v96
	v_cvt_pk_bf16_f32 v96, v100, v101
	v_cvt_pk_bf16_f32 v97, v102, v103
	v_mov_b32_e32 v102, v106
	s_mov_b64 s[2:3], 0x100
	v_cvt_pk_bf16_f32 v98, v98, v99
	v_cvt_pk_bf16_f32 v99, v104, v105
	v_lshl_add_u64 v[100:101], v[108:109], 0, s[2:3]
	global_store_dwordx4 v[100:101], v[96:99], off sc1
	s_nop 1
	s_waitcnt lgkmcnt(0)
; __device__ __forceinline__ unsigned cvt_pk_bf16(float lo, float hi) { unsigned r; asm volatile("v_cvt_pk_bf16_f32 %0, %1, %2" : "=v"(r) : "v"(lo), "v"(hi)); return r; }
; __device__ __forceinline__ float bf_lo(unsigned w) { return __uint_as_float(w << 16); }
; __device__ __forceinline__ float bf_hi(unsigned w) { return __uint_as_float(w & 0xffff0000u); }
; template <int M> __device__ __forceinline__ float swz_xor(float v) { return __int_as_float(__builtin_amdgcn_ds_swizzle(__float_as_int(v), (M << 10) | 0x1f)); }
; __device__ __forceinline__ float half_sum(float v) { auto rr = __builtin_amdgcn_permlane32_swap(__float_as_uint(v), __float_as_uint(v), false, false); return __uint_as_float(rr[0]) + __uint_as_float(rr[1]); }
; __device__ __forceinline__ void st16_wt(void* p, u32x4 w) { asm volatile("global_store_dwordx4 %0, %1, off sc1\n\ts_nop 1" :: "v"(p), "v"(w) : "memory"); }
;     __device__ __forceinline__ bool operator()(f32x4 (&acc)[2][2][4][2], const pg8::Unit& u, int wr, int wc, int fr, int fq) const {
;     ...
;             for (int m = 0; m < 4; ++m) { const int row = row0 + ai * 128 + m * 16; float ss = 0.f;
; #pragma unroll
;                 for (int bj = 0; bj < 2; ++bj) { const size_t off = (size_t)row * DM + colb + bj * 128; const u32x4 xw = xin[m][bj];
;                     f32x4 a = {bf_lo(xw.x), bf_hi(xw.x), bf_lo(xw.y), bf_hi(xw.y)}, b = {bf_lo(xw.z), bf_hi(xw.z), bf_lo(xw.w), bf_hi(xw.w)};
;                     a += acc[ai][bj][m][0]; b += acc[ai][bj][m][1];
;                     ss += ((a[0] * a[0] + a[1] * a[1]) + (a[2] * a[2] + a[3] * a[3])) + ((b[0] * b[0] + b[1] * b[1]) + (b[2] * b[2] + b[3] * b[3]));
;                     { u32x4 w; w.x = cvt_pk_bf16(a[0], a[1]); w.y = cvt_pk_bf16(a[2], a[3]); w.z = cvt_pk_bf16(b[0], b[1]); w.w = cvt_pk_bf16(b[2], b[3]); st16_wt(xb + off, w); } }
;                 ss += swz_xor<16>(ss); ss = half_sum(ss);
;                 if (fq == 0) xch[(ai * 128 + wr * 64 + m * 16 + fr) * 4 + wc] = ss; } }
	s_nop 1
	v_permlane16_swap_b32_e32 v102, v106
	v_add_f32_e32 v96, v106, v102
	v_mov_b32_e32 v97, v96
	s_nop 1
	v_permlane32_swap_b32_e32 v96, v97
	s_and_saveexec_b64 s[4:5], s[10:11]
	v_add_f32_e32 v96, v96, v97
	ds_write_b32 v186, v96 offset:256
	s_or_b64 exec, exec, s[4:5]
	v_lshlrev_b32_e32 v96, 16, v140
	v_and_b32_e32 v97, 0xffff0000, v140
	v_lshlrev_b32_e32 v98, 16, v141
	v_and_b32_e32 v99, 0xffff0000, v141
	v_lshlrev_b32_e32 v100, 16, v142
	v_and_b32_e32 v101, 0xffff0000, v142
	v_lshlrev_b32_e32 v102, 16, v143
	v_and_b32_e32 v103, 0xffff0000, v143
	v_pk_add_f32 v[94:95], v[94:95], v[98:99]
	v_pk_add_f32 v[92:93], v[92:93], v[96:97]
	v_pk_add_f32 v[96:97], v[90:91], v[102:103]
	v_pk_add_f32 v[90:91], v[88:89], v[100:101]
	v_mul_f32_e32 v88, v93, v93
	v_mul_f32_e32 v89, v95, v95
	v_fmac_f32_e32 v88, v92, v92
	v_fmac_f32_e32 v89, v94, v94
	v_add_f32_e32 v88, v88, v89
	v_mul_f32_e32 v89, v91, v91
	v_mul_f32_e32 v98, v97, v97
	v_fmac_f32_e32 v89, v90, v90
	v_fmac_f32_e32 v98, v96, v96
	v_readlane_b32 s2, v252, 8
	v_add_f32_e32 v89, v89, v98
	v_readlane_b32 s3, v252, 9
	v_add_f32_e32 v98, v88, v89
	v_cvt_pk_bf16_f32 v88, v92, v93
	v_cvt_pk_bf16_f32 v89, v94, v95
	v_cvt_pk_bf16_f32 v90, v90, v91
	v_cvt_pk_bf16_f32 v91, v96, v97
	s_nop 0
	v_lshl_add_u64 v[92:93], s[2:3], 0, v[172:173]
	v_lshl_add_u64 v[92:93], v[164:165], 1, v[92:93]
	global_store_dwordx4 v[92:93], v[88:91], off sc1
	s_nop 1
	v_lshlrev_b32_e32 v88, 16, v136
	v_and_b32_e32 v89, 0xffff0000, v136
	v_lshlrev_b32_e32 v90, 16, v137
	v_and_b32_e32 v91, 0xffff0000, v137
	v_lshlrev_b32_e32 v94, 16, v138
	v_and_b32_e32 v95, 0xffff0000, v138
	v_lshlrev_b32_e32 v96, 16, v139
	v_and_b32_e32 v97, 0xffff0000, v139
	v_pk_add_f32 v[86:87], v[86:87], v[90:91]
	v_pk_add_f32 v[84:85], v[84:85], v[88:89]
	v_pk_add_f32 v[88:89], v[82:83], v[96:97]
	v_pk_add_f32 v[82:83], v[80:81], v[94:95]
	v_mul_f32_e32 v80, v85, v85
	v_mul_f32_e32 v81, v87, v87
	v_fmac_f32_e32 v80, v84, v84
	v_fmac_f32_e32 v81, v86, v86
	v_add_f32_e32 v80, v80, v81
	v_mul_f32_e32 v81, v83, v83
	v_mul_f32_e32 v90, v89, v89
	v_fmac_f32_e32 v81, v82, v82
	v_fmac_f32_e32 v90, v88, v88
	v_add_f32_e32 v81, v81, v90
	v_add_f32_e32 v80, v80, v81
	v_add_f32_e32 v90, v98, v80
	v_cvt_pk_bf16_f32 v80, v84, v85
	v_cvt_pk_bf16_f32 v81, v86, v87
	v_mov_b32_e32 v86, v90
	s_mov_b64 s[2:3], 0x100
	v_cvt_pk_bf16_f32 v82, v82, v83
	v_cvt_pk_bf16_f32 v83, v88, v89
	v_lshl_add_u64 v[84:85], v[92:93], 0, s[2:3]
	global_store_dwordx4 v[84:85], v[80:83], off sc1
	s_nop 1
	s_waitcnt lgkmcnt(0)
	s_nop 1
	v_permlane16_swap_b32_e32 v86, v90
	v_add_f32_e32 v80, v90, v86
	v_mov_b32_e32 v81, v80
	s_nop 1
	v_permlane32_swap_b32_e32 v80, v81
	s_and_saveexec_b64 s[4:5], s[10:11]
	v_add_f32_e32 v80, v80, v81
	ds_write_b32 v186, v80 offset:512
	s_or_b64 exec, exec, s[4:5]
	v_lshlrev_b32_e32 v80, 16, v132
	v_and_b32_e32 v81, 0xffff0000, v132
	v_lshlrev_b32_e32 v82, 16, v133
	v_and_b32_e32 v83, 0xffff0000, v133
	v_lshlrev_b32_e32 v84, 16, v134
	v_and_b32_e32 v85, 0xffff0000, v134
	v_lshlrev_b32_e32 v86, 16, v135
	v_and_b32_e32 v87, 0xffff0000, v135
	v_pk_add_f32 v[78:79], v[78:79], v[82:83]
	v_pk_add_f32 v[76:77], v[76:77], v[80:81]
	v_pk_add_f32 v[80:81], v[74:75], v[86:87]
	v_pk_add_f32 v[74:75], v[72:73], v[84:85]
	v_mul_f32_e32 v72, v77, v77
	v_mul_f32_e32 v73, v79, v79
	v_fmac_f32_e32 v72, v76, v76
	v_fmac_f32_e32 v73, v78, v78
	v_add_f32_e32 v72, v72, v73
	v_mul_f32_e32 v73, v75, v75
	v_mul_f32_e32 v82, v81, v81
	v_fmac_f32_e32 v73, v74, v74
	v_fmac_f32_e32 v82, v80, v80
	v_readlane_b32 s2, v252, 8
	v_add_f32_e32 v73, v73, v82
	v_readlane_b32 s3, v252, 9
	v_add_f32_e32 v82, v72, v73
	v_cvt_pk_bf16_f32 v72, v76, v77
	v_cvt_pk_bf16_f32 v73, v78, v79
	v_cvt_pk_bf16_f32 v74, v74, v75
	v_cvt_pk_bf16_f32 v75, v80, v81
	s_nop 0
	v_lshl_add_u64 v[76:77], s[2:3], 0, v[170:171]
	v_lshl_add_u64 v[76:77], v[164:165], 1, v[76:77]
	global_store_dwordx4 v[76:77], v[72:75], off sc1
	s_nop 1
	v_lshlrev_b32_e32 v72, 16, v128
	v_and_b32_e32 v73, 0xffff0000, v128
	v_lshlrev_b32_e32 v74, 16, v129
	v_and_b32_e32 v75, 0xffff0000, v129
	v_lshlrev_b32_e32 v78, 16, v130
	v_and_b32_e32 v79, 0xffff0000, v130
	v_lshlrev_b32_e32 v80, 16, v131
	v_and_b32_e32 v81, 0xffff0000, v131
	v_pk_add_f32 v[70:71], v[70:71], v[74:75]
	v_pk_add_f32 v[68:69], v[68:69], v[72:73]
	v_pk_add_f32 v[72:73], v[66:67], v[80:81]
	v_pk_add_f32 v[66:67], v[64:65], v[78:79]
	v_mul_f32_e32 v64, v69, v69
	v_mul_f32_e32 v65, v71, v71
	v_fmac_f32_e32 v64, v68, v68
	v_fmac_f32_e32 v65, v70, v70
	v_add_f32_e32 v64, v64, v65
	v_mul_f32_e32 v65, v67, v67
	v_mul_f32_e32 v74, v73, v73
	v_fmac_f32_e32 v65, v66, v66
	v_fmac_f32_e32 v74, v72, v72
	v_add_f32_e32 v65, v65, v74
	v_add_f32_e32 v64, v64, v65
	v_add_f32_e32 v74, v82, v64
	v_cvt_pk_bf16_f32 v64, v68, v69
	v_cvt_pk_bf16_f32 v65, v70, v71
	v_mov_b32_e32 v70, v74
	s_mov_b64 s[2:3], 0x100
	v_cvt_pk_bf16_f32 v66, v66, v67
	v_cvt_pk_bf16_f32 v67, v72, v73
	v_lshl_add_u64 v[68:69], v[76:77], 0, s[2:3]
	global_store_dwordx4 v[68:69], v[64:67], off sc1
	s_nop 1
	s_waitcnt lgkmcnt(0)
; __device__ __forceinline__ unsigned cvt_pk_bf16(float lo, float hi) { unsigned r; asm volatile("v_cvt_pk_bf16_f32 %0, %1, %2" : "=v"(r) : "v"(lo), "v"(hi)); return r; }
; __device__ __forceinline__ float bf_lo(unsigned w) { return __uint_as_float(w << 16); }
; __device__ __forceinline__ float bf_hi(unsigned w) { return __uint_as_float(w & 0xffff0000u); }
; template <int M> __device__ __forceinline__ float swz_xor(float v) { return __int_as_float(__builtin_amdgcn_ds_swizzle(__float_as_int(v), (M << 10) | 0x1f)); }
; __device__ __forceinline__ float half_sum(float v) { auto rr = __builtin_amdgcn_permlane32_swap(__float_as_uint(v), __float_as_uint(v), false, false); return __uint_as_float(rr[0]) + __uint_as_float(rr[1]); }
; __device__ __forceinline__ void st16_wt(void* p, u32x4 w) { asm volatile("global_store_dwordx4 %0, %1, off sc1\n\ts_nop 1" :: "v"(p), "v"(w) : "memory"); }
;     __device__ __forceinline__ bool operator()(f32x4 (&acc)[2][2][4][2], const pg8::Unit& u, int wr, int wc, int fr, int fq) const {
;     ...
;         for (int ai = 0; ai < 2; ++ai) {
;             u32x4 xin[4][2];
; #pragma unroll
;             for (int m = 0; m < 4; ++m)
; #pragma unroll
;                 for (int bj = 0; bj < 2; ++bj) xin[m][bj] = *(const u32x4*)(xbase + (size_t)(row0 + ai * 128 + m * 16) * DM + colb + bj * 128);
; #pragma unroll
;             for (int m = 0; m < 4; ++m) { const int row = row0 + ai * 128 + m * 16; float ss = 0.f;
; #pragma unroll
;                 for (int bj = 0; bj < 2; ++bj) { const size_t off = (size_t)row * DM + colb + bj * 128; const u32x4 xw = xin[m][bj];
;                     f32x4 a = {bf_lo(xw.x), bf_hi(xw.x), bf_lo(xw.y), bf_hi(xw.y)}, b = {bf_lo(xw.z), bf_hi(xw.z), bf_lo(xw.w), bf_hi(xw.w)};
;                     a += acc[ai][bj][m][0]; b += acc[ai][bj][m][1];
;                     ss += ((a[0] * a[0] + a[1] * a[1]) + (a[2] * a[2] + a[3] * a[3])) + ((b[0] * b[0] + b[1] * b[1]) + (b[2] * b[2] + b[3] * b[3]));
;                     { u32x4 w; w.x = cvt_pk_bf16(a[0], a[1]); w.y = cvt_pk_bf16(a[2], a[3]); w.z = cvt_pk_bf16(b[0], b[1]); w.w = cvt_pk_bf16(b[2], b[3]); st16_wt(xb + off, w); } }
;                 ss += swz_xor<16>(ss); ss = half_sum(ss);
;                 if (fq == 0) xch[(ai * 128 + wr * 64 + m * 16 + fr) * 4 + wc] = ss; } }
	s_nop 1
	v_permlane16_swap_b32_e32 v70, v74
	v_add_f32_e32 v64, v74, v70
	v_mov_b32_e32 v65, v64
	s_nop 1
	v_permlane32_swap_b32_e32 v64, v65
	s_and_saveexec_b64 s[4:5], s[10:11]
	v_add_f32_e32 v64, v64, v65
	ds_write_b32 v186, v64 offset:768
	s_or_b64 exec, exec, s[4:5]
	v_lshlrev_b64 v[64:65], 11, v[168:169]
	s_mov_b64 s[2:3], 0x40000
	v_lshl_add_u64 v[102:103], v[64:65], 0, s[2:3]
	v_lshl_add_u64 v[66:67], v[166:167], 0, v[102:103]
	global_load_dwordx4 v[94:97], v[66:67], off
	global_load_dwordx4 v[98:101], v[66:67], off offset:256
	s_mov_b64 s[2:3], 0x48000
	v_lshl_add_u64 v[92:93], v[64:65], 0, s[2:3]
	s_mov_b64 s[2:3], 0x50000
	v_lshl_add_u64 v[90:91], v[64:65], 0, s[2:3]
	s_mov_b64 s[2:3], 0x58000
	v_lshl_add_u64 v[66:67], v[166:167], 0, v[92:93]
	v_lshl_add_u64 v[88:89], v[64:65], 0, s[2:3]
	global_load_dwordx4 v[84:87], v[66:67], off
	global_load_dwordx4 v[80:83], v[66:67], off offset:256
	v_lshl_add_u64 v[66:67], v[166:167], 0, v[90:91]
	v_lshl_add_u64 v[64:65], v[166:167], 0, v[88:89]
	global_load_dwordx4 v[76:79], v[66:67], off
	global_load_dwordx4 v[72:75], v[66:67], off offset:256
	global_load_dwordx4 v[68:71], v[64:65], off
	s_nop 0
	global_load_dwordx4 v[64:67], v[64:65], off offset:256
	v_readlane_b32 s2, v252, 8
	v_readlane_b32 s3, v252, 9
	s_waitcnt vmcnt(7)
	v_lshlrev_b32_e32 v104, 16, v94
	v_and_b32_e32 v105, 0xffff0000, v94
	v_lshlrev_b32_e32 v94, 16, v95
	v_and_b32_e32 v95, 0xffff0000, v95
	v_lshlrev_b32_e32 v106, 16, v96
	v_and_b32_e32 v107, 0xffff0000, v96
	v_lshlrev_b32_e32 v96, 16, v97
	v_and_b32_e32 v97, 0xffff0000, v97
	v_pk_add_f32 v[62:63], v[62:63], v[94:95]
	v_pk_add_f32 v[60:61], v[60:61], v[104:105]
	v_pk_add_f32 v[94:95], v[58:59], v[96:97]
	v_pk_add_f32 v[58:59], v[56:57], v[106:107]
	v_mul_f32_e32 v56, v61, v61
	v_mul_f32_e32 v57, v63, v63
	v_fmac_f32_e32 v56, v60, v60
	v_fmac_f32_e32 v57, v62, v62
	v_add_f32_e32 v56, v56, v57
	v_mul_f32_e32 v57, v59, v59
	v_mul_f32_e32 v96, v95, v95
	v_fmac_f32_e32 v57, v58, v58
	v_fmac_f32_e32 v96, v94, v94
	v_add_f32_e32 v57, v57, v96
	v_add_f32_e32 v96, v56, v57
	v_cvt_pk_bf16_f32 v56, v60, v61
	v_cvt_pk_bf16_f32 v57, v62, v63
	v_cvt_pk_bf16_f32 v58, v58, v59
	v_cvt_pk_bf16_f32 v59, v94, v95
	v_lshl_add_u64 v[60:61], s[2:3], 0, v[102:103]
	v_lshl_add_u64 v[60:61], v[164:165], 1, v[60:61]
	global_store_dwordx4 v[60:61], v[56:59], off sc1
	s_nop 1
	s_waitcnt vmcnt(6)
	v_lshlrev_b32_e32 v56, 16, v98
	v_and_b32_e32 v57, 0xffff0000, v98
	v_lshlrev_b32_e32 v58, 16, v99
	v_and_b32_e32 v59, 0xffff0000, v99
	v_lshlrev_b32_e32 v62, 16, v100
	v_and_b32_e32 v63, 0xffff0000, v100
	v_lshlrev_b32_e32 v94, 16, v101
	v_and_b32_e32 v95, 0xffff0000, v101
	v_pk_add_f32 v[54:55], v[54:55], v[58:59]
	v_pk_add_f32 v[52:53], v[52:53], v[56:57]
	v_pk_add_f32 v[56:57], v[50:51], v[94:95]
	v_pk_add_f32 v[50:51], v[48:49], v[62:63]
	v_mul_f32_e32 v48, v53, v53
	v_mul_f32_e32 v49, v55, v55
	v_fmac_f32_e32 v48, v52, v52
	v_fmac_f32_e32 v49, v54, v54
	v_add_f32_e32 v48, v48, v49
	v_mul_f32_e32 v49, v51, v51
	v_mul_f32_e32 v58, v57, v57
	v_fmac_f32_e32 v49, v50, v50
	v_fmac_f32_e32 v58, v56, v56
	v_add_f32_e32 v49, v49, v58
	v_add_f32_e32 v48, v48, v49
	v_add_f32_e32 v58, v96, v48
	v_cvt_pk_bf16_f32 v48, v52, v53
	s_mov_b64 s[2:3], 0x100
	v_cvt_pk_bf16_f32 v49, v54, v55
	v_cvt_pk_bf16_f32 v50, v50, v51
	v_cvt_pk_bf16_f32 v51, v56, v57
	v_lshl_add_u64 v[52:53], v[60:61], 0, s[2:3]
	global_store_dwordx4 v[52:53], v[48:51], off sc1
	s_nop 1
	ds_swizzle_b32 v48, v58 offset:swizzle(SWAP,16)
	s_waitcnt lgkmcnt(0)
	v_add_f32_e32 v48, v58, v48
	v_mov_b32_e32 v49, v48
	s_nop 1
	v_permlane32_swap_b32_e32 v48, v49
	s_and_saveexec_b64 s[4:5], s[10:11]
	v_add_f32_e32 v48, v48, v49
	ds_write_b32 v186, v48 offset:2048
	s_or_b64 exec, exec, s[4:5]
	s_waitcnt vmcnt(5)
	v_lshlrev_b32_e32 v48, 16, v84
	v_and_b32_e32 v49, 0xffff0000, v84
	v_lshlrev_b32_e32 v50, 16, v85
	v_and_b32_e32 v51, 0xffff0000, v85
	v_lshlrev_b32_e32 v52, 16, v86
	v_and_b32_e32 v53, 0xffff0000, v86
	v_lshlrev_b32_e32 v54, 16, v87
	v_and_b32_e32 v55, 0xffff0000, v87
	v_pk_add_f32 v[46:47], v[46:47], v[50:51]
	v_pk_add_f32 v[44:45], v[44:45], v[48:49]
	v_pk_add_f32 v[48:49], v[42:43], v[54:55]
	v_pk_add_f32 v[42:43], v[40:41], v[52:53]
	v_mul_f32_e32 v40, v45, v45
	v_mul_f32_e32 v41, v47, v47
	v_fmac_f32_e32 v40, v44, v44
	v_fmac_f32_e32 v41, v46, v46
	v_add_f32_e32 v40, v40, v41
	v_mul_f32_e32 v41, v43, v43
	v_mul_f32_e32 v50, v49, v49
	v_fmac_f32_e32 v41, v42, v42
	v_fmac_f32_e32 v50, v48, v48
	v_readlane_b32 s2, v252, 8
	v_add_f32_e32 v41, v41, v50
	v_readlane_b32 s3, v252, 9
	v_add_f32_e32 v50, v40, v41
	v_cvt_pk_bf16_f32 v40, v44, v45
	v_cvt_pk_bf16_f32 v41, v46, v47
	v_cvt_pk_bf16_f32 v42, v42, v43
	v_cvt_pk_bf16_f32 v43, v48, v49
	s_nop 0
	v_lshl_add_u64 v[44:45], s[2:3], 0, v[92:93]
	v_lshl_add_u64 v[44:45], v[164:165], 1, v[44:45]
	global_store_dwordx4 v[44:45], v[40:43], off sc1
	s_nop 1
	s_waitcnt vmcnt(4)
	v_lshlrev_b32_e32 v40, 16, v80
	v_and_b32_e32 v41, 0xffff0000, v80
	v_lshlrev_b32_e32 v42, 16, v81
	v_and_b32_e32 v43, 0xffff0000, v81
	v_lshlrev_b32_e32 v46, 16, v82
	v_and_b32_e32 v47, 0xffff0000, v82
	v_lshlrev_b32_e32 v48, 16, v83
	v_and_b32_e32 v49, 0xffff0000, v83
	v_pk_add_f32 v[38:39], v[38:39], v[42:43]
	v_pk_add_f32 v[36:37], v[36:37], v[40:41]
	v_pk_add_f32 v[40:41], v[34:35], v[48:49]
	v_pk_add_f32 v[34:35], v[32:33], v[46:47]
	v_mul_f32_e32 v32, v37, v37
	v_mul_f32_e32 v33, v39, v39
	v_fmac_f32_e32 v32, v36, v36
	v_fmac_f32_e32 v33, v38, v38
	v_add_f32_e32 v32, v32, v33
	v_mul_f32_e32 v33, v35, v35
	v_mul_f32_e32 v42, v41, v41
	v_fmac_f32_e32 v33, v34, v34
	v_fmac_f32_e32 v42, v40, v40
	v_add_f32_e32 v33, v33, v42
	v_add_f32_e32 v32, v32, v33
	v_add_f32_e32 v42, v50, v32
	v_cvt_pk_bf16_f32 v32, v36, v37
	v_cvt_pk_bf16_f32 v33, v38, v39
	ds_swizzle_b32 v38, v42 offset:swizzle(SWAP,16)
	s_mov_b64 s[2:3], 0x100
	v_cvt_pk_bf16_f32 v34, v34, v35
	v_cvt_pk_bf16_f32 v35, v40, v41
	v_lshl_add_u64 v[36:37], v[44:45], 0, s[2:3]
	global_store_dwordx4 v[36:37], v[32:35], off sc1
	s_nop 1
	s_waitcnt lgkmcnt(0)
; #define LAS __attribute__((address_space(3)))
; __device__ __forceinline__ unsigned cvt_pk_bf16(float lo, float hi) { unsigned r; asm volatile("v_cvt_pk_bf16_f32 %0, %1, %2" : "=v"(r) : "v"(lo), "v"(hi)); return r; }
; __device__ __forceinline__ float bf_lo(unsigned w) { return __uint_as_float(w << 16); }
; __device__ __forceinline__ float bf_hi(unsigned w) { return __uint_as_float(w & 0xffff0000u); }
; template <int M> __device__ __forceinline__ float swz_xor(float v) { return __int_as_float(__builtin_amdgcn_ds_swizzle(__float_as_int(v), (M << 10) | 0x1f)); }
; __device__ __forceinline__ float half_sum(float v) { auto rr = __builtin_amdgcn_permlane32_swap(__float_as_uint(v), __float_as_uint(v), false, false); return __uint_as_float(rr[0]) + __uint_as_float(rr[1]); }
; __device__ __forceinline__ void st16_wt(void* p, u32x4 w) { asm volatile("global_store_dwordx4 %0, %1, off sc1\n\ts_nop 1" :: "v"(p), "v"(w) : "memory"); }
;     __device__ __forceinline__ bool operator()(f32x4 (&acc)[2][2][4][2], const pg8::Unit& u, int wr, int wc, int fr, int fq) const {
;     ...
;             for (int m = 0; m < 4; ++m) { const int row = row0 + ai * 128 + m * 16; float ss = 0.f;
; #pragma unroll
;                 for (int bj = 0; bj < 2; ++bj) { const size_t off = (size_t)row * DM + colb + bj * 128; const u32x4 xw = xin[m][bj];
;                     f32x4 a = {bf_lo(xw.x), bf_hi(xw.x), bf_lo(xw.y), bf_hi(xw.y)}, b = {bf_lo(xw.z), bf_hi(xw.z), bf_lo(xw.w), bf_hi(xw.w)};
;                     a += acc[ai][bj][m][0]; b += acc[ai][bj][m][1];
;                     ss += ((a[0] * a[0] + a[1] * a[1]) + (a[2] * a[2] + a[3] * a[3])) + ((b[0] * b[0] + b[1] * b[1]) + (b[2] * b[2] + b[3] * b[3]));
;                     { u32x4 w; w.x = cvt_pk_bf16(a[0], a[1]); w.y = cvt_pk_bf16(a[2], a[3]); w.z = cvt_pk_bf16(b[0], b[1]); w.w = cvt_pk_bf16(b[2], b[3]); st16_wt(xb + off, w); } }
;                 ss += swz_xor<16>(ss); ss = half_sum(ss);
;                 if (fq == 0) xch[(ai * 128 + wr * 64 + m * 16 + fr) * 4 + wc] = ss; } }
;         asm volatile("s_waitcnt lgkmcnt(0)" ::: "memory"); __builtin_amdgcn_s_barrier(); asm volatile("" ::: "memory");
;         const int tid_ = (wr * 4 + wc) * 64 + fq * 16 + fr;
;         if (tid_ < 256) st16f_wt(part + (size_t)(u.pm * 256 + tid_) * 16 + u.pn * 4, *(const LAS f32x4*)(xch + tid_ * 4));
;         wave_arrive(done + 64 * u.pm, (fr | fq) == 0);
	v_add_f32_e32 v32, v42, v38
	v_mov_b32_e32 v33, v32
	s_nop 1
	v_permlane32_swap_b32_e32 v32, v33
	s_and_saveexec_b64 s[4:5], s[10:11]
	v_add_f32_e32 v32, v32, v33
	ds_write_b32 v186, v32 offset:2304
	s_or_b64 exec, exec, s[4:5]
	s_waitcnt vmcnt(3)
	v_lshlrev_b32_e32 v32, 16, v76
	v_and_b32_e32 v33, 0xffff0000, v76
	v_lshlrev_b32_e32 v34, 16, v77
	v_and_b32_e32 v35, 0xffff0000, v77
	v_lshlrev_b32_e32 v36, 16, v78
	v_and_b32_e32 v37, 0xffff0000, v78
	v_lshlrev_b32_e32 v38, 16, v79
	v_and_b32_e32 v39, 0xffff0000, v79
	v_pk_add_f32 v[30:31], v[30:31], v[34:35]
	v_pk_add_f32 v[28:29], v[28:29], v[32:33]
	v_pk_add_f32 v[32:33], v[26:27], v[38:39]
	v_pk_add_f32 v[26:27], v[24:25], v[36:37]
	v_mul_f32_e32 v24, v29, v29
	v_mul_f32_e32 v25, v31, v31
	v_fmac_f32_e32 v24, v28, v28
	v_fmac_f32_e32 v25, v30, v30
	v_add_f32_e32 v24, v24, v25
	v_mul_f32_e32 v25, v27, v27
	v_mul_f32_e32 v34, v33, v33
	v_fmac_f32_e32 v25, v26, v26
	v_fmac_f32_e32 v34, v32, v32
	v_readlane_b32 s2, v252, 8
	v_add_f32_e32 v25, v25, v34
	v_readlane_b32 s3, v252, 9
	v_add_f32_e32 v34, v24, v25
	v_cvt_pk_bf16_f32 v24, v28, v29
	v_cvt_pk_bf16_f32 v25, v30, v31
	v_cvt_pk_bf16_f32 v26, v26, v27
	v_cvt_pk_bf16_f32 v27, v32, v33
	s_nop 0
	v_lshl_add_u64 v[28:29], s[2:3], 0, v[90:91]
	v_lshl_add_u64 v[28:29], v[164:165], 1, v[28:29]
	global_store_dwordx4 v[28:29], v[24:27], off sc1
	s_nop 1
	s_waitcnt vmcnt(2)
	v_lshlrev_b32_e32 v24, 16, v72
	v_and_b32_e32 v25, 0xffff0000, v72
	v_lshlrev_b32_e32 v26, 16, v73
	v_and_b32_e32 v27, 0xffff0000, v73
	v_lshlrev_b32_e32 v30, 16, v74
	v_and_b32_e32 v31, 0xffff0000, v74
	v_lshlrev_b32_e32 v32, 16, v75
	v_and_b32_e32 v33, 0xffff0000, v75
	v_pk_add_f32 v[22:23], v[22:23], v[26:27]
	v_pk_add_f32 v[20:21], v[20:21], v[24:25]
	v_pk_add_f32 v[24:25], v[18:19], v[32:33]
	v_pk_add_f32 v[18:19], v[16:17], v[30:31]
	v_mul_f32_e32 v16, v21, v21
	v_mul_f32_e32 v17, v23, v23
	v_fmac_f32_e32 v16, v20, v20
	v_fmac_f32_e32 v17, v22, v22
	v_add_f32_e32 v16, v16, v17
	v_mul_f32_e32 v17, v19, v19
	v_mul_f32_e32 v26, v25, v25
	v_fmac_f32_e32 v17, v18, v18
	v_fmac_f32_e32 v26, v24, v24
	v_add_f32_e32 v17, v17, v26
	v_add_f32_e32 v16, v16, v17
	v_add_f32_e32 v26, v34, v16
	v_cvt_pk_bf16_f32 v16, v20, v21
	v_cvt_pk_bf16_f32 v17, v22, v23
	ds_swizzle_b32 v22, v26 offset:swizzle(SWAP,16)
	s_mov_b64 s[2:3], 0x100
	v_cvt_pk_bf16_f32 v18, v18, v19
	v_cvt_pk_bf16_f32 v19, v24, v25
	v_lshl_add_u64 v[20:21], v[28:29], 0, s[2:3]
	global_store_dwordx4 v[20:21], v[16:19], off sc1
	s_nop 1
	s_waitcnt lgkmcnt(0)
	v_add_f32_e32 v16, v26, v22
	v_mov_b32_e32 v17, v16
	s_nop 1
	v_permlane32_swap_b32_e32 v16, v17
	s_and_saveexec_b64 s[4:5], s[10:11]
	v_add_f32_e32 v16, v16, v17
	ds_write_b32 v186, v16 offset:2560
	s_or_b64 exec, exec, s[4:5]
	s_waitcnt vmcnt(1)
	v_lshlrev_b32_e32 v16, 16, v68
	v_and_b32_e32 v17, 0xffff0000, v68
	v_lshlrev_b32_e32 v18, 16, v69
	v_and_b32_e32 v19, 0xffff0000, v69
	v_lshlrev_b32_e32 v20, 16, v70
	v_and_b32_e32 v21, 0xffff0000, v70
	v_lshlrev_b32_e32 v22, 16, v71
	v_and_b32_e32 v23, 0xffff0000, v71
	v_pk_add_f32 v[14:15], v[14:15], v[18:19]
	v_pk_add_f32 v[12:13], v[12:13], v[16:17]
	v_pk_add_f32 v[16:17], v[10:11], v[22:23]
	v_pk_add_f32 v[10:11], v[8:9], v[20:21]
	v_mul_f32_e32 v8, v13, v13
	v_mul_f32_e32 v9, v15, v15
	v_fmac_f32_e32 v8, v12, v12
	v_fmac_f32_e32 v9, v14, v14
	v_add_f32_e32 v8, v8, v9
	v_mul_f32_e32 v9, v11, v11
	v_mul_f32_e32 v18, v17, v17
	v_fmac_f32_e32 v9, v10, v10
	v_fmac_f32_e32 v18, v16, v16
	v_readlane_b32 s2, v252, 8
	v_add_f32_e32 v9, v9, v18
	v_readlane_b32 s3, v252, 9
	v_add_f32_e32 v18, v8, v9
	v_cvt_pk_bf16_f32 v8, v12, v13
	v_cvt_pk_bf16_f32 v9, v14, v15
	v_cvt_pk_bf16_f32 v10, v10, v11
	v_cvt_pk_bf16_f32 v11, v16, v17
	s_nop 0
	v_lshl_add_u64 v[12:13], s[2:3], 0, v[88:89]
	v_lshl_add_u64 v[12:13], v[164:165], 1, v[12:13]
	global_store_dwordx4 v[12:13], v[8:11], off sc1
	s_nop 1
	s_waitcnt vmcnt(0)
	v_lshlrev_b32_e32 v8, 16, v64
	v_and_b32_e32 v9, 0xffff0000, v64
	v_lshlrev_b32_e32 v10, 16, v65
	v_and_b32_e32 v11, 0xffff0000, v65
	v_lshlrev_b32_e32 v14, 16, v66
	v_and_b32_e32 v15, 0xffff0000, v66
	v_lshlrev_b32_e32 v16, 16, v67
	v_and_b32_e32 v17, 0xffff0000, v67
	v_pk_add_f32 v[6:7], v[6:7], v[10:11]
	v_pk_add_f32 v[4:5], v[4:5], v[8:9]
	v_pk_add_f32 v[8:9], v[2:3], v[16:17]
	v_pk_add_f32 v[2:3], v[0:1], v[14:15]
	v_mul_f32_e32 v0, v5, v5
	v_mul_f32_e32 v1, v7, v7
	v_fmac_f32_e32 v0, v4, v4
	v_fmac_f32_e32 v1, v6, v6
	v_add_f32_e32 v0, v0, v1
	v_mul_f32_e32 v1, v3, v3
	v_mul_f32_e32 v10, v9, v9
	v_fmac_f32_e32 v1, v2, v2
	v_fmac_f32_e32 v10, v8, v8
	v_add_f32_e32 v1, v1, v10
	v_add_f32_e32 v0, v0, v1
	v_add_f32_e32 v10, v18, v0
	v_cvt_pk_bf16_f32 v0, v4, v5
	v_cvt_pk_bf16_f32 v1, v6, v7
	ds_swizzle_b32 v6, v10 offset:swizzle(SWAP,16)
	s_mov_b64 s[2:3], 0x100
	v_cvt_pk_bf16_f32 v2, v2, v3
	v_cvt_pk_bf16_f32 v3, v8, v9
	v_lshl_add_u64 v[4:5], v[12:13], 0, s[2:3]
	global_store_dwordx4 v[4:5], v[0:3], off sc1
	s_nop 1
	s_waitcnt lgkmcnt(0)
	v_add_f32_e32 v0, v10, v6
	v_mov_b32_e32 v1, v0
	s_nop 1
	v_permlane32_swap_b32_e32 v0, v1
	s_and_saveexec_b64 s[4:5], s[10:11]
	v_add_f32_e32 v0, v0, v1
	ds_write_b32 v186, v0 offset:2816
	s_or_b64 exec, exec, s[4:5]
	s_waitcnt lgkmcnt(0)
	s_barrier
	s_and_saveexec_b64 s[4:5], s[12:13]
	s_cbranch_execz .LBB0_1049
	v_add_u32_e32 v0, s7, v182
	v_ashrrev_i32_e32 v1, 31, v0
	v_readlane_b32 s2, v251, 32
	v_lshlrev_b64 v[0:1], 6, v[0:1]
	v_readlane_b32 s3, v251, 33
	s_nop 1
	v_lshl_add_u64 v[0:1], s[2:3], 0, v[0:1]
	s_lshl_b32 s2, s45, 2
	s_ashr_i32 s3, s2, 31
	v_lshl_add_u64 v[4:5], s[2:3], 2, v[0:1]
	ds_read_b128 v[0:3], v185
	s_waitcnt lgkmcnt(0)
	global_store_dwordx4 v[4:5], v[0:3], off sc1
	s_nop 1

; template <int M> __device__ __forceinline__ float swz_xor(float v) { return __int_as_float(__builtin_amdgcn_ds_swizzle(__float_as_int(v), (M << 10) | 0x1f)); }
; __device__ __forceinline__ float half_sum(float v) { auto rr = __builtin_amdgcn_permlane32_swap(__float_as_uint(v), __float_as_uint(v), false, false); return __uint_as_float(rr[0]) + __uint_as_float(rr[1]); }
; __device__ __forceinline__ float half_max(float v) { auto rr = __builtin_amdgcn_permlane32_swap(__float_as_uint(v), __float_as_uint(v), false, false); return fmaxf(__uint_as_float(rr[0]), __uint_as_float(rr[1])); }
; __device__ __forceinline__ void row_rscale8(const float* part, const int (&rows)[2][4], int fq, float (&rs)[2][4]) {
;     f32x4 v[2][4];
; #pragma unroll
;     for (int ai = 0; ai < 2; ++ai)
; #pragma unroll
;         for (int m = 0; m < 4; ++m) v[ai][m] = *(const f32x4*)(part + (size_t)rows[ai][m] * 16 + fq * 4);
; #pragma unroll
;     for (int ai = 0; ai < 2; ++ai)
; #pragma unroll
;         for (int m = 0; m < 4; ++m) { float s = (v[ai][m][0] + v[ai][m][1]) + (v[ai][m][2] + v[ai][m][3]); s += swz_xor<16>(s); s = half_sum(s); rs[ai][m] = __builtin_amdgcn_rcpf(sqrtf(s * (1.0f / DM) + EPS)); }
;     __device__ __forceinline__ bool operator()(f32x4 (&acc)[2][2][4][2], const pg8::Unit& u, int wr, int wc, int fr, int fq) const {
;     ...
;             row_rscale8(part, rows_, fq, rs_); }
; #pragma unroll
;         for (int ai = 0; ai < 2; ++ai)
; #pragma unroll
;             for (int m = 0; m < 4; ++m) { const float r = rs_[ai][m]; float mx = -3.0e38f;
; #pragma unroll
;                 for (int bj = 0; bj < 2; ++bj)
; #pragma unroll
;                     for (int n = 0; n < 2; ++n) { acc[ai][bj][m][n] = acc[ai][bj][m][n] * r; const f32x4 v = acc[ai][bj][m][n]; mx = fmaxf(fmaxf(mx, fmaxf(v[0], v[1])), fmaxf(v[2], v[3])); }
;                 mx = fmaxf(mx, swz_xor<16>(mx)); mx = half_max(mx);
.LBB0_1106:
	v_lshl_add_u32 v150, s44, 8, v164
	v_or_b32_e32 v148, 16, v150
	v_ashrrev_i32_e32 v151, 31, v150
	v_ashrrev_i32_e32 v149, 31, v148
	v_or_b32_e32 v146, 32, v150
	v_lshlrev_b64 v[136:137], 6, v[150:151]
	v_lshlrev_b64 v[152:153], 6, v[148:149]
	v_or_b32_e32 v144, 48, v150
	v_lshl_add_u64 v[136:137], v[134:135], 0, v[136:137]
	v_lshl_add_u64 v[156:157], v[134:135], 0, v[152:153]
	v_ashrrev_i32_e32 v147, 31, v146
	global_load_dwordx4 v[152:155], v[136:137], off
	s_nop 0
	global_load_dwordx4 v[156:159], v[156:157], off
	v_lshlrev_b64 v[136:137], 6, v[146:147]
	v_ashrrev_i32_e32 v145, 31, v144
	v_lshl_add_u64 v[136:137], v[134:135], 0, v[136:137]
	v_lshlrev_b64 v[162:163], 6, v[144:145]
	v_lshl_add_u64 v[162:163], v[134:135], 0, v[162:163]
	global_load_dwordx4 v[170:173], v[136:137], off
	global_load_dwordx4 v[174:177], v[162:163], off
	v_add_u32_e32 v142, 0x80, v150
	v_add_u32_e32 v140, 0x90, v150
	v_ashrrev_i32_e32 v143, 31, v142
	v_add_u32_e32 v138, 0xa0, v150
	v_lshlrev_b64 v[136:137], 6, v[142:143]
	v_ashrrev_i32_e32 v141, 31, v140
	v_lshl_add_u64 v[136:137], v[134:135], 0, v[136:137]
	v_lshlrev_b64 v[162:163], 6, v[140:141]
	v_ashrrev_i32_e32 v139, 31, v138
	v_lshl_add_u64 v[162:163], v[134:135], 0, v[162:163]
	global_load_dwordx4 v[178:181], v[136:137], off
	global_load_dwordx4 v[182:185], v[162:163], off
	v_lshlrev_b64 v[136:137], 6, v[138:139]
	v_lshl_add_u64 v[136:137], v[134:135], 0, v[136:137]
	global_load_dwordx4 v[186:189], v[136:137], off
	v_add_u32_e32 v136, 0xb0, v150
	v_ashrrev_i32_e32 v137, 31, v136
	v_lshlrev_b64 v[162:163], 6, v[136:137]
	v_lshl_add_u64 v[162:163], v[134:135], 0, v[162:163]
	global_load_dwordx4 v[196:199], v[162:163], off
	s_mov_b32 s2, 0xf800000
	s_waitcnt vmcnt(0)
	v_mov_b32_e32 v162, v153
	v_mov_b32_e32 v163, v154
	v_mov_b32_e32 v153, v155
	v_pk_add_f32 v[152:153], v[162:163], v[152:153]
	v_add_f32_e32 v154, v156, v157
	v_add_f32_e32 v155, v158, v159
	v_add_f32_e32 v152, v152, v153
	v_add_f32_e32 v158, v174, v175
	v_add_f32_e32 v159, v176, v177
	v_add_f32_e32 v153, v154, v155
	v_add_f32_e32 v155, v158, v159
	ds_swizzle_b32 v158, v152 offset:swizzle(SWAP,16)
	ds_swizzle_b32 v159, v153 offset:swizzle(SWAP,16)
	v_add_f32_e32 v157, v172, v173
	v_add_f32_e32 v156, v170, v171
	v_add_f32_e32 v154, v156, v157
	s_waitcnt lgkmcnt(1)
	v_add_f32_e32 v152, v152, v158
	s_waitcnt lgkmcnt(0)
	v_add_f32_e32 v173, v153, v159
	v_mov_b32_e32 v153, v152
	s_nop 1
	v_permlane32_swap_b32_e32 v152, v153
	v_add_f32_e32 v152, v152, v153
	v_fmamk_f32 v152, v152, 0x3a800000, v212
	v_add_f32_e32 v162, v178, v179
	v_add_f32_e32 v163, v180, v181
	v_mul_f32_e32 v153, 0x4f800000, v152
	v_cmp_gt_f32_e32 vcc, s2, v152
	v_add_f32_e32 v169, v182, v183
	v_add_f32_e32 v170, v184, v185
	v_add_f32_e32 v156, v162, v163
	ds_swizzle_b32 v162, v154 offset:swizzle(SWAP,16)
	v_cndmask_b32_e32 v152, v152, v153, vcc
	v_add_f32_e32 v171, v186, v187
	v_add_f32_e32 v172, v188, v189
	v_add_f32_e32 v157, v169, v170
	ds_swizzle_b32 v163, v155 offset:swizzle(SWAP,16)
	ds_swizzle_b32 v170, v156 offset:swizzle(SWAP,16)
	v_sqrt_f32_e32 v153, v152
	v_add_f32_e32 v175, v171, v172
	ds_swizzle_b32 v172, v157 offset:swizzle(SWAP,16)
	s_waitcnt lgkmcnt(3)
	v_add_f32_e32 v171, v154, v162
	v_add_u32_e32 v154, -1, v153
	s_waitcnt lgkmcnt(2)
	v_add_f32_e32 v169, v155, v163
	s_waitcnt lgkmcnt(1)
	v_add_f32_e32 v162, v156, v170
	v_add_u32_e32 v155, 1, v153
	v_fma_f32 v156, -v154, v153, v152
	s_waitcnt lgkmcnt(0)
	v_add_f32_e32 v158, v157, v172
	v_fma_f32 v157, -v155, v153, v152
	v_cmp_ge_f32_e64 s[4:5], 0, v156
	v_mov_b32_e32 v176, v175
	s_mov_b32 s2, 0xff61b1e6
	v_cndmask_b32_e64 v153, v153, v154, s[4:5]
	v_cmp_lt_f32_e64 s[4:5], 0, v157
	v_mov_b32_e32 v174, v173
	s_waitcnt lgkmcnt(0)
	s_nop 1
	v_permlane16_swap_b32_e32 v176, v175
	v_add_f32_e32 v156, v175, v176
	v_cndmask_b32_e64 v153, v153, v155, s[4:5]
	v_mul_f32_e32 v154, 0x37800000, v153
	v_cndmask_b32_e32 v153, v153, v154, vcc
	v_cmp_class_f32_e32 vcc, v152, v248
	v_mov_b32_e32 v172, v171
	v_mov_b32_e32 v170, v169
	v_cndmask_b32_e32 v152, v153, v152, vcc
	v_rcp_f32_e32 v152, v152
	v_mov_b32_e32 v163, v162
	v_mov_b32_e32 v159, v158
	v_mov_b32_e32 v157, v156
	v_pk_mul_f32 v[126:127], v[126:127], v[152:153] op_sel_hi:[1,0]
	v_pk_mul_f32 v[124:125], v[124:125], v[152:153] op_sel_hi:[1,0]
	v_max_f32_e32 v154, v126, v127
	v_max_f32_e32 v153, v124, v125
	v_max3_f32 v153, v153, s2, v154
	v_pk_mul_f32 v[154:155], v[122:123], v[152:153] op_sel_hi:[1,0]
	v_pk_mul_f32 v[120:121], v[120:121], v[152:153] op_sel_hi:[1,0]
	v_max_f32_e32 v123, v154, v155
	v_max_f32_e32 v122, v120, v121
	v_pk_mul_f32 v[118:119], v[118:119], v[152:153] op_sel_hi:[1,0]
	v_max3_f32 v122, v153, v122, v123
	v_pk_mul_f32 v[116:117], v[116:117], v[152:153] op_sel_hi:[1,0]
	v_max_f32_e32 v153, v118, v119
	v_max_f32_e32 v123, v116, v117
	v_pk_mul_f32 v[176:177], v[114:115], v[152:153] op_sel_hi:[1,0]
	v_pk_mul_f32 v[178:179], v[112:113], v[152:153] op_sel_hi:[1,0]
	v_max3_f32 v122, v122, v123, v153
	v_max_f32_e32 v112, v178, v179
	v_max_f32_e32 v113, v176, v177
	v_max3_f32 v112, v122, v112, v113
	ds_swizzle_b32 v113, v112 offset:swizzle(SWAP,16)
	v_add_f32_e32 v114, v196, v197
	v_add_f32_e32 v115, v198, v199
	v_add_f32_e32 v153, v114, v115
	ds_swizzle_b32 v175, v153 offset:swizzle(SWAP,16)
	s_waitcnt lgkmcnt(1)
; #define LAS __attribute__((address_space(3)))
; template <int M> __device__ __forceinline__ float swz_xor(float v) { return __int_as_float(__builtin_amdgcn_ds_swizzle(__float_as_int(v), (M << 10) | 0x1f)); }
; __device__ __forceinline__ float half_sum(float v) { auto rr = __builtin_amdgcn_permlane32_swap(__float_as_uint(v), __float_as_uint(v), false, false); return __uint_as_float(rr[0]) + __uint_as_float(rr[1]); }
; __device__ __forceinline__ float half_max(float v) { auto rr = __builtin_amdgcn_permlane32_swap(__float_as_uint(v), __float_as_uint(v), false, false); return fmaxf(__uint_as_float(rr[0]), __uint_as_float(rr[1])); }
;     __device__ __forceinline__ bool operator()(f32x4 (&acc)[2][2][4][2], const pg8::Unit& u, int wr, int wc, int fr, int fq) const {
;     ...
;             for (int m = 0; m < 4; ++m) { const float r = rs_[ai][m]; float mx = -3.0e38f;
; #pragma unroll
;                 for (int bj = 0; bj < 2; ++bj)
; #pragma unroll
;                     for (int n = 0; n < 2; ++n) { acc[ai][bj][m][n] = acc[ai][bj][m][n] * r; const f32x4 v = acc[ai][bj][m][n]; mx = fmaxf(fmaxf(mx, fmaxf(v[0], v[1])), fmaxf(v[2], v[3])); }
;                 mx = fmaxf(mx, swz_xor<16>(mx)); mx = half_max(mx);
;                 float sm = 0.f;
; #pragma unroll
;                 for (int bj = 0; bj < 2; ++bj)
; #pragma unroll
;                     for (int n = 0; n < 2; ++n) { f32x4 v = acc[ai][bj][m][n];
; #pragma unroll
;                         for (int j = 0; j < 4; ++j) { v[j] = __builtin_amdgcn_exp2f(v[j] - mx); sm += v[j]; }
;                         acc[ai][bj][m][n] = v; }
;                 sm += swz_xor<16>(sm); sm = half_sum(sm);
;                 if (fq == 0) { LAS f32x2* x = (LAS f32x2*)xch + (ai * 128 + wr * 64 + m * 16 + fr) * 4 + wc; *x = (f32x2){mx, sm}; } }
	v_max_f32_e32 v113, v113, v113
	v_max_f32_e32 v112, v112, v113
	v_mov_b32_e32 v113, v112
	s_nop 1
	v_permlane32_swap_b32_e32 v112, v113
	v_max_f32_e32 v113, v113, v113
	v_max_f32_e32 v112, v112, v112
	v_max_f32_e32 v152, v112, v113
	v_sub_f32_e32 v112, v124, v152
	v_exp_f32_e32 v114, v112
	v_sub_f32_e32 v112, v125, v152
	v_exp_f32_e32 v115, v112
	v_sub_f32_e32 v112, v126, v152
	v_exp_f32_e32 v122, v112
	v_sub_f32_e32 v112, v127, v152
	v_exp_f32_e32 v123, v112
	v_sub_f32_e32 v113, v120, v152
	v_add_f32_e32 v112, 0, v114
	v_exp_f32_e32 v120, v113
	v_sub_f32_e32 v113, v121, v152
	v_add_f32_e32 v112, v115, v112
	v_exp_f32_e32 v121, v113
	v_sub_f32_e32 v113, v154, v152
	v_add_f32_e32 v112, v122, v112
	v_exp_f32_e32 v126, v113
	v_sub_f32_e32 v113, v155, v152
	v_add_f32_e32 v112, v123, v112
	v_exp_f32_e32 v127, v113
	v_add_f32_e32 v112, v120, v112
	v_add_f32_e32 v112, v121, v112
	v_add_f32_e32 v112, v126, v112
	v_add_f32_e32 v124, v127, v112
	v_sub_f32_e32 v112, v116, v152
	v_exp_f32_e32 v112, v112
	v_sub_f32_e32 v113, v117, v152
	v_exp_f32_e32 v113, v113
	v_sub_f32_e32 v116, v118, v152
	v_exp_f32_e32 v118, v116
	v_sub_f32_e32 v116, v119, v152
	v_exp_f32_e32 v119, v116
	v_add_f32_e32 v116, v112, v124
	v_add_f32_e32 v116, v113, v116
	v_add_f32_e32 v116, v118, v116
	v_add_f32_e32 v154, v119, v116
	v_sub_f32_e32 v116, v178, v152
	v_exp_f32_e32 v116, v116
	v_sub_f32_e32 v117, v179, v152
	v_exp_f32_e32 v117, v117
	v_sub_f32_e32 v124, v176, v152
	v_exp_f32_e32 v124, v124
	v_sub_f32_e32 v125, v177, v152
	v_exp_f32_e32 v125, v125
	v_add_f32_e32 v154, v116, v154
	v_add_f32_e32 v154, v117, v154
	v_add_f32_e32 v154, v124, v154
	v_add_f32_e32 v176, v125, v154
	ds_swizzle_b32 v177, v176 offset:swizzle(SWAP,16)
	s_waitcnt lgkmcnt(1)
	v_add_f32_e32 v154, v153, v175
	v_mov_b32_e32 v155, v154
	v_permlane32_swap_b32_e32 v173, v174
	s_waitcnt lgkmcnt(0)
	v_add_f32_e32 v153, v176, v177
	v_mov_b32_e32 v175, v153
	v_permlane32_swap_b32_e32 v171, v172
	v_permlane32_swap_b32_e32 v169, v170
	v_permlane32_swap_b32_e32 v162, v163
	v_permlane32_swap_b32_e32 v158, v159
	v_permlane32_swap_b32_e32 v156, v157
	v_permlane32_swap_b32_e32 v154, v155
	v_permlane32_swap_b32_e32 v153, v175
	s_and_saveexec_b64 s[4:5], s[10:11]
	s_cbranch_execz .LBB0_1108
	v_readlane_b32 s2, v253, 16
	v_add_f32_e32 v153, v153, v175
	s_nop 0
	v_add_u32_e32 v175, s2, v166
	ds_write_b64 v175, v[152:153]
.LBB0_1108:
	s_or_b64 exec, exec, s[4:5]
	v_add_f32_e32 v152, v173, v174
	v_fmamk_f32 v152, v152, 0x3a800000, v212
	s_mov_b32 s2, 0xf800000
	v_mul_f32_e32 v153, 0x4f800000, v152
	v_cmp_gt_f32_e32 vcc, s2, v152
	s_mov_b32 s2, 0xff61b1e6
	s_nop 0
	v_cndmask_b32_e32 v152, v152, v153, vcc
	v_sqrt_f32_e32 v153, v152
	s_nop 0
	v_add_u32_e32 v173, -1, v153
	v_fma_f32 v175, -v173, v153, v152
	v_add_u32_e32 v174, 1, v153
	v_cmp_ge_f32_e64 s[4:5], 0, v175
	s_nop 1
	v_cndmask_b32_e64 v173, v153, v173, s[4:5]
	v_fma_f32 v153, -v174, v153, v152
	v_cmp_lt_f32_e64 s[4:5], 0, v153
	s_nop 1
	v_cndmask_b32_e64 v153, v173, v174, s[4:5]
	v_mul_f32_e32 v173, 0x37800000, v153
	v_cndmask_b32_e32 v153, v153, v173, vcc
	v_cmp_class_f32_e32 vcc, v152, v248
	s_nop 1
	v_cndmask_b32_e32 v152, v153, v152, vcc
	v_rcp_f32_e32 v152, v152
	s_nop 0
	v_pk_mul_f32 v[110:111], v[110:111], v[152:153] op_sel_hi:[1,0]
	v_pk_mul_f32 v[108:109], v[108:109], v[152:153] op_sel_hi:[1,0]
	v_max_f32_e32 v173, v110, v111
	v_max_f32_e32 v153, v108, v109
	v_max3_f32 v153, v153, s2, v173
	v_pk_mul_f32 v[174:175], v[106:107], v[152:153] op_sel_hi:[1,0]
	v_pk_mul_f32 v[104:105], v[104:105], v[152:153] op_sel_hi:[1,0]
	v_max_f32_e32 v107, v174, v175
	v_max_f32_e32 v106, v104, v105
	v_pk_mul_f32 v[102:103], v[102:103], v[152:153] op_sel_hi:[1,0]
	v_max3_f32 v106, v153, v106, v107
	v_pk_mul_f32 v[100:101], v[100:101], v[152:153] op_sel_hi:[1,0]
	v_max_f32_e32 v153, v102, v103
	v_max_f32_e32 v107, v100, v101
	v_pk_mul_f32 v[176:177], v[98:99], v[152:153] op_sel_hi:[1,0]
	v_pk_mul_f32 v[178:179], v[96:97], v[152:153] op_sel_hi:[1,0]
	v_max3_f32 v106, v106, v107, v153
	v_max_f32_e32 v96, v178, v179
	v_max_f32_e32 v97, v176, v177
	v_max3_f32 v96, v106, v96, v97
	ds_swizzle_b32 v97, v96 offset:swizzle(SWAP,16)
	s_waitcnt lgkmcnt(0)
	v_max_f32_e32 v97, v97, v97
	v_max_f32_e32 v96, v96, v97
	v_mov_b32_e32 v97, v96
	s_nop 1
	v_permlane32_swap_b32_e32 v96, v97
	v_max_f32_e32 v97, v97, v97
	v_max_f32_e32 v96, v96, v96
	v_max_f32_e32 v152, v96, v97
	v_sub_f32_e32 v96, v108, v152
	v_exp_f32_e32 v98, v96
	v_sub_f32_e32 v96, v109, v152
	v_exp_f32_e32 v99, v96
	v_sub_f32_e32 v96, v110, v152
	v_exp_f32_e32 v106, v96
	v_sub_f32_e32 v96, v111, v152
	v_exp_f32_e32 v107, v96
	v_sub_f32_e32 v97, v104, v152
	v_add_f32_e32 v96, 0, v98
	v_exp_f32_e32 v104, v97
	v_sub_f32_e32 v97, v105, v152
	v_add_f32_e32 v96, v99, v96
	v_exp_f32_e32 v105, v97
	v_sub_f32_e32 v97, v174, v152
	v_add_f32_e32 v96, v106, v96
	v_exp_f32_e32 v110, v97
	v_sub_f32_e32 v97, v175, v152
	v_add_f32_e32 v96, v107, v96
	v_exp_f32_e32 v111, v97
	v_add_f32_e32 v96, v104, v96
	v_add_f32_e32 v96, v105, v96
	v_add_f32_e32 v96, v110, v96
	v_add_f32_e32 v108, v111, v96
	v_sub_f32_e32 v96, v100, v152
	v_exp_f32_e32 v96, v96
	v_sub_f32_e32 v97, v101, v152
	v_exp_f32_e32 v97, v97
	v_sub_f32_e32 v100, v102, v152
	v_exp_f32_e32 v102, v100
	v_sub_f32_e32 v100, v103, v152
	v_exp_f32_e32 v103, v100
	v_add_f32_e32 v100, v96, v108
	v_add_f32_e32 v100, v97, v100
	v_add_f32_e32 v100, v102, v100
	v_add_f32_e32 v153, v103, v100
	v_sub_f32_e32 v100, v178, v152
	v_exp_f32_e32 v100, v100
	v_sub_f32_e32 v101, v179, v152
	v_exp_f32_e32 v101, v101
	v_sub_f32_e32 v108, v176, v152
	v_exp_f32_e32 v108, v108
	v_sub_f32_e32 v109, v177, v152
	v_exp_f32_e32 v109, v109
	v_add_f32_e32 v153, v100, v153
	v_add_f32_e32 v153, v101, v153
	v_add_f32_e32 v153, v108, v153
	v_add_f32_e32 v153, v109, v153
	v_mov_b32_e32 v173, v153
	s_waitcnt lgkmcnt(0)
	s_nop 1
	v_permlane16_swap_b32_e32 v173, v153
	v_add_f32_e32 v153, v153, v173
	v_mov_b32_e32 v173, v153
	s_nop 1
	v_permlane32_swap_b32_e32 v153, v173
	s_and_saveexec_b64 s[4:5], s[10:11]
	s_cbranch_execz .LBB0_1110
	v_readlane_b32 s2, v253, 18
	v_add_f32_e32 v153, v153, v173
	s_nop 0
	v_add_u32_e32 v173, s2, v166
	ds_write_b64 v173, v[152:153]
; #define LAS __attribute__((address_space(3)))
; template <int M> __device__ __forceinline__ float swz_xor(float v) { return __int_as_float(__builtin_amdgcn_ds_swizzle(__float_as_int(v), (M << 10) | 0x1f)); }
; __device__ __forceinline__ float half_sum(float v) { auto rr = __builtin_amdgcn_permlane32_swap(__float_as_uint(v), __float_as_uint(v), false, false); return __uint_as_float(rr[0]) + __uint_as_float(rr[1]); }
; __device__ __forceinline__ float half_max(float v) { auto rr = __builtin_amdgcn_permlane32_swap(__float_as_uint(v), __float_as_uint(v), false, false); return fmaxf(__uint_as_float(rr[0]), __uint_as_float(rr[1])); }
;     __device__ __forceinline__ bool operator()(f32x4 (&acc)[2][2][4][2], const pg8::Unit& u, int wr, int wc, int fr, int fq) const {
;     ...
;             for (int m = 0; m < 4; ++m) { const float r = rs_[ai][m]; float mx = -3.0e38f;
; #pragma unroll
;                 for (int bj = 0; bj < 2; ++bj)
; #pragma unroll
;                     for (int n = 0; n < 2; ++n) { acc[ai][bj][m][n] = acc[ai][bj][m][n] * r; const f32x4 v = acc[ai][bj][m][n]; mx = fmaxf(fmaxf(mx, fmaxf(v[0], v[1])), fmaxf(v[2], v[3])); }
;                 mx = fmaxf(mx, swz_xor<16>(mx)); mx = half_max(mx);
;                 float sm = 0.f;
; #pragma unroll
;                 for (int bj = 0; bj < 2; ++bj)
; #pragma unroll
;                     for (int n = 0; n < 2; ++n) { f32x4 v = acc[ai][bj][m][n];
; #pragma unroll
;                         for (int j = 0; j < 4; ++j) { v[j] = __builtin_amdgcn_exp2f(v[j] - mx); sm += v[j]; }
;                         acc[ai][bj][m][n] = v; }
;                 sm += swz_xor<16>(sm); sm = half_sum(sm);
;                 if (fq == 0) { LAS f32x2* x = (LAS f32x2*)xch + (ai * 128 + wr * 64 + m * 16 + fr) * 4 + wc; *x = (f32x2){mx, sm}; } }
.LBB0_1110:
	s_or_b64 exec, exec, s[4:5]
	v_add_f32_e32 v152, v171, v172
	v_fmamk_f32 v152, v152, 0x3a800000, v212
	s_mov_b32 s2, 0xf800000
	v_mul_f32_e32 v153, 0x4f800000, v152
	v_cmp_gt_f32_e32 vcc, s2, v152
	s_mov_b32 s2, 0xff61b1e6
	s_nop 0
	v_cndmask_b32_e32 v152, v152, v153, vcc
	v_sqrt_f32_e32 v153, v152
	s_nop 0
	v_add_u32_e32 v171, -1, v153
	v_fma_f32 v173, -v171, v153, v152
	v_add_u32_e32 v172, 1, v153
	v_cmp_ge_f32_e64 s[4:5], 0, v173
	s_nop 1
	v_cndmask_b32_e64 v171, v153, v171, s[4:5]
	v_fma_f32 v153, -v172, v153, v152
	v_cmp_lt_f32_e64 s[4:5], 0, v153
	s_nop 1
	v_cndmask_b32_e64 v153, v171, v172, s[4:5]
	v_mul_f32_e32 v171, 0x37800000, v153
	v_cndmask_b32_e32 v153, v153, v171, vcc
	v_cmp_class_f32_e32 vcc, v152, v248
	s_nop 1
	v_cndmask_b32_e32 v152, v153, v152, vcc
	v_rcp_f32_e32 v152, v152
	s_nop 0
	v_pk_mul_f32 v[94:95], v[94:95], v[152:153] op_sel_hi:[1,0]
	v_pk_mul_f32 v[92:93], v[92:93], v[152:153] op_sel_hi:[1,0]
	v_max_f32_e32 v171, v94, v95
	v_max_f32_e32 v153, v92, v93
	v_max3_f32 v153, v153, s2, v171
	v_pk_mul_f32 v[172:173], v[90:91], v[152:153] op_sel_hi:[1,0]
	v_pk_mul_f32 v[88:89], v[88:89], v[152:153] op_sel_hi:[1,0]
	v_max_f32_e32 v91, v172, v173
	v_max_f32_e32 v90, v88, v89
	v_pk_mul_f32 v[86:87], v[86:87], v[152:153] op_sel_hi:[1,0]
	v_max3_f32 v90, v153, v90, v91
	v_pk_mul_f32 v[84:85], v[84:85], v[152:153] op_sel_hi:[1,0]
	v_max_f32_e32 v153, v86, v87
	v_max_f32_e32 v91, v84, v85
	v_pk_mul_f32 v[174:175], v[82:83], v[152:153] op_sel_hi:[1,0]
	v_pk_mul_f32 v[176:177], v[80:81], v[152:153] op_sel_hi:[1,0]
	v_max3_f32 v90, v90, v91, v153
	v_max_f32_e32 v80, v176, v177
	v_max_f32_e32 v81, v174, v175
	v_max3_f32 v80, v90, v80, v81
	ds_swizzle_b32 v81, v80 offset:swizzle(SWAP,16)
	s_waitcnt lgkmcnt(0)
	v_max_f32_e32 v81, v81, v81
	v_max_f32_e32 v80, v80, v81
	v_mov_b32_e32 v81, v80
	s_nop 1
	v_permlane32_swap_b32_e32 v80, v81
	v_max_f32_e32 v81, v81, v81
	v_max_f32_e32 v80, v80, v80
	v_max_f32_e32 v152, v80, v81
	v_sub_f32_e32 v80, v92, v152
	v_exp_f32_e32 v82, v80
	v_sub_f32_e32 v80, v93, v152
	v_exp_f32_e32 v83, v80
	v_sub_f32_e32 v80, v94, v152
	v_exp_f32_e32 v90, v80
	v_sub_f32_e32 v80, v95, v152
	v_exp_f32_e32 v91, v80
	v_sub_f32_e32 v81, v88, v152
	v_add_f32_e32 v80, 0, v82
	v_exp_f32_e32 v88, v81
	v_sub_f32_e32 v81, v89, v152
	v_add_f32_e32 v80, v83, v80
	v_exp_f32_e32 v89, v81
	v_sub_f32_e32 v81, v172, v152
	v_add_f32_e32 v80, v90, v80
	v_exp_f32_e32 v94, v81
	v_sub_f32_e32 v81, v173, v152
	v_add_f32_e32 v80, v91, v80
	v_exp_f32_e32 v95, v81
	v_add_f32_e32 v80, v88, v80
	v_add_f32_e32 v80, v89, v80
	v_add_f32_e32 v80, v94, v80
	v_add_f32_e32 v92, v95, v80
	v_sub_f32_e32 v80, v84, v152
	v_exp_f32_e32 v80, v80
	v_sub_f32_e32 v81, v85, v152
	v_exp_f32_e32 v81, v81
	v_sub_f32_e32 v84, v86, v152
	v_exp_f32_e32 v86, v84
	v_sub_f32_e32 v84, v87, v152
	v_exp_f32_e32 v87, v84
	v_add_f32_e32 v84, v80, v92
	v_add_f32_e32 v84, v81, v84
	v_add_f32_e32 v84, v86, v84
	v_add_f32_e32 v153, v87, v84
	v_sub_f32_e32 v84, v176, v152
	v_exp_f32_e32 v84, v84
	v_sub_f32_e32 v85, v177, v152
	v_exp_f32_e32 v85, v85
	v_sub_f32_e32 v92, v174, v152
	v_exp_f32_e32 v92, v92
	v_sub_f32_e32 v93, v175, v152
	v_exp_f32_e32 v93, v93
	v_add_f32_e32 v153, v84, v153
	v_add_f32_e32 v153, v85, v153
	v_add_f32_e32 v153, v92, v153
	v_add_f32_e32 v153, v93, v153
	v_mov_b32_e32 v171, v153
	s_waitcnt lgkmcnt(0)
	s_nop 1
	v_permlane16_swap_b32_e32 v171, v153
	v_add_f32_e32 v153, v153, v171
	v_mov_b32_e32 v171, v153
	s_nop 1
	v_permlane32_swap_b32_e32 v153, v171
	s_and_saveexec_b64 s[4:5], s[10:11]
	s_cbranch_execz .LBB0_1112
	v_readlane_b32 s2, v253, 19
	v_add_f32_e32 v153, v153, v171
	s_nop 0
	v_add_u32_e32 v171, s2, v166
	ds_write_b64 v171, v[152:153]
.LBB0_1112:
	s_or_b64 exec, exec, s[4:5]
	v_add_f32_e32 v152, v169, v170
	v_fmamk_f32 v152, v152, 0x3a800000, v212
	s_mov_b32 s2, 0xf800000
	v_mul_f32_e32 v153, 0x4f800000, v152
	v_cmp_gt_f32_e32 vcc, s2, v152
	s_mov_b32 s2, 0xff61b1e6
	s_nop 0
	v_cndmask_b32_e32 v152, v152, v153, vcc
	v_sqrt_f32_e32 v153, v152
	s_nop 0
	v_add_u32_e32 v169, -1, v153
	v_fma_f32 v171, -v169, v153, v152
	v_add_u32_e32 v170, 1, v153
	v_cmp_ge_f32_e64 s[4:5], 0, v171
	s_nop 1
	v_cndmask_b32_e64 v169, v153, v169, s[4:5]
	v_fma_f32 v153, -v170, v153, v152
	v_cmp_lt_f32_e64 s[4:5], 0, v153
	s_nop 1
	v_cndmask_b32_e64 v153, v169, v170, s[4:5]
	v_mul_f32_e32 v169, 0x37800000, v153
	v_cndmask_b32_e32 v153, v153, v169, vcc
	v_cmp_class_f32_e32 vcc, v152, v248
	s_nop 1
	v_cndmask_b32_e32 v152, v153, v152, vcc
	v_rcp_f32_e32 v152, v152
	s_nop 0
	v_pk_mul_f32 v[78:79], v[78:79], v[152:153] op_sel_hi:[1,0]
	v_pk_mul_f32 v[76:77], v[76:77], v[152:153] op_sel_hi:[1,0]
	v_max_f32_e32 v169, v78, v79
	v_max_f32_e32 v153, v76, v77
	v_max3_f32 v153, v153, s2, v169
	v_pk_mul_f32 v[170:171], v[74:75], v[152:153] op_sel_hi:[1,0]
	v_pk_mul_f32 v[72:73], v[72:73], v[152:153] op_sel_hi:[1,0]
	v_max_f32_e32 v75, v170, v171
	v_max_f32_e32 v74, v72, v73
	v_pk_mul_f32 v[70:71], v[70:71], v[152:153] op_sel_hi:[1,0]
	v_max3_f32 v74, v153, v74, v75
	v_pk_mul_f32 v[68:69], v[68:69], v[152:153] op_sel_hi:[1,0]
	v_max_f32_e32 v153, v70, v71
	v_max_f32_e32 v75, v68, v69
	v_pk_mul_f32 v[172:173], v[66:67], v[152:153] op_sel_hi:[1,0]
	v_pk_mul_f32 v[174:175], v[64:65], v[152:153] op_sel_hi:[1,0]
	v_max3_f32 v74, v74, v75, v153
	v_max_f32_e32 v64, v174, v175
	v_max_f32_e32 v65, v172, v173
	v_max3_f32 v64, v74, v64, v65
	ds_swizzle_b32 v65, v64 offset:swizzle(SWAP,16)
	s_waitcnt lgkmcnt(0)
; #define LAS __attribute__((address_space(3)))
; template <int M> __device__ __forceinline__ float swz_xor(float v) { return __int_as_float(__builtin_amdgcn_ds_swizzle(__float_as_int(v), (M << 10) | 0x1f)); }
; __device__ __forceinline__ float half_sum(float v) { auto rr = __builtin_amdgcn_permlane32_swap(__float_as_uint(v), __float_as_uint(v), false, false); return __uint_as_float(rr[0]) + __uint_as_float(rr[1]); }
; __device__ __forceinline__ float half_max(float v) { auto rr = __builtin_amdgcn_permlane32_swap(__float_as_uint(v), __float_as_uint(v), false, false); return fmaxf(__uint_as_float(rr[0]), __uint_as_float(rr[1])); }
;     __device__ __forceinline__ bool operator()(f32x4 (&acc)[2][2][4][2], const pg8::Unit& u, int wr, int wc, int fr, int fq) const {
;     ...
;             for (int m = 0; m < 4; ++m) { const float r = rs_[ai][m]; float mx = -3.0e38f;
; #pragma unroll
;                 for (int bj = 0; bj < 2; ++bj)
; #pragma unroll
;                     for (int n = 0; n < 2; ++n) { acc[ai][bj][m][n] = acc[ai][bj][m][n] * r; const f32x4 v = acc[ai][bj][m][n]; mx = fmaxf(fmaxf(mx, fmaxf(v[0], v[1])), fmaxf(v[2], v[3])); }
;                 mx = fmaxf(mx, swz_xor<16>(mx)); mx = half_max(mx);
;                 float sm = 0.f;
; #pragma unroll
;                 for (int bj = 0; bj < 2; ++bj)
; #pragma unroll
;                     for (int n = 0; n < 2; ++n) { f32x4 v = acc[ai][bj][m][n];
; #pragma unroll
;                         for (int j = 0; j < 4; ++j) { v[j] = __builtin_amdgcn_exp2f(v[j] - mx); sm += v[j]; }
;                         acc[ai][bj][m][n] = v; }
;                 sm += swz_xor<16>(sm); sm = half_sum(sm);
;                 if (fq == 0) { LAS f32x2* x = (LAS f32x2*)xch + (ai * 128 + wr * 64 + m * 16 + fr) * 4 + wc; *x = (f32x2){mx, sm}; } }
	v_max_f32_e32 v65, v65, v65
	v_max_f32_e32 v64, v64, v65
	v_mov_b32_e32 v65, v64
	s_nop 1
	v_permlane32_swap_b32_e32 v64, v65
	v_max_f32_e32 v65, v65, v65
	v_max_f32_e32 v64, v64, v64
	v_max_f32_e32 v152, v64, v65
	v_sub_f32_e32 v64, v76, v152
	v_exp_f32_e32 v66, v64
	v_sub_f32_e32 v64, v77, v152
	v_exp_f32_e32 v67, v64
	v_sub_f32_e32 v64, v78, v152
	v_exp_f32_e32 v74, v64
	v_sub_f32_e32 v64, v79, v152
	v_exp_f32_e32 v75, v64
	v_sub_f32_e32 v65, v72, v152
	v_add_f32_e32 v64, 0, v66
	v_exp_f32_e32 v72, v65
	v_sub_f32_e32 v65, v73, v152
	v_add_f32_e32 v64, v67, v64
	v_exp_f32_e32 v73, v65
	v_sub_f32_e32 v65, v170, v152
	v_add_f32_e32 v64, v74, v64
	v_exp_f32_e32 v78, v65
	v_sub_f32_e32 v65, v171, v152
	v_add_f32_e32 v64, v75, v64
	v_exp_f32_e32 v79, v65
	v_add_f32_e32 v64, v72, v64
	v_add_f32_e32 v64, v73, v64
	v_add_f32_e32 v64, v78, v64
	v_add_f32_e32 v76, v79, v64
	v_sub_f32_e32 v64, v68, v152
	v_exp_f32_e32 v64, v64
	v_sub_f32_e32 v65, v69, v152
	v_exp_f32_e32 v65, v65
	v_sub_f32_e32 v68, v70, v152
	v_exp_f32_e32 v70, v68
	v_sub_f32_e32 v68, v71, v152
	v_exp_f32_e32 v71, v68
	v_add_f32_e32 v68, v64, v76
	v_add_f32_e32 v68, v65, v68
	v_add_f32_e32 v68, v70, v68
	v_add_f32_e32 v153, v71, v68
	v_sub_f32_e32 v68, v174, v152
	v_exp_f32_e32 v68, v68
	v_sub_f32_e32 v69, v175, v152
	v_exp_f32_e32 v69, v69
	v_sub_f32_e32 v76, v172, v152
	v_exp_f32_e32 v76, v76
	v_sub_f32_e32 v77, v173, v152
	v_exp_f32_e32 v77, v77
	v_add_f32_e32 v153, v68, v153
	v_add_f32_e32 v153, v69, v153
	v_add_f32_e32 v153, v76, v153
	v_add_f32_e32 v153, v77, v153
	v_mov_b32_e32 v169, v153
	s_waitcnt lgkmcnt(0)
	s_nop 1
	v_permlane16_swap_b32_e32 v169, v153
	v_add_f32_e32 v153, v153, v169
	v_mov_b32_e32 v169, v153
	s_nop 1
	v_permlane32_swap_b32_e32 v153, v169
	s_and_saveexec_b64 s[4:5], s[10:11]
	s_cbranch_execz .LBB0_1114
	v_readlane_b32 s2, v253, 20
	v_add_f32_e32 v153, v153, v169
	s_nop 0
	v_add_u32_e32 v169, s2, v166
	ds_write_b64 v169, v[152:153]
.LBB0_1114:
	s_or_b64 exec, exec, s[4:5]
	v_add_f32_e32 v152, v162, v163
	v_fmamk_f32 v152, v152, 0x3a800000, v212
	s_mov_b32 s2, 0xf800000
	v_mul_f32_e32 v153, 0x4f800000, v152
	v_cmp_gt_f32_e32 vcc, s2, v152
	s_mov_b32 s2, 0xff61b1e6
	s_nop 0
	v_cndmask_b32_e32 v152, v152, v153, vcc
	v_sqrt_f32_e32 v153, v152
	s_nop 0
	v_add_u32_e32 v162, -1, v153
	v_fma_f32 v169, -v162, v153, v152
	v_add_u32_e32 v163, 1, v153
	v_cmp_ge_f32_e64 s[4:5], 0, v169
	s_nop 1
	v_cndmask_b32_e64 v162, v153, v162, s[4:5]
	v_fma_f32 v153, -v163, v153, v152
	v_cmp_lt_f32_e64 s[4:5], 0, v153
	s_nop 1
	v_cndmask_b32_e64 v153, v162, v163, s[4:5]
	v_mul_f32_e32 v162, 0x37800000, v153
	v_cndmask_b32_e32 v153, v153, v162, vcc
	v_cmp_class_f32_e32 vcc, v152, v248
	s_nop 1
	v_cndmask_b32_e32 v152, v153, v152, vcc
	v_rcp_f32_e32 v152, v152
	s_nop 0
	v_pk_mul_f32 v[62:63], v[62:63], v[152:153] op_sel_hi:[1,0]
	v_pk_mul_f32 v[60:61], v[60:61], v[152:153] op_sel_hi:[1,0]
	v_max_f32_e32 v162, v62, v63
	v_max_f32_e32 v153, v60, v61
	v_max3_f32 v153, v153, s2, v162
	v_pk_mul_f32 v[162:163], v[58:59], v[152:153] op_sel_hi:[1,0]
	v_pk_mul_f32 v[56:57], v[56:57], v[152:153] op_sel_hi:[1,0]
	v_max_f32_e32 v59, v162, v163
	v_max_f32_e32 v58, v56, v57
	v_pk_mul_f32 v[54:55], v[54:55], v[152:153] op_sel_hi:[1,0]
	v_max3_f32 v58, v153, v58, v59
	v_pk_mul_f32 v[52:53], v[52:53], v[152:153] op_sel_hi:[1,0]
	v_max_f32_e32 v153, v54, v55
	v_max_f32_e32 v59, v52, v53
	v_pk_mul_f32 v[170:171], v[50:51], v[152:153] op_sel_hi:[1,0]
	v_pk_mul_f32 v[172:173], v[48:49], v[152:153] op_sel_hi:[1,0]
	v_max3_f32 v58, v58, v59, v153
	v_max_f32_e32 v48, v172, v173
	v_max_f32_e32 v49, v170, v171
	v_max3_f32 v48, v58, v48, v49
	ds_swizzle_b32 v49, v48 offset:swizzle(SWAP,16)
	s_waitcnt lgkmcnt(0)
	v_max_f32_e32 v49, v49, v49
	v_max_f32_e32 v48, v48, v49
	v_mov_b32_e32 v49, v48
	s_nop 1
	v_permlane32_swap_b32_e32 v48, v49
	v_max_f32_e32 v49, v49, v49
	v_max_f32_e32 v48, v48, v48
	v_max_f32_e32 v152, v48, v49
	v_sub_f32_e32 v48, v60, v152
	v_exp_f32_e32 v50, v48
	v_sub_f32_e32 v48, v61, v152
	v_exp_f32_e32 v51, v48
	v_sub_f32_e32 v48, v62, v152
	v_exp_f32_e32 v58, v48
	v_sub_f32_e32 v48, v63, v152
	v_exp_f32_e32 v59, v48
	v_sub_f32_e32 v49, v56, v152
	v_add_f32_e32 v48, 0, v50
	v_exp_f32_e32 v56, v49
	v_sub_f32_e32 v49, v57, v152
	v_add_f32_e32 v48, v51, v48
	v_exp_f32_e32 v57, v49
	v_sub_f32_e32 v49, v162, v152
	v_add_f32_e32 v48, v58, v48
	v_exp_f32_e32 v62, v49
	v_sub_f32_e32 v49, v163, v152
	v_add_f32_e32 v48, v59, v48
	v_exp_f32_e32 v63, v49
	v_add_f32_e32 v48, v56, v48
	v_add_f32_e32 v48, v57, v48
	v_add_f32_e32 v48, v62, v48
	v_add_f32_e32 v60, v63, v48
	v_sub_f32_e32 v48, v52, v152
	v_exp_f32_e32 v48, v48
	v_sub_f32_e32 v49, v53, v152
	v_exp_f32_e32 v49, v49
	v_sub_f32_e32 v52, v54, v152
	v_exp_f32_e32 v54, v52
	v_sub_f32_e32 v52, v55, v152
	v_exp_f32_e32 v55, v52
	v_add_f32_e32 v52, v48, v60
	v_add_f32_e32 v52, v49, v52
	v_add_f32_e32 v52, v54, v52
	v_add_f32_e32 v153, v55, v52
	v_sub_f32_e32 v52, v172, v152
	v_exp_f32_e32 v52, v52
	v_sub_f32_e32 v53, v173, v152
	v_exp_f32_e32 v53, v53
	v_sub_f32_e32 v60, v170, v152
	v_exp_f32_e32 v60, v60
	v_sub_f32_e32 v61, v171, v152
	v_exp_f32_e32 v61, v61
	v_add_f32_e32 v153, v52, v153
	v_add_f32_e32 v153, v53, v153
	v_add_f32_e32 v153, v60, v153
	v_add_f32_e32 v153, v61, v153
	v_mov_b32_e32 v162, v153
	s_waitcnt lgkmcnt(0)
	s_nop 1
	v_permlane16_swap_b32_e32 v162, v153
	v_add_f32_e32 v153, v153, v162
	v_mov_b32_e32 v162, v153
	s_nop 1
	v_permlane32_swap_b32_e32 v153, v162
	s_and_saveexec_b64 s[4:5], s[10:11]
	s_cbranch_execz .LBB0_1116
	v_readlane_b32 s2, v253, 21
	v_add_f32_e32 v153, v153, v162
	s_nop 0
	v_add_u32_e32 v162, s2, v166
	ds_write_b64 v162, v[152:153]
; #define LAS __attribute__((address_space(3)))
; template <int M> __device__ __forceinline__ float swz_xor(float v) { return __int_as_float(__builtin_amdgcn_ds_swizzle(__float_as_int(v), (M << 10) | 0x1f)); }
; __device__ __forceinline__ float half_sum(float v) { auto rr = __builtin_amdgcn_permlane32_swap(__float_as_uint(v), __float_as_uint(v), false, false); return __uint_as_float(rr[0]) + __uint_as_float(rr[1]); }
; __device__ __forceinline__ float half_max(float v) { auto rr = __builtin_amdgcn_permlane32_swap(__float_as_uint(v), __float_as_uint(v), false, false); return fmaxf(__uint_as_float(rr[0]), __uint_as_float(rr[1])); }
;     __device__ __forceinline__ bool operator()(f32x4 (&acc)[2][2][4][2], const pg8::Unit& u, int wr, int wc, int fr, int fq) const {
;     ...
;             for (int m = 0; m < 4; ++m) { const float r = rs_[ai][m]; float mx = -3.0e38f;
; #pragma unroll
;                 for (int bj = 0; bj < 2; ++bj)
; #pragma unroll
;                     for (int n = 0; n < 2; ++n) { acc[ai][bj][m][n] = acc[ai][bj][m][n] * r; const f32x4 v = acc[ai][bj][m][n]; mx = fmaxf(fmaxf(mx, fmaxf(v[0], v[1])), fmaxf(v[2], v[3])); }
;                 mx = fmaxf(mx, swz_xor<16>(mx)); mx = half_max(mx);
;                 float sm = 0.f;
; #pragma unroll
;                 for (int bj = 0; bj < 2; ++bj)
; #pragma unroll
;                     for (int n = 0; n < 2; ++n) { f32x4 v = acc[ai][bj][m][n];
; #pragma unroll
;                         for (int j = 0; j < 4; ++j) { v[j] = __builtin_amdgcn_exp2f(v[j] - mx); sm += v[j]; }
;                         acc[ai][bj][m][n] = v; }
;                 sm += swz_xor<16>(sm); sm = half_sum(sm);
;                 if (fq == 0) { LAS f32x2* x = (LAS f32x2*)xch + (ai * 128 + wr * 64 + m * 16 + fr) * 4 + wc; *x = (f32x2){mx, sm}; } }
.LBB0_1116:
	s_or_b64 exec, exec, s[4:5]
	v_add_f32_e32 v152, v158, v159
	v_fmamk_f32 v152, v152, 0x3a800000, v212
	s_mov_b32 s2, 0xf800000
	v_mul_f32_e32 v153, 0x4f800000, v152
	v_cmp_gt_f32_e32 vcc, s2, v152
	s_mov_b32 s2, 0xff61b1e6
	s_nop 0
	v_cndmask_b32_e32 v152, v152, v153, vcc
	v_sqrt_f32_e32 v153, v152
	s_nop 0
	v_add_u32_e32 v158, -1, v153
	v_fma_f32 v162, -v158, v153, v152
	v_add_u32_e32 v159, 1, v153
	v_cmp_ge_f32_e64 s[4:5], 0, v162
	s_nop 1
	v_cndmask_b32_e64 v158, v153, v158, s[4:5]
	v_fma_f32 v153, -v159, v153, v152
	v_cmp_lt_f32_e64 s[4:5], 0, v153
	s_nop 1
	v_cndmask_b32_e64 v153, v158, v159, s[4:5]
	v_mul_f32_e32 v158, 0x37800000, v153
	v_cndmask_b32_e32 v153, v153, v158, vcc
	v_cmp_class_f32_e32 vcc, v152, v248
	s_nop 1
	v_cndmask_b32_e32 v152, v153, v152, vcc
	v_rcp_f32_e32 v152, v152
	s_nop 0
	v_pk_mul_f32 v[158:159], v[46:47], v[152:153] op_sel_hi:[1,0]
	v_pk_mul_f32 v[44:45], v[44:45], v[152:153] op_sel_hi:[1,0]
	v_max_f32_e32 v47, v158, v159
	v_max_f32_e32 v46, v44, v45
	v_pk_mul_f32 v[162:163], v[42:43], v[152:153] op_sel_hi:[1,0]
	v_pk_mul_f32 v[40:41], v[40:41], v[152:153] op_sel_hi:[1,0]
	v_max3_f32 v46, v46, s2, v47
	v_max_f32_e32 v42, v40, v41
	v_max_f32_e32 v43, v162, v163
	v_pk_mul_f32 v[38:39], v[38:39], v[152:153] op_sel_hi:[1,0]
	v_pk_mul_f32 v[36:37], v[36:37], v[152:153] op_sel_hi:[1,0]
	v_max3_f32 v42, v46, v42, v43
	v_max_f32_e32 v43, v36, v37
	v_max_f32_e32 v46, v38, v39
	v_pk_mul_f32 v[170:171], v[34:35], v[152:153] op_sel_hi:[1,0]
	v_pk_mul_f32 v[172:173], v[32:33], v[152:153] op_sel_hi:[1,0]
	v_max3_f32 v42, v42, v43, v46
	v_max_f32_e32 v32, v172, v173
	v_max_f32_e32 v33, v170, v171
	v_max3_f32 v32, v42, v32, v33
	ds_swizzle_b32 v33, v32 offset:swizzle(SWAP,16)
	s_waitcnt lgkmcnt(0)
	v_max_f32_e32 v33, v33, v33
	v_max_f32_e32 v32, v32, v33
	v_mov_b32_e32 v33, v32
	s_nop 1
	v_permlane32_swap_b32_e32 v32, v33
	v_max_f32_e32 v33, v33, v33
	v_max_f32_e32 v32, v32, v32
	v_max_f32_e32 v46, v32, v33
	v_sub_f32_e32 v32, v44, v46
	v_exp_f32_e32 v34, v32
	v_sub_f32_e32 v32, v45, v46
	v_exp_f32_e32 v35, v32
	v_sub_f32_e32 v32, v158, v46
	v_exp_f32_e32 v42, v32
	v_sub_f32_e32 v32, v159, v46
	v_exp_f32_e32 v43, v32
	v_sub_f32_e32 v33, v40, v46
	v_add_f32_e32 v32, 0, v34
	v_exp_f32_e32 v40, v33
	v_sub_f32_e32 v33, v41, v46
	v_add_f32_e32 v32, v35, v32
	v_exp_f32_e32 v41, v33
	v_sub_f32_e32 v33, v162, v46
	v_add_f32_e32 v32, v42, v32
	v_exp_f32_e32 v152, v33
	v_sub_f32_e32 v33, v163, v46
	v_add_f32_e32 v32, v43, v32
	v_exp_f32_e32 v153, v33
	v_add_f32_e32 v32, v40, v32
	v_add_f32_e32 v32, v41, v32
	v_add_f32_e32 v32, v152, v32
	v_add_f32_e32 v44, v153, v32
	v_sub_f32_e32 v32, v36, v46
	v_exp_f32_e32 v32, v32
	v_sub_f32_e32 v33, v37, v46
	v_exp_f32_e32 v33, v33
	v_sub_f32_e32 v36, v38, v46
	v_exp_f32_e32 v38, v36
	v_sub_f32_e32 v36, v39, v46
	v_exp_f32_e32 v39, v36
	v_add_f32_e32 v36, v32, v44
	v_add_f32_e32 v36, v33, v36
	v_add_f32_e32 v36, v38, v36
	v_add_f32_e32 v47, v39, v36
	v_sub_f32_e32 v36, v172, v46
	v_exp_f32_e32 v36, v36
	v_sub_f32_e32 v37, v173, v46
	v_exp_f32_e32 v37, v37
	v_sub_f32_e32 v44, v170, v46
	v_exp_f32_e32 v44, v44
	v_sub_f32_e32 v45, v171, v46
	v_exp_f32_e32 v45, v45
	v_add_f32_e32 v47, v36, v47
	v_add_f32_e32 v47, v37, v47
	v_add_f32_e32 v47, v44, v47
	v_add_f32_e32 v47, v45, v47
	v_mov_b32_e32 v158, v47
	s_waitcnt lgkmcnt(0)
	s_nop 1
	v_permlane16_swap_b32_e32 v158, v47
	v_add_f32_e32 v47, v47, v158
	v_mov_b32_e32 v158, v47
	s_nop 1
	v_permlane32_swap_b32_e32 v47, v158
	s_and_saveexec_b64 s[4:5], s[10:11]
	s_cbranch_execz .LBB0_1118
	v_readlane_b32 s2, v253, 22
	v_add_f32_e32 v47, v47, v158
	s_nop 0
	v_add_u32_e32 v158, s2, v166
	ds_write_b64 v158, v[46:47]
.LBB0_1118:
	s_or_b64 exec, exec, s[4:5]
	v_add_f32_e32 v46, v156, v157
	v_fmamk_f32 v46, v46, 0x3a800000, v212
	s_mov_b32 s2, 0xf800000
	v_mul_f32_e32 v47, 0x4f800000, v46
	v_cmp_gt_f32_e32 vcc, s2, v46
	s_mov_b32 s2, 0xff61b1e6
	s_nop 0
	v_cndmask_b32_e32 v46, v46, v47, vcc
	v_sqrt_f32_e32 v47, v46
	s_nop 0
	v_add_u32_e32 v156, -1, v47
	v_fma_f32 v158, -v156, v47, v46
	v_add_u32_e32 v157, 1, v47
	v_cmp_ge_f32_e64 s[4:5], 0, v158
	s_nop 1
	v_cndmask_b32_e64 v156, v47, v156, s[4:5]
	v_fma_f32 v47, -v157, v47, v46
	v_cmp_lt_f32_e64 s[4:5], 0, v47
	s_nop 1
	v_cndmask_b32_e64 v47, v156, v157, s[4:5]
	v_mul_f32_e32 v156, 0x37800000, v47
	v_cndmask_b32_e32 v47, v47, v156, vcc
	v_cmp_class_f32_e32 vcc, v46, v248
	s_nop 1
	v_cndmask_b32_e32 v46, v47, v46, vcc
	v_rcp_f32_e32 v46, v46
	s_nop 0
	v_pk_mul_f32 v[30:31], v[30:31], v[46:47] op_sel_hi:[1,0]
	v_pk_mul_f32 v[156:157], v[28:29], v[46:47] op_sel_hi:[1,0]
	v_max_f32_e32 v29, v30, v31
	v_max_f32_e32 v28, v156, v157
	v_pk_mul_f32 v[158:159], v[26:27], v[46:47] op_sel_hi:[1,0]
	v_pk_mul_f32 v[24:25], v[24:25], v[46:47] op_sel_hi:[1,0]
	v_max3_f32 v28, v28, s2, v29
	v_max_f32_e32 v26, v24, v25
	v_max_f32_e32 v27, v158, v159
	v_pk_mul_f32 v[22:23], v[22:23], v[46:47] op_sel_hi:[1,0]
	v_pk_mul_f32 v[20:21], v[20:21], v[46:47] op_sel_hi:[1,0]
	v_max3_f32 v26, v28, v26, v27
	v_max_f32_e32 v27, v20, v21
	v_max_f32_e32 v28, v22, v23
	v_pk_mul_f32 v[162:163], v[18:19], v[46:47] op_sel_hi:[1,0]
	v_pk_mul_f32 v[46:47], v[16:17], v[46:47] op_sel_hi:[1,0]
	v_max3_f32 v26, v26, v27, v28
	v_max_f32_e32 v16, v46, v47
	v_max_f32_e32 v17, v162, v163
	v_max3_f32 v16, v26, v16, v17
	ds_swizzle_b32 v17, v16 offset:swizzle(SWAP,16)
	s_waitcnt lgkmcnt(0)
; #define LAS __attribute__((address_space(3)))
; template <int M> __device__ __forceinline__ float swz_xor(float v) { return __int_as_float(__builtin_amdgcn_ds_swizzle(__float_as_int(v), (M << 10) | 0x1f)); }
; __device__ __forceinline__ float half_sum(float v) { auto rr = __builtin_amdgcn_permlane32_swap(__float_as_uint(v), __float_as_uint(v), false, false); return __uint_as_float(rr[0]) + __uint_as_float(rr[1]); }
; __device__ __forceinline__ float half_max(float v) { auto rr = __builtin_amdgcn_permlane32_swap(__float_as_uint(v), __float_as_uint(v), false, false); return fmaxf(__uint_as_float(rr[0]), __uint_as_float(rr[1])); }
;     __device__ __forceinline__ bool operator()(f32x4 (&acc)[2][2][4][2], const pg8::Unit& u, int wr, int wc, int fr, int fq) const {
;     ...
;             for (int m = 0; m < 4; ++m) { const float r = rs_[ai][m]; float mx = -3.0e38f;
; #pragma unroll
;                 for (int bj = 0; bj < 2; ++bj)
; #pragma unroll
;                     for (int n = 0; n < 2; ++n) { acc[ai][bj][m][n] = acc[ai][bj][m][n] * r; const f32x4 v = acc[ai][bj][m][n]; mx = fmaxf(fmaxf(mx, fmaxf(v[0], v[1])), fmaxf(v[2], v[3])); }
;                 mx = fmaxf(mx, swz_xor<16>(mx)); mx = half_max(mx);
;                 float sm = 0.f;
; #pragma unroll
;                 for (int bj = 0; bj < 2; ++bj)
; #pragma unroll
;                     for (int n = 0; n < 2; ++n) { f32x4 v = acc[ai][bj][m][n];
; #pragma unroll
;                         for (int j = 0; j < 4; ++j) { v[j] = __builtin_amdgcn_exp2f(v[j] - mx); sm += v[j]; }
;                         acc[ai][bj][m][n] = v; }
;                 sm += swz_xor<16>(sm); sm = half_sum(sm);
;                 if (fq == 0) { LAS f32x2* x = (LAS f32x2*)xch + (ai * 128 + wr * 64 + m * 16 + fr) * 4 + wc; *x = (f32x2){mx, sm}; } }
	v_max_f32_e32 v17, v17, v17
	v_max_f32_e32 v16, v16, v17
	v_mov_b32_e32 v17, v16
	s_nop 1
	v_permlane32_swap_b32_e32 v16, v17
	v_max_f32_e32 v17, v17, v17
	v_max_f32_e32 v16, v16, v16
	v_max_f32_e32 v28, v16, v17
	v_sub_f32_e32 v16, v156, v28
	v_exp_f32_e32 v18, v16
	v_sub_f32_e32 v16, v157, v28
	v_exp_f32_e32 v19, v16
	v_sub_f32_e32 v16, v30, v28
	v_exp_f32_e32 v26, v16
	v_sub_f32_e32 v16, v31, v28
	v_exp_f32_e32 v27, v16
	v_sub_f32_e32 v17, v24, v28
	v_add_f32_e32 v16, 0, v18
	v_exp_f32_e32 v24, v17
	v_sub_f32_e32 v17, v25, v28
	v_add_f32_e32 v16, v19, v16
	v_exp_f32_e32 v25, v17
	v_sub_f32_e32 v17, v158, v28
	v_add_f32_e32 v16, v26, v16
	v_exp_f32_e32 v156, v17
	v_sub_f32_e32 v17, v159, v28
	v_add_f32_e32 v16, v27, v16
	v_exp_f32_e32 v157, v17
	v_add_f32_e32 v16, v24, v16
	v_add_f32_e32 v16, v25, v16
	v_add_f32_e32 v16, v156, v16
	v_add_f32_e32 v29, v157, v16
	v_sub_f32_e32 v16, v20, v28
	v_exp_f32_e32 v16, v16
	v_sub_f32_e32 v17, v21, v28
	v_exp_f32_e32 v17, v17
	v_sub_f32_e32 v20, v22, v28
	v_exp_f32_e32 v22, v20
	v_sub_f32_e32 v20, v23, v28
	v_exp_f32_e32 v23, v20
	v_add_f32_e32 v20, v16, v29
	v_add_f32_e32 v20, v17, v20
	v_add_f32_e32 v20, v22, v20
	v_add_f32_e32 v29, v23, v20
	v_sub_f32_e32 v20, v46, v28
	v_exp_f32_e32 v20, v20
	v_sub_f32_e32 v21, v47, v28
	v_exp_f32_e32 v21, v21
	v_sub_f32_e32 v30, v162, v28
	v_exp_f32_e32 v46, v30
	v_sub_f32_e32 v30, v163, v28
	v_exp_f32_e32 v47, v30
	v_add_f32_e32 v29, v20, v29
	v_add_f32_e32 v29, v21, v29
	v_add_f32_e32 v29, v46, v29
	v_add_f32_e32 v29, v47, v29
	v_mov_b32_e32 v30, v29
	s_waitcnt lgkmcnt(0)
	s_nop 1
	v_permlane16_swap_b32_e32 v30, v29
	v_add_f32_e32 v29, v29, v30
	v_mov_b32_e32 v30, v29
	s_nop 1
	v_permlane32_swap_b32_e32 v29, v30
	s_and_saveexec_b64 s[4:5], s[10:11]
	s_cbranch_execz .LBB0_1120
	v_readlane_b32 s2, v253, 23
	v_add_f32_e32 v29, v29, v30
	s_nop 0
	v_add_u32_e32 v30, s2, v166
	ds_write_b64 v30, v[28:29]
.LBB0_1120:
	s_or_b64 exec, exec, s[4:5]
	v_add_f32_e32 v28, v154, v155
	v_fmamk_f32 v28, v28, 0x3a800000, v212
	s_mov_b32 s2, 0xf800000
	v_mul_f32_e32 v29, 0x4f800000, v28
	v_cmp_gt_f32_e32 vcc, s2, v28
	s_mov_b32 s2, 0xff61b1e6
	s_nop 0
	v_cndmask_b32_e32 v28, v28, v29, vcc
	v_sqrt_f32_e32 v29, v28
	s_nop 0
	v_add_u32_e32 v30, -1, v29
	v_fma_f32 v154, -v30, v29, v28
	v_add_u32_e32 v31, 1, v29
	v_cmp_ge_f32_e64 s[4:5], 0, v154
	s_nop 1
	v_cndmask_b32_e64 v30, v29, v30, s[4:5]
	v_fma_f32 v29, -v31, v29, v28
	v_cmp_lt_f32_e64 s[4:5], 0, v29
	s_nop 1
	v_cndmask_b32_e64 v29, v30, v31, s[4:5]
	v_mul_f32_e32 v30, 0x37800000, v29
	v_cndmask_b32_e32 v29, v29, v30, vcc
	v_cmp_class_f32_e32 vcc, v28, v248
	s_nop 1
	v_cndmask_b32_e32 v28, v29, v28, vcc
	v_rcp_f32_e32 v28, v28
	s_nop 0
	v_pk_mul_f32 v[14:15], v[14:15], v[28:29] op_sel_hi:[1,0]
	v_pk_mul_f32 v[12:13], v[12:13], v[28:29] op_sel_hi:[1,0]
	v_max_f32_e32 v30, v14, v15
	v_max_f32_e32 v29, v12, v13
	v_max3_f32 v29, v29, s2, v30
	v_pk_mul_f32 v[154:155], v[10:11], v[28:29] op_sel_hi:[1,0]
	v_pk_mul_f32 v[8:9], v[8:9], v[28:29] op_sel_hi:[1,0]
	v_max_f32_e32 v11, v154, v155
	v_max_f32_e32 v10, v8, v9
	v_pk_mul_f32 v[6:7], v[6:7], v[28:29] op_sel_hi:[1,0]
	v_max3_f32 v10, v29, v10, v11
	v_pk_mul_f32 v[4:5], v[4:5], v[28:29] op_sel_hi:[1,0]
	v_max_f32_e32 v29, v6, v7
	v_max_f32_e32 v11, v4, v5
	v_pk_mul_f32 v[2:3], v[2:3], v[28:29] op_sel_hi:[1,0]
	v_pk_mul_f32 v[162:163], v[0:1], v[28:29] op_sel_hi:[1,0]
	v_max3_f32 v10, v10, v11, v29
	v_max_f32_e32 v0, v162, v163
	v_max_f32_e32 v1, v2, v3
	v_max3_f32 v0, v10, v0, v1
	ds_swizzle_b32 v1, v0 offset:swizzle(SWAP,16)
	s_waitcnt lgkmcnt(0)
	v_max_f32_e32 v1, v1, v1
	v_max_f32_e32 v0, v0, v1
	v_mov_b32_e32 v1, v0
	s_nop 1
	v_permlane32_swap_b32_e32 v0, v1
	v_max_f32_e32 v1, v1, v1
	v_max_f32_e32 v0, v0, v0
	v_max_f32_e32 v0, v0, v1
	v_sub_f32_e32 v1, v12, v0
	v_exp_f32_e32 v10, v1
	v_sub_f32_e32 v1, v13, v0
	v_exp_f32_e32 v11, v1
	v_sub_f32_e32 v1, v14, v0
	v_exp_f32_e32 v30, v1
	v_sub_f32_e32 v1, v15, v0
	v_exp_f32_e32 v31, v1
	v_sub_f32_e32 v8, v8, v0
	v_add_f32_e32 v1, 0, v10
	v_exp_f32_e32 v28, v8
	v_sub_f32_e32 v8, v9, v0
	v_add_f32_e32 v1, v11, v1
	v_exp_f32_e32 v29, v8
	v_sub_f32_e32 v8, v154, v0
	v_add_f32_e32 v1, v30, v1
	v_exp_f32_e32 v158, v8
	v_sub_f32_e32 v8, v155, v0
	v_add_f32_e32 v1, v31, v1
	v_exp_f32_e32 v159, v8
	v_sub_f32_e32 v4, v4, v0
	v_add_f32_e32 v1, v28, v1
	v_exp_f32_e32 v8, v4
	v_sub_f32_e32 v4, v5, v0
	v_add_f32_e32 v1, v29, v1
	v_exp_f32_e32 v9, v4
	v_sub_f32_e32 v4, v6, v0
	v_add_f32_e32 v1, v158, v1
	v_exp_f32_e32 v14, v4
	v_sub_f32_e32 v4, v7, v0
	v_add_f32_e32 v1, v159, v1
	v_exp_f32_e32 v15, v4
	v_sub_f32_e32 v4, v162, v0
	v_add_f32_e32 v1, v8, v1
	v_exp_f32_e32 v12, v4
	v_sub_f32_e32 v4, v163, v0
	v_add_f32_e32 v1, v9, v1
	v_exp_f32_e32 v13, v4
	v_sub_f32_e32 v2, v2, v0
	v_add_f32_e32 v1, v14, v1
	v_exp_f32_e32 v154, v2
	v_sub_f32_e32 v2, v3, v0
	v_add_f32_e32 v1, v15, v1
	v_exp_f32_e32 v155, v2
	v_add_f32_e32 v1, v12, v1
	v_add_f32_e32 v1, v13, v1
	v_add_f32_e32 v1, v154, v1
	v_add_f32_e32 v1, v155, v1
	v_mov_b32_e32 v2, v1
	s_waitcnt lgkmcnt(0)
	s_nop 1
	v_permlane16_swap_b32_e32 v2, v1
	v_add_f32_e32 v1, v1, v2
	v_mov_b32_e32 v2, v1
	s_nop 1
	v_permlane32_swap_b32_e32 v1, v2
	s_and_saveexec_b64 s[4:5], s[10:11]
	s_cbranch_execz .LBB0_1122
	v_readlane_b32 s2, v253, 24
	v_add_f32_e32 v1, v1, v2
	s_nop 0
	v_add_u32_e32 v2, s2, v166
	ds_write_b64 v2, v[0:1]

; __device__ __forceinline__ unsigned cvt_pk_bf16(float lo, float hi) { unsigned r; asm volatile("v_cvt_pk_bf16_f32 %0, %1, %2" : "=v"(r) : "v"(lo), "v"(hi)); return r; }
; __device__ __forceinline__ float bf_lo(unsigned w) { return __uint_as_float(w << 16); }
; __device__ __forceinline__ float bf_hi(unsigned w) { return __uint_as_float(w & 0xffff0000u); }
; template <int M> __device__ __forceinline__ float swz_xor(float v) { return __int_as_float(__builtin_amdgcn_ds_swizzle(__float_as_int(v), (M << 10) | 0x1f)); }
; __device__ __forceinline__ float half_sum(float v) { auto rr = __builtin_amdgcn_permlane32_swap(__float_as_uint(v), __float_as_uint(v), false, false); return __uint_as_float(rr[0]) + __uint_as_float(rr[1]); }
; __device__ __forceinline__ void st16_wt(void* p, u32x4 w) { asm volatile("global_store_dwordx4 %0, %1, off sc1\n\ts_nop 1" :: "v"(p), "v"(w) : "memory"); }
;     __device__ __forceinline__ bool operator()(f32x4 (&acc)[2][2][4][2], const pg8::Unit& u, int wr, int wc, int fr, int fq) const {
;         const int row0 = u.pm * 256 + wr * 64 + fr, colb = u.pn * 256 + wc * 32 + 8 * fq;
; #pragma unroll
;         for (int ai = 0; ai < 2; ++ai) {
;             u32x4 xin[4][2];
; #pragma unroll
;             for (int m = 0; m < 4; ++m)
; #pragma unroll
;                 for (int bj = 0; bj < 2; ++bj) xin[m][bj] = *(const u32x4*)(xbase + (size_t)(row0 + ai * 128 + m * 16) * DM + colb + bj * 128);
; #pragma unroll
;             for (int m = 0; m < 4; ++m) { const int row = row0 + ai * 128 + m * 16; float ss = 0.f;
; #pragma unroll
;                 for (int bj = 0; bj < 2; ++bj) { const size_t off = (size_t)row * DM + colb + bj * 128; const u32x4 xw = xin[m][bj];
;                     f32x4 a = {bf_lo(xw.x), bf_hi(xw.x), bf_lo(xw.y), bf_hi(xw.y)}, b = {bf_lo(xw.z), bf_hi(xw.z), bf_lo(xw.w), bf_hi(xw.w)};
;                     a += acc[ai][bj][m][0]; b += acc[ai][bj][m][1];
;                     ss += ((a[0] * a[0] + a[1] * a[1]) + (a[2] * a[2] + a[3] * a[3])) + ((b[0] * b[0] + b[1] * b[1]) + (b[2] * b[2] + b[3] * b[3]));
;                     { u32x4 w; w.x = cvt_pk_bf16(a[0], a[1]); w.y = cvt_pk_bf16(a[2], a[3]); w.z = cvt_pk_bf16(b[0], b[1]); w.w = cvt_pk_bf16(b[2], b[3]); st16_wt(xb + off, w); } }
;                 ss += swz_xor<16>(ss); ss = half_sum(ss);
;                 if (fq == 0) xch[(ai * 128 + wr * 64 + m * 16 + fr) * 4 + wc] = ss; } }
.LBB0_1219:
	s_lshl_b32 s5, s40, 8
	v_lshl_or_b32 v164, s41, 8, v183
	v_add_u32_e32 v168, s5, v180
	v_ashrrev_i32_e32 v165, 31, v164
	v_readlane_b32 s2, v252, 8
	v_lshlrev_b64 v[176:177], 1, v[164:165]
	v_readlane_b32 s3, v252, 9
	v_ashrrev_i32_e32 v169, 31, v168
	v_lshlrev_b64 v[178:179], 11, v[168:169]
	v_lshl_add_u64 v[166:167], s[2:3], 0, v[176:177]
	v_lshl_add_u64 v[128:129], v[166:167], 0, v[178:179]
	global_load_dwordx4 v[196:199], v[128:129], off
	global_load_dwordx4 v[152:155], v[128:129], off offset:256
	v_or_b32_e32 v128, 16, v168
	v_ashrrev_i32_e32 v129, 31, v128
	v_lshlrev_b64 v[174:175], 11, v[128:129]
	v_lshl_add_u64 v[128:129], v[166:167], 0, v[174:175]
	global_load_dwordx4 v[148:151], v[128:129], off
	global_load_dwordx4 v[144:147], v[128:129], off offset:256
	v_or_b32_e32 v128, 32, v168
	v_ashrrev_i32_e32 v129, 31, v128
	v_lshlrev_b64 v[172:173], 11, v[128:129]
	v_lshl_add_u64 v[128:129], v[166:167], 0, v[172:173]
	global_load_dwordx4 v[140:143], v[128:129], off
	global_load_dwordx4 v[136:139], v[128:129], off offset:256
	v_or_b32_e32 v128, 48, v168
	v_ashrrev_i32_e32 v129, 31, v128
	v_lshlrev_b64 v[170:171], 11, v[128:129]
	v_lshl_add_u64 v[128:129], v[166:167], 0, v[170:171]
	global_load_dwordx4 v[132:135], v[128:129], off
	s_nop 0
	global_load_dwordx4 v[128:131], v[128:129], off offset:256
	s_waitcnt vmcnt(0)
	v_lshlrev_b32_e32 v188, 16, v196
	v_and_b32_e32 v189, 0xffff0000, v196
	v_lshlrev_b32_e32 v190, 16, v197
	v_and_b32_e32 v191, 0xffff0000, v197
	v_lshlrev_b32_e32 v192, 16, v198
	v_and_b32_e32 v193, 0xffff0000, v198
	v_lshlrev_b32_e32 v196, 16, v199
	v_and_b32_e32 v197, 0xffff0000, v199
	v_pk_add_f32 v[126:127], v[126:127], v[190:191]
	v_pk_add_f32 v[124:125], v[124:125], v[188:189]
	v_pk_add_f32 v[188:189], v[122:123], v[196:197]
	v_pk_add_f32 v[122:123], v[120:121], v[192:193]
	v_mul_f32_e32 v120, v125, v125
	v_mul_f32_e32 v121, v127, v127
	v_fmac_f32_e32 v120, v124, v124
	v_fmac_f32_e32 v121, v126, v126
	v_add_f32_e32 v120, v120, v121
	v_mul_f32_e32 v121, v123, v123
	v_mul_f32_e32 v187, v189, v189
	v_fmac_f32_e32 v121, v122, v122
	v_fmac_f32_e32 v187, v188, v188
	v_add_f32_e32 v121, v121, v187
	v_add_f32_e32 v187, v120, v121
	v_cvt_pk_bf16_f32 v120, v124, v125
	v_cvt_pk_bf16_f32 v121, v126, v127
	v_cvt_pk_bf16_f32 v122, v122, v123
	v_cvt_pk_bf16_f32 v123, v188, v189
	v_lshl_add_u64 v[124:125], s[2:3], 0, v[178:179]
	v_lshl_add_u64 v[124:125], v[124:125], 0, v[176:177]
	global_store_dwordx4 v[124:125], v[120:123], off sc1
	s_nop 1
	v_lshlrev_b32_e32 v120, 16, v152
	v_and_b32_e32 v121, 0xffff0000, v152
	v_lshlrev_b32_e32 v122, 16, v153
	v_and_b32_e32 v123, 0xffff0000, v153
	v_lshlrev_b32_e32 v126, 16, v154
	v_and_b32_e32 v127, 0xffff0000, v154
	v_lshlrev_b32_e32 v152, 16, v155
	v_and_b32_e32 v153, 0xffff0000, v155
	v_pk_add_f32 v[118:119], v[118:119], v[122:123]
	v_pk_add_f32 v[116:117], v[116:117], v[120:121]
	v_pk_add_f32 v[120:121], v[114:115], v[152:153]
	v_pk_add_f32 v[114:115], v[112:113], v[126:127]
	v_mul_f32_e32 v112, v117, v117
	v_mul_f32_e32 v113, v119, v119
	v_fmac_f32_e32 v112, v116, v116
	v_fmac_f32_e32 v113, v118, v118
	v_add_f32_e32 v112, v112, v113
	v_mul_f32_e32 v113, v115, v115
	v_mul_f32_e32 v122, v121, v121
	v_fmac_f32_e32 v113, v114, v114
	v_fmac_f32_e32 v122, v120, v120
	v_add_f32_e32 v113, v113, v122
	v_add_f32_e32 v112, v112, v113
	v_add_f32_e32 v122, v187, v112
	v_cvt_pk_bf16_f32 v112, v116, v117
	s_mov_b64 s[2:3], 0x100
	v_cvt_pk_bf16_f32 v113, v118, v119
	v_cvt_pk_bf16_f32 v114, v114, v115
	v_cvt_pk_bf16_f32 v115, v120, v121
	v_lshl_add_u64 v[116:117], v[124:125], 0, s[2:3]
	global_store_dwordx4 v[116:117], v[112:115], off sc1
	s_nop 1
	ds_swizzle_b32 v112, v122 offset:swizzle(SWAP,16)
	s_waitcnt lgkmcnt(0)
	v_add_f32_e32 v112, v122, v112
	v_mov_b32_e32 v113, v112
	s_nop 1
	v_permlane32_swap_b32_e32 v112, v113
	s_and_saveexec_b64 s[20:21], s[0:1]
	v_add_f32_e32 v112, v112, v113
	ds_write_b32 v186, v112
	s_or_b64 exec, exec, s[20:21]
	v_lshlrev_b32_e32 v112, 16, v148
	v_and_b32_e32 v113, 0xffff0000, v148
	v_lshlrev_b32_e32 v114, 16, v149
	v_and_b32_e32 v115, 0xffff0000, v149
	v_lshlrev_b32_e32 v116, 16, v150
	v_and_b32_e32 v117, 0xffff0000, v150
	v_lshlrev_b32_e32 v118, 16, v151
	v_and_b32_e32 v119, 0xffff0000, v151
	v_pk_add_f32 v[110:111], v[110:111], v[114:115]
	v_pk_add_f32 v[108:109], v[108:109], v[112:113]
	v_pk_add_f32 v[112:113], v[106:107], v[118:119]
	v_pk_add_f32 v[106:107], v[104:105], v[116:117]
	v_mul_f32_e32 v104, v109, v109
	v_mul_f32_e32 v105, v111, v111
	v_fmac_f32_e32 v104, v108, v108
	v_fmac_f32_e32 v105, v110, v110
	v_add_f32_e32 v104, v104, v105
	v_mul_f32_e32 v105, v107, v107
	v_mul_f32_e32 v114, v113, v113
	v_fmac_f32_e32 v105, v106, v106
	v_fmac_f32_e32 v114, v112, v112
	v_readlane_b32 s2, v252, 8
	v_add_f32_e32 v105, v105, v114
	v_readlane_b32 s3, v252, 9
	v_add_f32_e32 v114, v104, v105
	v_cvt_pk_bf16_f32 v104, v108, v109
	v_cvt_pk_bf16_f32 v105, v110, v111
	v_cvt_pk_bf16_f32 v106, v106, v107
	v_cvt_pk_bf16_f32 v107, v112, v113
	s_nop 0
	v_lshl_add_u64 v[108:109], s[2:3], 0, v[174:175]
	v_lshl_add_u64 v[108:109], v[164:165], 1, v[108:109]
	global_store_dwordx4 v[108:109], v[104:107], off sc1
	s_nop 1
	v_lshlrev_b32_e32 v104, 16, v144
	v_and_b32_e32 v105, 0xffff0000, v144
	v_lshlrev_b32_e32 v106, 16, v145
	v_and_b32_e32 v107, 0xffff0000, v145
	v_lshlrev_b32_e32 v110, 16, v146
	v_and_b32_e32 v111, 0xffff0000, v146
	v_lshlrev_b32_e32 v112, 16, v147
	v_and_b32_e32 v113, 0xffff0000, v147
	v_pk_add_f32 v[102:103], v[102:103], v[106:107]
	v_pk_add_f32 v[100:101], v[100:101], v[104:105]
	v_pk_add_f32 v[104:105], v[98:99], v[112:113]
	v_pk_add_f32 v[98:99], v[96:97], v[110:111]
	v_mul_f32_e32 v96, v101, v101
	v_mul_f32_e32 v97, v103, v103
	v_fmac_f32_e32 v96, v100, v100
	v_fmac_f32_e32 v97, v102, v102
	v_add_f32_e32 v96, v96, v97
	v_mul_f32_e32 v97, v99, v99
	v_mul_f32_e32 v106, v105, v105
	v_fmac_f32_e32 v97, v98, v98
	v_fmac_f32_e32 v106, v104, v104
	v_add_f32_e32 v97, v97, v106
	v_add_f32_e32 v96, v96, v97
	v_add_f32_e32 v106, v114, v96
	v_cvt_pk_bf16_f32 v96, v100, v101
	v_cvt_pk_bf16_f32 v97, v102, v103
	v_mov_b32_e32 v102, v106
	s_mov_b64 s[2:3], 0x100
	v_cvt_pk_bf16_f32 v98, v98, v99
	v_cvt_pk_bf16_f32 v99, v104, v105
	v_lshl_add_u64 v[100:101], v[108:109], 0, s[2:3]
	global_store_dwordx4 v[100:101], v[96:99], off sc1
	s_nop 1
	s_waitcnt lgkmcnt(0)
; __device__ __forceinline__ unsigned cvt_pk_bf16(float lo, float hi) { unsigned r; asm volatile("v_cvt_pk_bf16_f32 %0, %1, %2" : "=v"(r) : "v"(lo), "v"(hi)); return r; }
; __device__ __forceinline__ float bf_lo(unsigned w) { return __uint_as_float(w << 16); }
; __device__ __forceinline__ float bf_hi(unsigned w) { return __uint_as_float(w & 0xffff0000u); }
; template <int M> __device__ __forceinline__ float swz_xor(float v) { return __int_as_float(__builtin_amdgcn_ds_swizzle(__float_as_int(v), (M << 10) | 0x1f)); }
; __device__ __forceinline__ float half_sum(float v) { auto rr = __builtin_amdgcn_permlane32_swap(__float_as_uint(v), __float_as_uint(v), false, false); return __uint_as_float(rr[0]) + __uint_as_float(rr[1]); }
; __device__ __forceinline__ void st16_wt(void* p, u32x4 w) { asm volatile("global_store_dwordx4 %0, %1, off sc1\n\ts_nop 1" :: "v"(p), "v"(w) : "memory"); }
;     __device__ __forceinline__ bool operator()(f32x4 (&acc)[2][2][4][2], const pg8::Unit& u, int wr, int wc, int fr, int fq) const {
;     ...
;             for (int m = 0; m < 4; ++m) { const int row = row0 + ai * 128 + m * 16; float ss = 0.f;
; #pragma unroll
;                 for (int bj = 0; bj < 2; ++bj) { const size_t off = (size_t)row * DM + colb + bj * 128; const u32x4 xw = xin[m][bj];
;                     f32x4 a = {bf_lo(xw.x), bf_hi(xw.x), bf_lo(xw.y), bf_hi(xw.y)}, b = {bf_lo(xw.z), bf_hi(xw.z), bf_lo(xw.w), bf_hi(xw.w)};
;                     a += acc[ai][bj][m][0]; b += acc[ai][bj][m][1];
;                     ss += ((a[0] * a[0] + a[1] * a[1]) + (a[2] * a[2] + a[3] * a[3])) + ((b[0] * b[0] + b[1] * b[1]) + (b[2] * b[2] + b[3] * b[3]));
;                     { u32x4 w; w.x = cvt_pk_bf16(a[0], a[1]); w.y = cvt_pk_bf16(a[2], a[3]); w.z = cvt_pk_bf16(b[0], b[1]); w.w = cvt_pk_bf16(b[2], b[3]); st16_wt(xb + off, w); } }
;                 ss += swz_xor<16>(ss); ss = half_sum(ss);
;                 if (fq == 0) xch[(ai * 128 + wr * 64 + m * 16 + fr) * 4 + wc] = ss; } }
	s_nop 1
	v_permlane16_swap_b32_e32 v102, v106
	v_add_f32_e32 v96, v106, v102
	v_mov_b32_e32 v97, v96
	s_nop 1
	v_permlane32_swap_b32_e32 v96, v97
	s_and_saveexec_b64 s[20:21], s[0:1]
	v_add_f32_e32 v96, v96, v97
	ds_write_b32 v186, v96 offset:256
	s_or_b64 exec, exec, s[20:21]
	v_lshlrev_b32_e32 v96, 16, v140
	v_and_b32_e32 v97, 0xffff0000, v140
	v_lshlrev_b32_e32 v98, 16, v141
	v_and_b32_e32 v99, 0xffff0000, v141
	v_lshlrev_b32_e32 v100, 16, v142
	v_and_b32_e32 v101, 0xffff0000, v142
	v_lshlrev_b32_e32 v102, 16, v143
	v_and_b32_e32 v103, 0xffff0000, v143
	v_pk_add_f32 v[94:95], v[94:95], v[98:99]
	v_pk_add_f32 v[92:93], v[92:93], v[96:97]
	v_pk_add_f32 v[96:97], v[90:91], v[102:103]
	v_pk_add_f32 v[90:91], v[88:89], v[100:101]
	v_mul_f32_e32 v88, v93, v93
	v_mul_f32_e32 v89, v95, v95
	v_fmac_f32_e32 v88, v92, v92
	v_fmac_f32_e32 v89, v94, v94
	v_add_f32_e32 v88, v88, v89
	v_mul_f32_e32 v89, v91, v91
	v_mul_f32_e32 v98, v97, v97
	v_fmac_f32_e32 v89, v90, v90
	v_fmac_f32_e32 v98, v96, v96
	v_readlane_b32 s2, v252, 8
	v_add_f32_e32 v89, v89, v98
	v_readlane_b32 s3, v252, 9
	v_add_f32_e32 v98, v88, v89
	v_cvt_pk_bf16_f32 v88, v92, v93
	v_cvt_pk_bf16_f32 v89, v94, v95
	v_cvt_pk_bf16_f32 v90, v90, v91
	v_cvt_pk_bf16_f32 v91, v96, v97
	s_nop 0
	v_lshl_add_u64 v[92:93], s[2:3], 0, v[172:173]
	v_lshl_add_u64 v[92:93], v[164:165], 1, v[92:93]
	global_store_dwordx4 v[92:93], v[88:91], off sc1
	s_nop 1
	v_lshlrev_b32_e32 v88, 16, v136
	v_and_b32_e32 v89, 0xffff0000, v136
	v_lshlrev_b32_e32 v90, 16, v137
	v_and_b32_e32 v91, 0xffff0000, v137
	v_lshlrev_b32_e32 v94, 16, v138
	v_and_b32_e32 v95, 0xffff0000, v138
	v_lshlrev_b32_e32 v96, 16, v139
	v_and_b32_e32 v97, 0xffff0000, v139
	v_pk_add_f32 v[86:87], v[86:87], v[90:91]
	v_pk_add_f32 v[84:85], v[84:85], v[88:89]
	v_pk_add_f32 v[88:89], v[82:83], v[96:97]
	v_pk_add_f32 v[82:83], v[80:81], v[94:95]
	v_mul_f32_e32 v80, v85, v85
	v_mul_f32_e32 v81, v87, v87
	v_fmac_f32_e32 v80, v84, v84
	v_fmac_f32_e32 v81, v86, v86
	v_add_f32_e32 v80, v80, v81
	v_mul_f32_e32 v81, v83, v83
	v_mul_f32_e32 v90, v89, v89
	v_fmac_f32_e32 v81, v82, v82
	v_fmac_f32_e32 v90, v88, v88
	v_add_f32_e32 v81, v81, v90
	v_add_f32_e32 v80, v80, v81
	v_add_f32_e32 v90, v98, v80
	v_cvt_pk_bf16_f32 v80, v84, v85
	v_cvt_pk_bf16_f32 v81, v86, v87
	v_mov_b32_e32 v86, v90
	s_mov_b64 s[2:3], 0x100
	v_cvt_pk_bf16_f32 v82, v82, v83
	v_cvt_pk_bf16_f32 v83, v88, v89
	v_lshl_add_u64 v[84:85], v[92:93], 0, s[2:3]
	global_store_dwordx4 v[84:85], v[80:83], off sc1
	s_nop 1
	s_waitcnt lgkmcnt(0)
	s_nop 1
	v_permlane16_swap_b32_e32 v86, v90
	v_add_f32_e32 v80, v90, v86
	v_mov_b32_e32 v81, v80
	s_nop 1
	v_permlane32_swap_b32_e32 v80, v81
	s_and_saveexec_b64 s[20:21], s[0:1]
	v_add_f32_e32 v80, v80, v81
	ds_write_b32 v186, v80 offset:512
	s_or_b64 exec, exec, s[20:21]
	v_lshlrev_b32_e32 v80, 16, v132
	v_and_b32_e32 v81, 0xffff0000, v132
	v_lshlrev_b32_e32 v82, 16, v133
	v_and_b32_e32 v83, 0xffff0000, v133
	v_lshlrev_b32_e32 v84, 16, v134
	v_and_b32_e32 v85, 0xffff0000, v134
	v_lshlrev_b32_e32 v86, 16, v135
	v_and_b32_e32 v87, 0xffff0000, v135
	v_pk_add_f32 v[78:79], v[78:79], v[82:83]
	v_pk_add_f32 v[76:77], v[76:77], v[80:81]
	v_pk_add_f32 v[80:81], v[74:75], v[86:87]
	v_pk_add_f32 v[74:75], v[72:73], v[84:85]
	v_mul_f32_e32 v72, v77, v77
	v_mul_f32_e32 v73, v79, v79
	v_fmac_f32_e32 v72, v76, v76
	v_fmac_f32_e32 v73, v78, v78
	v_add_f32_e32 v72, v72, v73
	v_mul_f32_e32 v73, v75, v75
	v_mul_f32_e32 v82, v81, v81
	v_fmac_f32_e32 v73, v74, v74
	v_fmac_f32_e32 v82, v80, v80
	v_readlane_b32 s2, v252, 8
	v_add_f32_e32 v73, v73, v82
	v_readlane_b32 s3, v252, 9
	v_add_f32_e32 v82, v72, v73
	v_cvt_pk_bf16_f32 v72, v76, v77
	v_cvt_pk_bf16_f32 v73, v78, v79
	v_cvt_pk_bf16_f32 v74, v74, v75
	v_cvt_pk_bf16_f32 v75, v80, v81
	s_nop 0
	v_lshl_add_u64 v[76:77], s[2:3], 0, v[170:171]
	v_lshl_add_u64 v[76:77], v[164:165], 1, v[76:77]
	global_store_dwordx4 v[76:77], v[72:75], off sc1
	s_nop 1
	v_lshlrev_b32_e32 v72, 16, v128
	v_and_b32_e32 v73, 0xffff0000, v128
	v_lshlrev_b32_e32 v74, 16, v129
	v_and_b32_e32 v75, 0xffff0000, v129
	v_lshlrev_b32_e32 v78, 16, v130
	v_and_b32_e32 v79, 0xffff0000, v130
	v_lshlrev_b32_e32 v80, 16, v131
	v_and_b32_e32 v81, 0xffff0000, v131
	v_pk_add_f32 v[70:71], v[70:71], v[74:75]
	v_pk_add_f32 v[68:69], v[68:69], v[72:73]
	v_pk_add_f32 v[72:73], v[66:67], v[80:81]
	v_pk_add_f32 v[66:67], v[64:65], v[78:79]
	v_mul_f32_e32 v64, v69, v69
	v_mul_f32_e32 v65, v71, v71
	v_fmac_f32_e32 v64, v68, v68
	v_fmac_f32_e32 v65, v70, v70
	v_add_f32_e32 v64, v64, v65
	v_mul_f32_e32 v65, v67, v67
	v_mul_f32_e32 v74, v73, v73
	v_fmac_f32_e32 v65, v66, v66
	v_fmac_f32_e32 v74, v72, v72
	v_add_f32_e32 v65, v65, v74
	v_add_f32_e32 v64, v64, v65
	v_add_f32_e32 v74, v82, v64
	v_cvt_pk_bf16_f32 v64, v68, v69
	v_cvt_pk_bf16_f32 v65, v70, v71
	v_mov_b32_e32 v70, v74
	s_mov_b64 s[2:3], 0x100
	v_cvt_pk_bf16_f32 v66, v66, v67
	v_cvt_pk_bf16_f32 v67, v72, v73
	v_lshl_add_u64 v[68:69], v[76:77], 0, s[2:3]
	global_store_dwordx4 v[68:69], v[64:67], off sc1
	s_nop 1
	s_waitcnt lgkmcnt(0)
; __device__ __forceinline__ unsigned cvt_pk_bf16(float lo, float hi) { unsigned r; asm volatile("v_cvt_pk_bf16_f32 %0, %1, %2" : "=v"(r) : "v"(lo), "v"(hi)); return r; }
; __device__ __forceinline__ float bf_lo(unsigned w) { return __uint_as_float(w << 16); }
; __device__ __forceinline__ float bf_hi(unsigned w) { return __uint_as_float(w & 0xffff0000u); }
; template <int M> __device__ __forceinline__ float swz_xor(float v) { return __int_as_float(__builtin_amdgcn_ds_swizzle(__float_as_int(v), (M << 10) | 0x1f)); }
; __device__ __forceinline__ float half_sum(float v) { auto rr = __builtin_amdgcn_permlane32_swap(__float_as_uint(v), __float_as_uint(v), false, false); return __uint_as_float(rr[0]) + __uint_as_float(rr[1]); }
; __device__ __forceinline__ void st16_wt(void* p, u32x4 w) { asm volatile("global_store_dwordx4 %0, %1, off sc1\n\ts_nop 1" :: "v"(p), "v"(w) : "memory"); }
;     __device__ __forceinline__ bool operator()(f32x4 (&acc)[2][2][4][2], const pg8::Unit& u, int wr, int wc, int fr, int fq) const {
;     ...
;         for (int ai = 0; ai < 2; ++ai) {
;             u32x4 xin[4][2];
; #pragma unroll
;             for (int m = 0; m < 4; ++m)
; #pragma unroll
;                 for (int bj = 0; bj < 2; ++bj) xin[m][bj] = *(const u32x4*)(xbase + (size_t)(row0 + ai * 128 + m * 16) * DM + colb + bj * 128);
; #pragma unroll
;             for (int m = 0; m < 4; ++m) { const int row = row0 + ai * 128 + m * 16; float ss = 0.f;
; #pragma unroll
;                 for (int bj = 0; bj < 2; ++bj) { const size_t off = (size_t)row * DM + colb + bj * 128; const u32x4 xw = xin[m][bj];
;                     f32x4 a = {bf_lo(xw.x), bf_hi(xw.x), bf_lo(xw.y), bf_hi(xw.y)}, b = {bf_lo(xw.z), bf_hi(xw.z), bf_lo(xw.w), bf_hi(xw.w)};
;                     a += acc[ai][bj][m][0]; b += acc[ai][bj][m][1];
;                     ss += ((a[0] * a[0] + a[1] * a[1]) + (a[2] * a[2] + a[3] * a[3])) + ((b[0] * b[0] + b[1] * b[1]) + (b[2] * b[2] + b[3] * b[3]));
;                     { u32x4 w; w.x = cvt_pk_bf16(a[0], a[1]); w.y = cvt_pk_bf16(a[2], a[3]); w.z = cvt_pk_bf16(b[0], b[1]); w.w = cvt_pk_bf16(b[2], b[3]); st16_wt(xb + off, w); } }
;                 ss += swz_xor<16>(ss); ss = half_sum(ss);
;                 if (fq == 0) xch[(ai * 128 + wr * 64 + m * 16 + fr) * 4 + wc] = ss; } }
	s_nop 1
	v_permlane16_swap_b32_e32 v70, v74
	v_add_f32_e32 v64, v74, v70
	v_mov_b32_e32 v65, v64
	s_nop 1
	v_permlane32_swap_b32_e32 v64, v65
	s_and_saveexec_b64 s[20:21], s[0:1]
	v_add_f32_e32 v64, v64, v65
	ds_write_b32 v186, v64 offset:768
	s_or_b64 exec, exec, s[20:21]
	v_lshlrev_b64 v[64:65], 11, v[168:169]
	s_mov_b64 s[2:3], 0x40000
	v_lshl_add_u64 v[102:103], v[64:65], 0, s[2:3]
	v_lshl_add_u64 v[66:67], v[166:167], 0, v[102:103]
	global_load_dwordx4 v[94:97], v[66:67], off
	global_load_dwordx4 v[98:101], v[66:67], off offset:256
	s_mov_b64 s[2:3], 0x48000
	v_lshl_add_u64 v[92:93], v[64:65], 0, s[2:3]
	s_mov_b64 s[2:3], 0x50000
	v_lshl_add_u64 v[90:91], v[64:65], 0, s[2:3]
	s_mov_b64 s[2:3], 0x58000
	v_lshl_add_u64 v[66:67], v[166:167], 0, v[92:93]
	v_lshl_add_u64 v[88:89], v[64:65], 0, s[2:3]
	global_load_dwordx4 v[84:87], v[66:67], off
	global_load_dwordx4 v[80:83], v[66:67], off offset:256
	v_lshl_add_u64 v[66:67], v[166:167], 0, v[90:91]
	v_lshl_add_u64 v[64:65], v[166:167], 0, v[88:89]
	global_load_dwordx4 v[76:79], v[66:67], off
	global_load_dwordx4 v[72:75], v[66:67], off offset:256
	global_load_dwordx4 v[68:71], v[64:65], off
	s_nop 0
	global_load_dwordx4 v[64:67], v[64:65], off offset:256
	v_readlane_b32 s2, v252, 8
	v_readlane_b32 s3, v252, 9
	s_waitcnt vmcnt(7)
	v_lshlrev_b32_e32 v104, 16, v94
	v_and_b32_e32 v105, 0xffff0000, v94
	v_lshlrev_b32_e32 v94, 16, v95
	v_and_b32_e32 v95, 0xffff0000, v95
	v_lshlrev_b32_e32 v106, 16, v96
	v_and_b32_e32 v107, 0xffff0000, v96
	v_lshlrev_b32_e32 v96, 16, v97
	v_and_b32_e32 v97, 0xffff0000, v97
	v_pk_add_f32 v[62:63], v[62:63], v[94:95]
	v_pk_add_f32 v[60:61], v[60:61], v[104:105]
	v_pk_add_f32 v[94:95], v[58:59], v[96:97]
	v_pk_add_f32 v[58:59], v[56:57], v[106:107]
	v_mul_f32_e32 v56, v61, v61
	v_mul_f32_e32 v57, v63, v63
	v_fmac_f32_e32 v56, v60, v60
	v_fmac_f32_e32 v57, v62, v62
	v_add_f32_e32 v56, v56, v57
	v_mul_f32_e32 v57, v59, v59
	v_mul_f32_e32 v96, v95, v95
	v_fmac_f32_e32 v57, v58, v58
	v_fmac_f32_e32 v96, v94, v94
	v_add_f32_e32 v57, v57, v96
	v_add_f32_e32 v96, v56, v57
	v_cvt_pk_bf16_f32 v56, v60, v61
	v_cvt_pk_bf16_f32 v57, v62, v63
	v_cvt_pk_bf16_f32 v58, v58, v59
	v_cvt_pk_bf16_f32 v59, v94, v95
	v_lshl_add_u64 v[60:61], s[2:3], 0, v[102:103]
	v_lshl_add_u64 v[60:61], v[164:165], 1, v[60:61]
	global_store_dwordx4 v[60:61], v[56:59], off sc1
	s_nop 1
	s_waitcnt vmcnt(6)
	v_lshlrev_b32_e32 v56, 16, v98
	v_and_b32_e32 v57, 0xffff0000, v98
	v_lshlrev_b32_e32 v58, 16, v99
	v_and_b32_e32 v59, 0xffff0000, v99
	v_lshlrev_b32_e32 v62, 16, v100
	v_and_b32_e32 v63, 0xffff0000, v100
	v_lshlrev_b32_e32 v94, 16, v101
	v_and_b32_e32 v95, 0xffff0000, v101
	v_pk_add_f32 v[54:55], v[54:55], v[58:59]
	v_pk_add_f32 v[52:53], v[52:53], v[56:57]
	v_pk_add_f32 v[56:57], v[50:51], v[94:95]
	v_pk_add_f32 v[50:51], v[48:49], v[62:63]
	v_mul_f32_e32 v48, v53, v53
	v_mul_f32_e32 v49, v55, v55
	v_fmac_f32_e32 v48, v52, v52
	v_fmac_f32_e32 v49, v54, v54
	v_add_f32_e32 v48, v48, v49
	v_mul_f32_e32 v49, v51, v51
	v_mul_f32_e32 v58, v57, v57
	v_fmac_f32_e32 v49, v50, v50
	v_fmac_f32_e32 v58, v56, v56
	v_add_f32_e32 v49, v49, v58
	v_add_f32_e32 v48, v48, v49
	v_add_f32_e32 v58, v96, v48
	v_cvt_pk_bf16_f32 v48, v52, v53
	s_mov_b64 s[2:3], 0x100
	v_cvt_pk_bf16_f32 v49, v54, v55
	v_cvt_pk_bf16_f32 v50, v50, v51
	v_cvt_pk_bf16_f32 v51, v56, v57
	v_lshl_add_u64 v[52:53], v[60:61], 0, s[2:3]
	global_store_dwordx4 v[52:53], v[48:51], off sc1
	s_nop 1
	ds_swizzle_b32 v48, v58 offset:swizzle(SWAP,16)
	s_waitcnt lgkmcnt(0)
	v_add_f32_e32 v48, v58, v48
	v_mov_b32_e32 v49, v48
	s_nop 1
	v_permlane32_swap_b32_e32 v48, v49
	s_and_saveexec_b64 s[20:21], s[0:1]
	v_add_f32_e32 v48, v48, v49
	ds_write_b32 v186, v48 offset:2048
	s_or_b64 exec, exec, s[20:21]
	s_waitcnt vmcnt(5)
	v_lshlrev_b32_e32 v48, 16, v84
	v_and_b32_e32 v49, 0xffff0000, v84
	v_lshlrev_b32_e32 v50, 16, v85
	v_and_b32_e32 v51, 0xffff0000, v85
	v_lshlrev_b32_e32 v52, 16, v86
	v_and_b32_e32 v53, 0xffff0000, v86
	v_lshlrev_b32_e32 v54, 16, v87
	v_and_b32_e32 v55, 0xffff0000, v87
	v_pk_add_f32 v[46:47], v[46:47], v[50:51]
	v_pk_add_f32 v[44:45], v[44:45], v[48:49]
	v_pk_add_f32 v[48:49], v[42:43], v[54:55]
	v_pk_add_f32 v[42:43], v[40:41], v[52:53]
	v_mul_f32_e32 v40, v45, v45
	v_mul_f32_e32 v41, v47, v47
	v_fmac_f32_e32 v40, v44, v44
	v_fmac_f32_e32 v41, v46, v46
	v_add_f32_e32 v40, v40, v41
	v_mul_f32_e32 v41, v43, v43
	v_mul_f32_e32 v50, v49, v49
	v_fmac_f32_e32 v41, v42, v42
	v_fmac_f32_e32 v50, v48, v48
	v_readlane_b32 s2, v252, 8
	v_add_f32_e32 v41, v41, v50
	v_readlane_b32 s3, v252, 9
	v_add_f32_e32 v50, v40, v41
	v_cvt_pk_bf16_f32 v40, v44, v45
	v_cvt_pk_bf16_f32 v41, v46, v47
	v_cvt_pk_bf16_f32 v42, v42, v43
	v_cvt_pk_bf16_f32 v43, v48, v49
	s_nop 0
	v_lshl_add_u64 v[44:45], s[2:3], 0, v[92:93]
	v_lshl_add_u64 v[44:45], v[164:165], 1, v[44:45]
	global_store_dwordx4 v[44:45], v[40:43], off sc1
	s_nop 1
	s_waitcnt vmcnt(4)
	v_lshlrev_b32_e32 v40, 16, v80
	v_and_b32_e32 v41, 0xffff0000, v80
	v_lshlrev_b32_e32 v42, 16, v81
	v_and_b32_e32 v43, 0xffff0000, v81
	v_lshlrev_b32_e32 v46, 16, v82
	v_and_b32_e32 v47, 0xffff0000, v82
	v_lshlrev_b32_e32 v48, 16, v83
	v_and_b32_e32 v49, 0xffff0000, v83
	v_pk_add_f32 v[38:39], v[38:39], v[42:43]
	v_pk_add_f32 v[36:37], v[36:37], v[40:41]
	v_pk_add_f32 v[40:41], v[34:35], v[48:49]
	v_pk_add_f32 v[34:35], v[32:33], v[46:47]
	v_mul_f32_e32 v32, v37, v37
	v_mul_f32_e32 v33, v39, v39
	v_fmac_f32_e32 v32, v36, v36
	v_fmac_f32_e32 v33, v38, v38
	v_add_f32_e32 v32, v32, v33
	v_mul_f32_e32 v33, v35, v35
	v_mul_f32_e32 v42, v41, v41
	v_fmac_f32_e32 v33, v34, v34
	v_fmac_f32_e32 v42, v40, v40
	v_add_f32_e32 v33, v33, v42
	v_add_f32_e32 v32, v32, v33
	v_add_f32_e32 v42, v50, v32
	v_cvt_pk_bf16_f32 v32, v36, v37
	v_cvt_pk_bf16_f32 v33, v38, v39
	ds_swizzle_b32 v38, v42 offset:swizzle(SWAP,16)
	s_mov_b64 s[2:3], 0x100
	v_cvt_pk_bf16_f32 v34, v34, v35
	v_cvt_pk_bf16_f32 v35, v40, v41
	v_lshl_add_u64 v[36:37], v[44:45], 0, s[2:3]
	global_store_dwordx4 v[36:37], v[32:35], off sc1
	s_nop 1
	s_waitcnt lgkmcnt(0)
; #define LAS __attribute__((address_space(3)))
; __device__ __forceinline__ unsigned cvt_pk_bf16(float lo, float hi) { unsigned r; asm volatile("v_cvt_pk_bf16_f32 %0, %1, %2" : "=v"(r) : "v"(lo), "v"(hi)); return r; }
; __device__ __forceinline__ float bf_lo(unsigned w) { return __uint_as_float(w << 16); }
; __device__ __forceinline__ float bf_hi(unsigned w) { return __uint_as_float(w & 0xffff0000u); }
; template <int M> __device__ __forceinline__ float swz_xor(float v) { return __int_as_float(__builtin_amdgcn_ds_swizzle(__float_as_int(v), (M << 10) | 0x1f)); }
; __device__ __forceinline__ float half_sum(float v) { auto rr = __builtin_amdgcn_permlane32_swap(__float_as_uint(v), __float_as_uint(v), false, false); return __uint_as_float(rr[0]) + __uint_as_float(rr[1]); }
; __device__ __forceinline__ void st16_wt(void* p, u32x4 w) { asm volatile("global_store_dwordx4 %0, %1, off sc1\n\ts_nop 1" :: "v"(p), "v"(w) : "memory"); }
;     __device__ __forceinline__ bool operator()(f32x4 (&acc)[2][2][4][2], const pg8::Unit& u, int wr, int wc, int fr, int fq) const {
;     ...
;             for (int m = 0; m < 4; ++m) { const int row = row0 + ai * 128 + m * 16; float ss = 0.f;
; #pragma unroll
;                 for (int bj = 0; bj < 2; ++bj) { const size_t off = (size_t)row * DM + colb + bj * 128; const u32x4 xw = xin[m][bj];
;                     f32x4 a = {bf_lo(xw.x), bf_hi(xw.x), bf_lo(xw.y), bf_hi(xw.y)}, b = {bf_lo(xw.z), bf_hi(xw.z), bf_lo(xw.w), bf_hi(xw.w)};
;                     a += acc[ai][bj][m][0]; b += acc[ai][bj][m][1];
;                     ss += ((a[0] * a[0] + a[1] * a[1]) + (a[2] * a[2] + a[3] * a[3])) + ((b[0] * b[0] + b[1] * b[1]) + (b[2] * b[2] + b[3] * b[3]));
;                     { u32x4 w; w.x = cvt_pk_bf16(a[0], a[1]); w.y = cvt_pk_bf16(a[2], a[3]); w.z = cvt_pk_bf16(b[0], b[1]); w.w = cvt_pk_bf16(b[2], b[3]); st16_wt(xb + off, w); } }
;                 ss += swz_xor<16>(ss); ss = half_sum(ss);
;                 if (fq == 0) xch[(ai * 128 + wr * 64 + m * 16 + fr) * 4 + wc] = ss; } }
;         asm volatile("s_waitcnt lgkmcnt(0)" ::: "memory"); __builtin_amdgcn_s_barrier(); asm volatile("" ::: "memory");
;         const int tid_ = (wr * 4 + wc) * 64 + fq * 16 + fr;
;         if (tid_ < 256) st16f_wt(part + (size_t)(u.pm * 256 + tid_) * 16 + u.pn * 4, *(const LAS f32x4*)(xch + tid_ * 4));
;         wave_arrive(done + 64 * u.pm, (fr | fq) == 0);
	v_add_f32_e32 v32, v42, v38
	v_mov_b32_e32 v33, v32
	s_nop 1
	v_permlane32_swap_b32_e32 v32, v33
	s_and_saveexec_b64 s[20:21], s[0:1]
	v_add_f32_e32 v32, v32, v33
	ds_write_b32 v186, v32 offset:2304
	s_or_b64 exec, exec, s[20:21]
	s_waitcnt vmcnt(3)
	v_lshlrev_b32_e32 v32, 16, v76
	v_and_b32_e32 v33, 0xffff0000, v76
	v_lshlrev_b32_e32 v34, 16, v77
	v_and_b32_e32 v35, 0xffff0000, v77
	v_lshlrev_b32_e32 v36, 16, v78
	v_and_b32_e32 v37, 0xffff0000, v78
	v_lshlrev_b32_e32 v38, 16, v79
	v_and_b32_e32 v39, 0xffff0000, v79
	v_pk_add_f32 v[30:31], v[30:31], v[34:35]
	v_pk_add_f32 v[28:29], v[28:29], v[32:33]
	v_pk_add_f32 v[32:33], v[26:27], v[38:39]
	v_pk_add_f32 v[26:27], v[24:25], v[36:37]
	v_mul_f32_e32 v24, v29, v29
	v_mul_f32_e32 v25, v31, v31
	v_fmac_f32_e32 v24, v28, v28
	v_fmac_f32_e32 v25, v30, v30
	v_add_f32_e32 v24, v24, v25
	v_mul_f32_e32 v25, v27, v27
	v_mul_f32_e32 v34, v33, v33
	v_fmac_f32_e32 v25, v26, v26
	v_fmac_f32_e32 v34, v32, v32
	v_readlane_b32 s2, v252, 8
	v_add_f32_e32 v25, v25, v34
	v_readlane_b32 s3, v252, 9
	v_add_f32_e32 v34, v24, v25
	v_cvt_pk_bf16_f32 v24, v28, v29
	v_cvt_pk_bf16_f32 v25, v30, v31
	v_cvt_pk_bf16_f32 v26, v26, v27
	v_cvt_pk_bf16_f32 v27, v32, v33
	s_nop 0
	v_lshl_add_u64 v[28:29], s[2:3], 0, v[90:91]
	v_lshl_add_u64 v[28:29], v[164:165], 1, v[28:29]
	global_store_dwordx4 v[28:29], v[24:27], off sc1
	s_nop 1
	s_waitcnt vmcnt(2)
	v_lshlrev_b32_e32 v24, 16, v72
	v_and_b32_e32 v25, 0xffff0000, v72
	v_lshlrev_b32_e32 v26, 16, v73
	v_and_b32_e32 v27, 0xffff0000, v73
	v_lshlrev_b32_e32 v30, 16, v74
	v_and_b32_e32 v31, 0xffff0000, v74
	v_lshlrev_b32_e32 v32, 16, v75
	v_and_b32_e32 v33, 0xffff0000, v75
	v_pk_add_f32 v[22:23], v[22:23], v[26:27]
	v_pk_add_f32 v[20:21], v[20:21], v[24:25]
	v_pk_add_f32 v[24:25], v[18:19], v[32:33]
	v_pk_add_f32 v[18:19], v[16:17], v[30:31]
	v_mul_f32_e32 v16, v21, v21
	v_mul_f32_e32 v17, v23, v23
	v_fmac_f32_e32 v16, v20, v20
	v_fmac_f32_e32 v17, v22, v22
	v_add_f32_e32 v16, v16, v17
	v_mul_f32_e32 v17, v19, v19
	v_mul_f32_e32 v26, v25, v25
	v_fmac_f32_e32 v17, v18, v18
	v_fmac_f32_e32 v26, v24, v24
	v_add_f32_e32 v17, v17, v26
	v_add_f32_e32 v16, v16, v17
	v_add_f32_e32 v26, v34, v16
	v_cvt_pk_bf16_f32 v16, v20, v21
	v_cvt_pk_bf16_f32 v17, v22, v23
	ds_swizzle_b32 v22, v26 offset:swizzle(SWAP,16)
	s_mov_b64 s[2:3], 0x100
	v_cvt_pk_bf16_f32 v18, v18, v19
	v_cvt_pk_bf16_f32 v19, v24, v25
	v_lshl_add_u64 v[20:21], v[28:29], 0, s[2:3]
	global_store_dwordx4 v[20:21], v[16:19], off sc1
	s_nop 1
	s_waitcnt lgkmcnt(0)
	v_add_f32_e32 v16, v26, v22
	v_mov_b32_e32 v17, v16
	s_nop 1
	v_permlane32_swap_b32_e32 v16, v17
	s_and_saveexec_b64 s[20:21], s[0:1]
	v_add_f32_e32 v16, v16, v17
	ds_write_b32 v186, v16 offset:2560
	s_or_b64 exec, exec, s[20:21]
	s_waitcnt vmcnt(1)
	v_lshlrev_b32_e32 v16, 16, v68
	v_and_b32_e32 v17, 0xffff0000, v68
	v_lshlrev_b32_e32 v18, 16, v69
	v_and_b32_e32 v19, 0xffff0000, v69
	v_lshlrev_b32_e32 v20, 16, v70
	v_and_b32_e32 v21, 0xffff0000, v70
	v_lshlrev_b32_e32 v22, 16, v71
	v_and_b32_e32 v23, 0xffff0000, v71
	v_pk_add_f32 v[14:15], v[14:15], v[18:19]
	v_pk_add_f32 v[12:13], v[12:13], v[16:17]
	v_pk_add_f32 v[16:17], v[10:11], v[22:23]
	v_pk_add_f32 v[10:11], v[8:9], v[20:21]
	v_mul_f32_e32 v8, v13, v13
	v_mul_f32_e32 v9, v15, v15
	v_fmac_f32_e32 v8, v12, v12
	v_fmac_f32_e32 v9, v14, v14
	v_add_f32_e32 v8, v8, v9
	v_mul_f32_e32 v9, v11, v11
	v_mul_f32_e32 v18, v17, v17
	v_fmac_f32_e32 v9, v10, v10
	v_fmac_f32_e32 v18, v16, v16
	v_readlane_b32 s2, v252, 8
	v_add_f32_e32 v9, v9, v18
	v_readlane_b32 s3, v252, 9
	v_add_f32_e32 v18, v8, v9
	v_cvt_pk_bf16_f32 v8, v12, v13
	v_cvt_pk_bf16_f32 v9, v14, v15
	v_cvt_pk_bf16_f32 v10, v10, v11
	v_cvt_pk_bf16_f32 v11, v16, v17
	s_nop 0
	v_lshl_add_u64 v[12:13], s[2:3], 0, v[88:89]
	v_lshl_add_u64 v[12:13], v[164:165], 1, v[12:13]
	global_store_dwordx4 v[12:13], v[8:11], off sc1
	s_nop 1
	s_waitcnt vmcnt(0)
	v_lshlrev_b32_e32 v8, 16, v64
	v_and_b32_e32 v9, 0xffff0000, v64
	v_lshlrev_b32_e32 v10, 16, v65
	v_and_b32_e32 v11, 0xffff0000, v65
	v_lshlrev_b32_e32 v14, 16, v66
	v_and_b32_e32 v15, 0xffff0000, v66
	v_lshlrev_b32_e32 v16, 16, v67
	v_and_b32_e32 v17, 0xffff0000, v67
	v_pk_add_f32 v[6:7], v[6:7], v[10:11]
	v_pk_add_f32 v[4:5], v[4:5], v[8:9]
	v_pk_add_f32 v[8:9], v[2:3], v[16:17]
	v_pk_add_f32 v[2:3], v[0:1], v[14:15]
	v_mul_f32_e32 v0, v5, v5
	v_mul_f32_e32 v1, v7, v7
	v_fmac_f32_e32 v0, v4, v4
	v_fmac_f32_e32 v1, v6, v6
	v_add_f32_e32 v0, v0, v1
	v_mul_f32_e32 v1, v3, v3
	v_mul_f32_e32 v10, v9, v9
	v_fmac_f32_e32 v1, v2, v2
	v_fmac_f32_e32 v10, v8, v8
	v_add_f32_e32 v1, v1, v10
	v_add_f32_e32 v0, v0, v1
	v_add_f32_e32 v10, v18, v0
	v_cvt_pk_bf16_f32 v0, v4, v5
	v_cvt_pk_bf16_f32 v1, v6, v7
	ds_swizzle_b32 v6, v10 offset:swizzle(SWAP,16)
	s_mov_b64 s[2:3], 0x100
	v_cvt_pk_bf16_f32 v2, v2, v3
	v_cvt_pk_bf16_f32 v3, v8, v9
	v_lshl_add_u64 v[4:5], v[12:13], 0, s[2:3]
	global_store_dwordx4 v[4:5], v[0:3], off sc1
	s_nop 1
	s_waitcnt lgkmcnt(0)
	v_add_f32_e32 v0, v10, v6
	v_mov_b32_e32 v1, v0
	s_nop 1
	v_permlane32_swap_b32_e32 v0, v1
	s_and_saveexec_b64 s[20:21], s[0:1]
	v_add_f32_e32 v0, v0, v1
	ds_write_b32 v186, v0 offset:2816
	s_or_b64 exec, exec, s[20:21]
	s_waitcnt lgkmcnt(0)
	s_barrier
	s_and_saveexec_b64 s[20:21], s[10:11]
	s_cbranch_execz .LBB0_1237
	v_add_u32_e32 v0, s5, v182
	v_ashrrev_i32_e32 v1, 31, v0
	v_readlane_b32 s2, v251, 32
	v_lshlrev_b64 v[0:1], 6, v[0:1]
	v_readlane_b32 s3, v251, 33
	s_nop 1
	v_lshl_add_u64 v[0:1], s[2:3], 0, v[0:1]
	s_lshl_b32 s2, s41, 2
	s_ashr_i32 s3, s2, 31
	v_lshl_add_u64 v[4:5], s[2:3], 2, v[0:1]
	ds_read_b128 v[0:3], v185
	s_waitcnt lgkmcnt(0)
	global_store_dwordx4 v[4:5], v[0:3], off sc1
	s_nop 1

; template <int M> __device__ __forceinline__ float swz_xor(float v) { return __int_as_float(__builtin_amdgcn_ds_swizzle(__float_as_int(v), (M << 10) | 0x1f)); }
; __device__ __forceinline__ float half_sum(float v) { auto rr = __builtin_amdgcn_permlane32_swap(__float_as_uint(v), __float_as_uint(v), false, false); return __uint_as_float(rr[0]) + __uint_as_float(rr[1]); }
; __device__ __forceinline__ void row_rscale8(const float* part, const int (&rows)[2][4], int fq, float (&rs)[2][4]) {
;     f32x4 v[2][4];
; #pragma unroll
;     for (int ai = 0; ai < 2; ++ai)
; #pragma unroll
;         for (int m = 0; m < 4; ++m) v[ai][m] = *(const f32x4*)(part + (size_t)rows[ai][m] * 16 + fq * 4);
; #pragma unroll
;     for (int ai = 0; ai < 2; ++ai)
; #pragma unroll
;         for (int m = 0; m < 4; ++m) { float s = (v[ai][m][0] + v[ai][m][1]) + (v[ai][m][2] + v[ai][m][3]); s += swz_xor<16>(s); s = half_sum(s); rs[ai][m] = __builtin_amdgcn_rcpf(sqrtf(s * (1.0f / DM) + EPS)); }
; }
;     __device__ __forceinline__ bool operator()(f32x4 (&acc)[2][2][4][2], const pg8::Unit& u, int wr, int wc, int fr, int fq) const {
;     ...
;         float rs_[2][4]; { int rows_[2][4];
; #pragma unroll
;             for (int ai = 0; ai < 2; ++ai)
; #pragma unroll
;                 for (int m = 0; m < 4; ++m) { const int rl = ai * 128 + wr * 64 + m * 16 + fr; rows_[ai][m] = (rl < u.nvalid) ? u.gidx[rl] : 0; }
;             row_rscale8(part, rows_, fq, rs_); }
.LBB0_1499:
	v_lshlrev_b32_e32 v140, 2, v162
	v_mov_b32_e32 v216, 0
	v_mov_b32_e32 v218, 0
	v_mov_b32_e32 v220, 0
	v_mov_b32_e32 v222, 0
	v_mov_b32_e32 v224, 0
	v_mov_b32_e32 v226, 0
	v_mov_b32_e32 v228, 0
	v_mov_b32_e32 v232, 0
	v_cmp_gt_i32_e32 vcc, s36, v162
	s_and_saveexec_b64 s[4:5], vcc
	global_load_dword v216, v140, s[6:7]
	s_or_b64 exec, exec, s[4:5]
	v_cmp_gt_i32_e32 vcc, s36, v171
	s_and_saveexec_b64 s[4:5], vcc
	global_load_dword v218, v140, s[6:7] offset:64
	s_or_b64 exec, exec, s[4:5]
	v_cmp_gt_i32_e32 vcc, s36, v183
	s_and_saveexec_b64 s[4:5], vcc
	global_load_dword v220, v140, s[6:7] offset:128
	s_or_b64 exec, exec, s[4:5]
	v_cmp_gt_i32_e32 vcc, s36, v201
	s_and_saveexec_b64 s[4:5], vcc
	global_load_dword v222, v140, s[6:7] offset:192
	s_or_b64 exec, exec, s[4:5]
	v_cmp_gt_i32_e32 vcc, s36, v213
	s_and_saveexec_b64 s[4:5], vcc
	global_load_dword v224, v140, s[6:7] offset:512
	s_or_b64 exec, exec, s[4:5]
	v_cmp_gt_i32_e32 vcc, s36, v186
	s_and_saveexec_b64 s[4:5], vcc
	global_load_dword v226, v140, s[6:7] offset:576
	s_or_b64 exec, exec, s[4:5]
	v_cmp_gt_i32_e32 vcc, s36, v187
	s_and_saveexec_b64 s[4:5], vcc
	global_load_dword v228, v140, s[6:7] offset:640
	s_or_b64 exec, exec, s[4:5]
	v_cmp_gt_i32_e32 vcc, s36, v188
	s_and_saveexec_b64 s[4:5], vcc
	global_load_dword v232, v140, s[6:7] offset:704
	s_or_b64 exec, exec, s[4:5]
	v_mov_b64_e32 v[236:237], v[246:247]
	v_mov_b64_e32 v[230:231], v[184:185]
	s_waitcnt vmcnt(0)
	v_ashrrev_i32_e32 v217, 31, v216
	v_ashrrev_i32_e32 v219, 31, v218
	v_ashrrev_i32_e32 v221, 31, v220
	v_ashrrev_i32_e32 v223, 31, v222
	v_ashrrev_i32_e32 v225, 31, v224
	v_ashrrev_i32_e32 v227, 31, v226
	v_ashrrev_i32_e32 v229, 31, v228
	v_ashrrev_i32_e32 v233, 31, v232
	v_lshlrev_b64 v[130:131], 6, v[216:217]
	v_lshlrev_b64 v[128:129], 6, v[218:219]
	v_lshlrev_b64 v[134:135], 6, v[220:221]
	v_lshlrev_b64 v[132:133], 6, v[222:223]
	v_lshlrev_b64 v[138:139], 6, v[224:225]
	v_lshlrev_b64 v[136:137], 6, v[226:227]
	v_lshlrev_b64 v[178:179], 6, v[228:229]
	v_lshlrev_b64 v[176:177], 6, v[232:233]
	v_lshl_add_u64 v[130:131], v[166:167], 0, v[130:131]
	global_load_dwordx4 v[190:193], v[130:131], off
	v_lshl_add_u64 v[128:129], v[166:167], 0, v[128:129]
	global_load_dwordx4 v[202:205], v[128:129], off
	v_lshl_add_u64 v[128:129], v[166:167], 0, v[134:135]
	global_load_dwordx4 v[148:151], v[128:129], off
	v_lshl_add_u64 v[128:129], v[166:167], 0, v[132:133]
	global_load_dwordx4 v[144:147], v[128:129], off
	v_lshl_add_u64 v[128:129], v[166:167], 0, v[138:139]
	global_load_dwordx4 v[140:143], v[128:129], off
	v_lshl_add_u64 v[128:129], v[166:167], 0, v[136:137]
	global_load_dwordx4 v[136:139], v[128:129], off
	v_lshl_add_u64 v[128:129], v[166:167], 0, v[178:179]
	global_load_dwordx4 v[132:135], v[128:129], off
	v_lshl_add_u64 v[128:129], v[166:167], 0, v[176:177]
	s_mov_b32 s2, 0xf800000
	global_load_dwordx4 v[128:131], v[128:129], off
	v_lshl_or_b32 v174, s45, 7, v189
	s_waitcnt vmcnt(0)
	v_mov_b32_e32 v176, v191
	v_mov_b32_e32 v177, v192
	v_mov_b32_e32 v191, v193
	v_pk_add_f32 v[176:177], v[176:177], v[190:191]
	v_mov_b32_e32 v178, v203
	v_add_f32_e32 v160, v176, v177
	v_mov_b32_e32 v165, v160
	v_mov_b32_e32 v179, v204
	v_mov_b32_e32 v203, v205
	v_pk_add_f32 v[178:179], v[178:179], v[202:203]
	s_waitcnt lgkmcnt(0)
	s_nop 1
	v_permlane16_swap_b32_e32 v165, v160
	v_add_f32_e32 v160, v160, v165
	v_mov_b32_e32 v165, v160
	s_nop 1
	v_permlane32_swap_b32_e32 v160, v165
	v_add_f32_e32 v160, v160, v165
	v_fmamk_f32 v160, v160, 0x3a800000, v212
	v_cmp_gt_f32_e32 vcc, s2, v160
	v_mul_f32_e32 v165, 0x4f800000, v160
	s_nop 0
	v_cndmask_b32_e32 v160, v160, v165, vcc
	v_sqrt_f32_e32 v165, v160
	s_nop 0
	v_add_u32_e32 v173, -1, v165
	v_fma_f32 v175, -v173, v165, v160
	v_cmp_ge_f32_e64 s[4:5], 0, v175
	v_add_u32_e32 v175, 1, v165
	s_nop 0
	v_cndmask_b32_e64 v173, v165, v173, s[4:5]
	v_fma_f32 v165, -v175, v165, v160
	v_cmp_lt_f32_e64 s[4:5], 0, v165
	s_nop 1
	v_cndmask_b32_e64 v165, v173, v175, s[4:5]
	v_mul_f32_e32 v173, 0x37800000, v165
	v_cndmask_b32_e32 v165, v165, v173, vcc
	v_cmp_class_f32_e32 vcc, v160, v248
	s_nop 1
	v_cndmask_b32_e32 v160, v165, v160, vcc
	v_rcp_f32_e32 v176, v160
	v_add_f32_e32 v160, v178, v179
	v_mov_b32_e32 v165, v160
	v_mov_b32_e32 v178, v149
	v_mov_b32_e32 v179, v150
	v_mov_b32_e32 v149, v151
	v_pk_add_f32 v[148:149], v[178:179], v[148:149]
	s_waitcnt lgkmcnt(0)
	s_nop 1
	v_permlane16_swap_b32_e32 v165, v160
	v_add_f32_e32 v160, v160, v165
	v_mov_b32_e32 v165, v160
	s_nop 1
	v_permlane32_swap_b32_e32 v160, v165
	v_add_f32_e32 v160, v160, v165
	v_fmamk_f32 v160, v160, 0x3a800000, v212
	v_cmp_gt_f32_e32 vcc, s2, v160
	v_mul_f32_e32 v165, 0x4f800000, v160
	v_add_f32_e32 v148, v148, v149
	v_cndmask_b32_e32 v160, v160, v165, vcc
	v_sqrt_f32_e32 v165, v160
	v_mov_b32_e32 v149, v148
	v_add_u32_e32 v173, -1, v165
	v_fma_f32 v175, -v173, v165, v160
	v_cmp_ge_f32_e64 s[4:5], 0, v175
	v_add_u32_e32 v175, 1, v165
	s_waitcnt lgkmcnt(0)
; template <int M> __device__ __forceinline__ float swz_xor(float v) { return __int_as_float(__builtin_amdgcn_ds_swizzle(__float_as_int(v), (M << 10) | 0x1f)); }
; __device__ __forceinline__ float half_sum(float v) { auto rr = __builtin_amdgcn_permlane32_swap(__float_as_uint(v), __float_as_uint(v), false, false); return __uint_as_float(rr[0]) + __uint_as_float(rr[1]); }
; __device__ __forceinline__ void row_rscale8(const float* part, const int (&rows)[2][4], int fq, float (&rs)[2][4]) {
;     ...
; #pragma unroll
;     for (int ai = 0; ai < 2; ++ai)
; #pragma unroll
;         for (int m = 0; m < 4; ++m) { float s = (v[ai][m][0] + v[ai][m][1]) + (v[ai][m][2] + v[ai][m][3]); s += swz_xor<16>(s); s = half_sum(s); rs[ai][m] = __builtin_amdgcn_rcpf(sqrtf(s * (1.0f / DM) + EPS)); }
; }
	s_nop 1
	v_permlane16_swap_b32_e32 v149, v148
	v_add_f32_e32 v148, v148, v149
	v_cndmask_b32_e64 v173, v165, v173, s[4:5]
	v_fma_f32 v165, -v175, v165, v160
	v_cmp_lt_f32_e64 s[4:5], 0, v165
	v_mov_b32_e32 v149, v148
	s_nop 1
	v_permlane32_swap_b32_e32 v148, v149
	v_cndmask_b32_e64 v165, v173, v175, s[4:5]
	v_mul_f32_e32 v173, 0x37800000, v165
	v_add_f32_e32 v148, v148, v149
	v_cndmask_b32_e32 v165, v165, v173, vcc
	v_cmp_class_f32_e32 vcc, v160, v248
	v_fmamk_f32 v148, v148, 0x3a800000, v212
	v_mul_f32_e32 v149, 0x4f800000, v148
	v_cndmask_b32_e32 v160, v165, v160, vcc
	v_cmp_gt_f32_e32 vcc, s2, v148
	v_rcp_f32_e32 v160, v160
	v_ashrrev_i32_e32 v175, 31, v174
	v_cndmask_b32_e32 v148, v148, v149, vcc
	v_sqrt_f32_e32 v149, v148
	s_nop 0
	v_add_u32_e32 v150, -1, v149
	v_fma_f32 v151, -v150, v149, v148
	v_cmp_ge_f32_e64 s[4:5], 0, v151
	v_add_u32_e32 v151, 1, v149
	s_nop 0
	v_cndmask_b32_e64 v150, v149, v150, s[4:5]
	v_fma_f32 v149, -v151, v149, v148
	v_cmp_lt_f32_e64 s[4:5], 0, v149
	s_nop 1
	v_cndmask_b32_e64 v149, v150, v151, s[4:5]
	v_mul_f32_e32 v150, 0x37800000, v149
	v_cndmask_b32_e32 v149, v149, v150, vcc
	v_mov_b32_e32 v150, v145
	v_mov_b32_e32 v151, v146
	v_mov_b32_e32 v145, v147
	v_pk_add_f32 v[144:145], v[150:151], v[144:145]
	v_cmp_class_f32_e32 vcc, v148, v248
	v_add_f32_e32 v144, v144, v145
	v_mov_b32_e32 v145, v144
	v_cndmask_b32_e32 v148, v149, v148, vcc
	v_rcp_f32_e32 v148, v148
	s_waitcnt lgkmcnt(0)
	s_nop 1
	v_permlane16_swap_b32_e32 v145, v144
	v_add_f32_e32 v144, v144, v145
	v_mov_b32_e32 v145, v144
	s_nop 1
	v_permlane32_swap_b32_e32 v144, v145
	v_add_f32_e32 v144, v144, v145
	v_fmamk_f32 v144, v144, 0x3a800000, v212
	v_cmp_gt_f32_e32 vcc, s2, v144
	v_mul_f32_e32 v145, 0x4f800000, v144
	s_nop 0
	v_cndmask_b32_e32 v144, v144, v145, vcc
	v_sqrt_f32_e32 v145, v144
	s_nop 0
	v_add_u32_e32 v146, -1, v145
	v_fma_f32 v147, -v146, v145, v144
	v_cmp_ge_f32_e64 s[4:5], 0, v147
	v_add_u32_e32 v147, 1, v145
	s_nop 0
	v_cndmask_b32_e64 v146, v145, v146, s[4:5]
	v_fma_f32 v145, -v147, v145, v144
	v_cmp_lt_f32_e64 s[4:5], 0, v145
	s_nop 1
	v_cndmask_b32_e64 v145, v146, v147, s[4:5]
	v_mul_f32_e32 v146, 0x37800000, v145
	v_cndmask_b32_e32 v145, v145, v146, vcc
	v_mov_b32_e32 v146, v141
	v_mov_b32_e32 v147, v142
	v_mov_b32_e32 v141, v143
	v_pk_add_f32 v[140:141], v[146:147], v[140:141]
	v_cmp_class_f32_e32 vcc, v144, v248
	v_add_f32_e32 v140, v140, v141
	v_mov_b32_e32 v141, v140
	v_cndmask_b32_e32 v144, v145, v144, vcc
	v_rcp_f32_e32 v144, v144
	s_waitcnt lgkmcnt(0)
	s_nop 1
	v_permlane16_swap_b32_e32 v141, v140
	v_add_f32_e32 v140, v140, v141
	v_mov_b32_e32 v141, v140
	s_nop 1
	v_permlane32_swap_b32_e32 v140, v141
	v_add_f32_e32 v140, v140, v141
	v_fmamk_f32 v140, v140, 0x3a800000, v212
	v_cmp_gt_f32_e32 vcc, s2, v140
	v_mul_f32_e32 v141, 0x4f800000, v140
	s_nop 0
	v_cndmask_b32_e32 v140, v140, v141, vcc
	v_sqrt_f32_e32 v141, v140
	s_nop 0
	v_add_u32_e32 v142, -1, v141
	v_fma_f32 v143, -v142, v141, v140
	v_cmp_ge_f32_e64 s[4:5], 0, v143
	v_add_u32_e32 v143, 1, v141
	s_nop 0
	v_cndmask_b32_e64 v142, v141, v142, s[4:5]
	v_fma_f32 v141, -v143, v141, v140
	v_cmp_lt_f32_e64 s[4:5], 0, v141
	s_nop 1
	v_cndmask_b32_e64 v141, v142, v143, s[4:5]
	v_mul_f32_e32 v142, 0x37800000, v141
	v_cndmask_b32_e32 v141, v141, v142, vcc
	v_mov_b32_e32 v142, v137
	v_mov_b32_e32 v143, v138
	v_mov_b32_e32 v137, v139
	v_pk_add_f32 v[136:137], v[142:143], v[136:137]
	v_cmp_class_f32_e32 vcc, v140, v248
	v_add_f32_e32 v136, v136, v137
	v_mov_b32_e32 v137, v136
	v_cndmask_b32_e32 v140, v141, v140, vcc
	v_rcp_f32_e32 v140, v140
	s_waitcnt lgkmcnt(0)
	s_nop 1
	v_permlane16_swap_b32_e32 v137, v136
	v_add_f32_e32 v136, v136, v137
	v_mov_b32_e32 v137, v136
	s_nop 1
	v_permlane32_swap_b32_e32 v136, v137
	v_add_f32_e32 v136, v136, v137
	v_fmamk_f32 v136, v136, 0x3a800000, v212
	v_cmp_gt_f32_e32 vcc, s2, v136
	v_mul_f32_e32 v137, 0x4f800000, v136
	s_nop 0
	v_cndmask_b32_e32 v136, v136, v137, vcc
	v_sqrt_f32_e32 v137, v136
	s_nop 0
	v_add_u32_e32 v138, -1, v137
	v_fma_f32 v139, -v138, v137, v136
	v_cmp_ge_f32_e64 s[4:5], 0, v139
	v_add_u32_e32 v139, 1, v137
	s_nop 0
	v_cndmask_b32_e64 v138, v137, v138, s[4:5]
	v_fma_f32 v137, -v139, v137, v136
	v_cmp_lt_f32_e64 s[4:5], 0, v137
	s_nop 1
	v_cndmask_b32_e64 v137, v138, v139, s[4:5]
	v_mul_f32_e32 v138, 0x37800000, v137
	v_cndmask_b32_e32 v137, v137, v138, vcc
	v_mov_b32_e32 v138, v133
	v_mov_b32_e32 v139, v134
	v_mov_b32_e32 v133, v135
	v_pk_add_f32 v[132:133], v[138:139], v[132:133]
	v_cmp_class_f32_e32 vcc, v136, v248
	v_add_f32_e32 v132, v132, v133
	v_mov_b32_e32 v133, v132
	v_cndmask_b32_e32 v136, v137, v136, vcc
	v_rcp_f32_e32 v136, v136
	s_waitcnt lgkmcnt(0)
	s_nop 1
	v_permlane16_swap_b32_e32 v133, v132
	v_add_f32_e32 v132, v132, v133
	v_mov_b32_e32 v133, v132
	s_nop 1
	v_permlane32_swap_b32_e32 v132, v133
	v_add_f32_e32 v132, v132, v133
	v_fmamk_f32 v132, v132, 0x3a800000, v212
	v_cmp_gt_f32_e32 vcc, s2, v132
	v_mul_f32_e32 v133, 0x4f800000, v132
	s_nop 0
	v_cndmask_b32_e32 v132, v132, v133, vcc
	v_sqrt_f32_e32 v133, v132
	s_nop 0
	v_add_u32_e32 v134, -1, v133
	v_fma_f32 v135, -v134, v133, v132
	v_cmp_ge_f32_e64 s[4:5], 0, v135
	v_add_u32_e32 v135, 1, v133
	s_nop 0
	v_cndmask_b32_e64 v134, v133, v134, s[4:5]
	v_fma_f32 v133, -v135, v133, v132
	v_cmp_lt_f32_e64 s[4:5], 0, v133
	s_nop 1
	v_cndmask_b32_e64 v133, v134, v135, s[4:5]
	v_mul_f32_e32 v134, 0x37800000, v133
	v_cndmask_b32_e32 v133, v133, v134, vcc
	v_mov_b32_e32 v134, v129
	v_mov_b32_e32 v135, v130
	v_mov_b32_e32 v129, v131
	v_pk_add_f32 v[128:129], v[134:135], v[128:129]
	v_cmp_class_f32_e32 vcc, v132, v248
	v_add_f32_e32 v128, v128, v129
	v_mov_b32_e32 v129, v128
	v_cndmask_b32_e32 v132, v133, v132, vcc
	v_rcp_f32_e32 v132, v132
	s_waitcnt lgkmcnt(0)
; __device__ __forceinline__ float sigmoidf_(float x) { return rcpf_(1.0f + __expf(-x)); }
;     __device__ __forceinline__ bool operator()(f32x4 (&acc)[2][2][4][2], const pg8::Unit& u, int wr, int wc, int fr, int fq) const {
;     ...
; #pragma unroll
;         for (int ai = 0; ai < 2; ++ai)
; #pragma unroll
;             for (int m = 0; m < 4; ++m) { const int rl = ai * 128 + wr * 64 + m * 16 + fr; const float s = rs_[ai][m];
;                 f32x4 o[2];
; #pragma unroll
;                 for (int n = 0; n < 2; ++n) { const f32x4 g = acc[ai][0][m][n] * s, up = acc[ai][1][m][n] * s;
; #pragma unroll
;                     for (int j = 0; j < 4; ++j) o[n][j] = g[j] * sigmoidf_(g[j]) * up[j]; }
;                 st8_wt(ACT + (size_t)(u.pm * 256 + rl) * DE + colb, o[0], o[1]); }
	s_nop 1
	v_permlane16_swap_b32_e32 v129, v128
	v_add_f32_e32 v128, v128, v129
	v_mov_b32_e32 v129, v128
	s_nop 1
	v_permlane32_swap_b32_e32 v128, v129
	v_add_f32_e32 v128, v128, v129
	v_fmamk_f32 v128, v128, 0x3a800000, v212
	v_cmp_gt_f32_e32 vcc, s2, v128
	v_mul_f32_e32 v129, 0x4f800000, v128
	v_readlane_b32 s2, v251, 54
	v_cndmask_b32_e32 v128, v128, v129, vcc
	v_sqrt_f32_e32 v129, v128
	v_readlane_b32 s3, v251, 55
	v_add_u32_e32 v130, -1, v129
	v_fma_f32 v131, -v130, v129, v128
	v_cmp_ge_f32_e64 s[4:5], 0, v131
	v_add_u32_e32 v131, 1, v129
	s_nop 0
	v_cndmask_b32_e64 v130, v129, v130, s[4:5]
	v_fma_f32 v129, -v131, v129, v128
	v_cmp_lt_f32_e64 s[4:5], 0, v129
	s_nop 1
	v_cndmask_b32_e64 v129, v130, v131, s[4:5]
	v_mul_f32_e32 v130, 0x37800000, v129
	v_cndmask_b32_e32 v129, v129, v130, vcc
	v_mov_b32_e32 v130, v68
	v_mov_b32_e32 v131, v104
	v_cmp_class_f32_e32 vcc, v128, v248
	v_pk_mul_f32 v[130:131], v[130:131], v[176:177] op_sel_hi:[1,0]
	s_lshl_b32 s4, s44, 8
	v_cndmask_b32_e32 v128, v129, v128, vcc
	v_mul_f32_e32 v129, 0xbfb8aa3b, v131
	v_exp_f32_e32 v129, v129
	s_movk_i32 s5, 0x600
	v_rcp_f32_e32 v128, v128
	v_add_f32_e32 v129, 1.0, v129
	v_rcp_f32_e32 v129, v129
	s_nop 0
	s_nop 0
	v_mul_f32_e32 v129, v131, v129
	v_mul_f32_e32 v129, v130, v129
	v_mov_b32_e32 v130, v69
	v_mov_b32_e32 v131, v105
	v_pk_mul_f32 v[130:131], v[130:131], v[176:177] op_sel_hi:[1,0]
	s_nop 0
	v_mul_f32_e32 v133, 0xbfb8aa3b, v131
	v_exp_f32_e32 v133, v133
	s_nop 0
	v_add_f32_e32 v133, 1.0, v133
	v_rcp_f32_e32 v133, v133
	s_nop 0
	s_nop 0
	v_mul_f32_e32 v131, v131, v133
	v_mul_f32_e32 v133, v130, v131
	v_mov_b32_e32 v130, v70
	v_mov_b32_e32 v131, v106
	v_pk_mul_f32 v[130:131], v[130:131], v[176:177] op_sel_hi:[1,0]
	s_nop 0
	v_mul_f32_e32 v134, 0xbfb8aa3b, v131
	v_exp_f32_e32 v134, v134
	s_nop 0
	v_add_f32_e32 v134, 1.0, v134
	v_rcp_f32_e32 v134, v134
	s_nop 0
	s_nop 0
	v_mul_f32_e32 v131, v131, v134
	v_mul_f32_e32 v137, v130, v131
	v_mov_b32_e32 v130, v71
	v_mov_b32_e32 v131, v107
	v_pk_mul_f32 v[130:131], v[130:131], v[176:177] op_sel_hi:[1,0]
	s_nop 0
	v_mul_f32_e32 v134, 0xbfb8aa3b, v131
	v_exp_f32_e32 v134, v134
	s_nop 0
	v_add_f32_e32 v134, 1.0, v134
	v_rcp_f32_e32 v134, v134
	s_nop 0
	s_nop 0
	v_mul_f32_e32 v131, v131, v134
	v_mul_f32_e32 v141, v130, v131
	v_mov_b32_e32 v130, v64
	v_mov_b32_e32 v131, v96
	v_pk_mul_f32 v[130:131], v[130:131], v[176:177] op_sel_hi:[1,0]
	s_nop 0
	v_mul_f32_e32 v134, 0xbfb8aa3b, v131
	v_exp_f32_e32 v134, v134
	s_nop 0
	v_add_f32_e32 v134, 1.0, v134
	v_rcp_f32_e32 v134, v134
	s_nop 0
	s_nop 0
	v_mul_f32_e32 v131, v131, v134
	v_mul_f32_e32 v142, v130, v131
	v_mov_b32_e32 v130, v65
	v_mov_b32_e32 v131, v97
	v_pk_mul_f32 v[130:131], v[130:131], v[176:177] op_sel_hi:[1,0]
	s_nop 0
	v_mul_f32_e32 v134, 0xbfb8aa3b, v131
	v_exp_f32_e32 v134, v134
	s_nop 0
	v_add_f32_e32 v134, 1.0, v134
	v_rcp_f32_e32 v134, v134
	s_nop 0
	s_nop 0
	v_mul_f32_e32 v131, v131, v134
	v_mul_f32_e32 v143, v130, v131
	v_mov_b32_e32 v130, v66
	v_mov_b32_e32 v131, v98
	v_pk_mul_f32 v[130:131], v[130:131], v[176:177] op_sel_hi:[1,0]
	s_nop 0
	v_mul_f32_e32 v134, 0xbfb8aa3b, v131
	v_exp_f32_e32 v134, v134
	s_nop 0
	v_add_f32_e32 v134, 1.0, v134
	v_rcp_f32_e32 v134, v134
	s_nop 0
	s_nop 0
	v_mul_f32_e32 v131, v131, v134
	v_mul_f32_e32 v145, v130, v131
	v_mov_b32_e32 v130, v67
	v_mov_b32_e32 v131, v99
	v_pk_mul_f32 v[130:131], v[130:131], v[176:177] op_sel_hi:[1,0]
	s_nop 0
	v_mul_f32_e32 v134, 0xbfb8aa3b, v131
	v_exp_f32_e32 v134, v134
	s_nop 0
	v_add_f32_e32 v134, 1.0, v134
	v_rcp_f32_e32 v134, v134
	s_nop 0
	s_nop 0
	v_mul_f32_e32 v131, v131, v134
	v_mul_f32_e32 v146, v130, v131
	v_add_u32_e32 v134, s4, v162
	v_mov_b64_e32 v[130:131], s[2:3]
	v_mad_i64_i32 v[138:139], s[2:3], v134, s5, v[130:131]
	v_lshlrev_b64 v[134:135], 1, v[174:175]
	v_lshl_add_u64 v[138:139], v[138:139], 0, v[134:135]
	v_cvt_pk_bf16_f32 v174, v129, v133
	v_cvt_pk_bf16_f32 v175, v137, v141
	v_cvt_pk_bf16_f32 v176, v142, v143
	v_cvt_pk_bf16_f32 v177, v145, v146
	s_nop 0
	global_store_dwordx4 v[138:139], v[174:177], off sc1
	s_nop 1
	v_mov_b32_e32 v138, v60
	v_mov_b32_e32 v139, v92
	v_pk_mul_f32 v[138:139], v[138:139], v[160:161] op_sel_hi:[1,0]
	s_nop 0
	v_mul_f32_e32 v129, 0xbfb8aa3b, v139
	v_exp_f32_e32 v129, v129
	s_nop 0
	v_add_f32_e32 v129, 1.0, v129
	v_rcp_f32_e32 v129, v129
	s_nop 0
	s_nop 0
	v_mul_f32_e32 v129, v139, v129
	v_mul_f32_e32 v129, v138, v129
	v_mov_b32_e32 v138, v61
	v_mov_b32_e32 v139, v93
	v_pk_mul_f32 v[138:139], v[138:139], v[160:161] op_sel_hi:[1,0]
	s_nop 0
	v_mul_f32_e32 v133, 0xbfb8aa3b, v139
	v_exp_f32_e32 v133, v133
	s_nop 0
	v_add_f32_e32 v133, 1.0, v133
	v_rcp_f32_e32 v133, v133
	s_nop 0
	s_nop 0
	v_mul_f32_e32 v133, v139, v133
	v_mul_f32_e32 v133, v138, v133
	v_mov_b32_e32 v138, v62
	v_mov_b32_e32 v139, v94
	v_pk_mul_f32 v[138:139], v[138:139], v[160:161] op_sel_hi:[1,0]
	s_nop 0
	v_mul_f32_e32 v137, 0xbfb8aa3b, v139
	v_exp_f32_e32 v137, v137
	s_nop 0
	v_add_f32_e32 v137, 1.0, v137
	v_rcp_f32_e32 v137, v137
	s_nop 0
	s_nop 0
	v_mul_f32_e32 v137, v139, v137
	v_mul_f32_e32 v137, v138, v137
	v_mov_b32_e32 v138, v63
	v_mov_b32_e32 v139, v95
	v_pk_mul_f32 v[138:139], v[138:139], v[160:161] op_sel_hi:[1,0]
	s_nop 0
	v_mul_f32_e32 v141, 0xbfb8aa3b, v139
	v_exp_f32_e32 v141, v141
	s_nop 0
	v_add_f32_e32 v141, 1.0, v141
	v_rcp_f32_e32 v141, v141
	s_nop 0
	s_nop 0
	v_mul_f32_e32 v139, v139, v141
	v_mul_f32_e32 v141, v138, v139
	v_mov_b32_e32 v138, v56
	v_mov_b32_e32 v139, v88
	v_pk_mul_f32 v[138:139], v[138:139], v[160:161] op_sel_hi:[1,0]
	s_nop 0
	v_mul_f32_e32 v142, 0xbfb8aa3b, v139
	v_exp_f32_e32 v142, v142
	s_nop 0
	v_add_f32_e32 v142, 1.0, v142
; __device__ __forceinline__ float sigmoidf_(float x) { return rcpf_(1.0f + __expf(-x)); }
;     __device__ __forceinline__ bool operator()(f32x4 (&acc)[2][2][4][2], const pg8::Unit& u, int wr, int wc, int fr, int fq) const {
;     ...
; #pragma unroll
;         for (int ai = 0; ai < 2; ++ai)
; #pragma unroll
;             for (int m = 0; m < 4; ++m) { const int rl = ai * 128 + wr * 64 + m * 16 + fr; const float s = rs_[ai][m];
;                 f32x4 o[2];
; #pragma unroll
;                 for (int n = 0; n < 2; ++n) { const f32x4 g = acc[ai][0][m][n] * s, up = acc[ai][1][m][n] * s;
; #pragma unroll
;                     for (int j = 0; j < 4; ++j) o[n][j] = g[j] * sigmoidf_(g[j]) * up[j]; }
;                 st8_wt(ACT + (size_t)(u.pm * 256 + rl) * DE + colb, o[0], o[1]); }
	v_rcp_f32_e32 v142, v142
	s_nop 0
	s_nop 0
	v_mul_f32_e32 v139, v139, v142
	v_mul_f32_e32 v142, v138, v139
	v_mov_b32_e32 v138, v57
	v_mov_b32_e32 v139, v89
	v_pk_mul_f32 v[138:139], v[138:139], v[160:161] op_sel_hi:[1,0]
	s_nop 0
	v_mul_f32_e32 v143, 0xbfb8aa3b, v139
	v_exp_f32_e32 v143, v143
	s_nop 0
	v_add_f32_e32 v143, 1.0, v143
	v_rcp_f32_e32 v143, v143
	s_nop 0
	s_nop 0
	v_mul_f32_e32 v139, v139, v143
	v_mul_f32_e32 v143, v138, v139
	v_mov_b32_e32 v138, v58
	v_mov_b32_e32 v139, v90
	v_pk_mul_f32 v[138:139], v[138:139], v[160:161] op_sel_hi:[1,0]
	s_nop 0
	v_mul_f32_e32 v145, 0xbfb8aa3b, v139
	v_exp_f32_e32 v145, v145
	s_nop 0
	v_add_f32_e32 v145, 1.0, v145
	v_rcp_f32_e32 v145, v145
	s_nop 0
	s_nop 0
	v_mul_f32_e32 v139, v139, v145
	v_mul_f32_e32 v145, v138, v139
	v_mov_b32_e32 v138, v59
	v_mov_b32_e32 v139, v91
	v_pk_mul_f32 v[138:139], v[138:139], v[160:161] op_sel_hi:[1,0]
	s_nop 0
	v_mul_f32_e32 v146, 0xbfb8aa3b, v139
	v_exp_f32_e32 v146, v146
	s_nop 0
	v_add_f32_e32 v146, 1.0, v146
	v_rcp_f32_e32 v146, v146
	s_nop 0
	v_cvt_pk_bf16_f32 v174, v129, v133
	v_cvt_pk_bf16_f32 v175, v137, v141
	v_cvt_pk_bf16_f32 v176, v142, v143
	s_nop 0
	v_mul_f32_e32 v139, v139, v146
	v_mul_f32_e32 v146, v138, v139
	v_add_u32_e32 v138, s4, v171
	v_mad_i64_i32 v[138:139], s[2:3], v138, s5, v[130:131]
	v_lshl_add_u64 v[138:139], v[138:139], 0, v[134:135]
	v_cvt_pk_bf16_f32 v177, v145, v146
	s_nop 0
	global_store_dwordx4 v[138:139], v[174:177], off sc1
	s_nop 1
	v_mov_b32_e32 v138, v52
	v_mov_b32_e32 v139, v84
	v_pk_mul_f32 v[138:139], v[138:139], v[148:149] op_sel_hi:[1,0]
	s_nop 0
	v_mul_f32_e32 v129, 0xbfb8aa3b, v139
	v_exp_f32_e32 v129, v129
	s_nop 0
	v_add_f32_e32 v129, 1.0, v129
	v_rcp_f32_e32 v129, v129
	s_nop 0
	s_nop 0
	v_mul_f32_e32 v129, v139, v129
	v_mul_f32_e32 v129, v138, v129
	v_mov_b32_e32 v138, v53
	v_mov_b32_e32 v139, v85
	v_pk_mul_f32 v[138:139], v[138:139], v[148:149] op_sel_hi:[1,0]
	s_nop 0
	v_mul_f32_e32 v133, 0xbfb8aa3b, v139
	v_exp_f32_e32 v133, v133
	s_nop 0
	v_add_f32_e32 v133, 1.0, v133
	v_rcp_f32_e32 v133, v133
	s_nop 0
	s_nop 0
	v_mul_f32_e32 v133, v139, v133
	v_mul_f32_e32 v133, v138, v133
	v_mov_b32_e32 v138, v54
	v_mov_b32_e32 v139, v86
	v_pk_mul_f32 v[138:139], v[138:139], v[148:149] op_sel_hi:[1,0]
	s_nop 0
	v_mul_f32_e32 v137, 0xbfb8aa3b, v139
	v_exp_f32_e32 v137, v137
	s_nop 0
	v_add_f32_e32 v137, 1.0, v137
	v_rcp_f32_e32 v137, v137
	s_nop 0
	s_nop 0
	v_mul_f32_e32 v137, v139, v137
	v_mul_f32_e32 v137, v138, v137
	v_mov_b32_e32 v138, v55
	v_mov_b32_e32 v139, v87
	v_pk_mul_f32 v[138:139], v[138:139], v[148:149] op_sel_hi:[1,0]
	s_nop 0
	v_mul_f32_e32 v141, 0xbfb8aa3b, v139
	v_exp_f32_e32 v141, v141
	s_nop 0
	v_add_f32_e32 v141, 1.0, v141
	v_rcp_f32_e32 v141, v141
	s_nop 0
	s_nop 0
	v_mul_f32_e32 v139, v139, v141
	v_mul_f32_e32 v141, v138, v139
	v_mov_b32_e32 v138, v48
	v_mov_b32_e32 v139, v80
	v_pk_mul_f32 v[138:139], v[138:139], v[148:149] op_sel_hi:[1,0]
	s_nop 0
	v_mul_f32_e32 v142, 0xbfb8aa3b, v139
	v_exp_f32_e32 v142, v142
	s_nop 0
	v_add_f32_e32 v142, 1.0, v142
	v_rcp_f32_e32 v142, v142
	s_nop 0
	s_nop 0
	v_mul_f32_e32 v139, v139, v142
	v_mul_f32_e32 v142, v138, v139
	v_mov_b32_e32 v138, v49
	v_mov_b32_e32 v139, v81
	v_pk_mul_f32 v[138:139], v[138:139], v[148:149] op_sel_hi:[1,0]
	s_nop 0
	v_mul_f32_e32 v143, 0xbfb8aa3b, v139
	v_exp_f32_e32 v143, v143
	s_nop 0
	v_add_f32_e32 v143, 1.0, v143
	v_rcp_f32_e32 v143, v143
	s_nop 0
	s_nop 0
	v_mul_f32_e32 v139, v139, v143
	v_mul_f32_e32 v143, v138, v139
	v_mov_b32_e32 v138, v50
	v_mov_b32_e32 v139, v82
	v_pk_mul_f32 v[138:139], v[138:139], v[148:149] op_sel_hi:[1,0]
	s_nop 0
	v_mul_f32_e32 v145, 0xbfb8aa3b, v139
	v_exp_f32_e32 v145, v145
	s_nop 0
	v_add_f32_e32 v145, 1.0, v145
	v_rcp_f32_e32 v145, v145
	s_nop 0
	s_nop 0
	v_mul_f32_e32 v139, v139, v145
	v_mul_f32_e32 v145, v138, v139
	v_mov_b32_e32 v138, v51
	v_mov_b32_e32 v139, v83
	v_pk_mul_f32 v[138:139], v[138:139], v[148:149] op_sel_hi:[1,0]
	s_nop 0
	v_mul_f32_e32 v146, 0xbfb8aa3b, v139
	v_exp_f32_e32 v146, v146
	s_nop 0
	v_add_f32_e32 v146, 1.0, v146
	v_rcp_f32_e32 v146, v146
	s_nop 0
	s_nop 0
	v_mul_f32_e32 v139, v139, v146
	v_mul_f32_e32 v149, v138, v139
	v_add_u32_e32 v138, s4, v183
	v_mad_i64_i32 v[138:139], s[2:3], v138, s5, v[130:131]
	v_lshl_add_u64 v[138:139], v[138:139], 0, v[134:135]
	v_cvt_pk_bf16_f32 v146, v129, v133
	v_cvt_pk_bf16_f32 v147, v137, v141
	v_cvt_pk_bf16_f32 v148, v142, v143
	v_cvt_pk_bf16_f32 v149, v145, v149
	s_nop 0
	global_store_dwordx4 v[138:139], v[146:149], off sc1
	s_nop 1
	v_mov_b32_e32 v138, v44
	v_mov_b32_e32 v139, v76
	v_pk_mul_f32 v[138:139], v[138:139], v[144:145] op_sel_hi:[1,0]
	s_nop 0
	v_mul_f32_e32 v129, 0xbfb8aa3b, v139
	v_exp_f32_e32 v129, v129
	s_nop 0
	v_add_f32_e32 v129, 1.0, v129
	v_rcp_f32_e32 v129, v129
	s_nop 0
	s_nop 0
	v_mul_f32_e32 v129, v139, v129
	v_mul_f32_e32 v129, v138, v129
	v_mov_b32_e32 v138, v45
	v_mov_b32_e32 v139, v77
	v_pk_mul_f32 v[138:139], v[138:139], v[144:145] op_sel_hi:[1,0]
	s_nop 0
	v_mul_f32_e32 v133, 0xbfb8aa3b, v139
	v_exp_f32_e32 v133, v133
	s_nop 0
	v_add_f32_e32 v133, 1.0, v133
	v_rcp_f32_e32 v133, v133
	s_nop 0
	s_nop 0
	v_mul_f32_e32 v133, v139, v133
	v_mul_f32_e32 v133, v138, v133
	v_mov_b32_e32 v138, v46
	v_mov_b32_e32 v139, v78
	v_pk_mul_f32 v[138:139], v[138:139], v[144:145] op_sel_hi:[1,0]
	s_nop 0
	v_mul_f32_e32 v137, 0xbfb8aa3b, v139
	v_exp_f32_e32 v137, v137
	s_nop 0
	v_add_f32_e32 v137, 1.0, v137
	v_rcp_f32_e32 v137, v137
	s_nop 0
	s_nop 0
	v_mul_f32_e32 v137, v139, v137
	v_mul_f32_e32 v137, v138, v137
	v_mov_b32_e32 v138, v47
	v_mov_b32_e32 v139, v79
	v_pk_mul_f32 v[138:139], v[138:139], v[144:145] op_sel_hi:[1,0]
; __device__ __forceinline__ float sigmoidf_(float x) { return rcpf_(1.0f + __expf(-x)); }
;     __device__ __forceinline__ bool operator()(f32x4 (&acc)[2][2][4][2], const pg8::Unit& u, int wr, int wc, int fr, int fq) const {
;     ...
; #pragma unroll
;         for (int ai = 0; ai < 2; ++ai)
; #pragma unroll
;             for (int m = 0; m < 4; ++m) { const int rl = ai * 128 + wr * 64 + m * 16 + fr; const float s = rs_[ai][m];
;                 f32x4 o[2];
; #pragma unroll
;                 for (int n = 0; n < 2; ++n) { const f32x4 g = acc[ai][0][m][n] * s, up = acc[ai][1][m][n] * s;
; #pragma unroll
;                     for (int j = 0; j < 4; ++j) o[n][j] = g[j] * sigmoidf_(g[j]) * up[j]; }
;                 st8_wt(ACT + (size_t)(u.pm * 256 + rl) * DE + colb, o[0], o[1]); }
	s_nop 0
	v_mul_f32_e32 v141, 0xbfb8aa3b, v139
	v_exp_f32_e32 v141, v141
	s_nop 0
	v_add_f32_e32 v141, 1.0, v141
	v_rcp_f32_e32 v141, v141
	s_nop 0
	s_nop 0
	v_mul_f32_e32 v139, v139, v141
	v_mul_f32_e32 v141, v138, v139
	v_mov_b32_e32 v138, v40
	v_mov_b32_e32 v139, v72
	v_pk_mul_f32 v[138:139], v[138:139], v[144:145] op_sel_hi:[1,0]
	s_nop 0
	v_mul_f32_e32 v142, 0xbfb8aa3b, v139
	v_exp_f32_e32 v142, v142
	s_nop 0
	v_add_f32_e32 v142, 1.0, v142
	v_rcp_f32_e32 v142, v142
	s_nop 0
	s_nop 0
	v_mul_f32_e32 v139, v139, v142
	v_mul_f32_e32 v145, v138, v139
	v_mov_b32_e32 v138, v41
	v_mov_b32_e32 v139, v73
	v_pk_mul_f32 v[138:139], v[138:139], v[144:145] op_sel_hi:[1,0]
	s_nop 0
	v_mul_f32_e32 v142, 0xbfb8aa3b, v139
	v_exp_f32_e32 v142, v142
	s_nop 0
	v_add_f32_e32 v142, 1.0, v142
	v_rcp_f32_e32 v142, v142
	s_nop 0
	s_nop 0
	v_mul_f32_e32 v139, v139, v142
	v_mul_f32_e32 v146, v138, v139
	v_mov_b32_e32 v138, v42
	v_mov_b32_e32 v139, v74
	v_pk_mul_f32 v[138:139], v[138:139], v[144:145] op_sel_hi:[1,0]
	s_nop 0
	v_mul_f32_e32 v142, 0xbfb8aa3b, v139
	v_exp_f32_e32 v142, v142
	s_nop 0
	v_add_f32_e32 v142, 1.0, v142
	v_rcp_f32_e32 v142, v142
	s_nop 0
	s_nop 0
	v_mul_f32_e32 v139, v139, v142
	v_mul_f32_e32 v147, v138, v139
	v_mov_b32_e32 v138, v43
	v_mov_b32_e32 v139, v75
	v_pk_mul_f32 v[138:139], v[138:139], v[144:145] op_sel_hi:[1,0]
	s_nop 0
	v_mul_f32_e32 v142, 0xbfb8aa3b, v139
	v_exp_f32_e32 v142, v142
	s_nop 0
	v_add_f32_e32 v142, 1.0, v142
	v_rcp_f32_e32 v142, v142
	s_nop 0
	s_nop 0
	v_mul_f32_e32 v139, v139, v142
	v_mul_f32_e32 v148, v138, v139
	v_add_u32_e32 v138, s4, v201
	v_mad_i64_i32 v[138:139], s[2:3], v138, s5, v[130:131]
	v_lshl_add_u64 v[138:139], v[138:139], 0, v[134:135]
	v_cvt_pk_bf16_f32 v142, v129, v133
	v_cvt_pk_bf16_f32 v143, v137, v141
	v_cvt_pk_bf16_f32 v144, v145, v146
	v_cvt_pk_bf16_f32 v145, v147, v148
	s_nop 0
	global_store_dwordx4 v[138:139], v[142:145], off sc1
	s_nop 1
	v_mov_b32_e32 v138, v4
	v_mov_b32_e32 v139, v36
	v_pk_mul_f32 v[138:139], v[138:139], v[140:141] op_sel_hi:[1,0]
	s_nop 0
	v_mul_f32_e32 v129, 0xbfb8aa3b, v139
	v_exp_f32_e32 v129, v129
	s_nop 0
	v_add_f32_e32 v129, 1.0, v129
	v_rcp_f32_e32 v129, v129
	s_nop 0
	s_nop 0
	v_mul_f32_e32 v129, v139, v129
	v_mul_f32_e32 v129, v138, v129
	v_mov_b32_e32 v138, v5
	v_mov_b32_e32 v139, v37
	v_pk_mul_f32 v[138:139], v[138:139], v[140:141] op_sel_hi:[1,0]
	s_nop 0
	v_mul_f32_e32 v133, 0xbfb8aa3b, v139
	v_exp_f32_e32 v133, v133
	s_nop 0
	v_add_f32_e32 v133, 1.0, v133
	v_rcp_f32_e32 v133, v133
	s_nop 0
	s_nop 0
	v_mul_f32_e32 v133, v139, v133
	v_mul_f32_e32 v133, v138, v133
	v_mov_b32_e32 v138, v6
	v_mov_b32_e32 v139, v38
	v_pk_mul_f32 v[138:139], v[138:139], v[140:141] op_sel_hi:[1,0]
	s_nop 0
	v_mul_f32_e32 v137, 0xbfb8aa3b, v139
	v_exp_f32_e32 v137, v137
	s_nop 0
	v_add_f32_e32 v137, 1.0, v137
	v_rcp_f32_e32 v137, v137
	s_nop 0
	s_nop 0
	v_mul_f32_e32 v137, v139, v137
	v_mul_f32_e32 v137, v138, v137
	v_mov_b32_e32 v138, v7
	v_mov_b32_e32 v139, v39
	v_pk_mul_f32 v[138:139], v[138:139], v[140:141] op_sel_hi:[1,0]
	s_nop 0
	v_mul_f32_e32 v141, 0xbfb8aa3b, v139
	v_exp_f32_e32 v141, v141
	s_nop 0
	v_add_f32_e32 v141, 1.0, v141
	v_rcp_f32_e32 v141, v141
	s_nop 0
	s_nop 0
	v_mul_f32_e32 v139, v139, v141
	v_mul_f32_e32 v141, v138, v139
	v_mov_b32_e32 v138, v0
	v_mov_b32_e32 v139, v32
	v_pk_mul_f32 v[138:139], v[138:139], v[140:141] op_sel_hi:[1,0]
	s_nop 0
	v_mul_f32_e32 v142, 0xbfb8aa3b, v139
	v_exp_f32_e32 v142, v142
	s_nop 0
	v_add_f32_e32 v142, 1.0, v142
	v_rcp_f32_e32 v142, v142
	s_nop 0
	s_nop 0
	v_mul_f32_e32 v139, v139, v142
	v_mul_f32_e32 v144, v138, v139
	v_mov_b32_e32 v138, v1
	v_mov_b32_e32 v139, v33
	v_pk_mul_f32 v[138:139], v[138:139], v[140:141] op_sel_hi:[1,0]
	s_nop 0
	v_mul_f32_e32 v142, 0xbfb8aa3b, v139
	v_exp_f32_e32 v142, v142
	s_nop 0
	v_add_f32_e32 v142, 1.0, v142
	v_rcp_f32_e32 v142, v142
	s_nop 0
	s_nop 0
	v_mul_f32_e32 v139, v139, v142
	v_mul_f32_e32 v145, v138, v139
	v_mov_b32_e32 v138, v2
	v_mov_b32_e32 v139, v34
	v_pk_mul_f32 v[138:139], v[138:139], v[140:141] op_sel_hi:[1,0]
	s_nop 0
	v_mul_f32_e32 v142, 0xbfb8aa3b, v139
	v_exp_f32_e32 v142, v142
	s_nop 0
	v_add_f32_e32 v142, 1.0, v142
	v_rcp_f32_e32 v142, v142
	s_nop 0
	s_nop 0
	v_mul_f32_e32 v139, v139, v142
	v_mul_f32_e32 v146, v138, v139
	v_mov_b32_e32 v138, v3
	v_mov_b32_e32 v139, v35
	v_pk_mul_f32 v[138:139], v[138:139], v[140:141] op_sel_hi:[1,0]
	s_nop 0
	v_mul_f32_e32 v140, 0xbfb8aa3b, v139
	v_exp_f32_e32 v140, v140
	s_nop 0
	v_add_f32_e32 v140, 1.0, v140
	v_rcp_f32_e32 v140, v140
	s_nop 0
	s_nop 0
	v_mul_f32_e32 v139, v139, v140
	v_mul_f32_e32 v147, v138, v139
	v_add_u32_e32 v138, s4, v213
	v_mad_i64_i32 v[138:139], s[2:3], v138, s5, v[130:131]
	v_lshl_add_u64 v[142:143], v[138:139], 0, v[134:135]
	v_cvt_pk_bf16_f32 v138, v129, v133
	v_cvt_pk_bf16_f32 v139, v137, v141
	v_cvt_pk_bf16_f32 v140, v144, v145
	v_cvt_pk_bf16_f32 v141, v146, v147
	s_nop 0
	global_store_dwordx4 v[142:143], v[138:141], off sc1
	s_nop 1
	v_mov_b32_e32 v138, v100
	v_mov_b32_e32 v139, v28
	v_pk_mul_f32 v[138:139], v[138:139], v[136:137] op_sel_hi:[1,0]
	s_nop 0
	v_mul_f32_e32 v129, 0xbfb8aa3b, v139
	v_exp_f32_e32 v129, v129
	s_nop 0
	v_add_f32_e32 v129, 1.0, v129
	v_rcp_f32_e32 v129, v129
	s_nop 0
	s_nop 0
	v_mul_f32_e32 v129, v139, v129
	v_mul_f32_e32 v129, v138, v129
	v_mov_b32_e32 v138, v101
	v_mov_b32_e32 v139, v29
	v_pk_mul_f32 v[138:139], v[138:139], v[136:137] op_sel_hi:[1,0]
	s_nop 0
	v_mul_f32_e32 v133, 0xbfb8aa3b, v139
	v_exp_f32_e32 v133, v133
	s_nop 0
	v_add_f32_e32 v133, 1.0, v133
	v_rcp_f32_e32 v133, v133
	s_nop 0
	s_nop 0
	v_mul_f32_e32 v133, v139, v133
	v_mul_f32_e32 v133, v138, v133
; __device__ __forceinline__ float sigmoidf_(float x) { return rcpf_(1.0f + __expf(-x)); }
;     __device__ __forceinline__ bool operator()(f32x4 (&acc)[2][2][4][2], const pg8::Unit& u, int wr, int wc, int fr, int fq) const {
;     ...
; #pragma unroll
;         for (int ai = 0; ai < 2; ++ai)
; #pragma unroll
;             for (int m = 0; m < 4; ++m) { const int rl = ai * 128 + wr * 64 + m * 16 + fr; const float s = rs_[ai][m];
;                 f32x4 o[2];
; #pragma unroll
;                 for (int n = 0; n < 2; ++n) { const f32x4 g = acc[ai][0][m][n] * s, up = acc[ai][1][m][n] * s;
; #pragma unroll
;                     for (int j = 0; j < 4; ++j) o[n][j] = g[j] * sigmoidf_(g[j]) * up[j]; }
;                 st8_wt(ACT + (size_t)(u.pm * 256 + rl) * DE + colb, o[0], o[1]); }
	v_mov_b32_e32 v138, v102
	v_mov_b32_e32 v139, v30
	v_pk_mul_f32 v[138:139], v[138:139], v[136:137] op_sel_hi:[1,0]
	s_nop 0
	v_mul_f32_e32 v137, 0xbfb8aa3b, v139
	v_exp_f32_e32 v137, v137
	s_nop 0
	v_add_f32_e32 v137, 1.0, v137
	v_rcp_f32_e32 v137, v137
	s_nop 0
	s_nop 0
	v_mul_f32_e32 v137, v139, v137
	v_mul_f32_e32 v142, v138, v137
	v_mov_b32_e32 v138, v103
	v_mov_b32_e32 v139, v31
	v_pk_mul_f32 v[138:139], v[138:139], v[136:137] op_sel_hi:[1,0]
	s_nop 0
	v_mul_f32_e32 v137, 0xbfb8aa3b, v139
	v_exp_f32_e32 v137, v137
	s_nop 0
	v_add_f32_e32 v137, 1.0, v137
	v_rcp_f32_e32 v137, v137
	s_nop 0
	s_nop 0
	v_mul_f32_e32 v137, v139, v137
	v_mul_f32_e32 v143, v138, v137
	v_mov_b32_e32 v138, v108
	v_mov_b32_e32 v139, v24
	v_pk_mul_f32 v[138:139], v[138:139], v[136:137] op_sel_hi:[1,0]
	s_nop 0
	v_mul_f32_e32 v137, 0xbfb8aa3b, v139
	v_exp_f32_e32 v137, v137
	s_nop 0
	v_add_f32_e32 v137, 1.0, v137
	v_rcp_f32_e32 v137, v137
	s_nop 0
	s_nop 0
	v_mul_f32_e32 v137, v139, v137
	v_mul_f32_e32 v144, v138, v137
	v_mov_b32_e32 v138, v109
	v_mov_b32_e32 v139, v25
	v_pk_mul_f32 v[138:139], v[138:139], v[136:137] op_sel_hi:[1,0]
	s_nop 0
	v_mul_f32_e32 v137, 0xbfb8aa3b, v139
	v_exp_f32_e32 v137, v137
	s_nop 0
	v_add_f32_e32 v137, 1.0, v137
	v_rcp_f32_e32 v137, v137
	s_nop 0
	s_nop 0
	v_mul_f32_e32 v137, v139, v137
	v_mul_f32_e32 v145, v138, v137
	v_mov_b32_e32 v138, v110
	v_mov_b32_e32 v139, v26
	v_pk_mul_f32 v[138:139], v[138:139], v[136:137] op_sel_hi:[1,0]
	s_nop 0
	v_mul_f32_e32 v137, 0xbfb8aa3b, v139
	v_exp_f32_e32 v137, v137
	s_nop 0
	v_add_f32_e32 v137, 1.0, v137
	v_rcp_f32_e32 v137, v137
	s_nop 0
	s_nop 0
	v_mul_f32_e32 v137, v139, v137
	v_mul_f32_e32 v146, v138, v137
	v_mov_b32_e32 v138, v111
	v_mov_b32_e32 v139, v27
	v_pk_mul_f32 v[136:137], v[138:139], v[136:137] op_sel_hi:[1,0]
	s_nop 0
	v_mul_f32_e32 v138, 0xbfb8aa3b, v137
	v_exp_f32_e32 v138, v138
	s_nop 0
	v_add_f32_e32 v138, 1.0, v138
	v_rcp_f32_e32 v138, v138
	s_nop 0
	s_nop 0
	v_mul_f32_e32 v137, v137, v138
	v_mul_f32_e32 v139, v136, v137
	v_add_u32_e32 v136, s4, v186
	v_mad_i64_i32 v[136:137], s[2:3], v136, s5, v[130:131]
	v_lshl_add_u64 v[140:141], v[136:137], 0, v[134:135]
	v_cvt_pk_bf16_f32 v136, v129, v133
	v_cvt_pk_bf16_f32 v137, v142, v143
	v_cvt_pk_bf16_f32 v138, v144, v145
	v_cvt_pk_bf16_f32 v139, v146, v139
	s_nop 0
	global_store_dwordx4 v[140:141], v[136:139], off sc1
	s_nop 1
	v_mov_b32_e32 v136, v112
	v_mov_b32_e32 v137, v20
	v_pk_mul_f32 v[136:137], v[136:137], v[132:133] op_sel_hi:[1,0]
	s_nop 0
	v_mul_f32_e32 v129, 0xbfb8aa3b, v137
	v_exp_f32_e32 v129, v129
	s_nop 0
	v_add_f32_e32 v129, 1.0, v129
	v_rcp_f32_e32 v129, v129
	s_nop 0
	s_nop 0
	v_mul_f32_e32 v129, v137, v129
	v_mul_f32_e32 v129, v136, v129
	v_mov_b32_e32 v136, v113
	v_mov_b32_e32 v137, v21
	v_pk_mul_f32 v[136:137], v[136:137], v[132:133] op_sel_hi:[1,0]
	s_nop 0
	v_mul_f32_e32 v133, 0xbfb8aa3b, v137
	v_exp_f32_e32 v133, v133
	s_nop 0
	v_add_f32_e32 v133, 1.0, v133
	v_rcp_f32_e32 v133, v133
	s_nop 0
	s_nop 0
	v_mul_f32_e32 v133, v137, v133
	v_mul_f32_e32 v138, v136, v133
	v_mov_b32_e32 v136, v114
	v_mov_b32_e32 v137, v22
	v_pk_mul_f32 v[136:137], v[136:137], v[132:133] op_sel_hi:[1,0]
	s_nop 0
	v_mul_f32_e32 v133, 0xbfb8aa3b, v137
	v_exp_f32_e32 v133, v133
	s_nop 0
	v_add_f32_e32 v133, 1.0, v133
	v_rcp_f32_e32 v133, v133
	s_nop 0
	s_nop 0
	v_mul_f32_e32 v133, v137, v133
	v_mul_f32_e32 v139, v136, v133
	v_mov_b32_e32 v136, v115
	v_mov_b32_e32 v137, v23
	v_pk_mul_f32 v[136:137], v[136:137], v[132:133] op_sel_hi:[1,0]
	s_nop 0
	v_mul_f32_e32 v133, 0xbfb8aa3b, v137
	v_exp_f32_e32 v133, v133
	s_nop 0
	v_add_f32_e32 v133, 1.0, v133
	v_rcp_f32_e32 v133, v133
	s_nop 0
	s_nop 0
	v_mul_f32_e32 v133, v137, v133
	v_mul_f32_e32 v140, v136, v133
	v_mov_b32_e32 v136, v116
	v_mov_b32_e32 v137, v16
	v_pk_mul_f32 v[136:137], v[136:137], v[132:133] op_sel_hi:[1,0]
	s_nop 0
	v_mul_f32_e32 v133, 0xbfb8aa3b, v137
	v_exp_f32_e32 v133, v133
	s_nop 0
	v_add_f32_e32 v133, 1.0, v133
	v_rcp_f32_e32 v133, v133
	s_nop 0
	s_nop 0
	v_mul_f32_e32 v133, v137, v133
	v_mul_f32_e32 v141, v136, v133
	v_mov_b32_e32 v136, v117
	v_mov_b32_e32 v137, v17
	v_pk_mul_f32 v[136:137], v[136:137], v[132:133] op_sel_hi:[1,0]
	s_nop 0
	v_mul_f32_e32 v133, 0xbfb8aa3b, v137
	v_exp_f32_e32 v133, v133
	s_nop 0
	v_add_f32_e32 v133, 1.0, v133
	v_rcp_f32_e32 v133, v133
	s_nop 0
	s_nop 0
	v_mul_f32_e32 v133, v137, v133
	v_mul_f32_e32 v142, v136, v133
	v_mov_b32_e32 v136, v118
	v_mov_b32_e32 v137, v18
	v_pk_mul_f32 v[136:137], v[136:137], v[132:133] op_sel_hi:[1,0]
; __device__ __forceinline__ float sigmoidf_(float x) { return rcpf_(1.0f + __expf(-x)); }
;     __device__ __forceinline__ bool operator()(f32x4 (&acc)[2][2][4][2], const pg8::Unit& u, int wr, int wc, int fr, int fq) const {
;     ...
; #pragma unroll
;         for (int ai = 0; ai < 2; ++ai)
; #pragma unroll
;             for (int m = 0; m < 4; ++m) { const int rl = ai * 128 + wr * 64 + m * 16 + fr; const float s = rs_[ai][m];
;                 f32x4 o[2];
; #pragma unroll
;                 for (int n = 0; n < 2; ++n) { const f32x4 g = acc[ai][0][m][n] * s, up = acc[ai][1][m][n] * s;
; #pragma unroll
;                     for (int j = 0; j < 4; ++j) o[n][j] = g[j] * sigmoidf_(g[j]) * up[j]; }
;                 st8_wt(ACT + (size_t)(u.pm * 256 + rl) * DE + colb, o[0], o[1]); }
;         asm volatile("s_waitcnt vmcnt(0)" ::: "memory");
;         if ((fr | fq) == 0) __hip_atomic_fetch_add(done + 64 * u.pm, 1u, __ATOMIC_RELAXED, __HIP_MEMORY_SCOPE_AGENT);
;         return false;
	s_nop 0
	v_mul_f32_e32 v133, 0xbfb8aa3b, v137
	v_exp_f32_e32 v133, v133
	s_nop 0
	v_add_f32_e32 v133, 1.0, v133
	v_rcp_f32_e32 v133, v133
	s_nop 0
	s_nop 0
	v_mul_f32_e32 v133, v137, v133
	v_mul_f32_e32 v143, v136, v133
	v_mov_b32_e32 v136, v119
	v_mov_b32_e32 v137, v19
	v_pk_mul_f32 v[132:133], v[136:137], v[132:133] op_sel_hi:[1,0]
	s_nop 0
	v_mul_f32_e32 v136, 0xbfb8aa3b, v133
	v_exp_f32_e32 v136, v136
	s_nop 0
	v_add_f32_e32 v136, 1.0, v136
	v_rcp_f32_e32 v136, v136
	s_nop 0
	s_nop 0
	v_mul_f32_e32 v133, v133, v136
	v_mul_f32_e32 v144, v132, v133
	v_add_u32_e32 v132, s4, v187
	v_mad_i64_i32 v[132:133], s[2:3], v132, s5, v[130:131]
	v_lshl_add_u64 v[132:133], v[132:133], 0, v[134:135]
	v_cvt_pk_bf16_f32 v136, v129, v138
	v_cvt_pk_bf16_f32 v137, v139, v140
	v_cvt_pk_bf16_f32 v138, v141, v142
	v_cvt_pk_bf16_f32 v139, v143, v144
	s_nop 0
	global_store_dwordx4 v[132:133], v[136:139], off sc1
	s_nop 1
	v_mov_b32_e32 v132, v120
	v_mov_b32_e32 v133, v12
	v_pk_mul_f32 v[132:133], v[132:133], v[128:129] op_sel_hi:[1,0]
	s_nop 0
	v_mul_f32_e32 v129, 0xbfb8aa3b, v133
	v_exp_f32_e32 v129, v129
	s_nop 0
	v_add_f32_e32 v129, 1.0, v129
	v_rcp_f32_e32 v129, v129
	s_nop 0
	s_nop 0
	v_mul_f32_e32 v129, v133, v129
	v_mul_f32_e32 v136, v132, v129
	v_mov_b32_e32 v132, v121
	v_mov_b32_e32 v133, v13
	v_pk_mul_f32 v[132:133], v[132:133], v[128:129] op_sel_hi:[1,0]
	s_nop 0
	v_mul_f32_e32 v129, 0xbfb8aa3b, v133
	v_exp_f32_e32 v129, v129
	s_nop 0
	v_add_f32_e32 v129, 1.0, v129
	v_rcp_f32_e32 v129, v129
	s_nop 0
	s_nop 0
	v_mul_f32_e32 v129, v133, v129
	v_mul_f32_e32 v137, v132, v129
	v_mov_b32_e32 v132, v122
	v_mov_b32_e32 v133, v14
	v_pk_mul_f32 v[132:133], v[132:133], v[128:129] op_sel_hi:[1,0]
	s_nop 0
	v_mul_f32_e32 v129, 0xbfb8aa3b, v133
	v_exp_f32_e32 v129, v129
	s_nop 0
	v_add_f32_e32 v129, 1.0, v129
	v_rcp_f32_e32 v129, v129
	s_nop 0
	s_nop 0
	v_mul_f32_e32 v129, v133, v129
	v_mul_f32_e32 v138, v132, v129
	v_mov_b32_e32 v132, v123
	v_mov_b32_e32 v133, v15
	v_pk_mul_f32 v[132:133], v[132:133], v[128:129] op_sel_hi:[1,0]
	s_nop 0
	v_mul_f32_e32 v129, 0xbfb8aa3b, v133
	v_exp_f32_e32 v129, v129
	s_nop 0
	v_add_f32_e32 v129, 1.0, v129
	v_rcp_f32_e32 v129, v129
	s_nop 0
	s_nop 0
	v_mul_f32_e32 v129, v133, v129
	v_mul_f32_e32 v139, v132, v129
	v_mov_b32_e32 v132, v124
	v_mov_b32_e32 v133, v8
	v_pk_mul_f32 v[132:133], v[132:133], v[128:129] op_sel_hi:[1,0]
	s_nop 0
	v_mul_f32_e32 v129, 0xbfb8aa3b, v133
	v_exp_f32_e32 v129, v129
	s_nop 0
	v_add_f32_e32 v129, 1.0, v129
	v_rcp_f32_e32 v129, v129
	s_nop 0
	s_nop 0
	v_mul_f32_e32 v129, v133, v129
	v_mul_f32_e32 v140, v132, v129
	v_mov_b32_e32 v132, v125
	v_mov_b32_e32 v133, v9
	v_pk_mul_f32 v[132:133], v[132:133], v[128:129] op_sel_hi:[1,0]
	s_nop 0
	v_mul_f32_e32 v129, 0xbfb8aa3b, v133
	v_exp_f32_e32 v129, v129
	s_nop 0
	v_add_f32_e32 v129, 1.0, v129
	v_rcp_f32_e32 v129, v129
	s_nop 0
	s_nop 0
	v_mul_f32_e32 v129, v133, v129
	v_mul_f32_e32 v141, v132, v129
	v_mov_b32_e32 v132, v126
	v_mov_b32_e32 v133, v10
	v_pk_mul_f32 v[132:133], v[132:133], v[128:129] op_sel_hi:[1,0]
	s_nop 0
	v_mul_f32_e32 v129, 0xbfb8aa3b, v133
	v_exp_f32_e32 v129, v129
	s_nop 0
	v_add_f32_e32 v129, 1.0, v129
	v_rcp_f32_e32 v129, v129
	s_nop 0
	s_nop 0
	v_mul_f32_e32 v129, v133, v129
	v_mul_f32_e32 v142, v132, v129
	v_mov_b32_e32 v132, v127
	v_mov_b32_e32 v133, v11
	v_pk_mul_f32 v[128:129], v[132:133], v[128:129] op_sel_hi:[1,0]
	s_nop 0
	v_mul_f32_e32 v132, 0xbfb8aa3b, v129
	v_exp_f32_e32 v132, v132
	s_nop 0
	v_add_f32_e32 v132, 1.0, v132
	v_rcp_f32_e32 v132, v132
	s_nop 0
	s_nop 0
	v_mul_f32_e32 v129, v129, v132
	v_mul_f32_e32 v143, v128, v129
	v_add_u32_e32 v128, s4, v188
	v_mad_i64_i32 v[128:129], s[2:3], v128, s5, v[130:131]
	v_lshl_add_u64 v[132:133], v[128:129], 0, v[134:135]
	v_cvt_pk_bf16_f32 v128, v136, v137
	v_cvt_pk_bf16_f32 v129, v138, v139
	v_cvt_pk_bf16_f32 v130, v140, v141
	v_cvt_pk_bf16_f32 v131, v142, v143
	s_nop 0
	global_store_dwordx4 v[132:133], v[128:131], off sc1
	s_nop 1
	s_waitcnt vmcnt(0)
	s_and_saveexec_b64 s[4:5], s[0:1]
	s_cbranch_execz .LBB0_1518
	s_mov_b64 s[26:27], exec
	v_mbcnt_lo_u32_b32 v128, s26, 0
	v_mbcnt_hi_u32_b32 v128, s27, v128
	v_cmp_eq_u32_e32 vcc, 0, v128
	s_and_b64 s[2:3], exec, vcc
	s_mov_b64 exec, s[2:3]
	s_cbranch_execz .LBB0_1518
	s_lshl_b32 s2, s44, 6
	s_ashr_i32 s3, s2, 31
	s_lshl_b64 s[2:3], s[2:3], 2
	s_add_u32 s2, s30, s2
	s_addc_u32 s3, s31, s3
	s_bcnt1_i32_b64 s8, s[26:27]
	v_mov_b32_e32 v128, s8
	global_atomic_add v161, v128, s[2:3]

; #define LAS __attribute__((address_space(3)))
; __device__ __forceinline__ f32x4 ld_bf4(const bf16_t* p) { const u32x2 w = *(const u32x2*)p; return (f32x4){bf_lo(w.x), bf_hi(w.x), bf_lo(w.y), bf_hi(w.y)}; }
; template <int NTK>
; __device__ __forceinline__ void combine_rows(int t0, int tstride, const LAS int* bst, const int* tok_e, const int* tok_pos, const float* tok_w, const bf16_t* Y, const bf16_t* xbi, float* xio, bf16_t* xb, float* part, const float* gfin, bool last, int lane) {
;     int tk[NTK]; size_t s0[NTK], s1[NTK]; float w0[NTK], w1[NTK]; bool ok[NTK];
; #pragma unroll
;     for (int i = 0; i < NTK; ++i) { const int t = t0 + i * tstride; ok[i] = t < T; tk[i] = ok[i] ? t : T - 1; }
; #pragma unroll
;     for (int i = 0; i < NTK; ++i) { const int t = tk[i]; const int e0 = tok_e[2 * t], e1 = tok_e[2 * t + 1]; w0[i] = tok_w[2 * t]; w1[i] = tok_w[2 * t + 1];
;         s0[i] = (size_t)bst[e0] * 256 + tok_pos[2 * t]; s1[i] = (size_t)bst[e1] * 256 + tok_pos[2 * t + 1]; }
;     f32x4 v[NTK][4]; u32x2 ya[NTK][4], yb[NTK][4];
; #pragma unroll
;     for (int i = 0; i < NTK; ++i)
; #pragma unroll
;         for (int j = 0; j < 4; ++j) { const int c = j * 256 + lane * 4; v[i][j] = ld_bf4(xbi + (size_t)tk[i] * DM + c); ya[i][j] = *(const u32x2*)(Y + s0[i] * DM + c); yb[i][j] = *(const u32x2*)(Y + s1[i] * DM + c); }
.LBB0_1633:
	s_add_i32 s6, s54, s12
	s_cmpk_lt_i32 s6, 0x4000
	s_cselect_b64 s[28:29], -1, 0
	s_and_b64 s[2:3], s[28:29], exec
	v_readlane_b32 s2, v252, 24
	s_cselect_b32 s26, s6, 0x3fff
	s_add_i32 s6, s2, s12
	s_cmpk_lt_i32 s6, 0x4000
	s_cselect_b64 s[24:25], -1, 0
	s_and_b64 s[2:3], s[24:25], exec
	v_readlane_b32 s2, v251, 2
	s_mul_i32 s2, s2, 24
	s_cselect_b32 s22, s6, 0x3fff
	s_add_i32 s6, s2, s12
	s_cmpk_lt_i32 s6, 0x4000
	s_cselect_b64 s[20:21], -1, 0
	s_and_b64 s[2:3], s[20:21], exec
	s_cselect_b32 s18, s6, 0x3fff
	s_ashr_i32 s17, s16, 31
	s_lshl_b64 s[6:7], s[16:17], 2
	v_readlane_b32 s10, v251, 34
	v_readlane_b32 s11, v251, 35
	s_add_u32 s2, s10, s6
	s_addc_u32 s3, s11, s7
	global_load_dwordx2 v[14:15], v161, s[2:3]
	s_add_i32 s2, s16, 1
	s_ashr_i32 s3, s2, 31
	v_readlane_b32 s34, v251, 38
	v_readlane_b32 s35, v251, 39
	s_add_u32 s8, s34, s6
	s_addc_u32 s9, s35, s7
	global_load_dword v82, v161, s[8:9]
	s_lshl_b64 s[8:9], s[2:3], 2
	s_add_u32 s2, s34, s8
	s_addc_u32 s3, s35, s9
	global_load_dword v84, v161, s[2:3]
	s_add_i32 s2, 0, 0x23900
	v_readlane_b32 s30, v251, 36
	v_readlane_b32 s31, v251, 37
	s_add_u32 s6, s30, s6
	s_addc_u32 s7, s31, s7
	global_load_dword v44, v161, s[6:7]
	s_add_u32 s6, s30, s8
	s_addc_u32 s7, s31, s9
	global_load_dword v46, v161, s[6:7]
	s_lshl_b32 s6, s26, 1
	s_ashr_i32 s7, s6, 31
	s_lshl_b64 s[6:7], s[6:7], 2
	s_add_u32 s8, s10, s6
	s_addc_u32 s9, s11, s7
	v_lshl_add_u64 v[102:103], s[52:53], 0, v[8:9]
	s_waitcnt vmcnt(0)
	v_lshlrev_b32_e32 v14, 2, v14
	v_add_u32_e32 v14, s2, v14
	ds_read_b32 v38, v14
	v_lshlrev_b32_e32 v14, 2, v15
	v_add_u32_e32 v14, s2, v14
	ds_read_b32 v42, v14
	global_load_dwordx2 v[14:15], v161, s[8:9]
	s_add_u32 s8, s34, s6
	s_addc_u32 s9, s35, s7
	s_add_u32 s6, s30, s6
	s_addc_u32 s7, s31, s7
	global_load_dwordx2 v[64:65], v161, s[8:9]
	global_load_dwordx2 v[16:17], v161, s[6:7]
	s_lshl_b32 s6, s22, 1
	s_ashr_i32 s7, s6, 31
	s_lshl_b64 s[6:7], s[6:7], 2
	s_add_u32 s8, s10, s6
	s_addc_u32 s9, s11, s7
	s_waitcnt lgkmcnt(1)
	v_ashrrev_i32_e32 v39, 31, v38
	v_ashrrev_i32_e32 v45, 31, v44
	s_waitcnt lgkmcnt(0)
	v_ashrrev_i32_e32 v43, 31, v42
	v_lshlrev_b64 v[38:39], 19, v[38:39]
	v_ashrrev_i32_e32 v47, 31, v46
	v_lshlrev_b64 v[44:45], 11, v[44:45]
	v_lshlrev_b64 v[42:43], 19, v[42:43]
	s_waitcnt vmcnt(2)
	v_lshlrev_b32_e32 v14, 2, v14
	v_add_u32_e32 v14, s2, v14
	ds_read_b32 v20, v14
	v_lshlrev_b32_e32 v14, 2, v15
	v_add_u32_e32 v14, s2, v14
	ds_read_b32 v26, v14
	global_load_dwordx2 v[14:15], v161, s[8:9]
	s_add_u32 s8, s34, s6
	s_addc_u32 s9, s35, s7
	s_add_u32 s6, s30, s6
	s_addc_u32 s7, s31, s7
	s_waitcnt vmcnt(1)
	v_ashrrev_i32_e32 v25, 31, v16
	v_mov_b32_e32 v24, v16
	v_ashrrev_i32_e32 v29, 31, v17
	v_mov_b32_e32 v28, v17
	global_load_dwordx2 v[16:17], v161, s[8:9]
	global_load_dwordx2 v[18:19], v161, s[6:7]
	s_lshl_b32 s6, s18, 1
	s_ashr_i32 s7, s6, 31
	s_lshl_b64 s[6:7], s[6:7], 2
	s_add_u32 s8, s10, s6
	s_addc_u32 s9, s11, s7
	s_waitcnt lgkmcnt(1)
	v_ashrrev_i32_e32 v21, 31, v20
	v_lshlrev_b64 v[20:21], 19, v[20:21]
	s_waitcnt lgkmcnt(0)
	v_ashrrev_i32_e32 v27, 31, v26
	v_lshlrev_b64 v[24:25], 11, v[24:25]
	s_waitcnt vmcnt(2)
	v_lshlrev_b32_e32 v14, 2, v14
	v_add_u32_e32 v14, s2, v14
	ds_read_b32 v30, v14
	s_waitcnt vmcnt(0)
	v_ashrrev_i32_e32 v33, 31, v18
	v_mov_b32_e32 v32, v18
	v_ashrrev_i32_e32 v37, 31, v19
	v_mov_b32_e32 v36, v19
	global_load_dwordx2 v[18:19], v161, s[8:9]
	s_add_u32 s8, s34, s6
	s_addc_u32 s9, s35, s7
	s_add_u32 s6, s30, s6
	s_addc_u32 s7, s31, s7
	s_ashr_i32 s27, s26, 31
	s_ashr_i32 s23, s22, 31
	s_ashr_i32 s19, s18, 31
	global_load_dwordx2 v[48:49], v161, s[6:7]
	s_waitcnt vmcnt(1)
	v_lshlrev_b32_e32 v18, 2, v18
	v_add_u32_e32 v18, s2, v18
	ds_read_b32 v40, v18
	v_lshlrev_b32_e32 v14, 2, v15
	v_lshlrev_b32_e32 v18, 2, v19
	v_add_u32_e32 v14, s2, v14
	v_add_u32_e32 v18, s2, v18
	ds_read_b32 v34, v14
	ds_read_b32 v18, v18
	global_load_dwordx2 v[14:15], v161, s[8:9]
	v_readlane_b32 s8, v251, 56
	v_readlane_b32 s9, v251, 57
	s_mov_b32 s2, 0x2a00000
	s_waitcnt lgkmcnt(3)
	v_ashrrev_i32_e32 v31, 31, v30
	v_lshl_add_u64 v[38:39], s[8:9], 0, v[38:39]
	v_lshl_add_u64 v[38:39], v[38:39], 0, v[44:45]
	v_lshlrev_b64 v[44:45], 11, v[46:47]
	v_lshl_add_u64 v[42:43], s[8:9], 0, v[42:43]
	v_lshl_add_u64 v[42:43], v[42:43], 0, v[44:45]
	v_add_co_u32_e32 v44, vcc, s2, v102
	v_readfirstlane_b32 s6, v38
	s_nop 0
	v_addc_co_u32_e32 v45, vcc, 0, v103, vcc
	v_readfirstlane_b32 s7, v39
	v_readfirstlane_b32 s10, v42
	v_readfirstlane_b32 s11, v43
	global_load_dwordx2 v[46:47], v[44:45], off
	v_lshl_add_u64 v[20:21], s[8:9], 0, v[20:21]
	v_lshl_add_u64 v[20:21], v[20:21], 0, v[24:25]
	global_load_dwordx2 v[110:111], v140, s[6:7]
	s_nop 0
	global_load_dwordx2 v[108:109], v140, s[10:11]
	global_load_dwordx2 v[38:39], v[44:45], off offset:512
	v_lshlrev_b64 v[24:25], 19, v[26:27]
	s_lshl_b64 s[2:3], s[26:27], 11
	v_lshlrev_b64 v[26:27], 11, v[28:29]
	v_lshl_add_u64 v[24:25], s[8:9], 0, v[24:25]
	v_lshl_add_u64 v[24:25], v[24:25], 0, v[26:27]
	v_lshl_add_u64 v[72:73], v[4:5], 0, s[2:3]
	v_readfirstlane_b32 s2, v20
	v_readfirstlane_b32 s3, v21
	v_lshlrev_b64 v[20:21], 19, v[30:31]
	s_waitcnt lgkmcnt(1)
	v_ashrrev_i32_e32 v35, 31, v34
	v_lshl_add_u64 v[20:21], s[8:9], 0, v[20:21]
	v_ashrrev_i32_e32 v41, 31, v40
	s_waitcnt lgkmcnt(0)
	v_ashrrev_i32_e32 v19, 31, v18
	v_lshlrev_b64 v[26:27], 11, v[36:37]
	v_lshlrev_b64 v[18:19], 19, v[18:19]
	v_lshl_add_u64 v[18:19], s[8:9], 0, v[18:19]
	s_andn2_b64 vcc, exec, s[14:15]
	s_waitcnt vmcnt(5)
	v_ashrrev_i32_e32 v67, 31, v48
	v_mov_b32_e32 v66, v48
	v_ashrrev_i32_e32 v23, 31, v49
	v_mov_b32_e32 v22, v49
	v_lshlrev_b64 v[22:23], 11, v[22:23]
	v_lshl_add_u64 v[22:23], v[18:19], 0, v[22:23]
	s_waitcnt vmcnt(3)
; __device__ __forceinline__ float bf_lo(unsigned w) { return __uint_as_float(w << 16); }
; __device__ __forceinline__ float bf_hi(unsigned w) { return __uint_as_float(w & 0xffff0000u); }
; __device__ __forceinline__ f32x4 ld_bf4(const bf16_t* p) { const u32x2 w = *(const u32x2*)p; return (f32x4){bf_lo(w.x), bf_hi(w.x), bf_lo(w.y), bf_hi(w.y)}; }
; template <int NTK>
; __device__ __forceinline__ void combine_rows(int t0, int tstride, const LAS int* bst, const int* tok_e, const int* tok_pos, const float* tok_w, const bf16_t* Y, const bf16_t* xbi, float* xio, bf16_t* xb, float* part, const float* gfin, bool last, int lane) {
;     ...
;     f32x4 v[NTK][4]; u32x2 ya[NTK][4], yb[NTK][4];
; #pragma unroll
;     for (int i = 0; i < NTK; ++i)
; #pragma unroll
;         for (int j = 0; j < 4; ++j) { const int c = j * 256 + lane * 4; v[i][j] = ld_bf4(xbi + (size_t)tk[i] * DM + c); ya[i][j] = *(const u32x2*)(Y + s0[i] * DM + c); yb[i][j] = *(const u32x2*)(Y + s1[i] * DM + c); }
; #pragma unroll
;     for (int i = 0; i < NTK; ++i) { float s = 0.f;
; #pragma unroll
;         for (int j = 0; j < 4; ++j) { const f32x4 a = {bf_lo(ya[i][j].x), bf_hi(ya[i][j].x), bf_lo(ya[i][j].y), bf_hi(ya[i][j].y)}, b = {bf_lo(yb[i][j].x), bf_hi(yb[i][j].x), bf_lo(yb[i][j].y), bf_hi(yb[i][j].y)};
;             v[i][j] = v[i][j] + w0[i] * a + w1[i] * b;
;             s += (v[i][j][0] * v[i][j][0] + v[i][j][1] * v[i][j][1]) + (v[i][j][2] * v[i][j][2] + v[i][j][3] * v[i][j][3]); }
	v_lshlrev_b32_e32 v106, 16, v46
	v_and_b32_e32 v107, 0xffff0000, v46
	v_lshlrev_b32_e32 v104, 16, v47
	v_and_b32_e32 v105, 0xffff0000, v47
	s_waitcnt vmcnt(0)
	v_lshlrev_b32_e32 v118, 16, v38
	v_and_b32_e32 v119, 0xffff0000, v38
	v_lshlrev_b32_e32 v114, 16, v39
	v_and_b32_e32 v115, 0xffff0000, v39
	global_load_dwordx2 v[130:131], v140, s[6:7] offset:512
	global_load_dwordx2 v[126:127], v140, s[10:11] offset:512
	global_load_dwordx2 v[38:39], v[44:45], off offset:1024
	v_lshlrev_b32_e32 v136, 16, v110
	v_and_b32_e32 v137, 0xffff0000, v110
	v_lshlrev_b32_e32 v110, 16, v111
	v_and_b32_e32 v111, 0xffff0000, v111
	v_lshlrev_b32_e32 v138, 16, v108
	v_and_b32_e32 v139, 0xffff0000, v108
	v_lshlrev_b32_e32 v108, 16, v109
	v_and_b32_e32 v109, 0xffff0000, v109
	v_pk_fma_f32 v[106:107], v[82:83], v[136:137], v[106:107] op_sel_hi:[0,1,1]
	v_pk_fma_f32 v[104:105], v[82:83], v[110:111], v[104:105] op_sel_hi:[0,1,1]
	v_pk_fma_f32 v[136:137], v[84:85], v[108:109], v[104:105] op_sel_hi:[0,1,1]
	v_pk_fma_f32 v[138:139], v[84:85], v[138:139], v[106:107] op_sel_hi:[0,1,1]
	v_mul_f32_e32 v83, v139, v139
	v_mul_f32_e32 v85, v137, v137
	v_fmac_f32_e32 v83, v138, v138
	v_fmac_f32_e32 v85, v136, v136
	v_add_f32_e32 v83, v83, v85
	s_waitcnt vmcnt(2)
	v_lshlrev_b32_e32 v104, 16, v130
	v_and_b32_e32 v105, 0xffff0000, v130
	s_waitcnt vmcnt(0)
	v_lshlrev_b32_e32 v116, 16, v38
	v_and_b32_e32 v117, 0xffff0000, v38
	v_lshlrev_b32_e32 v112, 16, v39
	v_and_b32_e32 v113, 0xffff0000, v39
	global_load_dwordx2 v[128:129], v140, s[6:7] offset:1024
	global_load_dwordx2 v[124:125], v140, s[10:11] offset:1024
	global_load_dwordx2 v[38:39], v[44:45], off offset:1536
	global_load_dwordx2 v[134:135], v140, s[6:7] offset:1536
	global_load_dwordx2 v[132:133], v140, s[10:11] offset:1536
	v_readfirstlane_b32 s6, v24
	v_readfirstlane_b32 s7, v25
	v_lshlrev_b64 v[24:25], 11, v[32:33]
	v_lshl_add_u64 v[24:25], v[20:21], 0, v[24:25]
	v_lshlrev_b64 v[20:21], 19, v[34:35]
	global_load_dwordx2 v[94:95], v[72:73], off
	global_load_dwordx2 v[92:93], v140, s[2:3]
	global_load_dwordx2 v[90:91], v140, s[6:7]
	global_load_dwordx2 v[100:101], v[72:73], off offset:512
	global_load_dwordx2 v[88:89], v140, s[2:3] offset:512
	global_load_dwordx2 v[86:87], v140, s[6:7] offset:512
	global_load_dwordx2 v[98:99], v[72:73], off offset:1024
	global_load_dwordx2 v[80:81], v140, s[2:3] offset:1024
	global_load_dwordx2 v[78:79], v140, s[6:7] offset:1024
	global_load_dwordx2 v[96:97], v[72:73], off offset:1536
	global_load_dwordx2 v[76:77], v140, s[2:3] offset:1536
	global_load_dwordx2 v[74:75], v140, s[6:7] offset:1536
	s_lshl_b64 s[2:3], s[22:23], 11
	v_lshl_add_u64 v[20:21], s[8:9], 0, v[20:21]
	v_lshl_add_u64 v[26:27], v[20:21], 0, v[26:27]
	v_lshl_add_u64 v[20:21], v[4:5], 0, s[2:3]
	v_readfirstlane_b32 s2, v24
	v_readfirstlane_b32 s3, v25
	v_lshlrev_b64 v[24:25], 19, v[40:41]
	v_readfirstlane_b32 s6, v26
	v_readfirstlane_b32 s7, v27
	v_lshlrev_b64 v[26:27], 11, v[66:67]
	v_lshl_add_u64 v[24:25], s[8:9], 0, v[24:25]
	global_load_dwordx2 v[56:57], v[20:21], off
	global_load_dwordx2 v[54:55], v140, s[2:3]
	v_lshl_add_u64 v[24:25], v[24:25], 0, v[26:27]
	v_readfirstlane_b32 s10, v22
	v_readfirstlane_b32 s11, v23
	v_lshlrev_b32_e32 v106, 16, v131
	v_and_b32_e32 v107, 0xffff0000, v131
	v_lshlrev_b32_e32 v108, 16, v126
	v_and_b32_e32 v109, 0xffff0000, v126
	v_lshlrev_b32_e32 v110, 16, v127
	v_and_b32_e32 v111, 0xffff0000, v127
	v_pk_fma_f32 v[118:119], v[82:83], v[104:105], v[118:119] op_sel_hi:[0,1,1]
	v_pk_fma_f32 v[104:105], v[82:83], v[106:107], v[114:115] op_sel_hi:[0,1,1]
	v_pk_fma_f32 v[104:105], v[84:85], v[110:111], v[104:105] op_sel_hi:[0,1,1]
	v_pk_fma_f32 v[108:109], v[84:85], v[108:109], v[118:119] op_sel_hi:[0,1,1]
	v_mul_f32_e32 v85, v109, v109
	v_mul_f32_e32 v106, v105, v105
	v_fmac_f32_e32 v85, v108, v108
	v_fmac_f32_e32 v106, v104, v104
	v_add_f32_e32 v85, v85, v106
	v_add_f32_e32 v83, v83, v85
	s_waitcnt vmcnt(18)
	v_lshlrev_b32_e32 v106, 16, v128
	v_and_b32_e32 v107, 0xffff0000, v128
	s_waitcnt vmcnt(16)
; __device__ __forceinline__ float bf_lo(unsigned w) { return __uint_as_float(w << 16); }
; __device__ __forceinline__ float bf_hi(unsigned w) { return __uint_as_float(w & 0xffff0000u); }
; __device__ __forceinline__ void st_bf4(bf16_t* p, f32x4 v) { u32x2 w; w.x = cvt_pk_bf16(v[0], v[1]); w.y = cvt_pk_bf16(v[2], v[3]); *(u32x2*)p = w; }
; template <int M> __device__ __forceinline__ float swz_xor(float v) { return __int_as_float(__builtin_amdgcn_ds_swizzle(__float_as_int(v), (M << 10) | 0x1f)); }
; __device__ __forceinline__ float half_sum(float v) { auto rr = __builtin_amdgcn_permlane32_swap(__float_as_uint(v), __float_as_uint(v), false, false); return __uint_as_float(rr[0]) + __uint_as_float(rr[1]); }
; __device__ __forceinline__ float sum32(float v) { v += swz_xor<1>(v); v += swz_xor<2>(v); v += swz_xor<4>(v); v += swz_xor<8>(v); v += swz_xor<16>(v); return v; }
; __device__ __forceinline__ float wave_sum(float v) { return half_sum(sum32(v)); }
; template <int NTK>
; __device__ __forceinline__ void combine_rows(int t0, int tstride, const LAS int* bst, const int* tok_e, const int* tok_pos, const float* tok_w, const bf16_t* Y, const bf16_t* xbi, float* xio, bf16_t* xb, float* part, const float* gfin, bool last, int lane) {
;     ...
;     for (int i = 0; i < NTK; ++i) { float s = 0.f;
; #pragma unroll
;         for (int j = 0; j < 4; ++j) { const f32x4 a = {bf_lo(ya[i][j].x), bf_hi(ya[i][j].x), bf_lo(ya[i][j].y), bf_hi(ya[i][j].y)}, b = {bf_lo(yb[i][j].x), bf_hi(yb[i][j].x), bf_lo(yb[i][j].y), bf_hi(yb[i][j].y)};
;             v[i][j] = v[i][j] + w0[i] * a + w1[i] * b;
;             s += (v[i][j][0] * v[i][j][0] + v[i][j][1] * v[i][j][1]) + (v[i][j][2] * v[i][j][2] + v[i][j][3] * v[i][j][3]); }
;         s = wave_sum(s);
;         if (ok[i]) { const int t = tk[i];
;             if (!last) {
; #pragma unroll
;                 for (int j = 0; j < 4; ++j) { const int c = j * 256 + lane * 4; st_bf4(xb + (size_t)t * DM + c, v[i][j]); }
;                 if (lane < 16) part[(size_t)t * 16 + lane] = lane == 0 ? s : 0.f;
	v_lshlrev_b32_e32 v122, 16, v38
	v_and_b32_e32 v123, 0xffff0000, v38
	v_lshlrev_b32_e32 v120, 16, v39
	v_and_b32_e32 v121, 0xffff0000, v39
	global_load_dwordx2 v[52:53], v140, s[6:7]
	global_load_dwordx2 v[62:63], v[20:21], off offset:512
	global_load_dwordx2 v[50:51], v140, s[2:3] offset:512
	global_load_dwordx2 v[48:49], v140, s[6:7] offset:512
	global_load_dwordx2 v[60:61], v[20:21], off offset:1024
	global_load_dwordx2 v[46:47], v140, s[2:3] offset:1024
	global_load_dwordx2 v[44:45], v140, s[6:7] offset:1024
	global_load_dwordx2 v[58:59], v[20:21], off offset:1536
	global_load_dwordx2 v[38:39], v140, s[2:3] offset:1536
	global_load_dwordx2 v[36:37], v140, s[6:7] offset:1536
	s_lshl_b64 s[6:7], s[18:19], 11
	v_lshl_add_u64 v[18:19], v[4:5], 0, s[6:7]
	v_readfirstlane_b32 s6, v24
	v_readfirstlane_b32 s7, v25
	global_load_dwordx2 v[32:33], v[18:19], off
	v_lshlrev_b32_e32 v110, 16, v129
	v_and_b32_e32 v111, 0xffff0000, v129
	v_lshlrev_b32_e32 v114, 16, v124
	v_and_b32_e32 v115, 0xffff0000, v124
	global_load_dwordx2 v[30:31], v140, s[6:7]
	global_load_dwordx2 v[34:35], v140, s[10:11]
	global_load_dwordx2 v[40:41], v[18:19], off offset:512
	global_load_dwordx2 v[26:27], v140, s[6:7] offset:512
	global_load_dwordx2 v[28:29], v140, s[10:11] offset:512
	global_load_dwordx2 v[42:43], v[18:19], off offset:1024
	global_load_dwordx2 v[22:23], v140, s[6:7] offset:1024
	global_load_dwordx2 v[24:25], v140, s[10:11] offset:1024
	global_load_dwordx2 v[70:71], v[18:19], off offset:1536
	global_load_dwordx2 v[66:67], v140, s[6:7] offset:1536
	global_load_dwordx2 v[68:69], v140, s[10:11] offset:1536
	v_lshlrev_b32_e32 v118, 16, v125
	v_and_b32_e32 v119, 0xffff0000, v125
	v_pk_fma_f32 v[116:117], v[82:83], v[106:107], v[116:117] op_sel_hi:[0,1,1]
	v_pk_fma_f32 v[106:107], v[82:83], v[110:111], v[112:113] op_sel_hi:[0,1,1]
	v_pk_fma_f32 v[106:107], v[84:85], v[118:119], v[106:107] op_sel_hi:[0,1,1]
	v_pk_fma_f32 v[110:111], v[84:85], v[114:115], v[116:117] op_sel_hi:[0,1,1]
	v_mul_f32_e32 v85, v111, v111
	v_mul_f32_e32 v112, v107, v107
	v_fmac_f32_e32 v85, v110, v110
	v_fmac_f32_e32 v112, v106, v106
	v_add_f32_e32 v85, v85, v112
	s_waitcnt vmcnt(37)
	v_lshlrev_b32_e32 v112, 16, v134
	v_and_b32_e32 v113, 0xffff0000, v134
	v_lshlrev_b32_e32 v114, 16, v135
	v_and_b32_e32 v115, 0xffff0000, v135
	v_add_f32_e32 v124, v83, v85
	s_waitcnt vmcnt(36)
	v_lshlrev_b32_e32 v116, 16, v132
	v_and_b32_e32 v117, 0xffff0000, v132
	v_lshlrev_b32_e32 v118, 16, v133
	v_and_b32_e32 v119, 0xffff0000, v133
	v_pk_fma_f32 v[112:113], v[82:83], v[112:113], v[122:123] op_sel_hi:[0,1,1]
	v_pk_fma_f32 v[82:83], v[82:83], v[114:115], v[120:121] op_sel_hi:[0,1,1]
	v_pk_fma_f32 v[82:83], v[84:85], v[118:119], v[82:83] op_sel_hi:[0,1,1]
	v_pk_fma_f32 v[84:85], v[84:85], v[116:117], v[112:113] op_sel_hi:[0,1,1]
	v_mul_f32_e32 v112, v85, v85
	v_mul_f32_e32 v113, v83, v83
	v_fmac_f32_e32 v112, v84, v84
	v_fmac_f32_e32 v113, v82, v82
	v_add_f32_e32 v112, v112, v113
	v_add_f32_e32 v112, v124, v112
	s_mov_b64 s[10:11], -1
	s_waitcnt lgkmcnt(0)
	s_nop 1
	v_add_f32_dpp v112, v112, v112 quad_perm:[1,0,3,2] row_mask:0xf bank_mask:0xf
	s_waitcnt lgkmcnt(0)
	s_nop 1
	v_add_f32_dpp v112, v112, v112 quad_perm:[2,3,0,1] row_mask:0xf bank_mask:0xf
	s_waitcnt lgkmcnt(0)
	s_nop 1
	v_add_f32_dpp v112, v112, v112 row_half_mirror row_mask:0xf bank_mask:0xf
	s_waitcnt lgkmcnt(0)
	s_nop 1
	v_add_f32_dpp v112, v112, v112 row_mirror row_mask:0xf bank_mask:0xf
	v_mov_b32_e32 v113, v112
	s_waitcnt lgkmcnt(0)
	s_nop 1
	v_permlane16_swap_b32_e32 v113, v112
	v_add_f32_e32 v112, v112, v113
	v_mov_b32_e32 v113, v112
	s_nop 1
	v_permlane32_swap_b32_e32 v112, v113
	v_add_f32_e32 v112, v112, v113
	v_cndmask_b32_e64 v113, 0, 1, s[14:15]
	v_cmp_ne_u32_e64 s[6:7], 1, v113
	s_cbranch_vccnz .LBB0_1637
	s_mov_b64 s[2:3], 0x2a00000
	v_lshl_add_u64 v[114:115], v[102:103], 0, s[2:3]
	s_mov_b64 s[2:3], 0x2a00200
	v_lshl_add_u64 v[116:117], v[102:103], 0, s[2:3]
	s_mov_b64 s[2:3], 0x2a00400
	v_lshl_add_u64 v[118:119], v[102:103], 0, s[2:3]
	s_mov_b64 s[2:3], 0x2a00600
	v_cvt_pk_bf16_f32 v120, v138, v139
	v_cvt_pk_bf16_f32 v121, v136, v137
	global_store_dwordx2 v[114:115], v[120:121], off
	v_cvt_pk_bf16_f32 v114, v108, v109
	v_cvt_pk_bf16_f32 v115, v104, v105
	v_lshl_add_u64 v[102:103], v[102:103], 0, s[2:3]
	global_store_dwordx2 v[116:117], v[114:115], off
	v_cvt_pk_bf16_f32 v114, v110, v111
	v_cvt_pk_bf16_f32 v115, v106, v107
	global_store_dwordx2 v[118:119], v[114:115], off
	v_cvt_pk_bf16_f32 v114, v84, v85
	v_cvt_pk_bf16_f32 v115, v82, v83
	global_store_dwordx2 v[102:103], v[114:115], off
	s_and_saveexec_b64 s[10:11], s[0:1]
	s_cbranch_execz .LBB0_1636
	v_cndmask_b32_e64 v113, 0, v112, s[4:5]
	v_lshl_add_u64 v[102:103], s[52:53], 0, v[12:13]
	global_store_dword v[102:103], v113, off

; __device__ __forceinline__ float bf_lo(unsigned w) { return __uint_as_float(w << 16); }
; __device__ __forceinline__ float bf_hi(unsigned w) { return __uint_as_float(w & 0xffff0000u); }
; __device__ __forceinline__ float wave_sum(float v) { return half_sum(sum32(v)); }
; __device__ __forceinline__ void st_bf4(bf16_t* p, f32x4 v) { u32x2 w; w.x = cvt_pk_bf16(v[0], v[1]); w.y = cvt_pk_bf16(v[2], v[3]); *(u32x2*)p = w; }
; template <int NTK>
; __device__ __forceinline__ void combine_rows(int t0, int tstride, const LAS int* bst, const int* tok_e, const int* tok_pos, const float* tok_w, const bf16_t* Y, const bf16_t* xbi, float* xio, bf16_t* xb, float* part, const float* gfin, bool last, int lane) {
;     ...
;     for (int i = 0; i < NTK; ++i) { float s = 0.f;
; #pragma unroll
;         for (int j = 0; j < 4; ++j) { const f32x4 a = {bf_lo(ya[i][j].x), bf_hi(ya[i][j].x), bf_lo(ya[i][j].y), bf_hi(ya[i][j].y)}, b = {bf_lo(yb[i][j].x), bf_hi(yb[i][j].x), bf_lo(yb[i][j].y), bf_hi(yb[i][j].y)};
;             v[i][j] = v[i][j] + w0[i] * a + w1[i] * b;
;             s += (v[i][j][0] * v[i][j][0] + v[i][j][1] * v[i][j][1]) + (v[i][j][2] * v[i][j][2] + v[i][j][3] * v[i][j][3]); }
;         s = wave_sum(s);
;         if (ok[i]) { const int t = tk[i];
;             if (!last) {
; #pragma unroll
;                 for (int j = 0; j < 4; ++j) { const int c = j * 256 + lane * 4; st_bf4(xb + (size_t)t * DM + c, v[i][j]); }
;                 if (lane < 16) part[(size_t)t * 16 + lane] = lane == 0 ? s : 0.f;
.LBB0_1639:
	s_waitcnt vmcnt(35)
	s_nop 0
	v_lshlrev_b32_e32 v82, 16, v94
	v_and_b32_e32 v83, 0xffff0000, v94
	v_lshlrev_b32_e32 v84, 16, v95
	v_and_b32_e32 v85, 0xffff0000, v95
	s_waitcnt vmcnt(34)
	v_lshlrev_b32_e32 v106, 16, v92
	v_and_b32_e32 v107, 0xffff0000, v92
	v_lshlrev_b32_e32 v92, 16, v93
	v_and_b32_e32 v93, 0xffff0000, v93
	s_waitcnt vmcnt(33)
	v_lshlrev_b32_e32 v108, 16, v90
	v_and_b32_e32 v109, 0xffff0000, v90
	v_lshlrev_b32_e32 v90, 16, v91
	v_and_b32_e32 v91, 0xffff0000, v91
	v_pk_fma_f32 v[82:83], v[64:65], v[106:107], v[82:83] op_sel_hi:[0,1,1]
	v_pk_fma_f32 v[84:85], v[64:65], v[92:93], v[84:85] op_sel_hi:[0,1,1]
	v_pk_fma_f32 v[90:91], v[64:65], v[90:91], v[84:85] op_sel:[1,0,0]
	v_pk_fma_f32 v[92:93], v[64:65], v[108:109], v[82:83] op_sel:[1,0,0]
	v_mul_f32_e32 v83, v91, v91
	v_mul_f32_e32 v82, v93, v93
	v_fmac_f32_e32 v82, v92, v92
	v_fmac_f32_e32 v83, v90, v90
	s_waitcnt vmcnt(32)
	v_lshlrev_b32_e32 v94, 16, v100
	v_and_b32_e32 v95, 0xffff0000, v100
	v_lshlrev_b32_e32 v100, 16, v101
	v_and_b32_e32 v101, 0xffff0000, v101
	v_add_f32_e32 v106, v82, v83
	s_waitcnt vmcnt(31)
	v_lshlrev_b32_e32 v82, 16, v88
	v_and_b32_e32 v83, 0xffff0000, v88
	v_lshlrev_b32_e32 v84, 16, v89
	v_and_b32_e32 v85, 0xffff0000, v89
	s_waitcnt vmcnt(30)
	v_lshlrev_b32_e32 v88, 16, v86
	v_and_b32_e32 v89, 0xffff0000, v86
	v_lshlrev_b32_e32 v86, 16, v87
	v_and_b32_e32 v87, 0xffff0000, v87
	v_pk_fma_f32 v[94:95], v[64:65], v[82:83], v[94:95] op_sel_hi:[0,1,1]
	v_pk_fma_f32 v[82:83], v[64:65], v[84:85], v[100:101] op_sel_hi:[0,1,1]
	v_pk_fma_f32 v[82:83], v[64:65], v[86:87], v[82:83] op_sel:[1,0,0]
	v_pk_fma_f32 v[84:85], v[64:65], v[88:89], v[94:95] op_sel:[1,0,0]
	v_mul_f32_e32 v87, v83, v83
	v_mul_f32_e32 v86, v85, v85
	v_fmac_f32_e32 v86, v84, v84
	v_fmac_f32_e32 v87, v82, v82
	v_add_f32_e32 v86, v86, v87
	s_waitcnt vmcnt(29)
	v_lshlrev_b32_e32 v102, 16, v98
	v_and_b32_e32 v103, 0xffff0000, v98
	v_lshlrev_b32_e32 v98, 16, v99
	v_and_b32_e32 v99, 0xffff0000, v99
	v_add_f32_e32 v94, v106, v86
	s_waitcnt vmcnt(28)
	v_lshlrev_b32_e32 v86, 16, v80
	v_and_b32_e32 v87, 0xffff0000, v80
	v_lshlrev_b32_e32 v80, 16, v81
	v_and_b32_e32 v81, 0xffff0000, v81
	s_waitcnt vmcnt(27)
	v_lshlrev_b32_e32 v88, 16, v78
	v_and_b32_e32 v89, 0xffff0000, v78
	v_lshlrev_b32_e32 v78, 16, v79
	v_and_b32_e32 v79, 0xffff0000, v79
	v_pk_fma_f32 v[86:87], v[64:65], v[86:87], v[102:103] op_sel_hi:[0,1,1]
	v_pk_fma_f32 v[80:81], v[64:65], v[80:81], v[98:99] op_sel_hi:[0,1,1]
	v_pk_fma_f32 v[78:79], v[64:65], v[78:79], v[80:81] op_sel:[1,0,0]
	v_pk_fma_f32 v[80:81], v[64:65], v[88:89], v[86:87] op_sel:[1,0,0]
	v_mul_f32_e32 v87, v79, v79
	v_mul_f32_e32 v86, v81, v81
	v_fmac_f32_e32 v86, v80, v80
	v_fmac_f32_e32 v87, v78, v78
	v_add_f32_e32 v86, v86, v87
	s_waitcnt vmcnt(26)
	v_lshlrev_b32_e32 v104, 16, v96
	v_and_b32_e32 v105, 0xffff0000, v96
	v_lshlrev_b32_e32 v96, 16, v97
	v_and_b32_e32 v97, 0xffff0000, v97
	v_add_f32_e32 v94, v94, v86
	s_waitcnt vmcnt(25)
	v_lshlrev_b32_e32 v86, 16, v76
	v_and_b32_e32 v87, 0xffff0000, v76
	v_lshlrev_b32_e32 v76, 16, v77
	v_and_b32_e32 v77, 0xffff0000, v77
	s_waitcnt vmcnt(24)
	v_lshlrev_b32_e32 v88, 16, v74
	v_and_b32_e32 v89, 0xffff0000, v74
	v_lshlrev_b32_e32 v74, 16, v75
	v_and_b32_e32 v75, 0xffff0000, v75
	v_pk_fma_f32 v[86:87], v[64:65], v[86:87], v[104:105] op_sel_hi:[0,1,1]
	v_pk_fma_f32 v[76:77], v[64:65], v[76:77], v[96:97] op_sel_hi:[0,1,1]
	v_pk_fma_f32 v[74:75], v[64:65], v[74:75], v[76:77] op_sel:[1,0,0]
	v_pk_fma_f32 v[64:65], v[64:65], v[88:89], v[86:87] op_sel:[1,0,0]
	v_mul_f32_e32 v77, v75, v75
	v_mul_f32_e32 v76, v65, v65
	v_fmac_f32_e32 v76, v64, v64
	v_fmac_f32_e32 v77, v74, v74
	v_add_f32_e32 v76, v76, v77
	v_add_f32_e32 v76, v94, v76
	ds_swizzle_b32 v77, v76 offset:swizzle(SWAP,1)
	s_andn2_b64 vcc, exec, s[28:29]
	s_waitcnt lgkmcnt(0)
	v_add_f32_e32 v76, v76, v77
	ds_swizzle_b32 v77, v76 offset:swizzle(SWAP,2)
	s_waitcnt lgkmcnt(0)
	v_add_f32_e32 v76, v76, v77
	ds_swizzle_b32 v77, v76 offset:swizzle(SWAP,4)
	s_waitcnt lgkmcnt(0)
	v_add_f32_e32 v76, v76, v77
	ds_swizzle_b32 v77, v76 offset:swizzle(SWAP,8)
	s_waitcnt lgkmcnt(0)
	v_add_f32_e32 v76, v76, v77
	v_mov_b32_e32 v77, v76
	s_waitcnt lgkmcnt(0)
	s_nop 1
	v_permlane16_swap_b32_e32 v77, v76
	v_add_f32_e32 v76, v76, v77
	v_mov_b32_e32 v77, v76
	s_nop 1
	v_permlane32_swap_b32_e32 v76, v77
	s_cbranch_vccnz .LBB0_1646
	v_add_f32_e32 v76, v76, v77
	s_and_b64 vcc, exec, s[6:7]
	s_mov_b64 s[10:11], -1
	s_cbranch_vccnz .LBB0_1644
	v_cvt_pk_bf16_f32 v86, v92, v93
	v_cvt_pk_bf16_f32 v87, v90, v91
	global_store_dwordx2 v[72:73], v[86:87], off
	v_cvt_pk_bf16_f32 v86, v84, v85
	v_cvt_pk_bf16_f32 v87, v82, v83
	global_store_dwordx2 v[72:73], v[86:87], off offset:512
	v_cvt_pk_bf16_f32 v86, v80, v81
	v_cvt_pk_bf16_f32 v87, v78, v79
	global_store_dwordx2 v[72:73], v[86:87], off offset:1024
	v_cvt_pk_bf16_f32 v86, v64, v65
	v_cvt_pk_bf16_f32 v87, v74, v75
	global_store_dwordx2 v[72:73], v[86:87], off offset:1536
	s_and_saveexec_b64 s[10:11], s[0:1]
	s_cbranch_execz .LBB0_1643
	s_lshl_b64 s[2:3], s[26:27], 6
	v_cndmask_b32_e64 v77, 0, v76, s[4:5]
	v_lshl_add_u64 v[72:73], v[0:1], 0, s[2:3]
	global_store_dword v[72:73], v77, off

; __device__ __forceinline__ float bf_lo(unsigned w) { return __uint_as_float(w << 16); }
; __device__ __forceinline__ float bf_hi(unsigned w) { return __uint_as_float(w & 0xffff0000u); }
; __device__ __forceinline__ float wave_sum(float v) { return half_sum(sum32(v)); }
; __device__ __forceinline__ void st_bf4(bf16_t* p, f32x4 v) { u32x2 w; w.x = cvt_pk_bf16(v[0], v[1]); w.y = cvt_pk_bf16(v[2], v[3]); *(u32x2*)p = w; }
; template <int NTK>
; __device__ __forceinline__ void combine_rows(int t0, int tstride, const LAS int* bst, const int* tok_e, const int* tok_pos, const float* tok_w, const bf16_t* Y, const bf16_t* xbi, float* xio, bf16_t* xb, float* part, const float* gfin, bool last, int lane) {
;     ...
;     for (int i = 0; i < NTK; ++i) { float s = 0.f;
; #pragma unroll
;         for (int j = 0; j < 4; ++j) { const f32x4 a = {bf_lo(ya[i][j].x), bf_hi(ya[i][j].x), bf_lo(ya[i][j].y), bf_hi(ya[i][j].y)}, b = {bf_lo(yb[i][j].x), bf_hi(yb[i][j].x), bf_lo(yb[i][j].y), bf_hi(yb[i][j].y)};
;             v[i][j] = v[i][j] + w0[i] * a + w1[i] * b;
;             s += (v[i][j][0] * v[i][j][0] + v[i][j][1] * v[i][j][1]) + (v[i][j][2] * v[i][j][2] + v[i][j][3] * v[i][j][3]); }
;         s = wave_sum(s);
;         if (ok[i]) { const int t = tk[i];
;             if (!last) {
; #pragma unroll
;                 for (int j = 0; j < 4; ++j) { const int c = j * 256 + lane * 4; st_bf4(xb + (size_t)t * DM + c, v[i][j]); }
;                 if (lane < 16) part[(size_t)t * 16 + lane] = lane == 0 ? s : 0.f;
.LBB0_1646:
	s_waitcnt vmcnt(23)
	v_lshlrev_b32_e32 v64, 16, v56
	v_and_b32_e32 v65, 0xffff0000, v56
	v_lshlrev_b32_e32 v56, 16, v57
	v_and_b32_e32 v57, 0xffff0000, v57
	s_waitcnt vmcnt(22)
	v_lshlrev_b32_e32 v78, 16, v54
	v_and_b32_e32 v79, 0xffff0000, v54
	v_lshlrev_b32_e32 v54, 16, v55
	v_and_b32_e32 v55, 0xffff0000, v55
	s_waitcnt vmcnt(21)
	v_lshlrev_b32_e32 v80, 16, v52
	v_and_b32_e32 v81, 0xffff0000, v52
	v_lshlrev_b32_e32 v52, 16, v53
	v_and_b32_e32 v53, 0xffff0000, v53
	v_pk_fma_f32 v[64:65], v[16:17], v[78:79], v[64:65] op_sel_hi:[0,1,1]
	v_pk_fma_f32 v[54:55], v[16:17], v[54:55], v[56:57] op_sel_hi:[0,1,1]
	v_pk_fma_f32 v[52:53], v[16:17], v[52:53], v[54:55] op_sel:[1,0,0]
	v_pk_fma_f32 v[54:55], v[16:17], v[80:81], v[64:65] op_sel:[1,0,0]
	v_mul_f32_e32 v57, v53, v53
	v_mul_f32_e32 v56, v55, v55
	v_fmac_f32_e32 v56, v54, v54
	v_fmac_f32_e32 v57, v52, v52
	s_waitcnt vmcnt(20)
	v_lshlrev_b32_e32 v72, 16, v62
	v_and_b32_e32 v73, 0xffff0000, v62
	v_lshlrev_b32_e32 v62, 16, v63
	v_and_b32_e32 v63, 0xffff0000, v63
	v_add_f32_e32 v78, v56, v57
	s_waitcnt vmcnt(19)
	v_lshlrev_b32_e32 v56, 16, v50
	v_and_b32_e32 v57, 0xffff0000, v50
	v_lshlrev_b32_e32 v50, 16, v51
	v_and_b32_e32 v51, 0xffff0000, v51
	s_waitcnt vmcnt(18)
	v_lshlrev_b32_e32 v64, 16, v48
	v_and_b32_e32 v65, 0xffff0000, v48
	v_lshlrev_b32_e32 v48, 16, v49
	v_and_b32_e32 v49, 0xffff0000, v49
	v_pk_fma_f32 v[56:57], v[16:17], v[56:57], v[72:73] op_sel_hi:[0,1,1]
	v_pk_fma_f32 v[50:51], v[16:17], v[50:51], v[62:63] op_sel_hi:[0,1,1]
	v_pk_fma_f32 v[48:49], v[16:17], v[48:49], v[50:51] op_sel:[1,0,0]
	v_pk_fma_f32 v[50:51], v[16:17], v[64:65], v[56:57] op_sel:[1,0,0]
	v_mul_f32_e32 v57, v49, v49
	v_mul_f32_e32 v56, v51, v51
	v_fmac_f32_e32 v56, v50, v50
	v_fmac_f32_e32 v57, v48, v48
	v_add_f32_e32 v56, v56, v57
	s_waitcnt vmcnt(17)
	v_lshlrev_b32_e32 v74, 16, v60
	v_and_b32_e32 v75, 0xffff0000, v60
	v_lshlrev_b32_e32 v60, 16, v61
	v_and_b32_e32 v61, 0xffff0000, v61
	v_add_f32_e32 v64, v78, v56
	s_waitcnt vmcnt(16)
	v_lshlrev_b32_e32 v56, 16, v46
	v_and_b32_e32 v57, 0xffff0000, v46
	v_lshlrev_b32_e32 v46, 16, v47
	v_and_b32_e32 v47, 0xffff0000, v47
	s_waitcnt vmcnt(15)
	v_lshlrev_b32_e32 v62, 16, v44
	v_and_b32_e32 v63, 0xffff0000, v44
	v_lshlrev_b32_e32 v44, 16, v45
	v_and_b32_e32 v45, 0xffff0000, v45
	v_pk_fma_f32 v[56:57], v[16:17], v[56:57], v[74:75] op_sel_hi:[0,1,1]
	v_pk_fma_f32 v[46:47], v[16:17], v[46:47], v[60:61] op_sel_hi:[0,1,1]
	v_pk_fma_f32 v[44:45], v[16:17], v[44:45], v[46:47] op_sel:[1,0,0]
	v_pk_fma_f32 v[46:47], v[16:17], v[62:63], v[56:57] op_sel:[1,0,0]
	v_mul_f32_e32 v57, v45, v45
	v_mul_f32_e32 v56, v47, v47
	v_fmac_f32_e32 v56, v46, v46
	v_fmac_f32_e32 v57, v44, v44
	v_add_f32_e32 v56, v56, v57
	s_waitcnt vmcnt(14)
	v_lshlrev_b32_e32 v76, 16, v58
	v_and_b32_e32 v77, 0xffff0000, v58
	v_lshlrev_b32_e32 v58, 16, v59
	v_and_b32_e32 v59, 0xffff0000, v59
	v_add_f32_e32 v62, v64, v56
	s_waitcnt vmcnt(13)
	v_lshlrev_b32_e32 v56, 16, v38
	v_and_b32_e32 v57, 0xffff0000, v38
	v_lshlrev_b32_e32 v38, 16, v39
	v_and_b32_e32 v39, 0xffff0000, v39
	s_waitcnt vmcnt(12)
	v_lshlrev_b32_e32 v60, 16, v36
	v_and_b32_e32 v61, 0xffff0000, v36
	v_lshlrev_b32_e32 v36, 16, v37
	v_and_b32_e32 v37, 0xffff0000, v37
	v_pk_fma_f32 v[56:57], v[16:17], v[56:57], v[76:77] op_sel_hi:[0,1,1]
	v_pk_fma_f32 v[38:39], v[16:17], v[38:39], v[58:59] op_sel_hi:[0,1,1]
	v_pk_fma_f32 v[36:37], v[16:17], v[36:37], v[38:39] op_sel:[1,0,0]
	v_pk_fma_f32 v[16:17], v[16:17], v[60:61], v[56:57] op_sel:[1,0,0]
	v_mul_f32_e32 v39, v37, v37
	v_mul_f32_e32 v38, v17, v17
	v_fmac_f32_e32 v38, v16, v16
	v_fmac_f32_e32 v39, v36, v36
	v_add_f32_e32 v38, v38, v39
	v_add_f32_e32 v38, v62, v38
	ds_swizzle_b32 v39, v38 offset:swizzle(SWAP,1)
	s_andn2_b64 vcc, exec, s[24:25]
	s_waitcnt lgkmcnt(0)
	v_add_f32_e32 v38, v38, v39
	ds_swizzle_b32 v39, v38 offset:swizzle(SWAP,2)
	s_waitcnt lgkmcnt(0)
	v_add_f32_e32 v38, v38, v39
	ds_swizzle_b32 v39, v38 offset:swizzle(SWAP,4)
	s_waitcnt lgkmcnt(0)
	v_add_f32_e32 v38, v38, v39
	ds_swizzle_b32 v39, v38 offset:swizzle(SWAP,8)
	s_waitcnt lgkmcnt(0)
	v_add_f32_e32 v38, v38, v39
	v_mov_b32_e32 v39, v38
	s_waitcnt lgkmcnt(0)
	s_nop 1
	v_permlane16_swap_b32_e32 v39, v38
	v_add_f32_e32 v38, v38, v39
	v_mov_b32_e32 v39, v38
	s_nop 1
	v_permlane32_swap_b32_e32 v38, v39
	s_cbranch_vccnz .LBB0_1653
	v_add_f32_e32 v38, v38, v39
	s_and_b64 vcc, exec, s[6:7]
	s_mov_b64 s[10:11], -1
	s_cbranch_vccnz .LBB0_1651
	v_cvt_pk_bf16_f32 v56, v54, v55
	v_cvt_pk_bf16_f32 v57, v52, v53
	global_store_dwordx2 v[20:21], v[56:57], off
	v_cvt_pk_bf16_f32 v56, v50, v51
	v_cvt_pk_bf16_f32 v57, v48, v49
	global_store_dwordx2 v[20:21], v[56:57], off offset:512
	v_cvt_pk_bf16_f32 v56, v46, v47
	v_cvt_pk_bf16_f32 v57, v44, v45
	global_store_dwordx2 v[20:21], v[56:57], off offset:1024
	v_cvt_pk_bf16_f32 v56, v16, v17
	v_cvt_pk_bf16_f32 v57, v36, v37
	global_store_dwordx2 v[20:21], v[56:57], off offset:1536
	s_and_saveexec_b64 s[10:11], s[0:1]
	s_cbranch_execz .LBB0_1650
	s_lshl_b64 s[2:3], s[22:23], 6
	v_cndmask_b32_e64 v39, 0, v38, s[4:5]
	v_lshl_add_u64 v[20:21], v[0:1], 0, s[2:3]
	global_store_dword v[20:21], v39, off

; __device__ __forceinline__ float bf_lo(unsigned w) { return __uint_as_float(w << 16); }
; __device__ __forceinline__ float bf_hi(unsigned w) { return __uint_as_float(w & 0xffff0000u); }
; __device__ __forceinline__ float wave_sum(float v) { return half_sum(sum32(v)); }
; __device__ __forceinline__ void st_bf4(bf16_t* p, f32x4 v) { u32x2 w; w.x = cvt_pk_bf16(v[0], v[1]); w.y = cvt_pk_bf16(v[2], v[3]); *(u32x2*)p = w; }
; template <int NTK>
; __device__ __forceinline__ void combine_rows(int t0, int tstride, const LAS int* bst, const int* tok_e, const int* tok_pos, const float* tok_w, const bf16_t* Y, const bf16_t* xbi, float* xio, bf16_t* xb, float* part, const float* gfin, bool last, int lane) {
;     ...
;     for (int i = 0; i < NTK; ++i) { float s = 0.f;
; #pragma unroll
;         for (int j = 0; j < 4; ++j) { const f32x4 a = {bf_lo(ya[i][j].x), bf_hi(ya[i][j].x), bf_lo(ya[i][j].y), bf_hi(ya[i][j].y)}, b = {bf_lo(yb[i][j].x), bf_hi(yb[i][j].x), bf_lo(yb[i][j].y), bf_hi(yb[i][j].y)};
;             v[i][j] = v[i][j] + w0[i] * a + w1[i] * b;
;             s += (v[i][j][0] * v[i][j][0] + v[i][j][1] * v[i][j][1]) + (v[i][j][2] * v[i][j][2] + v[i][j][3] * v[i][j][3]); }
;         s = wave_sum(s);
;         if (ok[i]) { const int t = tk[i];
;             if (!last) {
; #pragma unroll
;                 for (int j = 0; j < 4; ++j) { const int c = j * 256 + lane * 4; st_bf4(xb + (size_t)t * DM + c, v[i][j]); }
;                 if (lane < 16) part[(size_t)t * 16 + lane] = lane == 0 ? s : 0.f;
.LBB0_1653:
	s_waitcnt vmcnt(11)
	v_lshlrev_b32_e32 v16, 16, v32
	v_and_b32_e32 v17, 0xffff0000, v32
	v_lshlrev_b32_e32 v20, 16, v33
	v_and_b32_e32 v21, 0xffff0000, v33
	s_waitcnt vmcnt(10)
	v_lshlrev_b32_e32 v32, 16, v30
	v_and_b32_e32 v33, 0xffff0000, v30
	v_lshlrev_b32_e32 v30, 16, v31
	v_and_b32_e32 v31, 0xffff0000, v31
	s_waitcnt vmcnt(9)
	v_lshlrev_b32_e32 v48, 16, v34
	v_and_b32_e32 v49, 0xffff0000, v34
	v_lshlrev_b32_e32 v34, 16, v35
	v_and_b32_e32 v35, 0xffff0000, v35
	v_pk_fma_f32 v[16:17], v[14:15], v[32:33], v[16:17] op_sel_hi:[0,1,1]
	v_pk_fma_f32 v[20:21], v[14:15], v[30:31], v[20:21] op_sel_hi:[0,1,1]
	v_pk_fma_f32 v[30:31], v[14:15], v[34:35], v[20:21] op_sel:[1,0,0]
	v_pk_fma_f32 v[32:33], v[14:15], v[48:49], v[16:17] op_sel:[1,0,0]
	v_mul_f32_e32 v17, v31, v31
	v_mul_f32_e32 v16, v33, v33
	v_fmac_f32_e32 v16, v32, v32
	v_fmac_f32_e32 v17, v30, v30
	s_waitcnt vmcnt(8)
	v_lshlrev_b32_e32 v36, 16, v40
	v_and_b32_e32 v37, 0xffff0000, v40
	v_lshlrev_b32_e32 v38, 16, v41
	v_and_b32_e32 v39, 0xffff0000, v41
	v_add_f32_e32 v48, v16, v17
	s_waitcnt vmcnt(7)
	v_lshlrev_b32_e32 v16, 16, v26
	v_and_b32_e32 v17, 0xffff0000, v26
	v_lshlrev_b32_e32 v20, 16, v27
	v_and_b32_e32 v21, 0xffff0000, v27
	s_waitcnt vmcnt(6)
	v_lshlrev_b32_e32 v26, 16, v28
	v_and_b32_e32 v27, 0xffff0000, v28
	v_lshlrev_b32_e32 v28, 16, v29
	v_and_b32_e32 v29, 0xffff0000, v29
	v_pk_fma_f32 v[34:35], v[14:15], v[16:17], v[36:37] op_sel_hi:[0,1,1]
	v_pk_fma_f32 v[16:17], v[14:15], v[20:21], v[38:39] op_sel_hi:[0,1,1]
	v_pk_fma_f32 v[16:17], v[14:15], v[28:29], v[16:17] op_sel:[1,0,0]
	v_pk_fma_f32 v[26:27], v[14:15], v[26:27], v[34:35] op_sel:[1,0,0]
	v_mul_f32_e32 v21, v17, v17
	v_mul_f32_e32 v20, v27, v27
	v_fmac_f32_e32 v20, v26, v26
	v_fmac_f32_e32 v21, v16, v16
	v_add_f32_e32 v20, v20, v21
	s_waitcnt vmcnt(5)
	v_lshlrev_b32_e32 v40, 16, v42
	v_and_b32_e32 v41, 0xffff0000, v42
	v_lshlrev_b32_e32 v42, 16, v43
	v_and_b32_e32 v43, 0xffff0000, v43
	v_add_f32_e32 v36, v48, v20
	s_waitcnt vmcnt(4)
	v_lshlrev_b32_e32 v20, 16, v22
	v_and_b32_e32 v21, 0xffff0000, v22
	v_lshlrev_b32_e32 v22, 16, v23
	v_and_b32_e32 v23, 0xffff0000, v23
	s_waitcnt vmcnt(3)
	v_lshlrev_b32_e32 v28, 16, v24
	v_and_b32_e32 v29, 0xffff0000, v24
	v_lshlrev_b32_e32 v24, 16, v25
	v_and_b32_e32 v25, 0xffff0000, v25
	v_pk_fma_f32 v[34:35], v[14:15], v[20:21], v[40:41] op_sel_hi:[0,1,1]
	v_pk_fma_f32 v[20:21], v[14:15], v[22:23], v[42:43] op_sel_hi:[0,1,1]
	v_pk_fma_f32 v[20:21], v[14:15], v[24:25], v[20:21] op_sel:[1,0,0]
	v_pk_fma_f32 v[24:25], v[14:15], v[28:29], v[34:35] op_sel:[1,0,0]
	v_mul_f32_e32 v23, v21, v21
	v_mul_f32_e32 v22, v25, v25
	v_fmac_f32_e32 v22, v24, v24
	v_fmac_f32_e32 v23, v20, v20
	v_add_f32_e32 v22, v22, v23
	s_waitcnt vmcnt(2)
	v_lshlrev_b32_e32 v44, 16, v70
	v_and_b32_e32 v45, 0xffff0000, v70
	v_lshlrev_b32_e32 v46, 16, v71
	v_and_b32_e32 v47, 0xffff0000, v71
	v_add_f32_e32 v40, v36, v22
	s_waitcnt vmcnt(1)
	v_lshlrev_b32_e32 v22, 16, v66
	v_and_b32_e32 v23, 0xffff0000, v66
	v_lshlrev_b32_e32 v28, 16, v67
	v_and_b32_e32 v29, 0xffff0000, v67
	s_waitcnt vmcnt(0)
	v_lshlrev_b32_e32 v34, 16, v68
	v_and_b32_e32 v35, 0xffff0000, v68
	v_lshlrev_b32_e32 v36, 16, v69
	v_and_b32_e32 v37, 0xffff0000, v69
	v_pk_fma_f32 v[38:39], v[14:15], v[22:23], v[44:45] op_sel_hi:[0,1,1]
	v_pk_fma_f32 v[22:23], v[14:15], v[28:29], v[46:47] op_sel_hi:[0,1,1]
	v_pk_fma_f32 v[22:23], v[14:15], v[36:37], v[22:23] op_sel:[1,0,0]
	v_pk_fma_f32 v[14:15], v[14:15], v[34:35], v[38:39] op_sel:[1,0,0]
	v_mul_f32_e32 v29, v23, v23
	v_mul_f32_e32 v28, v15, v15
	v_fmac_f32_e32 v28, v14, v14
	v_fmac_f32_e32 v29, v22, v22
	v_add_f32_e32 v28, v28, v29
	v_add_f32_e32 v28, v40, v28
	ds_swizzle_b32 v29, v28 offset:swizzle(SWAP,1)
	s_andn2_b64 vcc, exec, s[20:21]
	s_waitcnt lgkmcnt(0)
	v_add_f32_e32 v28, v28, v29
	ds_swizzle_b32 v29, v28 offset:swizzle(SWAP,2)
	s_waitcnt lgkmcnt(0)
	v_add_f32_e32 v28, v28, v29
	ds_swizzle_b32 v29, v28 offset:swizzle(SWAP,4)
	s_waitcnt lgkmcnt(0)
	v_add_f32_e32 v28, v28, v29
	ds_swizzle_b32 v29, v28 offset:swizzle(SWAP,8)
	s_waitcnt lgkmcnt(0)
	v_add_f32_e32 v28, v28, v29
	v_mov_b32_e32 v29, v28
	s_waitcnt lgkmcnt(0)
	s_nop 1
	v_permlane16_swap_b32_e32 v29, v28
	v_add_f32_e32 v28, v28, v29
	v_mov_b32_e32 v29, v28
	s_nop 1
	v_permlane32_swap_b32_e32 v28, v29
	s_cbranch_vccnz .LBB0_1632
	v_add_f32_e32 v28, v28, v29
	s_and_b64 vcc, exec, s[6:7]
	s_mov_b64 s[6:7], -1
	s_cbranch_vccnz .LBB0_1658
	v_cvt_pk_bf16_f32 v34, v32, v33
	v_cvt_pk_bf16_f32 v35, v30, v31
	global_store_dwordx2 v[18:19], v[34:35], off
	v_cvt_pk_bf16_f32 v34, v26, v27
	v_cvt_pk_bf16_f32 v35, v16, v17
	global_store_dwordx2 v[18:19], v[34:35], off offset:512
	v_cvt_pk_bf16_f32 v34, v24, v25
	v_cvt_pk_bf16_f32 v35, v20, v21
	global_store_dwordx2 v[18:19], v[34:35], off offset:1024
	v_cvt_pk_bf16_f32 v34, v14, v15
	v_cvt_pk_bf16_f32 v35, v22, v23
	global_store_dwordx2 v[18:19], v[34:35], off offset:1536
	s_and_saveexec_b64 s[6:7], s[0:1]
	s_cbranch_execz .LBB0_1657
	s_lshl_b64 s[2:3], s[18:19], 6
	v_cndmask_b32_e64 v29, 0, v28, s[4:5]
	v_lshl_add_u64 v[18:19], v[0:1], 0, s[2:3]
	global_store_dword v[18:19], v29, off
